# GEMM K-loops: s_setprio 1 hoisted in front of each MFMA segment's opening barrier, duplicate lgkmcnt(0) behind it dropped, s_setprio 0 moved behind the closing barrier
# speedup vs baseline: 1.0042x; 1.0042x over previous
; #define PG8_STAGE(bufoff, gbase, voff) do { _Pragma("unroll") for (int _i = 0; _i < 2; ++_i) \
;         __builtin_amdgcn_global_load_lds((const unsigned*)((const char*)(gbase) + (voff)[_i]), (PG8_LAS unsigned*)(lds + (bufoff) + ldsw + _i * 8192), 16, 0, 0); } while (0)
; #define PG8_LDA(dst, b, h) do { _Pragma("unroll") for (int m = 0; m < 4; ++m) _Pragma("unroll") for (int k = 0; k < 2; ++k) dst[m][k] = *(const PG8_LAS bf16x8*)(lds + PG8_SA(b, h) + aoff + m * 2048 + k * 1024); } while (0)
; #define PG8_LDB(dst, b, h) do { _Pragma("unroll") for (int n = 0; n < 2; ++n) _Pragma("unroll") for (int k = 0; k < 2; ++k) dst[n][k] = *(const PG8_LAS bf16x8*)(lds + PG8_SB(b, h) + boff + n * 2048 + k * 1024); } while (0)
; #define PG8_WAIT_V(n) asm volatile("s_waitcnt vmcnt(" #n ")" ::: "memory")
; #define PG8_WAIT_L(n) asm volatile("s_waitcnt lgkmcnt(" #n ")" ::: "memory")
; #define PG8_BAR __builtin_amdgcn_s_barrier()
;     ...
;         for (int t = 0; t < nt; t += 2) {
;             const bool last = (t == nt - 2);
;             const char* a1 = cA + (size_t)(t + 1) * kstep;
;             const char* a2 = last ? nA : cA + (size_t)(t + 2) * kstep; const char* b2 = last ? nB : cB + (size_t)(t + 2) * kstep;
;             const char* a3 = a2 + kstep; const char* b3 = b2 + kstep;
;             if (last && has_next) S.a_ready(nxt);
;             PG8_LDB(B0, 0, 0); PG8_LDB(B1, 0, 1); PG8_SCHED; PG8_LDA(At, 0, 0); PG8_STAGE(PG8_SA(1, 1), a1 + hstep, voffA);
;             PG8_WAIT_V(8); PG8_WAIT_L(0); PG8_BAR; PG8_MMA(0, 0, At, B0); PG8_MMA(0, 1, At, B1); PG8_BAR; PG8_SCHED;
;             PG8_LDA(At, 0, 1); PG8_STAGE(PG8_SB(0, 0), b2, voffB); PG8_STAGE(PG8_SB(0, 1), b2 + hstep, voffB); PG8_STAGE(PG8_SA(0, 0), a2, voffA);
;             PG8_WAIT_V(8); PG8_WAIT_L(0); PG8_BAR; PG8_MMA(1, 0, At, B0); PG8_MMA(1, 1, At, B1); PG8_BAR; PG8_SCHED;
;             PG8_LDB(B0, 1, 0); PG8_LDB(B1, 1, 1); PG8_SCHED; PG8_LDA(At, 1, 0); PG8_STAGE(PG8_SA(0, 1), a2 + hstep, voffA);
;             PG8_WAIT_V(8); PG8_WAIT_L(0); PG8_BAR; PG8_MMA(0, 0, At, B0); PG8_MMA(0, 1, At, B1); PG8_BAR; PG8_SCHED;
;             PG8_LDA(At, 1, 1); PG8_STAGE(PG8_SB(1, 0), b3, voffB); PG8_STAGE(PG8_SB(1, 1), b3 + hstep, voffB); PG8_STAGE(PG8_SA(1, 0), a3, voffA);
;             PG8_WAIT_V(8); PG8_WAIT_L(0); PG8_BAR; PG8_MMA(1, 0, At, B0); PG8_MMA(1, 1, At, B1); PG8_BAR; PG8_SCHED;
.LBB0_190:
	ds_read_b128 v[150:153], v145
	ds_read_b128 v[154:157], v145 offset:1024
	ds_read_b128 v[158:161], v145 offset:2048
	ds_read_b128 v[162:165], v145 offset:3072
	ds_read_b128 v[166:169], v148
	ds_read_b128 v[170:173], v148 offset:1024
	ds_read_b128 v[174:177], v148 offset:2048
	ds_read_b128 v[178:181], v148 offset:3072
	s_add_u32 s24, s22, 0xfffc0080
	s_addc_u32 s25, s23, -1
	s_cmp_eq_u32 s46, 12
	s_cselect_b32 s27, s19, s25
	s_cselect_b32 s26, s18, s24
	s_cselect_b32 s25, s0, s45
	s_cselect_b32 s24, s15, s17
	v_lshl_add_u64 v[206:207], s[22:23], 0, v[138:139]
	s_add_i32 m0, s9, 0xc000
	ds_read_b128 v[182:185], v149
	ds_read_b128 v[186:189], v149 offset:1024
	ds_read_b128 v[190:193], v149 offset:2048
	ds_read_b128 v[194:197], v149 offset:3072
	ds_read_b128 v[198:201], v149 offset:4096
	ds_read_b128 v[202:205], v149 offset:5120
	ds_read_b128 v[210:213], v149 offset:6144
	ds_read_b128 v[214:217], v149 offset:7168
	global_load_lds_dwordx4 v[206:207], off
	v_lshl_add_u64 v[206:207], s[22:23], 0, v[140:141]
	s_add_i32 m0, s9, 0xe000
	s_nop 0
	global_load_lds_dwordx4 v[206:207], off
	s_waitcnt vmcnt(8)
	s_waitcnt lgkmcnt(0)
	s_setprio 1
	s_barrier
	v_mfma_f32_16x16x32_bf16 v[126:129], v[150:153], v[182:185], v[126:129]
	v_mfma_f32_16x16x32_bf16 v[122:125], v[158:161], v[182:185], v[122:125]
	v_mfma_f32_16x16x32_bf16 v[118:121], v[150:153], v[190:193], v[118:121]
	v_mfma_f32_16x16x32_bf16 v[114:117], v[158:161], v[190:193], v[114:117]
	v_mfma_f32_16x16x32_bf16 v[102:105], v[150:153], v[198:201], v[102:105]
	v_mfma_f32_16x16x32_bf16 v[98:101], v[158:161], v[198:201], v[98:101]
	v_mfma_f32_16x16x32_bf16 v[86:89], v[150:153], v[210:213], v[86:89]
	v_mfma_f32_16x16x32_bf16 v[82:85], v[158:161], v[210:213], v[82:85]
	v_mfma_f32_16x16x32_bf16 v[126:129], v[154:157], v[186:189], v[126:129]
	v_mfma_f32_16x16x32_bf16 v[122:125], v[162:165], v[186:189], v[122:125]
	v_mfma_f32_16x16x32_bf16 v[118:121], v[154:157], v[194:197], v[118:121]
	v_mfma_f32_16x16x32_bf16 v[114:117], v[162:165], v[194:197], v[114:117]
	v_mfma_f32_16x16x32_bf16 v[102:105], v[154:157], v[202:205], v[102:105]
	v_mfma_f32_16x16x32_bf16 v[98:101], v[162:165], v[202:205], v[98:101]
	v_mfma_f32_16x16x32_bf16 v[86:89], v[154:157], v[214:217], v[86:89]
	v_mfma_f32_16x16x32_bf16 v[82:85], v[162:165], v[214:217], v[82:85]
	s_setprio 0
	s_setprio 1
	v_mfma_f32_16x16x32_bf16 v[110:113], v[166:169], v[182:185], v[110:113]
	v_mfma_f32_16x16x32_bf16 v[106:109], v[174:177], v[182:185], v[106:109]
	v_mfma_f32_16x16x32_bf16 v[94:97], v[166:169], v[190:193], v[94:97]
	v_mfma_f32_16x16x32_bf16 v[90:93], v[174:177], v[190:193], v[90:93]
	v_mfma_f32_16x16x32_bf16 v[78:81], v[166:169], v[198:201], v[78:81]
	v_mfma_f32_16x16x32_bf16 v[74:77], v[174:177], v[198:201], v[74:77]
	v_mfma_f32_16x16x32_bf16 v[70:73], v[166:169], v[210:213], v[70:73]
	v_mfma_f32_16x16x32_bf16 v[66:69], v[174:177], v[210:213], v[66:69]
	v_mfma_f32_16x16x32_bf16 v[110:113], v[170:173], v[186:189], v[110:113]
	v_mfma_f32_16x16x32_bf16 v[106:109], v[178:181], v[186:189], v[106:109]
	v_mfma_f32_16x16x32_bf16 v[94:97], v[170:173], v[194:197], v[94:97]
	v_mfma_f32_16x16x32_bf16 v[90:93], v[178:181], v[194:197], v[90:93]
	v_mfma_f32_16x16x32_bf16 v[78:81], v[170:173], v[202:205], v[78:81]
	v_mfma_f32_16x16x32_bf16 v[74:77], v[178:181], v[202:205], v[74:77]
	v_mfma_f32_16x16x32_bf16 v[70:73], v[170:173], v[214:217], v[70:73]
	v_mfma_f32_16x16x32_bf16 v[66:69], v[178:181], v[214:217], v[66:69]
	s_barrier
	s_setprio 0
	s_add_i32 s47, s38, s11
	v_lshl_add_u64 v[206:207], s[24:25], 0, v[132:133]
	s_mov_b32 m0, s47
	ds_read_b128 v[182:185], v149 offset:16384
	ds_read_b128 v[186:189], v149 offset:17408
	ds_read_b128 v[190:193], v149 offset:18432
	ds_read_b128 v[194:197], v149 offset:19456
	ds_read_b128 v[198:201], v149 offset:20480
	ds_read_b128 v[202:205], v149 offset:21504
	ds_read_b128 v[210:213], v149 offset:22528
	ds_read_b128 v[214:217], v149 offset:23552
	global_load_lds_dwordx4 v[206:207], off
	s_add_i32 m0, s47, 0x2000
	s_add_u32 s50, s24, 0x40000
	v_lshl_add_u64 v[218:219], s[24:25], 0, v[136:137]
	s_addc_u32 s51, s25, 0
	s_add_i32 s47, s39, s11
	global_load_lds_dwordx4 v[218:219], off
	v_lshl_add_u64 v[220:221], s[50:51], 0, v[132:133]
	s_mov_b32 m0, s47
	v_lshl_add_u64 v[222:223], s[26:27], 0, v[134:135]
	global_load_lds_dwordx4 v[220:221], off
	v_lshl_add_u64 v[220:221], s[50:51], 0, v[136:137]
	s_add_i32 m0, s47, 0x2000
	s_nop 0
	global_load_lds_dwordx4 v[220:221], off
	v_lshl_add_u64 v[220:221], s[26:27], 0, v[130:131]
	s_mov_b32 m0, s9
	s_nop 0
	global_load_lds_dwordx4 v[220:221], off
	s_mov_b32 m0, s33
	s_nop 0
	global_load_lds_dwordx4 v[222:223], off
	s_waitcnt vmcnt(8)
	s_waitcnt lgkmcnt(0)
	s_setprio 1
	s_barrier
; #define PG8_STAGE(bufoff, gbase, voff) do { _Pragma("unroll") for (int _i = 0; _i < 2; ++_i) \
;         __builtin_amdgcn_global_load_lds((const unsigned*)((const char*)(gbase) + (voff)[_i]), (PG8_LAS unsigned*)(lds + (bufoff) + ldsw + _i * 8192), 16, 0, 0); } while (0)
; #define PG8_LDA(dst, b, h) do { _Pragma("unroll") for (int m = 0; m < 4; ++m) _Pragma("unroll") for (int k = 0; k < 2; ++k) dst[m][k] = *(const PG8_LAS bf16x8*)(lds + PG8_SA(b, h) + aoff + m * 2048 + k * 1024); } while (0)
; #define PG8_LDB(dst, b, h) do { _Pragma("unroll") for (int n = 0; n < 2; ++n) _Pragma("unroll") for (int k = 0; k < 2; ++k) dst[n][k] = *(const PG8_LAS bf16x8*)(lds + PG8_SB(b, h) + boff + n * 2048 + k * 1024); } while (0)
; #define PG8_MMA(ai, bj, At, Bt) do { __builtin_amdgcn_s_setprio(1); _Pragma("unroll") for (int m = 0; m < 4; ++m) _Pragma("unroll") for (int n = 0; n < 2; ++n) _Pragma("unroll") for (int k = 0; k < 2; ++k) \
;         acc[ai][bj][m][n] = __builtin_amdgcn_mfma_f32_16x16x32_bf16(Bt[n][k], At[m][k], acc[ai][bj][m][n], 0, 0, 0); __builtin_amdgcn_s_setprio(0); } while (0)
; #define PG8_WAIT_V(n) asm volatile("s_waitcnt vmcnt(" #n ")" ::: "memory")
; #define PG8_WAIT_L(n) asm volatile("s_waitcnt lgkmcnt(" #n ")" ::: "memory")
; #define PG8_BAR __builtin_amdgcn_s_barrier()
; #define PG8_SCHED __builtin_amdgcn_sched_barrier(0)
;     ...
;             PG8_LDA(At, 0, 1); PG8_STAGE(PG8_SB(0, 0), b2, voffB); PG8_STAGE(PG8_SB(0, 1), b2 + hstep, voffB); PG8_STAGE(PG8_SA(0, 0), a2, voffA);
;             PG8_WAIT_V(8); PG8_WAIT_L(0); PG8_BAR; PG8_MMA(1, 0, At, B0); PG8_MMA(1, 1, At, B1); PG8_BAR; PG8_SCHED;
;             PG8_LDB(B0, 1, 0); PG8_LDB(B1, 1, 1); PG8_SCHED; PG8_LDA(At, 1, 0); PG8_STAGE(PG8_SA(0, 1), a2 + hstep, voffA);
;             PG8_WAIT_V(8); PG8_WAIT_L(0); PG8_BAR; PG8_MMA(0, 0, At, B0); PG8_MMA(0, 1, At, B1); PG8_BAR; PG8_SCHED;
;             PG8_LDA(At, 1, 1); PG8_STAGE(PG8_SB(1, 0), b3, voffB); PG8_STAGE(PG8_SB(1, 1), b3 + hstep, voffB); PG8_STAGE(PG8_SA(1, 0), a3, voffA);
;             PG8_WAIT_V(8); PG8_WAIT_L(0); PG8_BAR; PG8_MMA(1, 0, At, B0); PG8_MMA(1, 1, At, B1); PG8_BAR; PG8_SCHED;
	v_mfma_f32_16x16x32_bf16 v[62:65], v[150:153], v[182:185], v[62:65]
	v_mfma_f32_16x16x32_bf16 v[58:61], v[158:161], v[182:185], v[58:61]
	v_mfma_f32_16x16x32_bf16 v[54:57], v[150:153], v[190:193], v[54:57]
	v_mfma_f32_16x16x32_bf16 v[50:53], v[158:161], v[190:193], v[50:53]
	v_mfma_f32_16x16x32_bf16 v[38:41], v[150:153], v[198:201], v[38:41]
	v_mfma_f32_16x16x32_bf16 v[34:37], v[158:161], v[198:201], v[34:37]
	v_mfma_f32_16x16x32_bf16 v[22:25], v[150:153], v[210:213], v[22:25]
	v_mfma_f32_16x16x32_bf16 v[18:21], v[158:161], v[210:213], v[18:21]
	v_mfma_f32_16x16x32_bf16 v[62:65], v[154:157], v[186:189], v[62:65]
	v_mfma_f32_16x16x32_bf16 v[58:61], v[162:165], v[186:189], v[58:61]
	v_mfma_f32_16x16x32_bf16 v[54:57], v[154:157], v[194:197], v[54:57]
	v_mfma_f32_16x16x32_bf16 v[50:53], v[162:165], v[194:197], v[50:53]
	v_mfma_f32_16x16x32_bf16 v[38:41], v[154:157], v[202:205], v[38:41]
	v_mfma_f32_16x16x32_bf16 v[34:37], v[162:165], v[202:205], v[34:37]
	v_mfma_f32_16x16x32_bf16 v[22:25], v[154:157], v[214:217], v[22:25]
	v_mfma_f32_16x16x32_bf16 v[18:21], v[162:165], v[214:217], v[18:21]
	s_setprio 0
	s_setprio 1
	v_mfma_f32_16x16x32_bf16 v[46:49], v[166:169], v[182:185], v[46:49]
	v_mfma_f32_16x16x32_bf16 v[42:45], v[174:177], v[182:185], v[42:45]
	v_mfma_f32_16x16x32_bf16 v[30:33], v[166:169], v[190:193], v[30:33]
	v_mfma_f32_16x16x32_bf16 v[26:29], v[174:177], v[190:193], v[26:29]
	v_mfma_f32_16x16x32_bf16 v[14:17], v[166:169], v[198:201], v[14:17]
	v_mfma_f32_16x16x32_bf16 v[10:13], v[174:177], v[198:201], v[10:13]
	v_mfma_f32_16x16x32_bf16 v[6:9], v[166:169], v[210:213], v[6:9]
	v_mfma_f32_16x16x32_bf16 v[2:5], v[174:177], v[210:213], v[2:5]
	v_mfma_f32_16x16x32_bf16 v[46:49], v[170:173], v[186:189], v[46:49]
	v_mfma_f32_16x16x32_bf16 v[42:45], v[178:181], v[186:189], v[42:45]
	v_mfma_f32_16x16x32_bf16 v[30:33], v[170:173], v[194:197], v[30:33]
	v_mfma_f32_16x16x32_bf16 v[26:29], v[178:181], v[194:197], v[26:29]
	v_mfma_f32_16x16x32_bf16 v[14:17], v[170:173], v[202:205], v[14:17]
	v_mfma_f32_16x16x32_bf16 v[10:13], v[178:181], v[202:205], v[10:13]
	v_mfma_f32_16x16x32_bf16 v[6:9], v[170:173], v[214:217], v[6:9]
	v_mfma_f32_16x16x32_bf16 v[2:5], v[178:181], v[214:217], v[2:5]
	s_barrier
	s_setprio 0
	s_add_i32 s47, 0, 0x18000
	s_add_i32 s50, 0, 0x1c000
	v_add_u32_e32 v162, s47, v143
	v_add_u32_e32 v178, s50, v143
	ds_read_b128 v[150:153], v162
	ds_read_b128 v[154:157], v162 offset:1024
	ds_read_b128 v[158:161], v162 offset:2048
	ds_read_b128 v[162:165], v162 offset:3072
	ds_read_b128 v[166:169], v178
	ds_read_b128 v[170:173], v178 offset:1024
	ds_read_b128 v[174:177], v178 offset:2048
	ds_read_b128 v[178:181], v178 offset:3072
	s_add_u32 s26, s26, 0x40000
	s_addc_u32 s27, s27, 0
	s_mov_b32 m0, s34
	v_lshl_add_u64 v[224:225], s[26:27], 0, v[130:131]
	ds_read_b128 v[182:185], v149 offset:32768
	ds_read_b128 v[186:189], v149 offset:33792
	ds_read_b128 v[190:193], v149 offset:34816
	ds_read_b128 v[194:197], v149 offset:35840
	ds_read_b128 v[198:201], v149 offset:36864
	ds_read_b128 v[202:205], v149 offset:37888
	ds_read_b128 v[210:213], v149 offset:38912
	ds_read_b128 v[214:217], v149 offset:39936
	global_load_lds_dwordx4 v[224:225], off
	v_lshl_add_u64 v[224:225], s[26:27], 0, v[134:135]
	s_mov_b32 m0, s35
	s_nop 0
	global_load_lds_dwordx4 v[224:225], off
	s_waitcnt vmcnt(8)
	s_waitcnt lgkmcnt(0)
	s_setprio 1
	s_barrier
	v_mfma_f32_16x16x32_bf16 v[126:129], v[150:153], v[182:185], v[126:129]
	v_mfma_f32_16x16x32_bf16 v[122:125], v[158:161], v[182:185], v[122:125]
	v_mfma_f32_16x16x32_bf16 v[118:121], v[150:153], v[190:193], v[118:121]
	v_mfma_f32_16x16x32_bf16 v[114:117], v[158:161], v[190:193], v[114:117]
	v_mfma_f32_16x16x32_bf16 v[102:105], v[150:153], v[198:201], v[102:105]
	v_mfma_f32_16x16x32_bf16 v[98:101], v[158:161], v[198:201], v[98:101]
	v_mfma_f32_16x16x32_bf16 v[86:89], v[150:153], v[210:213], v[86:89]
	v_mfma_f32_16x16x32_bf16 v[82:85], v[158:161], v[210:213], v[82:85]
	v_mfma_f32_16x16x32_bf16 v[126:129], v[154:157], v[186:189], v[126:129]
	v_mfma_f32_16x16x32_bf16 v[122:125], v[162:165], v[186:189], v[122:125]
	v_mfma_f32_16x16x32_bf16 v[118:121], v[154:157], v[194:197], v[118:121]
	v_mfma_f32_16x16x32_bf16 v[114:117], v[162:165], v[194:197], v[114:117]
	v_mfma_f32_16x16x32_bf16 v[102:105], v[154:157], v[202:205], v[102:105]
	v_mfma_f32_16x16x32_bf16 v[98:101], v[162:165], v[202:205], v[98:101]
	v_mfma_f32_16x16x32_bf16 v[86:89], v[154:157], v[214:217], v[86:89]
	v_mfma_f32_16x16x32_bf16 v[82:85], v[162:165], v[214:217], v[82:85]
	s_setprio 0
	s_setprio 1
	v_mfma_f32_16x16x32_bf16 v[110:113], v[166:169], v[182:185], v[110:113]
	v_mfma_f32_16x16x32_bf16 v[106:109], v[174:177], v[182:185], v[106:109]
	v_mfma_f32_16x16x32_bf16 v[94:97], v[166:169], v[190:193], v[94:97]
	v_mfma_f32_16x16x32_bf16 v[90:93], v[174:177], v[190:193], v[90:93]
	v_mfma_f32_16x16x32_bf16 v[78:81], v[166:169], v[198:201], v[78:81]
	v_mfma_f32_16x16x32_bf16 v[74:77], v[174:177], v[198:201], v[74:77]
	v_mfma_f32_16x16x32_bf16 v[70:73], v[166:169], v[210:213], v[70:73]
	v_mfma_f32_16x16x32_bf16 v[66:69], v[174:177], v[210:213], v[66:69]
	v_mfma_f32_16x16x32_bf16 v[110:113], v[170:173], v[186:189], v[110:113]
	v_mfma_f32_16x16x32_bf16 v[106:109], v[178:181], v[186:189], v[106:109]
	v_mfma_f32_16x16x32_bf16 v[94:97], v[170:173], v[194:197], v[94:97]
	v_mfma_f32_16x16x32_bf16 v[90:93], v[178:181], v[194:197], v[90:93]
	v_mfma_f32_16x16x32_bf16 v[78:81], v[170:173], v[202:205], v[78:81]
	v_mfma_f32_16x16x32_bf16 v[74:77], v[178:181], v[202:205], v[74:77]
	v_mfma_f32_16x16x32_bf16 v[70:73], v[170:173], v[214:217], v[70:73]
	v_mfma_f32_16x16x32_bf16 v[66:69], v[178:181], v[214:217], v[66:69]
	s_barrier
; #define PG8_STAGE(bufoff, gbase, voff) do { _Pragma("unroll") for (int _i = 0; _i < 2; ++_i) \
;         __builtin_amdgcn_global_load_lds((const unsigned*)((const char*)(gbase) + (voff)[_i]), (PG8_LAS unsigned*)(lds + (bufoff) + ldsw + _i * 8192), 16, 0, 0); } while (0)
; #define PG8_LDA(dst, b, h) do { _Pragma("unroll") for (int m = 0; m < 4; ++m) _Pragma("unroll") for (int k = 0; k < 2; ++k) dst[m][k] = *(const PG8_LAS bf16x8*)(lds + PG8_SA(b, h) + aoff + m * 2048 + k * 1024); } while (0)
; #define PG8_LDB(dst, b, h) do { _Pragma("unroll") for (int n = 0; n < 2; ++n) _Pragma("unroll") for (int k = 0; k < 2; ++k) dst[n][k] = *(const PG8_LAS bf16x8*)(lds + PG8_SB(b, h) + boff + n * 2048 + k * 1024); } while (0)
; #define PG8_MMA(ai, bj, At, Bt) do { __builtin_amdgcn_s_setprio(1); _Pragma("unroll") for (int m = 0; m < 4; ++m) _Pragma("unroll") for (int n = 0; n < 2; ++n) _Pragma("unroll") for (int k = 0; k < 2; ++k) \
;         acc[ai][bj][m][n] = __builtin_amdgcn_mfma_f32_16x16x32_bf16(Bt[n][k], At[m][k], acc[ai][bj][m][n], 0, 0, 0); __builtin_amdgcn_s_setprio(0); } while (0)
; #define PG8_WAIT_V(n) asm volatile("s_waitcnt vmcnt(" #n ")" ::: "memory")
; #define PG8_WAIT_L(n) asm volatile("s_waitcnt lgkmcnt(" #n ")" ::: "memory")
; #define PG8_BAR __builtin_amdgcn_s_barrier()
; #define PG8_SCHED __builtin_amdgcn_sched_barrier(0)
;     ...
;             PG8_LDB(B0, 1, 0); PG8_LDB(B1, 1, 1); PG8_SCHED; PG8_LDA(At, 1, 0); PG8_STAGE(PG8_SA(0, 1), a2 + hstep, voffA);
;             PG8_WAIT_V(8); PG8_WAIT_L(0); PG8_BAR; PG8_MMA(0, 0, At, B0); PG8_MMA(0, 1, At, B1); PG8_BAR; PG8_SCHED;
;             PG8_LDA(At, 1, 1); PG8_STAGE(PG8_SB(1, 0), b3, voffB); PG8_STAGE(PG8_SB(1, 1), b3 + hstep, voffB); PG8_STAGE(PG8_SA(1, 0), a3, voffA);
;             PG8_WAIT_V(8); PG8_WAIT_L(0); PG8_BAR; PG8_MMA(1, 0, At, B0); PG8_MMA(1, 1, At, B1); PG8_BAR; PG8_SCHED;
;         }
	s_setprio 0
	s_add_i32 s26, s47, s11
	v_lshl_add_u64 v[206:207], v[206:207], 0, s[6:7]
	s_mov_b32 m0, s26
	ds_read_b128 v[182:185], v149 offset:49152
	ds_read_b128 v[186:189], v149 offset:50176
	ds_read_b128 v[190:193], v149 offset:51200
	ds_read_b128 v[194:197], v149 offset:52224
	ds_read_b128 v[198:201], v149 offset:53248
	ds_read_b128 v[202:205], v149 offset:54272
	ds_read_b128 v[210:213], v149 offset:55296
	ds_read_b128 v[214:217], v149 offset:56320
	global_load_lds_dwordx4 v[206:207], off
	s_add_i32 m0, s26, 0x2000
	s_add_u32 s24, s24, 0x40080
	v_lshl_add_u64 v[206:207], v[218:219], 0, s[6:7]
	s_addc_u32 s25, s25, 0
	s_add_i32 s26, s50, s11
	global_load_lds_dwordx4 v[206:207], off
	v_lshl_add_u64 v[206:207], s[24:25], 0, v[132:133]
	s_mov_b32 m0, s26
	s_nop 0
	global_load_lds_dwordx4 v[206:207], off
	v_lshl_add_u64 v[206:207], s[24:25], 0, v[136:137]
	s_add_i32 m0, s26, 0x2000
	s_nop 0
	global_load_lds_dwordx4 v[206:207], off
	v_lshl_add_u64 v[206:207], v[220:221], 0, s[6:7]
	s_mov_b32 m0, s36
	s_nop 0
	global_load_lds_dwordx4 v[206:207], off
	v_lshl_add_u64 v[206:207], v[222:223], 0, s[6:7]
	s_mov_b32 m0, s37
	s_nop 0
	global_load_lds_dwordx4 v[206:207], off
	s_waitcnt vmcnt(8)
	s_waitcnt lgkmcnt(0)
	s_setprio 1
	s_barrier
	v_mfma_f32_16x16x32_bf16 v[62:65], v[150:153], v[182:185], v[62:65]
	v_mfma_f32_16x16x32_bf16 v[58:61], v[158:161], v[182:185], v[58:61]
	v_mfma_f32_16x16x32_bf16 v[54:57], v[150:153], v[190:193], v[54:57]
	v_mfma_f32_16x16x32_bf16 v[50:53], v[158:161], v[190:193], v[50:53]
	v_mfma_f32_16x16x32_bf16 v[38:41], v[150:153], v[198:201], v[38:41]
	v_mfma_f32_16x16x32_bf16 v[34:37], v[158:161], v[198:201], v[34:37]
	v_mfma_f32_16x16x32_bf16 v[22:25], v[150:153], v[210:213], v[22:25]
	v_mfma_f32_16x16x32_bf16 v[18:21], v[158:161], v[210:213], v[18:21]
	v_mfma_f32_16x16x32_bf16 v[62:65], v[154:157], v[186:189], v[62:65]
	v_mfma_f32_16x16x32_bf16 v[58:61], v[162:165], v[186:189], v[58:61]
	v_mfma_f32_16x16x32_bf16 v[54:57], v[154:157], v[194:197], v[54:57]
	v_mfma_f32_16x16x32_bf16 v[50:53], v[162:165], v[194:197], v[50:53]
	v_mfma_f32_16x16x32_bf16 v[38:41], v[154:157], v[202:205], v[38:41]
	v_mfma_f32_16x16x32_bf16 v[34:37], v[162:165], v[202:205], v[34:37]
	v_mfma_f32_16x16x32_bf16 v[22:25], v[154:157], v[214:217], v[22:25]
	v_mfma_f32_16x16x32_bf16 v[18:21], v[162:165], v[214:217], v[18:21]
	s_setprio 0
	s_setprio 1
	v_mfma_f32_16x16x32_bf16 v[46:49], v[166:169], v[182:185], v[46:49]
	v_mfma_f32_16x16x32_bf16 v[42:45], v[174:177], v[182:185], v[42:45]
	v_mfma_f32_16x16x32_bf16 v[30:33], v[166:169], v[190:193], v[30:33]
	v_mfma_f32_16x16x32_bf16 v[26:29], v[174:177], v[190:193], v[26:29]
	v_mfma_f32_16x16x32_bf16 v[14:17], v[166:169], v[198:201], v[14:17]
	v_mfma_f32_16x16x32_bf16 v[10:13], v[174:177], v[198:201], v[10:13]
	v_mfma_f32_16x16x32_bf16 v[6:9], v[166:169], v[210:213], v[6:9]
	v_mfma_f32_16x16x32_bf16 v[2:5], v[174:177], v[210:213], v[2:5]
	v_mfma_f32_16x16x32_bf16 v[46:49], v[170:173], v[186:189], v[46:49]
	v_mfma_f32_16x16x32_bf16 v[42:45], v[178:181], v[186:189], v[42:45]
	v_mfma_f32_16x16x32_bf16 v[30:33], v[170:173], v[194:197], v[30:33]
	v_mfma_f32_16x16x32_bf16 v[26:29], v[178:181], v[194:197], v[26:29]
	v_mfma_f32_16x16x32_bf16 v[14:17], v[170:173], v[202:205], v[14:17]
	v_mfma_f32_16x16x32_bf16 v[10:13], v[178:181], v[202:205], v[10:13]
	v_mfma_f32_16x16x32_bf16 v[6:9], v[170:173], v[214:217], v[6:9]
	v_mfma_f32_16x16x32_bf16 v[2:5], v[178:181], v[214:217], v[2:5]
	s_barrier
	s_setprio 0
	s_add_i32 s46, s46, 2
	s_add_u32 s22, s22, 0x100
	s_addc_u32 s23, s23, 0
	s_add_u32 s17, s17, 0x100
	s_addc_u32 s45, s45, 0
	s_cmp_gt_u32 s46, 13
	s_cbranch_scc0 .LBB0_190
	s_and_b64 vcc, exec, s[12:13]
	s_cbranch_vccz .LBB0_193
	s_barrier

; #define PG8_STAGE(bufoff, gbase, voff) do { _Pragma("unroll") for (int _i = 0; _i < 2; ++_i) \
;         __builtin_amdgcn_global_load_lds((const unsigned*)((const char*)(gbase) + (voff)[_i]), (PG8_LAS unsigned*)(lds + (bufoff) + ldsw + _i * 8192), 16, 0, 0); } while (0)
; #define PG8_LDA(dst, b, h) do { _Pragma("unroll") for (int m = 0; m < 4; ++m) _Pragma("unroll") for (int k = 0; k < 2; ++k) dst[m][k] = *(const PG8_LAS bf16x8*)(lds + PG8_SA(b, h) + aoff + m * 2048 + k * 1024); } while (0)
; #define PG8_LDB(dst, b, h) do { _Pragma("unroll") for (int n = 0; n < 2; ++n) _Pragma("unroll") for (int k = 0; k < 2; ++k) dst[n][k] = *(const PG8_LAS bf16x8*)(lds + PG8_SB(b, h) + boff + n * 2048 + k * 1024); } while (0)
; #define PG8_MMA(ai, bj, At, Bt) do { __builtin_amdgcn_s_setprio(1); _Pragma("unroll") for (int m = 0; m < 4; ++m) _Pragma("unroll") for (int n = 0; n < 2; ++n) _Pragma("unroll") for (int k = 0; k < 2; ++k) \
;         acc[ai][bj][m][n] = __builtin_amdgcn_mfma_f32_16x16x32_bf16(Bt[n][k], At[m][k], acc[ai][bj][m][n], 0, 0, 0); __builtin_amdgcn_s_setprio(0); } while (0)
; #define PG8_WAIT_V(n) asm volatile("s_waitcnt vmcnt(" #n ")" ::: "memory")
; #define PG8_WAIT_L(n) asm volatile("s_waitcnt lgkmcnt(" #n ")" ::: "memory")
; #define PG8_BAR __builtin_amdgcn_s_barrier()
; #define PG8_SCHED __builtin_amdgcn_sched_barrier(0)
;     ...
;         for (int t = 0; t < nt; t += 2) {
;             const bool last = (t == nt - 2);
;             const char* a1 = cA + (size_t)(t + 1) * kstep;
;             const char* a2 = last ? nA : cA + (size_t)(t + 2) * kstep; const char* b2 = last ? nB : cB + (size_t)(t + 2) * kstep;
;             const char* a3 = a2 + kstep; const char* b3 = b2 + kstep;
;             if (last && has_next) S.a_ready(nxt);
;             PG8_LDB(B0, 0, 0); PG8_LDB(B1, 0, 1); PG8_SCHED; PG8_LDA(At, 0, 0); PG8_STAGE(PG8_SA(1, 1), a1 + hstep, voffA);
;             PG8_WAIT_V(8); PG8_WAIT_L(0); PG8_BAR; PG8_MMA(0, 0, At, B0); PG8_MMA(0, 1, At, B1); PG8_BAR; PG8_SCHED;
;             PG8_LDA(At, 0, 1); PG8_STAGE(PG8_SB(0, 0), b2, voffB); PG8_STAGE(PG8_SB(0, 1), b2 + hstep, voffB); PG8_STAGE(PG8_SA(0, 0), a2, voffA);
.LBB0_841:
	ds_read_b128 v[130:133], v184
	ds_read_b128 v[134:137], v184 offset:1024
	ds_read_b128 v[138:141], v184 offset:2048
	ds_read_b128 v[142:145], v184 offset:3072
	ds_read_b128 v[188:191], v185
	ds_read_b128 v[192:195], v185 offset:1024
	ds_read_b128 v[196:199], v185 offset:2048
	ds_read_b128 v[200:203], v185 offset:3072
	s_add_u32 s20, s18, 0xfffc0080
	s_addc_u32 s21, s19, -1
	s_cmp_eq_u32 s50, 12
	s_cselect_b32 s23, s11, s21
	s_cselect_b32 s22, s17, s20
	s_cselect_b32 s21, s9, s49
	s_cselect_b32 s20, s47, s48
	v_lshl_add_u64 v[180:181], s[18:19], 0, v[172:173]
	s_add_i32 m0, s31, 0xc000
	ds_read_b128 v[204:207], v186
	ds_read_b128 v[210:213], v186 offset:1024
	ds_read_b128 v[214:217], v186 offset:2048
	ds_read_b128 v[218:221], v186 offset:3072
	ds_read_b128 v[222:225], v186 offset:4096
	ds_read_b128 v[226:229], v186 offset:5120
	ds_read_b128 v[230:233], v186 offset:6144
	ds_read_b128 v[234:237], v186 offset:7168
	global_load_lds_dwordx4 v[180:181], off
	v_lshl_add_u64 v[180:181], s[18:19], 0, v[174:175]
	s_add_i32 m0, s31, 0xe000
	s_nop 0
	global_load_lds_dwordx4 v[180:181], off
	s_waitcnt vmcnt(8)
	s_waitcnt lgkmcnt(0)
	s_setprio 1
	s_barrier
	v_mfma_f32_16x16x32_bf16 v[126:129], v[130:133], v[204:207], v[126:129]
	v_mfma_f32_16x16x32_bf16 v[122:125], v[138:141], v[204:207], v[122:125]
	v_mfma_f32_16x16x32_bf16 v[118:121], v[130:133], v[214:217], v[118:121]
	v_mfma_f32_16x16x32_bf16 v[110:113], v[138:141], v[214:217], v[110:113]
	v_mfma_f32_16x16x32_bf16 v[102:105], v[130:133], v[222:225], v[102:105]
	v_mfma_f32_16x16x32_bf16 v[94:97], v[138:141], v[222:225], v[94:97]
	v_mfma_f32_16x16x32_bf16 v[86:89], v[130:133], v[230:233], v[86:89]
	v_mfma_f32_16x16x32_bf16 v[78:81], v[138:141], v[230:233], v[78:81]
	v_mfma_f32_16x16x32_bf16 v[126:129], v[134:137], v[210:213], v[126:129]
	v_mfma_f32_16x16x32_bf16 v[122:125], v[142:145], v[210:213], v[122:125]
	v_mfma_f32_16x16x32_bf16 v[118:121], v[134:137], v[218:221], v[118:121]
	v_mfma_f32_16x16x32_bf16 v[110:113], v[142:145], v[218:221], v[110:113]
	v_mfma_f32_16x16x32_bf16 v[102:105], v[134:137], v[226:229], v[102:105]
	v_mfma_f32_16x16x32_bf16 v[94:97], v[142:145], v[226:229], v[94:97]
	v_mfma_f32_16x16x32_bf16 v[86:89], v[134:137], v[234:237], v[86:89]
	v_mfma_f32_16x16x32_bf16 v[78:81], v[142:145], v[234:237], v[78:81]
	s_setprio 0
	s_setprio 1
	v_mfma_f32_16x16x32_bf16 v[114:117], v[188:191], v[204:207], v[114:117]
	v_mfma_f32_16x16x32_bf16 v[106:109], v[196:199], v[204:207], v[106:109]
	v_mfma_f32_16x16x32_bf16 v[98:101], v[188:191], v[214:217], v[98:101]
	v_mfma_f32_16x16x32_bf16 v[90:93], v[196:199], v[214:217], v[90:93]
	v_mfma_f32_16x16x32_bf16 v[82:85], v[188:191], v[222:225], v[82:85]
	v_mfma_f32_16x16x32_bf16 v[74:77], v[196:199], v[222:225], v[74:77]
	v_mfma_f32_16x16x32_bf16 v[70:73], v[188:191], v[230:233], v[70:73]
	v_mfma_f32_16x16x32_bf16 v[66:69], v[196:199], v[230:233], v[66:69]
	v_mfma_f32_16x16x32_bf16 v[114:117], v[192:195], v[210:213], v[114:117]
	v_mfma_f32_16x16x32_bf16 v[106:109], v[200:203], v[210:213], v[106:109]
	v_mfma_f32_16x16x32_bf16 v[98:101], v[192:195], v[218:221], v[98:101]
	v_mfma_f32_16x16x32_bf16 v[90:93], v[200:203], v[218:221], v[90:93]
	v_mfma_f32_16x16x32_bf16 v[82:85], v[192:195], v[226:229], v[82:85]
	v_mfma_f32_16x16x32_bf16 v[74:77], v[200:203], v[226:229], v[74:77]
	v_mfma_f32_16x16x32_bf16 v[70:73], v[192:195], v[234:237], v[70:73]
	v_mfma_f32_16x16x32_bf16 v[66:69], v[200:203], v[234:237], v[66:69]
	s_barrier
	s_setprio 0
	s_add_i32 s51, s44, s28
	v_lshl_add_u64 v[180:181], s[20:21], 0, v[152:153]
	s_mov_b32 m0, s51
	ds_read_b128 v[204:207], v186 offset:16384
	ds_read_b128 v[210:213], v186 offset:17408
	ds_read_b128 v[214:217], v186 offset:18432
	ds_read_b128 v[218:221], v186 offset:19456
	ds_read_b128 v[222:225], v186 offset:20480
	ds_read_b128 v[226:229], v186 offset:21504
	ds_read_b128 v[230:233], v186 offset:22528
	ds_read_b128 v[234:237], v186 offset:23552
	global_load_lds_dwordx4 v[180:181], off
	s_add_i32 m0, s51, 0x2000
	s_add_u32 s52, s20, 0x40000
	v_lshl_add_u64 v[238:239], s[20:21], 0, v[148:149]
	s_addc_u32 s53, s21, 0
	s_add_i32 s51, s45, s28
	global_load_lds_dwordx4 v[238:239], off
	v_lshl_add_u64 v[240:241], s[52:53], 0, v[152:153]
	s_mov_b32 m0, s51
	v_lshl_add_u64 v[242:243], s[22:23], 0, v[150:151]
	global_load_lds_dwordx4 v[240:241], off
	v_lshl_add_u64 v[240:241], s[52:53], 0, v[148:149]
	s_add_i32 m0, s51, 0x2000
	s_nop 0
	global_load_lds_dwordx4 v[240:241], off
	v_lshl_add_u64 v[240:241], s[22:23], 0, v[154:155]
	s_mov_b32 m0, s31
	s_nop 0
	global_load_lds_dwordx4 v[240:241], off
	s_mov_b32 m0, s33
	s_nop 0
	global_load_lds_dwordx4 v[242:243], off
	s_waitcnt vmcnt(8)
	s_waitcnt lgkmcnt(0)
	s_setprio 1
	s_barrier
; #define PG8_STAGE(bufoff, gbase, voff) do { _Pragma("unroll") for (int _i = 0; _i < 2; ++_i) \
;         __builtin_amdgcn_global_load_lds((const unsigned*)((const char*)(gbase) + (voff)[_i]), (PG8_LAS unsigned*)(lds + (bufoff) + ldsw + _i * 8192), 16, 0, 0); } while (0)
; #define PG8_LDA(dst, b, h) do { _Pragma("unroll") for (int m = 0; m < 4; ++m) _Pragma("unroll") for (int k = 0; k < 2; ++k) dst[m][k] = *(const PG8_LAS bf16x8*)(lds + PG8_SA(b, h) + aoff + m * 2048 + k * 1024); } while (0)
; #define PG8_LDB(dst, b, h) do { _Pragma("unroll") for (int n = 0; n < 2; ++n) _Pragma("unroll") for (int k = 0; k < 2; ++k) dst[n][k] = *(const PG8_LAS bf16x8*)(lds + PG8_SB(b, h) + boff + n * 2048 + k * 1024); } while (0)
; #define PG8_MMA(ai, bj, At, Bt) do { __builtin_amdgcn_s_setprio(1); _Pragma("unroll") for (int m = 0; m < 4; ++m) _Pragma("unroll") for (int n = 0; n < 2; ++n) _Pragma("unroll") for (int k = 0; k < 2; ++k) \
;         acc[ai][bj][m][n] = __builtin_amdgcn_mfma_f32_16x16x32_bf16(Bt[n][k], At[m][k], acc[ai][bj][m][n], 0, 0, 0); __builtin_amdgcn_s_setprio(0); } while (0)
; #define PG8_WAIT_V(n) asm volatile("s_waitcnt vmcnt(" #n ")" ::: "memory")
; #define PG8_WAIT_L(n) asm volatile("s_waitcnt lgkmcnt(" #n ")" ::: "memory")
; #define PG8_BAR __builtin_amdgcn_s_barrier()
; #define PG8_SCHED __builtin_amdgcn_sched_barrier(0)
;     ...
;             PG8_WAIT_V(8); PG8_WAIT_L(0); PG8_BAR; PG8_MMA(1, 0, At, B0); PG8_MMA(1, 1, At, B1); PG8_BAR; PG8_SCHED;
;             PG8_LDB(B0, 1, 0); PG8_LDB(B1, 1, 1); PG8_SCHED; PG8_LDA(At, 1, 0); PG8_STAGE(PG8_SA(0, 1), a2 + hstep, voffA);
;             PG8_WAIT_V(8); PG8_WAIT_L(0); PG8_BAR; PG8_MMA(0, 0, At, B0); PG8_MMA(0, 1, At, B1); PG8_BAR; PG8_SCHED;
	v_mfma_f32_16x16x32_bf16 v[62:65], v[130:133], v[204:207], v[62:65]
	v_mfma_f32_16x16x32_bf16 v[58:61], v[138:141], v[204:207], v[58:61]
	v_mfma_f32_16x16x32_bf16 v[54:57], v[130:133], v[214:217], v[54:57]
	v_mfma_f32_16x16x32_bf16 v[46:49], v[138:141], v[214:217], v[46:49]
	v_mfma_f32_16x16x32_bf16 v[38:41], v[130:133], v[222:225], v[38:41]
	v_mfma_f32_16x16x32_bf16 v[30:33], v[138:141], v[222:225], v[30:33]
	v_mfma_f32_16x16x32_bf16 v[22:25], v[130:133], v[230:233], v[22:25]
	v_mfma_f32_16x16x32_bf16 v[14:17], v[138:141], v[230:233], v[14:17]
	v_mfma_f32_16x16x32_bf16 v[62:65], v[134:137], v[210:213], v[62:65]
	v_mfma_f32_16x16x32_bf16 v[58:61], v[142:145], v[210:213], v[58:61]
	v_mfma_f32_16x16x32_bf16 v[54:57], v[134:137], v[218:221], v[54:57]
	v_mfma_f32_16x16x32_bf16 v[46:49], v[142:145], v[218:221], v[46:49]
	v_mfma_f32_16x16x32_bf16 v[38:41], v[134:137], v[226:229], v[38:41]
	v_mfma_f32_16x16x32_bf16 v[30:33], v[142:145], v[226:229], v[30:33]
	v_mfma_f32_16x16x32_bf16 v[22:25], v[134:137], v[234:237], v[22:25]
	v_mfma_f32_16x16x32_bf16 v[14:17], v[142:145], v[234:237], v[14:17]
	s_setprio 0
	s_setprio 1
	v_mfma_f32_16x16x32_bf16 v[50:53], v[188:191], v[204:207], v[50:53]
	v_mfma_f32_16x16x32_bf16 v[42:45], v[196:199], v[204:207], v[42:45]
	v_mfma_f32_16x16x32_bf16 v[34:37], v[188:191], v[214:217], v[34:37]
	v_mfma_f32_16x16x32_bf16 v[26:29], v[196:199], v[214:217], v[26:29]
	v_mfma_f32_16x16x32_bf16 v[18:21], v[188:191], v[222:225], v[18:21]
	v_mfma_f32_16x16x32_bf16 v[10:13], v[196:199], v[222:225], v[10:13]
	v_mfma_f32_16x16x32_bf16 v[6:9], v[188:191], v[230:233], v[6:9]
	v_mfma_f32_16x16x32_bf16 v[2:5], v[196:199], v[230:233], v[2:5]
	v_mfma_f32_16x16x32_bf16 v[50:53], v[192:195], v[210:213], v[50:53]
	v_mfma_f32_16x16x32_bf16 v[42:45], v[200:203], v[210:213], v[42:45]
	v_mfma_f32_16x16x32_bf16 v[34:37], v[192:195], v[218:221], v[34:37]
	v_mfma_f32_16x16x32_bf16 v[26:29], v[200:203], v[218:221], v[26:29]
	v_mfma_f32_16x16x32_bf16 v[18:21], v[192:195], v[226:229], v[18:21]
	v_mfma_f32_16x16x32_bf16 v[10:13], v[200:203], v[226:229], v[10:13]
	v_mfma_f32_16x16x32_bf16 v[6:9], v[192:195], v[234:237], v[6:9]
	v_mfma_f32_16x16x32_bf16 v[2:5], v[200:203], v[234:237], v[2:5]
	s_barrier
	s_setprio 0
	s_add_i32 s51, 0, 0x18000
	s_add_i32 s52, 0, 0x1c000
	v_add_u32_e32 v142, s51, v182
	v_add_u32_e32 v187, s52, v182
	ds_read_b128 v[130:133], v142
	ds_read_b128 v[134:137], v142 offset:1024
	ds_read_b128 v[138:141], v142 offset:2048
	ds_read_b128 v[142:145], v142 offset:3072
	ds_read_b128 v[188:191], v187
	ds_read_b128 v[192:195], v187 offset:1024
	ds_read_b128 v[196:199], v187 offset:2048
	ds_read_b128 v[200:203], v187 offset:3072
	s_add_u32 s22, s22, 0x40000
	s_addc_u32 s23, s23, 0
	s_mov_b32 m0, s34
	v_lshl_add_u64 v[244:245], s[22:23], 0, v[154:155]
	ds_read_b128 v[204:207], v186 offset:32768
	ds_read_b128 v[210:213], v186 offset:33792
	ds_read_b128 v[214:217], v186 offset:34816
	ds_read_b128 v[218:221], v186 offset:35840
	ds_read_b128 v[222:225], v186 offset:36864
	ds_read_b128 v[226:229], v186 offset:37888
	ds_read_b128 v[230:233], v186 offset:38912
	ds_read_b128 v[234:237], v186 offset:39936
	global_load_lds_dwordx4 v[244:245], off
	v_lshl_add_u64 v[244:245], s[22:23], 0, v[150:151]
	s_mov_b32 m0, s35
	s_nop 0
	global_load_lds_dwordx4 v[244:245], off
	s_waitcnt vmcnt(8)
	s_waitcnt lgkmcnt(0)
	s_setprio 1
	s_barrier
	v_mfma_f32_16x16x32_bf16 v[126:129], v[130:133], v[204:207], v[126:129]
	v_mfma_f32_16x16x32_bf16 v[122:125], v[138:141], v[204:207], v[122:125]
	v_mfma_f32_16x16x32_bf16 v[118:121], v[130:133], v[214:217], v[118:121]
	v_mfma_f32_16x16x32_bf16 v[110:113], v[138:141], v[214:217], v[110:113]
	v_mfma_f32_16x16x32_bf16 v[102:105], v[130:133], v[222:225], v[102:105]
	v_mfma_f32_16x16x32_bf16 v[94:97], v[138:141], v[222:225], v[94:97]
	v_mfma_f32_16x16x32_bf16 v[86:89], v[130:133], v[230:233], v[86:89]
	v_mfma_f32_16x16x32_bf16 v[78:81], v[138:141], v[230:233], v[78:81]
	v_mfma_f32_16x16x32_bf16 v[126:129], v[134:137], v[210:213], v[126:129]
	v_mfma_f32_16x16x32_bf16 v[122:125], v[142:145], v[210:213], v[122:125]
	v_mfma_f32_16x16x32_bf16 v[118:121], v[134:137], v[218:221], v[118:121]
	v_mfma_f32_16x16x32_bf16 v[110:113], v[142:145], v[218:221], v[110:113]
	v_mfma_f32_16x16x32_bf16 v[102:105], v[134:137], v[226:229], v[102:105]
	v_mfma_f32_16x16x32_bf16 v[94:97], v[142:145], v[226:229], v[94:97]
	v_mfma_f32_16x16x32_bf16 v[86:89], v[134:137], v[234:237], v[86:89]
	v_mfma_f32_16x16x32_bf16 v[78:81], v[142:145], v[234:237], v[78:81]
	s_setprio 0
	s_setprio 1
	v_mfma_f32_16x16x32_bf16 v[114:117], v[188:191], v[204:207], v[114:117]
	v_mfma_f32_16x16x32_bf16 v[106:109], v[196:199], v[204:207], v[106:109]
	v_mfma_f32_16x16x32_bf16 v[98:101], v[188:191], v[214:217], v[98:101]
	v_mfma_f32_16x16x32_bf16 v[90:93], v[196:199], v[214:217], v[90:93]
	v_mfma_f32_16x16x32_bf16 v[82:85], v[188:191], v[222:225], v[82:85]
	v_mfma_f32_16x16x32_bf16 v[74:77], v[196:199], v[222:225], v[74:77]
	v_mfma_f32_16x16x32_bf16 v[70:73], v[188:191], v[230:233], v[70:73]
	v_mfma_f32_16x16x32_bf16 v[66:69], v[196:199], v[230:233], v[66:69]
	v_mfma_f32_16x16x32_bf16 v[114:117], v[192:195], v[210:213], v[114:117]
	v_mfma_f32_16x16x32_bf16 v[106:109], v[200:203], v[210:213], v[106:109]
	v_mfma_f32_16x16x32_bf16 v[98:101], v[192:195], v[218:221], v[98:101]
	v_mfma_f32_16x16x32_bf16 v[90:93], v[200:203], v[218:221], v[90:93]
	v_mfma_f32_16x16x32_bf16 v[82:85], v[192:195], v[226:229], v[82:85]
	v_mfma_f32_16x16x32_bf16 v[74:77], v[200:203], v[226:229], v[74:77]
	v_mfma_f32_16x16x32_bf16 v[70:73], v[192:195], v[234:237], v[70:73]
	v_mfma_f32_16x16x32_bf16 v[66:69], v[200:203], v[234:237], v[66:69]
	s_barrier
; #define PG8_STAGE(bufoff, gbase, voff) do { _Pragma("unroll") for (int _i = 0; _i < 2; ++_i) \
;         __builtin_amdgcn_global_load_lds((const unsigned*)((const char*)(gbase) + (voff)[_i]), (PG8_LAS unsigned*)(lds + (bufoff) + ldsw + _i * 8192), 16, 0, 0); } while (0)
; #define PG8_LDA(dst, b, h) do { _Pragma("unroll") for (int m = 0; m < 4; ++m) _Pragma("unroll") for (int k = 0; k < 2; ++k) dst[m][k] = *(const PG8_LAS bf16x8*)(lds + PG8_SA(b, h) + aoff + m * 2048 + k * 1024); } while (0)
; #define PG8_MMA(ai, bj, At, Bt) do { __builtin_amdgcn_s_setprio(1); _Pragma("unroll") for (int m = 0; m < 4; ++m) _Pragma("unroll") for (int n = 0; n < 2; ++n) _Pragma("unroll") for (int k = 0; k < 2; ++k) \
;         acc[ai][bj][m][n] = __builtin_amdgcn_mfma_f32_16x16x32_bf16(Bt[n][k], At[m][k], acc[ai][bj][m][n], 0, 0, 0); __builtin_amdgcn_s_setprio(0); } while (0)
; #define PG8_WAIT_V(n) asm volatile("s_waitcnt vmcnt(" #n ")" ::: "memory")
; #define PG8_WAIT_L(n) asm volatile("s_waitcnt lgkmcnt(" #n ")" ::: "memory")
; #define PG8_BAR __builtin_amdgcn_s_barrier()
; #define PG8_SCHED __builtin_amdgcn_sched_barrier(0)
;     ...
;             PG8_LDA(At, 1, 1); PG8_STAGE(PG8_SB(1, 0), b3, voffB); PG8_STAGE(PG8_SB(1, 1), b3 + hstep, voffB); PG8_STAGE(PG8_SA(1, 0), a3, voffA);
;             PG8_WAIT_V(8); PG8_WAIT_L(0); PG8_BAR; PG8_MMA(1, 0, At, B0); PG8_MMA(1, 1, At, B1); PG8_BAR; PG8_SCHED;
;         }
;         if constexpr (ALIGN_EPI) { if (wr == 0) PG8_BAR; }
;         E(acc, cur, wr, wc, fr, fq); S.done(cur);
;         if (!has_next) break;
	s_setprio 0
	s_add_i32 s22, s51, s28
	v_lshl_add_u64 v[180:181], v[180:181], 0, s[2:3]
	s_mov_b32 m0, s22
	ds_read_b128 v[204:207], v186 offset:49152
	ds_read_b128 v[210:213], v186 offset:50176
	ds_read_b128 v[214:217], v186 offset:51200
	ds_read_b128 v[218:221], v186 offset:52224
	ds_read_b128 v[222:225], v186 offset:53248
	ds_read_b128 v[226:229], v186 offset:54272
	ds_read_b128 v[230:233], v186 offset:55296
	ds_read_b128 v[234:237], v186 offset:56320
	global_load_lds_dwordx4 v[180:181], off
	s_add_i32 m0, s22, 0x2000
	s_add_u32 s20, s20, 0x40080
	v_lshl_add_u64 v[180:181], v[238:239], 0, s[2:3]
	s_addc_u32 s21, s21, 0
	s_add_i32 s22, s52, s28
	global_load_lds_dwordx4 v[180:181], off
	v_lshl_add_u64 v[180:181], s[20:21], 0, v[152:153]
	s_mov_b32 m0, s22
	s_nop 0
	global_load_lds_dwordx4 v[180:181], off
	v_lshl_add_u64 v[180:181], s[20:21], 0, v[148:149]
	s_add_i32 m0, s22, 0x2000
	s_nop 0
	global_load_lds_dwordx4 v[180:181], off
	v_lshl_add_u64 v[180:181], v[240:241], 0, s[2:3]
	s_mov_b32 m0, s37
	s_nop 0
	global_load_lds_dwordx4 v[180:181], off
	v_lshl_add_u64 v[180:181], v[242:243], 0, s[2:3]
	s_mov_b32 m0, s38
	s_nop 0
	global_load_lds_dwordx4 v[180:181], off
	s_waitcnt vmcnt(8)
	s_waitcnt lgkmcnt(0)
	s_setprio 1
	s_barrier
	v_mfma_f32_16x16x32_bf16 v[62:65], v[130:133], v[204:207], v[62:65]
	v_mfma_f32_16x16x32_bf16 v[58:61], v[138:141], v[204:207], v[58:61]
	v_mfma_f32_16x16x32_bf16 v[54:57], v[130:133], v[214:217], v[54:57]
	v_mfma_f32_16x16x32_bf16 v[46:49], v[138:141], v[214:217], v[46:49]
	v_mfma_f32_16x16x32_bf16 v[38:41], v[130:133], v[222:225], v[38:41]
	v_mfma_f32_16x16x32_bf16 v[30:33], v[138:141], v[222:225], v[30:33]
	v_mfma_f32_16x16x32_bf16 v[22:25], v[130:133], v[230:233], v[22:25]
	v_mfma_f32_16x16x32_bf16 v[14:17], v[138:141], v[230:233], v[14:17]
	v_mfma_f32_16x16x32_bf16 v[62:65], v[134:137], v[210:213], v[62:65]
	v_mfma_f32_16x16x32_bf16 v[58:61], v[142:145], v[210:213], v[58:61]
	v_mfma_f32_16x16x32_bf16 v[54:57], v[134:137], v[218:221], v[54:57]
	v_mfma_f32_16x16x32_bf16 v[46:49], v[142:145], v[218:221], v[46:49]
	v_mfma_f32_16x16x32_bf16 v[38:41], v[134:137], v[226:229], v[38:41]
	v_mfma_f32_16x16x32_bf16 v[30:33], v[142:145], v[226:229], v[30:33]
	v_mfma_f32_16x16x32_bf16 v[22:25], v[134:137], v[234:237], v[22:25]
	v_mfma_f32_16x16x32_bf16 v[14:17], v[142:145], v[234:237], v[14:17]
	s_setprio 0
	s_setprio 1
	v_mfma_f32_16x16x32_bf16 v[50:53], v[188:191], v[204:207], v[50:53]
	v_mfma_f32_16x16x32_bf16 v[42:45], v[196:199], v[204:207], v[42:45]
	v_mfma_f32_16x16x32_bf16 v[34:37], v[188:191], v[214:217], v[34:37]
	v_mfma_f32_16x16x32_bf16 v[26:29], v[196:199], v[214:217], v[26:29]
	v_mfma_f32_16x16x32_bf16 v[18:21], v[188:191], v[222:225], v[18:21]
	v_mfma_f32_16x16x32_bf16 v[10:13], v[196:199], v[222:225], v[10:13]
	v_mfma_f32_16x16x32_bf16 v[6:9], v[188:191], v[230:233], v[6:9]
	v_mfma_f32_16x16x32_bf16 v[2:5], v[196:199], v[230:233], v[2:5]
	v_mfma_f32_16x16x32_bf16 v[50:53], v[192:195], v[210:213], v[50:53]
	v_mfma_f32_16x16x32_bf16 v[42:45], v[200:203], v[210:213], v[42:45]
	v_mfma_f32_16x16x32_bf16 v[34:37], v[192:195], v[218:221], v[34:37]
	v_mfma_f32_16x16x32_bf16 v[26:29], v[200:203], v[218:221], v[26:29]
	v_mfma_f32_16x16x32_bf16 v[18:21], v[192:195], v[226:229], v[18:21]
	v_mfma_f32_16x16x32_bf16 v[10:13], v[200:203], v[226:229], v[10:13]
	v_mfma_f32_16x16x32_bf16 v[6:9], v[192:195], v[234:237], v[6:9]
	v_mfma_f32_16x16x32_bf16 v[2:5], v[200:203], v[234:237], v[2:5]
	s_barrier
	s_setprio 0
	s_add_i32 s50, s50, 2
	s_add_u32 s18, s18, 0x100
	s_addc_u32 s19, s19, 0
	s_add_u32 s48, s48, 0x100
	s_addc_u32 s49, s49, 0
	s_cmp_gt_u32 s50, 13
	s_cbranch_scc0 .LBB0_841
	s_and_b64 vcc, exec, s[6:7]
	s_cbranch_vccz .LBB0_844
	s_barrier

; #define PG8_STAGE(bufoff, gbase, voff) do { _Pragma("unroll") for (int _i = 0; _i < 2; ++_i) \
;         __builtin_amdgcn_global_load_lds((const unsigned*)((const char*)(gbase) + (voff)[_i]), (PG8_LAS unsigned*)(lds + (bufoff) + ldsw + _i * 8192), 16, 0, 0); } while (0)
; #define PG8_LDA(dst, b, h) do { _Pragma("unroll") for (int m = 0; m < 4; ++m) _Pragma("unroll") for (int k = 0; k < 2; ++k) dst[m][k] = *(const PG8_LAS bf16x8*)(lds + PG8_SA(b, h) + aoff + m * 2048 + k * 1024); } while (0)
; #define PG8_LDB(dst, b, h) do { _Pragma("unroll") for (int n = 0; n < 2; ++n) _Pragma("unroll") for (int k = 0; k < 2; ++k) dst[n][k] = *(const PG8_LAS bf16x8*)(lds + PG8_SB(b, h) + boff + n * 2048 + k * 1024); } while (0)
; #define PG8_MMA(ai, bj, At, Bt) do { __builtin_amdgcn_s_setprio(1); _Pragma("unroll") for (int m = 0; m < 4; ++m) _Pragma("unroll") for (int n = 0; n < 2; ++n) _Pragma("unroll") for (int k = 0; k < 2; ++k) \
;         acc[ai][bj][m][n] = __builtin_amdgcn_mfma_f32_16x16x32_bf16(Bt[n][k], At[m][k], acc[ai][bj][m][n], 0, 0, 0); __builtin_amdgcn_s_setprio(0); } while (0)
; #define PG8_WAIT_V(n) asm volatile("s_waitcnt vmcnt(" #n ")" ::: "memory")
; #define PG8_WAIT_L(n) asm volatile("s_waitcnt lgkmcnt(" #n ")" ::: "memory")
; #define PG8_BAR __builtin_amdgcn_s_barrier()
; #define PG8_SCHED __builtin_amdgcn_sched_barrier(0)
;     ...
;         for (int t = 0; t < nt; t += 2) {
;             const bool last = (t == nt - 2);
;             const char* a1 = cA + (size_t)(t + 1) * kstep;
;             const char* a2 = last ? nA : cA + (size_t)(t + 2) * kstep; const char* b2 = last ? nB : cB + (size_t)(t + 2) * kstep;
;             const char* a3 = a2 + kstep; const char* b3 = b2 + kstep;
;             if (last && has_next) S.a_ready(nxt);
;             PG8_LDB(B0, 0, 0); PG8_LDB(B1, 0, 1); PG8_SCHED; PG8_LDA(At, 0, 0); PG8_STAGE(PG8_SA(1, 1), a1 + hstep, voffA);
;             PG8_WAIT_V(8); PG8_WAIT_L(0); PG8_BAR; PG8_MMA(0, 0, At, B0); PG8_MMA(0, 1, At, B1); PG8_BAR; PG8_SCHED;
;             PG8_LDA(At, 0, 1); PG8_STAGE(PG8_SB(0, 0), b2, voffB); PG8_STAGE(PG8_SB(0, 1), b2 + hstep, voffB); PG8_STAGE(PG8_SA(0, 0), a2, voffA);
.LBB0_995:
	ds_read_b128 v[154:157], v151
	ds_read_b128 v[158:161], v151 offset:1024
	ds_read_b128 v[162:165], v151 offset:2048
	ds_read_b128 v[166:169], v151 offset:3072
	ds_read_b128 v[170:173], v152
	ds_read_b128 v[174:177], v152 offset:1024
	ds_read_b128 v[178:181], v152 offset:2048
	ds_read_b128 v[182:185], v152 offset:3072
	s_add_u32 s22, s20, 0xfffc0080
	s_addc_u32 s23, s21, -1
	s_cmp_eq_u32 s53, 12
	s_cselect_b32 s25, s13, s23
	s_cselect_b32 s24, s49, s22
	s_cselect_b32 s23, s11, s52
	s_cselect_b32 s22, s50, s51
	v_lshl_add_u64 v[146:147], s[20:21], 0, v[138:139]
	s_add_i32 m0, s19, 0xc000
	ds_read_b128 v[186:189], v153
	ds_read_b128 v[190:193], v153 offset:1024
	ds_read_b128 v[194:197], v153 offset:2048
	ds_read_b128 v[198:201], v153 offset:3072
	ds_read_b128 v[202:205], v153 offset:4096
	ds_read_b128 v[210:213], v153 offset:5120
	ds_read_b128 v[214:217], v153 offset:6144
	ds_read_b128 v[218:221], v153 offset:7168
	global_load_lds_dwordx4 v[146:147], off
	v_lshl_add_u64 v[146:147], s[20:21], 0, v[140:141]
	s_add_i32 m0, s19, 0xe000
	s_nop 0
	global_load_lds_dwordx4 v[146:147], off
	s_waitcnt vmcnt(8)
	s_waitcnt lgkmcnt(0)
	s_setprio 1
	s_barrier
	v_mfma_f32_16x16x32_bf16 v[126:129], v[154:157], v[186:189], v[126:129]
	v_mfma_f32_16x16x32_bf16 v[122:125], v[162:165], v[186:189], v[122:125]
	v_mfma_f32_16x16x32_bf16 v[110:113], v[154:157], v[194:197], v[110:113]
	v_mfma_f32_16x16x32_bf16 v[106:109], v[162:165], v[194:197], v[106:109]
	v_mfma_f32_16x16x32_bf16 v[94:97], v[154:157], v[202:205], v[94:97]
	v_mfma_f32_16x16x32_bf16 v[90:93], v[162:165], v[202:205], v[90:93]
	v_mfma_f32_16x16x32_bf16 v[78:81], v[154:157], v[214:217], v[78:81]
	v_mfma_f32_16x16x32_bf16 v[74:77], v[162:165], v[214:217], v[74:77]
	v_mfma_f32_16x16x32_bf16 v[126:129], v[158:161], v[190:193], v[126:129]
	v_mfma_f32_16x16x32_bf16 v[122:125], v[166:169], v[190:193], v[122:125]
	v_mfma_f32_16x16x32_bf16 v[110:113], v[158:161], v[198:201], v[110:113]
	v_mfma_f32_16x16x32_bf16 v[106:109], v[166:169], v[198:201], v[106:109]
	v_mfma_f32_16x16x32_bf16 v[94:97], v[158:161], v[210:213], v[94:97]
	v_mfma_f32_16x16x32_bf16 v[90:93], v[166:169], v[210:213], v[90:93]
	v_mfma_f32_16x16x32_bf16 v[78:81], v[158:161], v[218:221], v[78:81]
	v_mfma_f32_16x16x32_bf16 v[74:77], v[166:169], v[218:221], v[74:77]
	s_setprio 0
	s_setprio 1
	v_mfma_f32_16x16x32_bf16 v[118:121], v[170:173], v[186:189], v[118:121]
	v_mfma_f32_16x16x32_bf16 v[114:117], v[178:181], v[186:189], v[114:117]
	v_mfma_f32_16x16x32_bf16 v[102:105], v[170:173], v[194:197], v[102:105]
	v_mfma_f32_16x16x32_bf16 v[98:101], v[178:181], v[194:197], v[98:101]
	v_mfma_f32_16x16x32_bf16 v[86:89], v[170:173], v[202:205], v[86:89]
	v_mfma_f32_16x16x32_bf16 v[82:85], v[178:181], v[202:205], v[82:85]
	v_mfma_f32_16x16x32_bf16 v[70:73], v[170:173], v[214:217], v[70:73]
	v_mfma_f32_16x16x32_bf16 v[66:69], v[178:181], v[214:217], v[66:69]
	v_mfma_f32_16x16x32_bf16 v[118:121], v[174:177], v[190:193], v[118:121]
	v_mfma_f32_16x16x32_bf16 v[114:117], v[182:185], v[190:193], v[114:117]
	v_mfma_f32_16x16x32_bf16 v[102:105], v[174:177], v[198:201], v[102:105]
	v_mfma_f32_16x16x32_bf16 v[98:101], v[182:185], v[198:201], v[98:101]
	v_mfma_f32_16x16x32_bf16 v[86:89], v[174:177], v[210:213], v[86:89]
	v_mfma_f32_16x16x32_bf16 v[82:85], v[182:185], v[210:213], v[82:85]
	v_mfma_f32_16x16x32_bf16 v[70:73], v[174:177], v[218:221], v[70:73]
	v_mfma_f32_16x16x32_bf16 v[66:69], v[182:185], v[218:221], v[66:69]
	s_barrier
	s_setprio 0
	s_add_i32 s54, s45, s30
	v_lshl_add_u64 v[146:147], s[22:23], 0, v[134:135]
	s_mov_b32 m0, s54
	ds_read_b128 v[186:189], v153 offset:16384
	ds_read_b128 v[190:193], v153 offset:17408
	ds_read_b128 v[194:197], v153 offset:18432
	ds_read_b128 v[198:201], v153 offset:19456
	ds_read_b128 v[202:205], v153 offset:20480
	ds_read_b128 v[210:213], v153 offset:21504
	ds_read_b128 v[214:217], v153 offset:22528
	ds_read_b128 v[218:221], v153 offset:23552
	global_load_lds_dwordx4 v[146:147], off
	s_add_i32 m0, s54, 0x2000
	s_add_u32 s54, s22, 0x40000
	v_lshl_add_u64 v[206:207], s[22:23], 0, v[130:131]
	s_addc_u32 s55, s23, 0
	s_add_i32 s56, s46, s30
	global_load_lds_dwordx4 v[206:207], off
	v_lshl_add_u64 v[222:223], s[54:55], 0, v[134:135]
	s_mov_b32 m0, s56
	v_lshl_add_u64 v[224:225], s[24:25], 0, v[132:133]
	global_load_lds_dwordx4 v[222:223], off
	v_lshl_add_u64 v[222:223], s[54:55], 0, v[130:131]
	s_add_i32 m0, s56, 0x2000
	s_nop 0
	global_load_lds_dwordx4 v[222:223], off
	v_lshl_add_u64 v[222:223], s[24:25], 0, v[136:137]
	s_mov_b32 m0, s19
	s_nop 0
	global_load_lds_dwordx4 v[222:223], off
	s_mov_b32 m0, s34
	s_nop 0
	global_load_lds_dwordx4 v[224:225], off
	s_waitcnt vmcnt(8)
	s_waitcnt lgkmcnt(0)
	s_setprio 1
	s_barrier
; #define PG8_STAGE(bufoff, gbase, voff) do { _Pragma("unroll") for (int _i = 0; _i < 2; ++_i) \
;         __builtin_amdgcn_global_load_lds((const unsigned*)((const char*)(gbase) + (voff)[_i]), (PG8_LAS unsigned*)(lds + (bufoff) + ldsw + _i * 8192), 16, 0, 0); } while (0)
; #define PG8_LDA(dst, b, h) do { _Pragma("unroll") for (int m = 0; m < 4; ++m) _Pragma("unroll") for (int k = 0; k < 2; ++k) dst[m][k] = *(const PG8_LAS bf16x8*)(lds + PG8_SA(b, h) + aoff + m * 2048 + k * 1024); } while (0)
; #define PG8_LDB(dst, b, h) do { _Pragma("unroll") for (int n = 0; n < 2; ++n) _Pragma("unroll") for (int k = 0; k < 2; ++k) dst[n][k] = *(const PG8_LAS bf16x8*)(lds + PG8_SB(b, h) + boff + n * 2048 + k * 1024); } while (0)
; #define PG8_MMA(ai, bj, At, Bt) do { __builtin_amdgcn_s_setprio(1); _Pragma("unroll") for (int m = 0; m < 4; ++m) _Pragma("unroll") for (int n = 0; n < 2; ++n) _Pragma("unroll") for (int k = 0; k < 2; ++k) \
;         acc[ai][bj][m][n] = __builtin_amdgcn_mfma_f32_16x16x32_bf16(Bt[n][k], At[m][k], acc[ai][bj][m][n], 0, 0, 0); __builtin_amdgcn_s_setprio(0); } while (0)
; #define PG8_WAIT_V(n) asm volatile("s_waitcnt vmcnt(" #n ")" ::: "memory")
; #define PG8_WAIT_L(n) asm volatile("s_waitcnt lgkmcnt(" #n ")" ::: "memory")
; #define PG8_BAR __builtin_amdgcn_s_barrier()
; #define PG8_SCHED __builtin_amdgcn_sched_barrier(0)
;     ...
;             PG8_WAIT_V(8); PG8_WAIT_L(0); PG8_BAR; PG8_MMA(1, 0, At, B0); PG8_MMA(1, 1, At, B1); PG8_BAR; PG8_SCHED;
;             PG8_LDB(B0, 1, 0); PG8_LDB(B1, 1, 1); PG8_SCHED; PG8_LDA(At, 1, 0); PG8_STAGE(PG8_SA(0, 1), a2 + hstep, voffA);
;             PG8_WAIT_V(8); PG8_WAIT_L(0); PG8_BAR; PG8_MMA(0, 0, At, B0); PG8_MMA(0, 1, At, B1); PG8_BAR; PG8_SCHED;
	v_mfma_f32_16x16x32_bf16 v[62:65], v[154:157], v[186:189], v[62:65]
	v_mfma_f32_16x16x32_bf16 v[58:61], v[162:165], v[186:189], v[58:61]
	v_mfma_f32_16x16x32_bf16 v[46:49], v[154:157], v[194:197], v[46:49]
	v_mfma_f32_16x16x32_bf16 v[42:45], v[162:165], v[194:197], v[42:45]
	v_mfma_f32_16x16x32_bf16 v[30:33], v[154:157], v[202:205], v[30:33]
	v_mfma_f32_16x16x32_bf16 v[26:29], v[162:165], v[202:205], v[26:29]
	v_mfma_f32_16x16x32_bf16 v[14:17], v[154:157], v[214:217], v[14:17]
	v_mfma_f32_16x16x32_bf16 v[10:13], v[162:165], v[214:217], v[10:13]
	v_mfma_f32_16x16x32_bf16 v[62:65], v[158:161], v[190:193], v[62:65]
	v_mfma_f32_16x16x32_bf16 v[58:61], v[166:169], v[190:193], v[58:61]
	v_mfma_f32_16x16x32_bf16 v[46:49], v[158:161], v[198:201], v[46:49]
	v_mfma_f32_16x16x32_bf16 v[42:45], v[166:169], v[198:201], v[42:45]
	v_mfma_f32_16x16x32_bf16 v[30:33], v[158:161], v[210:213], v[30:33]
	v_mfma_f32_16x16x32_bf16 v[26:29], v[166:169], v[210:213], v[26:29]
	v_mfma_f32_16x16x32_bf16 v[14:17], v[158:161], v[218:221], v[14:17]
	v_mfma_f32_16x16x32_bf16 v[10:13], v[166:169], v[218:221], v[10:13]
	s_setprio 0
	s_setprio 1
	v_mfma_f32_16x16x32_bf16 v[54:57], v[170:173], v[186:189], v[54:57]
	v_mfma_f32_16x16x32_bf16 v[50:53], v[178:181], v[186:189], v[50:53]
	v_mfma_f32_16x16x32_bf16 v[38:41], v[170:173], v[194:197], v[38:41]
	v_mfma_f32_16x16x32_bf16 v[34:37], v[178:181], v[194:197], v[34:37]
	v_mfma_f32_16x16x32_bf16 v[22:25], v[170:173], v[202:205], v[22:25]
	v_mfma_f32_16x16x32_bf16 v[18:21], v[178:181], v[202:205], v[18:21]
	v_mfma_f32_16x16x32_bf16 v[6:9], v[170:173], v[214:217], v[6:9]
	v_mfma_f32_16x16x32_bf16 v[2:5], v[178:181], v[214:217], v[2:5]
	v_mfma_f32_16x16x32_bf16 v[54:57], v[174:177], v[190:193], v[54:57]
	v_mfma_f32_16x16x32_bf16 v[50:53], v[182:185], v[190:193], v[50:53]
	v_mfma_f32_16x16x32_bf16 v[38:41], v[174:177], v[198:201], v[38:41]
	v_mfma_f32_16x16x32_bf16 v[34:37], v[182:185], v[198:201], v[34:37]
	v_mfma_f32_16x16x32_bf16 v[22:25], v[174:177], v[210:213], v[22:25]
	v_mfma_f32_16x16x32_bf16 v[18:21], v[182:185], v[210:213], v[18:21]
	v_mfma_f32_16x16x32_bf16 v[6:9], v[174:177], v[218:221], v[6:9]
	v_mfma_f32_16x16x32_bf16 v[2:5], v[182:185], v[218:221], v[2:5]
	s_barrier
	s_setprio 0
	s_add_i32 s54, 0, 0x18000
	s_add_i32 s55, 0, 0x1c000
	v_add_u32_e32 v166, s54, v149
	v_add_u32_e32 v182, s55, v149
	ds_read_b128 v[154:157], v166
	ds_read_b128 v[158:161], v166 offset:1024
	ds_read_b128 v[162:165], v166 offset:2048
	ds_read_b128 v[166:169], v166 offset:3072
	ds_read_b128 v[170:173], v182
	ds_read_b128 v[174:177], v182 offset:1024
	ds_read_b128 v[178:181], v182 offset:2048
	ds_read_b128 v[182:185], v182 offset:3072
	s_add_u32 s24, s24, 0x40000
	s_addc_u32 s25, s25, 0
	s_mov_b32 m0, s35
	v_lshl_add_u64 v[226:227], s[24:25], 0, v[136:137]
	ds_read_b128 v[186:189], v153 offset:32768
	ds_read_b128 v[190:193], v153 offset:33792
	ds_read_b128 v[194:197], v153 offset:34816
	ds_read_b128 v[198:201], v153 offset:35840
	ds_read_b128 v[202:205], v153 offset:36864
	ds_read_b128 v[210:213], v153 offset:37888
	ds_read_b128 v[214:217], v153 offset:38912
	ds_read_b128 v[218:221], v153 offset:39936
	global_load_lds_dwordx4 v[226:227], off
	v_lshl_add_u64 v[226:227], s[24:25], 0, v[132:133]
	s_mov_b32 m0, s36
	s_nop 0
	global_load_lds_dwordx4 v[226:227], off
	s_waitcnt vmcnt(8)
	s_waitcnt lgkmcnt(0)
	s_setprio 1
	s_barrier
	v_mfma_f32_16x16x32_bf16 v[126:129], v[154:157], v[186:189], v[126:129]
	v_mfma_f32_16x16x32_bf16 v[122:125], v[162:165], v[186:189], v[122:125]
	v_mfma_f32_16x16x32_bf16 v[110:113], v[154:157], v[194:197], v[110:113]
	v_mfma_f32_16x16x32_bf16 v[106:109], v[162:165], v[194:197], v[106:109]
	v_mfma_f32_16x16x32_bf16 v[94:97], v[154:157], v[202:205], v[94:97]
	v_mfma_f32_16x16x32_bf16 v[90:93], v[162:165], v[202:205], v[90:93]
	v_mfma_f32_16x16x32_bf16 v[78:81], v[154:157], v[214:217], v[78:81]
	v_mfma_f32_16x16x32_bf16 v[74:77], v[162:165], v[214:217], v[74:77]
	v_mfma_f32_16x16x32_bf16 v[126:129], v[158:161], v[190:193], v[126:129]
	v_mfma_f32_16x16x32_bf16 v[122:125], v[166:169], v[190:193], v[122:125]
	v_mfma_f32_16x16x32_bf16 v[110:113], v[158:161], v[198:201], v[110:113]
	v_mfma_f32_16x16x32_bf16 v[106:109], v[166:169], v[198:201], v[106:109]
	v_mfma_f32_16x16x32_bf16 v[94:97], v[158:161], v[210:213], v[94:97]
	v_mfma_f32_16x16x32_bf16 v[90:93], v[166:169], v[210:213], v[90:93]
	v_mfma_f32_16x16x32_bf16 v[78:81], v[158:161], v[218:221], v[78:81]
	v_mfma_f32_16x16x32_bf16 v[74:77], v[166:169], v[218:221], v[74:77]
	s_setprio 0
	s_setprio 1
	v_mfma_f32_16x16x32_bf16 v[118:121], v[170:173], v[186:189], v[118:121]
	v_mfma_f32_16x16x32_bf16 v[114:117], v[178:181], v[186:189], v[114:117]
	v_mfma_f32_16x16x32_bf16 v[102:105], v[170:173], v[194:197], v[102:105]
	v_mfma_f32_16x16x32_bf16 v[98:101], v[178:181], v[194:197], v[98:101]
	v_mfma_f32_16x16x32_bf16 v[86:89], v[170:173], v[202:205], v[86:89]
	v_mfma_f32_16x16x32_bf16 v[82:85], v[178:181], v[202:205], v[82:85]
	v_mfma_f32_16x16x32_bf16 v[70:73], v[170:173], v[214:217], v[70:73]
	v_mfma_f32_16x16x32_bf16 v[66:69], v[178:181], v[214:217], v[66:69]
	v_mfma_f32_16x16x32_bf16 v[118:121], v[174:177], v[190:193], v[118:121]
	v_mfma_f32_16x16x32_bf16 v[114:117], v[182:185], v[190:193], v[114:117]
	v_mfma_f32_16x16x32_bf16 v[102:105], v[174:177], v[198:201], v[102:105]
	v_mfma_f32_16x16x32_bf16 v[98:101], v[182:185], v[198:201], v[98:101]
	v_mfma_f32_16x16x32_bf16 v[86:89], v[174:177], v[210:213], v[86:89]
	v_mfma_f32_16x16x32_bf16 v[82:85], v[182:185], v[210:213], v[82:85]
	v_mfma_f32_16x16x32_bf16 v[70:73], v[174:177], v[218:221], v[70:73]
	v_mfma_f32_16x16x32_bf16 v[66:69], v[182:185], v[218:221], v[66:69]
	s_barrier
; #define PG8_STAGE(bufoff, gbase, voff) do { _Pragma("unroll") for (int _i = 0; _i < 2; ++_i) \
;         __builtin_amdgcn_global_load_lds((const unsigned*)((const char*)(gbase) + (voff)[_i]), (PG8_LAS unsigned*)(lds + (bufoff) + ldsw + _i * 8192), 16, 0, 0); } while (0)
; #define PG8_LDA(dst, b, h) do { _Pragma("unroll") for (int m = 0; m < 4; ++m) _Pragma("unroll") for (int k = 0; k < 2; ++k) dst[m][k] = *(const PG8_LAS bf16x8*)(lds + PG8_SA(b, h) + aoff + m * 2048 + k * 1024); } while (0)
; #define PG8_MMA(ai, bj, At, Bt) do { __builtin_amdgcn_s_setprio(1); _Pragma("unroll") for (int m = 0; m < 4; ++m) _Pragma("unroll") for (int n = 0; n < 2; ++n) _Pragma("unroll") for (int k = 0; k < 2; ++k) \
;         acc[ai][bj][m][n] = __builtin_amdgcn_mfma_f32_16x16x32_bf16(Bt[n][k], At[m][k], acc[ai][bj][m][n], 0, 0, 0); __builtin_amdgcn_s_setprio(0); } while (0)
; #define PG8_WAIT_V(n) asm volatile("s_waitcnt vmcnt(" #n ")" ::: "memory")
; #define PG8_WAIT_L(n) asm volatile("s_waitcnt lgkmcnt(" #n ")" ::: "memory")
; #define PG8_BAR __builtin_amdgcn_s_barrier()
; #define PG8_SCHED __builtin_amdgcn_sched_barrier(0)
;     ...
;             PG8_LDA(At, 1, 1); PG8_STAGE(PG8_SB(1, 0), b3, voffB); PG8_STAGE(PG8_SB(1, 1), b3 + hstep, voffB); PG8_STAGE(PG8_SA(1, 0), a3, voffA);
;             PG8_WAIT_V(8); PG8_WAIT_L(0); PG8_BAR; PG8_MMA(1, 0, At, B0); PG8_MMA(1, 1, At, B1); PG8_BAR; PG8_SCHED;
;         }
;         if constexpr (ALIGN_EPI) { if (wr == 0) PG8_BAR; }
;         E(acc, cur, wr, wc, fr, fq); S.done(cur);
;         if (!has_next) break;
	s_setprio 0
	s_add_i32 s24, s54, s30
	v_lshl_add_u64 v[146:147], v[146:147], 0, s[6:7]
	s_mov_b32 m0, s24
	ds_read_b128 v[186:189], v153 offset:49152
	ds_read_b128 v[190:193], v153 offset:50176
	ds_read_b128 v[194:197], v153 offset:51200
	ds_read_b128 v[198:201], v153 offset:52224
	ds_read_b128 v[202:205], v153 offset:53248
	ds_read_b128 v[210:213], v153 offset:54272
	ds_read_b128 v[214:217], v153 offset:55296
	ds_read_b128 v[218:221], v153 offset:56320
	global_load_lds_dwordx4 v[146:147], off
	s_add_i32 m0, s24, 0x2000
	s_add_u32 s22, s22, 0x40080
	v_lshl_add_u64 v[146:147], v[206:207], 0, s[6:7]
	s_addc_u32 s23, s23, 0
	s_add_i32 s24, s55, s30
	global_load_lds_dwordx4 v[146:147], off
	v_lshl_add_u64 v[146:147], s[22:23], 0, v[134:135]
	s_mov_b32 m0, s24
	s_nop 0
	global_load_lds_dwordx4 v[146:147], off
	v_lshl_add_u64 v[146:147], s[22:23], 0, v[130:131]
	s_add_i32 m0, s24, 0x2000
	s_nop 0
	global_load_lds_dwordx4 v[146:147], off
	v_lshl_add_u64 v[146:147], v[222:223], 0, s[6:7]
	s_mov_b32 m0, s38
	s_nop 0
	global_load_lds_dwordx4 v[146:147], off
	v_lshl_add_u64 v[146:147], v[224:225], 0, s[6:7]
	s_mov_b32 m0, s39
	s_nop 0
	global_load_lds_dwordx4 v[146:147], off
	s_waitcnt vmcnt(8)
	s_waitcnt lgkmcnt(0)
	s_setprio 1
	s_barrier
	v_mfma_f32_16x16x32_bf16 v[62:65], v[154:157], v[186:189], v[62:65]
	v_mfma_f32_16x16x32_bf16 v[58:61], v[162:165], v[186:189], v[58:61]
	v_mfma_f32_16x16x32_bf16 v[46:49], v[154:157], v[194:197], v[46:49]
	v_mfma_f32_16x16x32_bf16 v[42:45], v[162:165], v[194:197], v[42:45]
	v_mfma_f32_16x16x32_bf16 v[30:33], v[154:157], v[202:205], v[30:33]
	v_mfma_f32_16x16x32_bf16 v[26:29], v[162:165], v[202:205], v[26:29]
	v_mfma_f32_16x16x32_bf16 v[14:17], v[154:157], v[214:217], v[14:17]
	v_mfma_f32_16x16x32_bf16 v[10:13], v[162:165], v[214:217], v[10:13]
	v_mfma_f32_16x16x32_bf16 v[62:65], v[158:161], v[190:193], v[62:65]
	v_mfma_f32_16x16x32_bf16 v[58:61], v[166:169], v[190:193], v[58:61]
	v_mfma_f32_16x16x32_bf16 v[46:49], v[158:161], v[198:201], v[46:49]
	v_mfma_f32_16x16x32_bf16 v[42:45], v[166:169], v[198:201], v[42:45]
	v_mfma_f32_16x16x32_bf16 v[30:33], v[158:161], v[210:213], v[30:33]
	v_mfma_f32_16x16x32_bf16 v[26:29], v[166:169], v[210:213], v[26:29]
	v_mfma_f32_16x16x32_bf16 v[14:17], v[158:161], v[218:221], v[14:17]
	v_mfma_f32_16x16x32_bf16 v[10:13], v[166:169], v[218:221], v[10:13]
	s_setprio 0
	s_setprio 1
	v_mfma_f32_16x16x32_bf16 v[54:57], v[170:173], v[186:189], v[54:57]
	v_mfma_f32_16x16x32_bf16 v[50:53], v[178:181], v[186:189], v[50:53]
	v_mfma_f32_16x16x32_bf16 v[38:41], v[170:173], v[194:197], v[38:41]
	v_mfma_f32_16x16x32_bf16 v[34:37], v[178:181], v[194:197], v[34:37]
	v_mfma_f32_16x16x32_bf16 v[22:25], v[170:173], v[202:205], v[22:25]
	v_mfma_f32_16x16x32_bf16 v[18:21], v[178:181], v[202:205], v[18:21]
	v_mfma_f32_16x16x32_bf16 v[6:9], v[170:173], v[214:217], v[6:9]
	v_mfma_f32_16x16x32_bf16 v[2:5], v[178:181], v[214:217], v[2:5]
	v_mfma_f32_16x16x32_bf16 v[54:57], v[174:177], v[190:193], v[54:57]
	v_mfma_f32_16x16x32_bf16 v[50:53], v[182:185], v[190:193], v[50:53]
	v_mfma_f32_16x16x32_bf16 v[38:41], v[174:177], v[198:201], v[38:41]
	v_mfma_f32_16x16x32_bf16 v[34:37], v[182:185], v[198:201], v[34:37]
	v_mfma_f32_16x16x32_bf16 v[22:25], v[174:177], v[210:213], v[22:25]
	v_mfma_f32_16x16x32_bf16 v[18:21], v[182:185], v[210:213], v[18:21]
	v_mfma_f32_16x16x32_bf16 v[6:9], v[174:177], v[218:221], v[6:9]
	v_mfma_f32_16x16x32_bf16 v[2:5], v[182:185], v[218:221], v[2:5]
	s_barrier
	s_setprio 0
	s_add_i32 s53, s53, 2
	s_add_u32 s20, s20, 0x100
	s_addc_u32 s21, s21, 0
	s_add_u32 s51, s51, 0x100
	s_addc_u32 s52, s52, 0
	s_cmp_gt_u32 s53, 13
	s_cbranch_scc0 .LBB0_995
	s_and_b64 vcc, exec, s[8:9]
	s_cbranch_vccz .LBB0_998
	s_barrier

; #define PG8_STAGE(bufoff, gbase, voff) do { _Pragma("unroll") for (int _i = 0; _i < 2; ++_i) \
;         __builtin_amdgcn_global_load_lds((const unsigned*)((const char*)(gbase) + (voff)[_i]), (PG8_LAS unsigned*)(lds + (bufoff) + ldsw + _i * 8192), 16, 0, 0); } while (0)
; #define PG8_LDA(dst, b, h) do { _Pragma("unroll") for (int m = 0; m < 4; ++m) _Pragma("unroll") for (int k = 0; k < 2; ++k) dst[m][k] = *(const PG8_LAS bf16x8*)(lds + PG8_SA(b, h) + aoff + m * 2048 + k * 1024); } while (0)
; #define PG8_LDB(dst, b, h) do { _Pragma("unroll") for (int n = 0; n < 2; ++n) _Pragma("unroll") for (int k = 0; k < 2; ++k) dst[n][k] = *(const PG8_LAS bf16x8*)(lds + PG8_SB(b, h) + boff + n * 2048 + k * 1024); } while (0)
; #define PG8_MMA(ai, bj, At, Bt) do { __builtin_amdgcn_s_setprio(1); _Pragma("unroll") for (int m = 0; m < 4; ++m) _Pragma("unroll") for (int n = 0; n < 2; ++n) _Pragma("unroll") for (int k = 0; k < 2; ++k) \
;         acc[ai][bj][m][n] = __builtin_amdgcn_mfma_f32_16x16x32_bf16(Bt[n][k], At[m][k], acc[ai][bj][m][n], 0, 0, 0); __builtin_amdgcn_s_setprio(0); } while (0)
; #define PG8_WAIT_V(n) asm volatile("s_waitcnt vmcnt(" #n ")" ::: "memory")
; #define PG8_WAIT_L(n) asm volatile("s_waitcnt lgkmcnt(" #n ")" ::: "memory")
; #define PG8_BAR __builtin_amdgcn_s_barrier()
; #define PG8_SCHED __builtin_amdgcn_sched_barrier(0)
;     ...
;         for (int t = 0; t < nt; t += 2) {
;             const bool last = (t == nt - 2);
;             const char* a1 = cA + (size_t)(t + 1) * kstep;
;             const char* a2 = last ? nA : cA + (size_t)(t + 2) * kstep; const char* b2 = last ? nB : cB + (size_t)(t + 2) * kstep;
;             const char* a3 = a2 + kstep; const char* b3 = b2 + kstep;
;             if (last && has_next) S.a_ready(nxt);
;             PG8_LDB(B0, 0, 0); PG8_LDB(B1, 0, 1); PG8_SCHED; PG8_LDA(At, 0, 0); PG8_STAGE(PG8_SA(1, 1), a1 + hstep, voffA);
;             PG8_WAIT_V(8); PG8_WAIT_L(0); PG8_BAR; PG8_MMA(0, 0, At, B0); PG8_MMA(0, 1, At, B1); PG8_BAR; PG8_SCHED;
;             PG8_LDA(At, 0, 1); PG8_STAGE(PG8_SB(0, 0), b2, voffB); PG8_STAGE(PG8_SB(0, 1), b2 + hstep, voffB); PG8_STAGE(PG8_SA(0, 0), a2, voffA);
.LBB0_1089:
	ds_read_b128 v[114:117], v217
	ds_read_b128 v[118:121], v217 offset:1024
	ds_read_b128 v[122:125], v217 offset:2048
	ds_read_b128 v[126:129], v217 offset:3072
	ds_read_b128 v[146:149], v218
	ds_read_b128 v[150:153], v218 offset:1024
	ds_read_b128 v[154:157], v218 offset:2048
	ds_read_b128 v[158:161], v218 offset:3072
	s_add_u32 s16, s14, 0xfff50080
	s_addc_u32 s17, s15, -1
	s_cmp_eq_u32 s47, 40
	s_cselect_b32 s19, s7, s17
	s_cselect_b32 s18, s6, s16
	s_cselect_b32 s17, s11, s46
	s_cselect_b32 s16, s10, s13
	v_lshl_add_u64 v[240:241], s[14:15], 0, v[194:195]
	s_add_i32 m0, s26, 0xc000
	ds_read_b128 v[162:165], v219
	ds_read_b128 v[166:169], v219 offset:1024
	ds_read_b128 v[202:205], v219 offset:2048
	ds_read_b128 v[220:223], v219 offset:3072
	ds_read_b128 v[224:227], v219 offset:4096
	ds_read_b128 v[228:231], v219 offset:5120
	ds_read_b128 v[232:235], v219 offset:6144
	ds_read_b128 v[236:239], v219 offset:7168
	global_load_lds_dwordx4 v[240:241], off
	v_lshl_add_u64 v[240:241], s[14:15], 0, v[196:197]
	s_add_i32 m0, s26, 0xe000
	s_nop 0
	global_load_lds_dwordx4 v[240:241], off
	s_waitcnt vmcnt(8)
	s_waitcnt lgkmcnt(0)
	s_setprio 1
	s_barrier
	v_mfma_f32_16x16x32_bf16 v[142:145], v[114:117], v[162:165], v[142:145]
	v_mfma_f32_16x16x32_bf16 v[138:141], v[122:125], v[162:165], v[138:141]
	v_mfma_f32_16x16x32_bf16 v[110:113], v[114:117], v[202:205], v[110:113]
	v_mfma_f32_16x16x32_bf16 v[106:109], v[122:125], v[202:205], v[106:109]
	v_mfma_f32_16x16x32_bf16 v[98:101], v[114:117], v[224:227], v[98:101]
	v_mfma_f32_16x16x32_bf16 v[90:93], v[122:125], v[224:227], v[90:93]
	v_mfma_f32_16x16x32_bf16 v[82:85], v[114:117], v[232:235], v[82:85]
	v_mfma_f32_16x16x32_bf16 v[74:77], v[122:125], v[232:235], v[74:77]
	v_mfma_f32_16x16x32_bf16 v[142:145], v[118:121], v[166:169], v[142:145]
	v_mfma_f32_16x16x32_bf16 v[138:141], v[126:129], v[166:169], v[138:141]
	v_mfma_f32_16x16x32_bf16 v[110:113], v[118:121], v[220:223], v[110:113]
	v_mfma_f32_16x16x32_bf16 v[106:109], v[126:129], v[220:223], v[106:109]
	v_mfma_f32_16x16x32_bf16 v[98:101], v[118:121], v[228:231], v[98:101]
	v_mfma_f32_16x16x32_bf16 v[90:93], v[126:129], v[228:231], v[90:93]
	v_mfma_f32_16x16x32_bf16 v[82:85], v[118:121], v[236:239], v[82:85]
	v_mfma_f32_16x16x32_bf16 v[74:77], v[126:129], v[236:239], v[74:77]
	s_setprio 0
	s_setprio 1
	v_mfma_f32_16x16x32_bf16 v[134:137], v[146:149], v[162:165], v[134:137]
	v_mfma_f32_16x16x32_bf16 v[130:133], v[154:157], v[162:165], v[130:133]
	v_mfma_f32_16x16x32_bf16 v[102:105], v[146:149], v[202:205], v[102:105]
	v_mfma_f32_16x16x32_bf16 v[94:97], v[154:157], v[202:205], v[94:97]
	v_mfma_f32_16x16x32_bf16 v[86:89], v[146:149], v[224:227], v[86:89]
	v_mfma_f32_16x16x32_bf16 v[78:81], v[154:157], v[224:227], v[78:81]
	v_mfma_f32_16x16x32_bf16 v[70:73], v[146:149], v[232:235], v[70:73]
	v_mfma_f32_16x16x32_bf16 v[66:69], v[154:157], v[232:235], v[66:69]
	v_mfma_f32_16x16x32_bf16 v[134:137], v[150:153], v[166:169], v[134:137]
	v_mfma_f32_16x16x32_bf16 v[130:133], v[158:161], v[166:169], v[130:133]
	v_mfma_f32_16x16x32_bf16 v[102:105], v[150:153], v[220:223], v[102:105]
	v_mfma_f32_16x16x32_bf16 v[94:97], v[158:161], v[220:223], v[94:97]
	v_mfma_f32_16x16x32_bf16 v[86:89], v[150:153], v[228:231], v[86:89]
	v_mfma_f32_16x16x32_bf16 v[78:81], v[158:161], v[228:231], v[78:81]
	v_mfma_f32_16x16x32_bf16 v[70:73], v[150:153], v[236:239], v[70:73]
	v_mfma_f32_16x16x32_bf16 v[66:69], v[158:161], v[236:239], v[66:69]
	s_barrier
	s_setprio 0
	s_add_i32 s48, s37, s25
	v_lshl_add_u64 v[240:241], s[16:17], 0, v[172:173]
	s_mov_b32 m0, s48
	ds_read_b128 v[162:165], v219 offset:16384
	ds_read_b128 v[166:169], v219 offset:17408
	ds_read_b128 v[202:205], v219 offset:18432
	ds_read_b128 v[220:223], v219 offset:19456
	ds_read_b128 v[224:227], v219 offset:20480
	ds_read_b128 v[228:231], v219 offset:21504
	ds_read_b128 v[232:235], v219 offset:22528
	ds_read_b128 v[236:239], v219 offset:23552
	global_load_lds_dwordx4 v[240:241], off
	s_add_i32 m0, s48, 0x2000
	s_add_u32 s48, s16, 0xb0000
	v_lshl_add_u64 v[242:243], s[16:17], 0, v[176:177]
	s_addc_u32 s49, s17, 0
	s_add_i32 s50, s38, s25
	global_load_lds_dwordx4 v[242:243], off
	v_lshl_add_u64 v[244:245], s[48:49], 0, v[172:173]
	s_mov_b32 m0, s50
	v_lshl_add_u64 v[246:247], s[18:19], 0, v[174:175]
	global_load_lds_dwordx4 v[244:245], off
	v_lshl_add_u64 v[244:245], s[48:49], 0, v[176:177]
	s_add_i32 m0, s50, 0x2000
	s_nop 0
	global_load_lds_dwordx4 v[244:245], off
	v_lshl_add_u64 v[244:245], s[18:19], 0, v[170:171]
	s_mov_b32 m0, s26
	s_nop 0
	global_load_lds_dwordx4 v[244:245], off
	s_mov_b32 m0, s27
	s_nop 0
	global_load_lds_dwordx4 v[246:247], off
	s_waitcnt vmcnt(8)
	s_waitcnt lgkmcnt(0)
	s_setprio 1
	s_barrier
; #define PG8_STAGE(bufoff, gbase, voff) do { _Pragma("unroll") for (int _i = 0; _i < 2; ++_i) \
;         __builtin_amdgcn_global_load_lds((const unsigned*)((const char*)(gbase) + (voff)[_i]), (PG8_LAS unsigned*)(lds + (bufoff) + ldsw + _i * 8192), 16, 0, 0); } while (0)
; #define PG8_LDA(dst, b, h) do { _Pragma("unroll") for (int m = 0; m < 4; ++m) _Pragma("unroll") for (int k = 0; k < 2; ++k) dst[m][k] = *(const PG8_LAS bf16x8*)(lds + PG8_SA(b, h) + aoff + m * 2048 + k * 1024); } while (0)
; #define PG8_LDB(dst, b, h) do { _Pragma("unroll") for (int n = 0; n < 2; ++n) _Pragma("unroll") for (int k = 0; k < 2; ++k) dst[n][k] = *(const PG8_LAS bf16x8*)(lds + PG8_SB(b, h) + boff + n * 2048 + k * 1024); } while (0)
; #define PG8_MMA(ai, bj, At, Bt) do { __builtin_amdgcn_s_setprio(1); _Pragma("unroll") for (int m = 0; m < 4; ++m) _Pragma("unroll") for (int n = 0; n < 2; ++n) _Pragma("unroll") for (int k = 0; k < 2; ++k) \
;         acc[ai][bj][m][n] = __builtin_amdgcn_mfma_f32_16x16x32_bf16(Bt[n][k], At[m][k], acc[ai][bj][m][n], 0, 0, 0); __builtin_amdgcn_s_setprio(0); } while (0)
; #define PG8_WAIT_V(n) asm volatile("s_waitcnt vmcnt(" #n ")" ::: "memory")
; #define PG8_WAIT_L(n) asm volatile("s_waitcnt lgkmcnt(" #n ")" ::: "memory")
; #define PG8_BAR __builtin_amdgcn_s_barrier()
; #define PG8_SCHED __builtin_amdgcn_sched_barrier(0)
;     ...
;             PG8_WAIT_V(8); PG8_WAIT_L(0); PG8_BAR; PG8_MMA(1, 0, At, B0); PG8_MMA(1, 1, At, B1); PG8_BAR; PG8_SCHED;
;             PG8_LDB(B0, 1, 0); PG8_LDB(B1, 1, 1); PG8_SCHED; PG8_LDA(At, 1, 0); PG8_STAGE(PG8_SA(0, 1), a2 + hstep, voffA);
;             PG8_WAIT_V(8); PG8_WAIT_L(0); PG8_BAR; PG8_MMA(0, 0, At, B0); PG8_MMA(0, 1, At, B1); PG8_BAR; PG8_SCHED;
	v_mfma_f32_16x16x32_bf16 v[62:65], v[114:117], v[162:165], v[62:65]
	v_mfma_f32_16x16x32_bf16 v[58:61], v[122:125], v[162:165], v[58:61]
	v_mfma_f32_16x16x32_bf16 v[50:53], v[114:117], v[202:205], v[50:53]
	v_mfma_f32_16x16x32_bf16 v[42:45], v[122:125], v[202:205], v[42:45]
	v_mfma_f32_16x16x32_bf16 v[34:37], v[114:117], v[224:227], v[34:37]
	v_mfma_f32_16x16x32_bf16 v[26:29], v[122:125], v[224:227], v[26:29]
	v_mfma_f32_16x16x32_bf16 v[18:21], v[114:117], v[232:235], v[18:21]
	v_mfma_f32_16x16x32_bf16 v[10:13], v[122:125], v[232:235], v[10:13]
	v_mfma_f32_16x16x32_bf16 v[62:65], v[118:121], v[166:169], v[62:65]
	v_mfma_f32_16x16x32_bf16 v[58:61], v[126:129], v[166:169], v[58:61]
	v_mfma_f32_16x16x32_bf16 v[50:53], v[118:121], v[220:223], v[50:53]
	v_mfma_f32_16x16x32_bf16 v[42:45], v[126:129], v[220:223], v[42:45]
	v_mfma_f32_16x16x32_bf16 v[34:37], v[118:121], v[228:231], v[34:37]
	v_mfma_f32_16x16x32_bf16 v[26:29], v[126:129], v[228:231], v[26:29]
	v_mfma_f32_16x16x32_bf16 v[18:21], v[118:121], v[236:239], v[18:21]
	v_mfma_f32_16x16x32_bf16 v[10:13], v[126:129], v[236:239], v[10:13]
	s_setprio 0
	s_setprio 1
	v_mfma_f32_16x16x32_bf16 v[54:57], v[146:149], v[162:165], v[54:57]
	v_mfma_f32_16x16x32_bf16 v[46:49], v[154:157], v[162:165], v[46:49]
	v_mfma_f32_16x16x32_bf16 v[38:41], v[146:149], v[202:205], v[38:41]
	v_mfma_f32_16x16x32_bf16 v[30:33], v[154:157], v[202:205], v[30:33]
	v_mfma_f32_16x16x32_bf16 v[22:25], v[146:149], v[224:227], v[22:25]
	v_mfma_f32_16x16x32_bf16 v[14:17], v[154:157], v[224:227], v[14:17]
	v_mfma_f32_16x16x32_bf16 v[6:9], v[146:149], v[232:235], v[6:9]
	v_mfma_f32_16x16x32_bf16 v[2:5], v[154:157], v[232:235], v[2:5]
	v_mfma_f32_16x16x32_bf16 v[54:57], v[150:153], v[166:169], v[54:57]
	v_mfma_f32_16x16x32_bf16 v[46:49], v[158:161], v[166:169], v[46:49]
	v_mfma_f32_16x16x32_bf16 v[38:41], v[150:153], v[220:223], v[38:41]
	v_mfma_f32_16x16x32_bf16 v[30:33], v[158:161], v[220:223], v[30:33]
	v_mfma_f32_16x16x32_bf16 v[22:25], v[150:153], v[228:231], v[22:25]
	v_mfma_f32_16x16x32_bf16 v[14:17], v[158:161], v[228:231], v[14:17]
	v_mfma_f32_16x16x32_bf16 v[6:9], v[150:153], v[236:239], v[6:9]
	v_mfma_f32_16x16x32_bf16 v[2:5], v[158:161], v[236:239], v[2:5]
	s_barrier
	s_setprio 0
	s_add_i32 s48, 0, 0x18000
	s_add_i32 s49, 0, 0x1c000
	v_add_u32_e32 v126, s48, v215
	v_add_u32_e32 v158, s49, v215
	ds_read_b128 v[114:117], v126
	ds_read_b128 v[118:121], v126 offset:1024
	ds_read_b128 v[122:125], v126 offset:2048
	ds_read_b128 v[126:129], v126 offset:3072
	ds_read_b128 v[146:149], v158
	ds_read_b128 v[150:153], v158 offset:1024
	ds_read_b128 v[154:157], v158 offset:2048
	ds_read_b128 v[158:161], v158 offset:3072
	s_add_u32 s18, s18, 0xb0000
	s_addc_u32 s19, s19, 0
	s_mov_b32 m0, s28
	v_lshl_add_u64 v[248:249], s[18:19], 0, v[170:171]
	ds_read_b128 v[162:165], v219 offset:32768
	ds_read_b128 v[166:169], v219 offset:33792
	ds_read_b128 v[202:205], v219 offset:34816
	ds_read_b128 v[220:223], v219 offset:35840
	ds_read_b128 v[224:227], v219 offset:36864
	ds_read_b128 v[228:231], v219 offset:37888
	ds_read_b128 v[232:235], v219 offset:38912
	ds_read_b128 v[236:239], v219 offset:39936
	global_load_lds_dwordx4 v[248:249], off
	v_lshl_add_u64 v[248:249], s[18:19], 0, v[174:175]
	s_mov_b32 m0, s29
	s_nop 0
	global_load_lds_dwordx4 v[248:249], off
	s_waitcnt vmcnt(8)
	s_waitcnt lgkmcnt(0)
	s_setprio 1
	s_barrier
	v_mfma_f32_16x16x32_bf16 v[142:145], v[114:117], v[162:165], v[142:145]
	v_mfma_f32_16x16x32_bf16 v[138:141], v[122:125], v[162:165], v[138:141]
	v_mfma_f32_16x16x32_bf16 v[110:113], v[114:117], v[202:205], v[110:113]
	v_mfma_f32_16x16x32_bf16 v[106:109], v[122:125], v[202:205], v[106:109]
	v_mfma_f32_16x16x32_bf16 v[98:101], v[114:117], v[224:227], v[98:101]
	v_mfma_f32_16x16x32_bf16 v[90:93], v[122:125], v[224:227], v[90:93]
	v_mfma_f32_16x16x32_bf16 v[82:85], v[114:117], v[232:235], v[82:85]
	v_mfma_f32_16x16x32_bf16 v[74:77], v[122:125], v[232:235], v[74:77]
	v_mfma_f32_16x16x32_bf16 v[142:145], v[118:121], v[166:169], v[142:145]
	v_mfma_f32_16x16x32_bf16 v[138:141], v[126:129], v[166:169], v[138:141]
	v_mfma_f32_16x16x32_bf16 v[110:113], v[118:121], v[220:223], v[110:113]
	v_mfma_f32_16x16x32_bf16 v[106:109], v[126:129], v[220:223], v[106:109]
	v_mfma_f32_16x16x32_bf16 v[98:101], v[118:121], v[228:231], v[98:101]
	v_mfma_f32_16x16x32_bf16 v[90:93], v[126:129], v[228:231], v[90:93]
	v_mfma_f32_16x16x32_bf16 v[82:85], v[118:121], v[236:239], v[82:85]
	v_mfma_f32_16x16x32_bf16 v[74:77], v[126:129], v[236:239], v[74:77]
	s_setprio 0
	s_setprio 1
	v_mfma_f32_16x16x32_bf16 v[134:137], v[146:149], v[162:165], v[134:137]
	v_mfma_f32_16x16x32_bf16 v[130:133], v[154:157], v[162:165], v[130:133]
	v_mfma_f32_16x16x32_bf16 v[102:105], v[146:149], v[202:205], v[102:105]
	v_mfma_f32_16x16x32_bf16 v[94:97], v[154:157], v[202:205], v[94:97]
	v_mfma_f32_16x16x32_bf16 v[86:89], v[146:149], v[224:227], v[86:89]
	v_mfma_f32_16x16x32_bf16 v[78:81], v[154:157], v[224:227], v[78:81]
	v_mfma_f32_16x16x32_bf16 v[70:73], v[146:149], v[232:235], v[70:73]
	v_mfma_f32_16x16x32_bf16 v[66:69], v[154:157], v[232:235], v[66:69]
	v_mfma_f32_16x16x32_bf16 v[134:137], v[150:153], v[166:169], v[134:137]
	v_mfma_f32_16x16x32_bf16 v[130:133], v[158:161], v[166:169], v[130:133]
	v_mfma_f32_16x16x32_bf16 v[102:105], v[150:153], v[220:223], v[102:105]
	v_mfma_f32_16x16x32_bf16 v[94:97], v[158:161], v[220:223], v[94:97]
	v_mfma_f32_16x16x32_bf16 v[86:89], v[150:153], v[228:231], v[86:89]
	v_mfma_f32_16x16x32_bf16 v[78:81], v[158:161], v[228:231], v[78:81]
	v_mfma_f32_16x16x32_bf16 v[70:73], v[150:153], v[236:239], v[70:73]
	v_mfma_f32_16x16x32_bf16 v[66:69], v[158:161], v[236:239], v[66:69]
	s_barrier
; #define PG8_STAGE(bufoff, gbase, voff) do { _Pragma("unroll") for (int _i = 0; _i < 2; ++_i) \
;         __builtin_amdgcn_global_load_lds((const unsigned*)((const char*)(gbase) + (voff)[_i]), (PG8_LAS unsigned*)(lds + (bufoff) + ldsw + _i * 8192), 16, 0, 0); } while (0)
; #define PG8_LDA(dst, b, h) do { _Pragma("unroll") for (int m = 0; m < 4; ++m) _Pragma("unroll") for (int k = 0; k < 2; ++k) dst[m][k] = *(const PG8_LAS bf16x8*)(lds + PG8_SA(b, h) + aoff + m * 2048 + k * 1024); } while (0)
; #define PG8_MMA(ai, bj, At, Bt) do { __builtin_amdgcn_s_setprio(1); _Pragma("unroll") for (int m = 0; m < 4; ++m) _Pragma("unroll") for (int n = 0; n < 2; ++n) _Pragma("unroll") for (int k = 0; k < 2; ++k) \
;         acc[ai][bj][m][n] = __builtin_amdgcn_mfma_f32_16x16x32_bf16(Bt[n][k], At[m][k], acc[ai][bj][m][n], 0, 0, 0); __builtin_amdgcn_s_setprio(0); } while (0)
; #define PG8_WAIT_V(n) asm volatile("s_waitcnt vmcnt(" #n ")" ::: "memory")
; #define PG8_WAIT_L(n) asm volatile("s_waitcnt lgkmcnt(" #n ")" ::: "memory")
; #define PG8_BAR __builtin_amdgcn_s_barrier()
; #define PG8_SCHED __builtin_amdgcn_sched_barrier(0)
;     ...
;             PG8_LDA(At, 1, 1); PG8_STAGE(PG8_SB(1, 0), b3, voffB); PG8_STAGE(PG8_SB(1, 1), b3 + hstep, voffB); PG8_STAGE(PG8_SA(1, 0), a3, voffA);
;             PG8_WAIT_V(8); PG8_WAIT_L(0); PG8_BAR; PG8_MMA(1, 0, At, B0); PG8_MMA(1, 1, At, B1); PG8_BAR; PG8_SCHED;
;         }
;         if constexpr (ALIGN_EPI) { if (wr == 0) PG8_BAR; }
;         E(acc, cur, wr, wc, fr, fq); S.done(cur);
;         if (!has_next) break;
	s_setprio 0
	s_add_i32 s18, s48, s25
	v_lshl_add_u64 v[240:241], v[240:241], 0, s[2:3]
	s_mov_b32 m0, s18
	ds_read_b128 v[162:165], v219 offset:49152
	ds_read_b128 v[166:169], v219 offset:50176
	ds_read_b128 v[202:205], v219 offset:51200
	ds_read_b128 v[220:223], v219 offset:52224
	ds_read_b128 v[224:227], v219 offset:53248
	ds_read_b128 v[228:231], v219 offset:54272
	ds_read_b128 v[232:235], v219 offset:55296
	ds_read_b128 v[236:239], v219 offset:56320
	global_load_lds_dwordx4 v[240:241], off
	s_add_i32 m0, s18, 0x2000
	s_add_u32 s16, s16, 0xb0080
	v_lshl_add_u64 v[240:241], v[242:243], 0, s[2:3]
	s_addc_u32 s17, s17, 0
	s_add_i32 s18, s49, s25
	global_load_lds_dwordx4 v[240:241], off
	v_lshl_add_u64 v[240:241], s[16:17], 0, v[172:173]
	s_mov_b32 m0, s18
	s_nop 0
	global_load_lds_dwordx4 v[240:241], off
	v_lshl_add_u64 v[240:241], s[16:17], 0, v[176:177]
	s_add_i32 m0, s18, 0x2000
	s_nop 0
	global_load_lds_dwordx4 v[240:241], off
	v_lshl_add_u64 v[240:241], v[244:245], 0, s[2:3]
	s_mov_b32 m0, s34
	s_nop 0
	global_load_lds_dwordx4 v[240:241], off
	v_lshl_add_u64 v[240:241], v[246:247], 0, s[2:3]
	s_mov_b32 m0, s35
	s_nop 0
	global_load_lds_dwordx4 v[240:241], off
	s_waitcnt vmcnt(8)
	s_waitcnt lgkmcnt(0)
	s_setprio 1
	s_barrier
	v_mfma_f32_16x16x32_bf16 v[62:65], v[114:117], v[162:165], v[62:65]
	v_mfma_f32_16x16x32_bf16 v[58:61], v[122:125], v[162:165], v[58:61]
	v_mfma_f32_16x16x32_bf16 v[50:53], v[114:117], v[202:205], v[50:53]
	v_mfma_f32_16x16x32_bf16 v[42:45], v[122:125], v[202:205], v[42:45]
	v_mfma_f32_16x16x32_bf16 v[34:37], v[114:117], v[224:227], v[34:37]
	v_mfma_f32_16x16x32_bf16 v[26:29], v[122:125], v[224:227], v[26:29]
	v_mfma_f32_16x16x32_bf16 v[18:21], v[114:117], v[232:235], v[18:21]
	v_mfma_f32_16x16x32_bf16 v[10:13], v[122:125], v[232:235], v[10:13]
	v_mfma_f32_16x16x32_bf16 v[62:65], v[118:121], v[166:169], v[62:65]
	v_mfma_f32_16x16x32_bf16 v[58:61], v[126:129], v[166:169], v[58:61]
	v_mfma_f32_16x16x32_bf16 v[50:53], v[118:121], v[220:223], v[50:53]
	v_mfma_f32_16x16x32_bf16 v[42:45], v[126:129], v[220:223], v[42:45]
	v_mfma_f32_16x16x32_bf16 v[34:37], v[118:121], v[228:231], v[34:37]
	v_mfma_f32_16x16x32_bf16 v[26:29], v[126:129], v[228:231], v[26:29]
	v_mfma_f32_16x16x32_bf16 v[18:21], v[118:121], v[236:239], v[18:21]
	v_mfma_f32_16x16x32_bf16 v[10:13], v[126:129], v[236:239], v[10:13]
	s_setprio 0
	s_setprio 1
	v_mfma_f32_16x16x32_bf16 v[54:57], v[146:149], v[162:165], v[54:57]
	v_mfma_f32_16x16x32_bf16 v[46:49], v[154:157], v[162:165], v[46:49]
	v_mfma_f32_16x16x32_bf16 v[38:41], v[146:149], v[202:205], v[38:41]
	v_mfma_f32_16x16x32_bf16 v[30:33], v[154:157], v[202:205], v[30:33]
	v_mfma_f32_16x16x32_bf16 v[22:25], v[146:149], v[224:227], v[22:25]
	v_mfma_f32_16x16x32_bf16 v[14:17], v[154:157], v[224:227], v[14:17]
	v_mfma_f32_16x16x32_bf16 v[6:9], v[146:149], v[232:235], v[6:9]
	v_mfma_f32_16x16x32_bf16 v[2:5], v[154:157], v[232:235], v[2:5]
	v_mfma_f32_16x16x32_bf16 v[54:57], v[150:153], v[166:169], v[54:57]
	v_mfma_f32_16x16x32_bf16 v[46:49], v[158:161], v[166:169], v[46:49]
	v_mfma_f32_16x16x32_bf16 v[38:41], v[150:153], v[220:223], v[38:41]
	v_mfma_f32_16x16x32_bf16 v[30:33], v[158:161], v[220:223], v[30:33]
	v_mfma_f32_16x16x32_bf16 v[22:25], v[150:153], v[228:231], v[22:25]
	v_mfma_f32_16x16x32_bf16 v[14:17], v[158:161], v[228:231], v[14:17]
	v_mfma_f32_16x16x32_bf16 v[6:9], v[150:153], v[236:239], v[6:9]
	v_mfma_f32_16x16x32_bf16 v[2:5], v[158:161], v[236:239], v[2:5]
	s_barrier
	s_setprio 0
	s_add_i32 s47, s47, 2
	s_add_u32 s14, s14, 0x100
	s_addc_u32 s15, s15, 0
	s_add_u32 s13, s13, 0x100
	s_addc_u32 s46, s46, 0
	s_cmp_gt_u32 s47, 41
	s_cbranch_scc0 .LBB0_1089
	s_and_b64 vcc, exec, s[8:9]
	s_cbranch_vccz .LBB0_1092
	s_barrier

; #define PG8_STAGE(bufoff, gbase, voff) do { _Pragma("unroll") for (int _i = 0; _i < 2; ++_i) \
;         __builtin_amdgcn_global_load_lds((const unsigned*)((const char*)(gbase) + (voff)[_i]), (PG8_LAS unsigned*)(lds + (bufoff) + ldsw + _i * 8192), 16, 0, 0); } while (0)
; #define PG8_LDA(dst, b, h) do { _Pragma("unroll") for (int m = 0; m < 4; ++m) _Pragma("unroll") for (int k = 0; k < 2; ++k) dst[m][k] = *(const PG8_LAS bf16x8*)(lds + PG8_SA(b, h) + aoff + m * 2048 + k * 1024); } while (0)
; #define PG8_LDB(dst, b, h) do { _Pragma("unroll") for (int n = 0; n < 2; ++n) _Pragma("unroll") for (int k = 0; k < 2; ++k) dst[n][k] = *(const PG8_LAS bf16x8*)(lds + PG8_SB(b, h) + boff + n * 2048 + k * 1024); } while (0)
; #define PG8_MMA(ai, bj, At, Bt) do { __builtin_amdgcn_s_setprio(1); _Pragma("unroll") for (int m = 0; m < 4; ++m) _Pragma("unroll") for (int n = 0; n < 2; ++n) _Pragma("unroll") for (int k = 0; k < 2; ++k) \
;         acc[ai][bj][m][n] = __builtin_amdgcn_mfma_f32_16x16x32_bf16(Bt[n][k], At[m][k], acc[ai][bj][m][n], 0, 0, 0); __builtin_amdgcn_s_setprio(0); } while (0)
; #define PG8_WAIT_V(n) asm volatile("s_waitcnt vmcnt(" #n ")" ::: "memory")
; #define PG8_WAIT_L(n) asm volatile("s_waitcnt lgkmcnt(" #n ")" ::: "memory")
; #define PG8_BAR __builtin_amdgcn_s_barrier()
; #define PG8_SCHED __builtin_amdgcn_sched_barrier(0)
;     ...
;         for (int t = 0; t < nt; t += 2) {
;             const bool last = (t == nt - 2);
;             const char* a1 = cA + (size_t)(t + 1) * kstep;
;             const char* a2 = last ? nA : cA + (size_t)(t + 2) * kstep; const char* b2 = last ? nB : cB + (size_t)(t + 2) * kstep;
;             const char* a3 = a2 + kstep; const char* b3 = b2 + kstep;
;             if (last && has_next) S.a_ready(nxt);
;             PG8_LDB(B0, 0, 0); PG8_LDB(B1, 0, 1); PG8_SCHED; PG8_LDA(At, 0, 0); PG8_STAGE(PG8_SA(1, 1), a1 + hstep, voffA);
;             PG8_WAIT_V(8); PG8_WAIT_L(0); PG8_BAR; PG8_MMA(0, 0, At, B0); PG8_MMA(0, 1, At, B1); PG8_BAR; PG8_SCHED;
;             PG8_LDA(At, 0, 1); PG8_STAGE(PG8_SB(0, 0), b2, voffB); PG8_STAGE(PG8_SB(0, 1), b2 + hstep, voffB); PG8_STAGE(PG8_SA(0, 0), a2, voffA);
.LBB0_1117:
	ds_read_b128 v[130:133], v163
	ds_read_b128 v[134:137], v163 offset:1024
	ds_read_b128 v[138:141], v163 offset:2048
	ds_read_b128 v[142:145], v163 offset:3072
	ds_read_b128 v[154:157], v164
	ds_read_b128 v[166:169], v164 offset:1024
	ds_read_b128 v[178:181], v164 offset:2048
	ds_read_b128 v[182:185], v164 offset:3072
	s_add_u32 s16, s14, 0xfff50080
	s_addc_u32 s17, s15, -1
	s_cmp_eq_u32 s48, 18
	s_cselect_b32 s19, s7, s17
	s_cselect_b32 s18, s6, s16
	s_cselect_b32 s17, s13, s47
	s_cselect_b32 s16, s12, s0
	v_lshl_add_u64 v[158:159], s[14:15], 0, v[146:147]
	s_add_i32 m0, s26, 0xc000
	ds_read_b128 v[186:189], v165
	ds_read_b128 v[190:193], v165 offset:1024
	ds_read_b128 v[194:197], v165 offset:2048
	ds_read_b128 v[198:201], v165 offset:3072
	ds_read_b128 v[202:205], v165 offset:4096
	ds_read_b128 v[210:213], v165 offset:5120
	ds_read_b128 v[214:217], v165 offset:6144
	ds_read_b128 v[218:221], v165 offset:7168
	global_load_lds_dwordx4 v[158:159], off
	v_lshl_add_u64 v[158:159], s[14:15], 0, v[148:149]
	s_add_i32 m0, s26, 0xe000
	s_nop 0
	global_load_lds_dwordx4 v[158:159], off
	s_waitcnt vmcnt(8)
	s_waitcnt lgkmcnt(0)
	s_setprio 1
	s_barrier
	v_mfma_f32_16x16x32_bf16 v[126:129], v[130:133], v[186:189], v[126:129]
	v_mfma_f32_16x16x32_bf16 v[122:125], v[138:141], v[186:189], v[122:125]
	v_mfma_f32_16x16x32_bf16 v[118:121], v[130:133], v[194:197], v[118:121]
	v_mfma_f32_16x16x32_bf16 v[114:117], v[138:141], v[194:197], v[114:117]
	v_mfma_f32_16x16x32_bf16 v[110:113], v[130:133], v[202:205], v[110:113]
	v_mfma_f32_16x16x32_bf16 v[102:105], v[138:141], v[202:205], v[102:105]
	v_mfma_f32_16x16x32_bf16 v[78:81], v[130:133], v[214:217], v[78:81]
	v_mfma_f32_16x16x32_bf16 v[74:77], v[138:141], v[214:217], v[74:77]
	v_mfma_f32_16x16x32_bf16 v[126:129], v[134:137], v[190:193], v[126:129]
	v_mfma_f32_16x16x32_bf16 v[122:125], v[142:145], v[190:193], v[122:125]
	v_mfma_f32_16x16x32_bf16 v[118:121], v[134:137], v[198:201], v[118:121]
	v_mfma_f32_16x16x32_bf16 v[114:117], v[142:145], v[198:201], v[114:117]
	v_mfma_f32_16x16x32_bf16 v[110:113], v[134:137], v[210:213], v[110:113]
	v_mfma_f32_16x16x32_bf16 v[102:105], v[142:145], v[210:213], v[102:105]
	v_mfma_f32_16x16x32_bf16 v[78:81], v[134:137], v[218:221], v[78:81]
	v_mfma_f32_16x16x32_bf16 v[74:77], v[142:145], v[218:221], v[74:77]
	s_setprio 0
	s_setprio 1
	v_mfma_f32_16x16x32_bf16 v[106:109], v[154:157], v[186:189], v[106:109]
	v_mfma_f32_16x16x32_bf16 v[98:101], v[178:181], v[186:189], v[98:101]
	v_mfma_f32_16x16x32_bf16 v[94:97], v[154:157], v[194:197], v[94:97]
	v_mfma_f32_16x16x32_bf16 v[90:93], v[178:181], v[194:197], v[90:93]
	v_mfma_f32_16x16x32_bf16 v[86:89], v[154:157], v[202:205], v[86:89]
	v_mfma_f32_16x16x32_bf16 v[82:85], v[178:181], v[202:205], v[82:85]
	v_mfma_f32_16x16x32_bf16 v[70:73], v[154:157], v[214:217], v[70:73]
	v_mfma_f32_16x16x32_bf16 v[66:69], v[178:181], v[214:217], v[66:69]
	v_mfma_f32_16x16x32_bf16 v[106:109], v[166:169], v[190:193], v[106:109]
	v_mfma_f32_16x16x32_bf16 v[98:101], v[182:185], v[190:193], v[98:101]
	v_mfma_f32_16x16x32_bf16 v[94:97], v[166:169], v[198:201], v[94:97]
	v_mfma_f32_16x16x32_bf16 v[90:93], v[182:185], v[198:201], v[90:93]
	v_mfma_f32_16x16x32_bf16 v[86:89], v[166:169], v[210:213], v[86:89]
	v_mfma_f32_16x16x32_bf16 v[82:85], v[182:185], v[210:213], v[82:85]
	v_mfma_f32_16x16x32_bf16 v[70:73], v[166:169], v[218:221], v[70:73]
	v_mfma_f32_16x16x32_bf16 v[66:69], v[182:185], v[218:221], v[66:69]
	s_barrier
	s_setprio 0
	s_add_i32 s49, s36, s25
	v_lshl_add_u64 v[158:159], s[16:17], 0, v[172:173]
	s_mov_b32 m0, s49
	ds_read_b128 v[186:189], v165 offset:16384
	ds_read_b128 v[190:193], v165 offset:17408
	ds_read_b128 v[194:197], v165 offset:18432
	ds_read_b128 v[198:201], v165 offset:19456
	ds_read_b128 v[202:205], v165 offset:20480
	ds_read_b128 v[210:213], v165 offset:21504
	ds_read_b128 v[214:217], v165 offset:22528
	ds_read_b128 v[218:221], v165 offset:23552
	global_load_lds_dwordx4 v[158:159], off
	s_add_i32 m0, s49, 0x2000
	s_add_u32 s50, s16, 0xb0000
	v_lshl_add_u64 v[206:207], s[16:17], 0, v[176:177]
	s_addc_u32 s51, s17, 0
	s_add_i32 s49, s37, s25
	global_load_lds_dwordx4 v[206:207], off
	v_lshl_add_u64 v[222:223], s[50:51], 0, v[172:173]
	s_mov_b32 m0, s49
	v_lshl_add_u64 v[224:225], s[18:19], 0, v[174:175]
	global_load_lds_dwordx4 v[222:223], off
	v_lshl_add_u64 v[222:223], s[50:51], 0, v[176:177]
	s_add_i32 m0, s49, 0x2000
	s_nop 0
	global_load_lds_dwordx4 v[222:223], off
	v_lshl_add_u64 v[222:223], s[18:19], 0, v[170:171]
	s_mov_b32 m0, s26
	s_nop 0
	global_load_lds_dwordx4 v[222:223], off
	s_mov_b32 m0, s27
	s_nop 0
	global_load_lds_dwordx4 v[224:225], off
	s_waitcnt vmcnt(8)
	s_waitcnt lgkmcnt(0)
	s_setprio 1
	s_barrier
; #define PG8_STAGE(bufoff, gbase, voff) do { _Pragma("unroll") for (int _i = 0; _i < 2; ++_i) \
;         __builtin_amdgcn_global_load_lds((const unsigned*)((const char*)(gbase) + (voff)[_i]), (PG8_LAS unsigned*)(lds + (bufoff) + ldsw + _i * 8192), 16, 0, 0); } while (0)
; #define PG8_LDA(dst, b, h) do { _Pragma("unroll") for (int m = 0; m < 4; ++m) _Pragma("unroll") for (int k = 0; k < 2; ++k) dst[m][k] = *(const PG8_LAS bf16x8*)(lds + PG8_SA(b, h) + aoff + m * 2048 + k * 1024); } while (0)
; #define PG8_LDB(dst, b, h) do { _Pragma("unroll") for (int n = 0; n < 2; ++n) _Pragma("unroll") for (int k = 0; k < 2; ++k) dst[n][k] = *(const PG8_LAS bf16x8*)(lds + PG8_SB(b, h) + boff + n * 2048 + k * 1024); } while (0)
; #define PG8_MMA(ai, bj, At, Bt) do { __builtin_amdgcn_s_setprio(1); _Pragma("unroll") for (int m = 0; m < 4; ++m) _Pragma("unroll") for (int n = 0; n < 2; ++n) _Pragma("unroll") for (int k = 0; k < 2; ++k) \
;         acc[ai][bj][m][n] = __builtin_amdgcn_mfma_f32_16x16x32_bf16(Bt[n][k], At[m][k], acc[ai][bj][m][n], 0, 0, 0); __builtin_amdgcn_s_setprio(0); } while (0)
; #define PG8_WAIT_V(n) asm volatile("s_waitcnt vmcnt(" #n ")" ::: "memory")
; #define PG8_WAIT_L(n) asm volatile("s_waitcnt lgkmcnt(" #n ")" ::: "memory")
; #define PG8_BAR __builtin_amdgcn_s_barrier()
; #define PG8_SCHED __builtin_amdgcn_sched_barrier(0)
;     ...
;             PG8_WAIT_V(8); PG8_WAIT_L(0); PG8_BAR; PG8_MMA(1, 0, At, B0); PG8_MMA(1, 1, At, B1); PG8_BAR; PG8_SCHED;
;             PG8_LDB(B0, 1, 0); PG8_LDB(B1, 1, 1); PG8_SCHED; PG8_LDA(At, 1, 0); PG8_STAGE(PG8_SA(0, 1), a2 + hstep, voffA);
;             PG8_WAIT_V(8); PG8_WAIT_L(0); PG8_BAR; PG8_MMA(0, 0, At, B0); PG8_MMA(0, 1, At, B1); PG8_BAR; PG8_SCHED;
	v_mfma_f32_16x16x32_bf16 v[62:65], v[130:133], v[186:189], v[62:65]
	v_mfma_f32_16x16x32_bf16 v[58:61], v[138:141], v[186:189], v[58:61]
	v_mfma_f32_16x16x32_bf16 v[54:57], v[130:133], v[194:197], v[54:57]
	v_mfma_f32_16x16x32_bf16 v[46:49], v[138:141], v[194:197], v[46:49]
	v_mfma_f32_16x16x32_bf16 v[38:41], v[130:133], v[202:205], v[38:41]
	v_mfma_f32_16x16x32_bf16 v[30:33], v[138:141], v[202:205], v[30:33]
	v_mfma_f32_16x16x32_bf16 v[22:25], v[130:133], v[214:217], v[22:25]
	v_mfma_f32_16x16x32_bf16 v[14:17], v[138:141], v[214:217], v[14:17]
	v_mfma_f32_16x16x32_bf16 v[62:65], v[134:137], v[190:193], v[62:65]
	v_mfma_f32_16x16x32_bf16 v[58:61], v[142:145], v[190:193], v[58:61]
	v_mfma_f32_16x16x32_bf16 v[54:57], v[134:137], v[198:201], v[54:57]
	v_mfma_f32_16x16x32_bf16 v[46:49], v[142:145], v[198:201], v[46:49]
	v_mfma_f32_16x16x32_bf16 v[38:41], v[134:137], v[210:213], v[38:41]
	v_mfma_f32_16x16x32_bf16 v[30:33], v[142:145], v[210:213], v[30:33]
	v_mfma_f32_16x16x32_bf16 v[22:25], v[134:137], v[218:221], v[22:25]
	v_mfma_f32_16x16x32_bf16 v[14:17], v[142:145], v[218:221], v[14:17]
	s_setprio 0
	s_setprio 1
	v_mfma_f32_16x16x32_bf16 v[50:53], v[154:157], v[186:189], v[50:53]
	v_mfma_f32_16x16x32_bf16 v[42:45], v[178:181], v[186:189], v[42:45]
	v_mfma_f32_16x16x32_bf16 v[34:37], v[154:157], v[194:197], v[34:37]
	v_mfma_f32_16x16x32_bf16 v[26:29], v[178:181], v[194:197], v[26:29]
	v_mfma_f32_16x16x32_bf16 v[18:21], v[154:157], v[202:205], v[18:21]
	v_mfma_f32_16x16x32_bf16 v[10:13], v[178:181], v[202:205], v[10:13]
	v_mfma_f32_16x16x32_bf16 v[6:9], v[154:157], v[214:217], v[6:9]
	v_mfma_f32_16x16x32_bf16 v[2:5], v[178:181], v[214:217], v[2:5]
	v_mfma_f32_16x16x32_bf16 v[50:53], v[166:169], v[190:193], v[50:53]
	v_mfma_f32_16x16x32_bf16 v[42:45], v[182:185], v[190:193], v[42:45]
	v_mfma_f32_16x16x32_bf16 v[34:37], v[166:169], v[198:201], v[34:37]
	v_mfma_f32_16x16x32_bf16 v[26:29], v[182:185], v[198:201], v[26:29]
	v_mfma_f32_16x16x32_bf16 v[18:21], v[166:169], v[210:213], v[18:21]
	v_mfma_f32_16x16x32_bf16 v[10:13], v[182:185], v[210:213], v[10:13]
	v_mfma_f32_16x16x32_bf16 v[6:9], v[166:169], v[218:221], v[6:9]
	v_mfma_f32_16x16x32_bf16 v[2:5], v[182:185], v[218:221], v[2:5]
	s_barrier
	s_setprio 0
	s_add_i32 s49, 0, 0x18000
	s_add_i32 s50, 0, 0x1c000
	v_add_u32_e32 v142, s49, v161
	v_add_u32_e32 v182, s50, v161
	ds_read_b128 v[130:133], v142
	ds_read_b128 v[134:137], v142 offset:1024
	ds_read_b128 v[138:141], v142 offset:2048
	ds_read_b128 v[142:145], v142 offset:3072
	ds_read_b128 v[154:157], v182
	ds_read_b128 v[166:169], v182 offset:1024
	ds_read_b128 v[178:181], v182 offset:2048
	ds_read_b128 v[182:185], v182 offset:3072
	s_add_u32 s18, s18, 0xb0000
	s_addc_u32 s19, s19, 0
	s_mov_b32 m0, s28
	v_lshl_add_u64 v[226:227], s[18:19], 0, v[170:171]
	ds_read_b128 v[186:189], v165 offset:32768
	ds_read_b128 v[190:193], v165 offset:33792
	ds_read_b128 v[194:197], v165 offset:34816
	ds_read_b128 v[198:201], v165 offset:35840
	ds_read_b128 v[202:205], v165 offset:36864
	ds_read_b128 v[210:213], v165 offset:37888
	ds_read_b128 v[214:217], v165 offset:38912
	ds_read_b128 v[218:221], v165 offset:39936
	global_load_lds_dwordx4 v[226:227], off
	v_lshl_add_u64 v[226:227], s[18:19], 0, v[174:175]
	s_mov_b32 m0, s29
	s_nop 0
	global_load_lds_dwordx4 v[226:227], off
	s_waitcnt vmcnt(8)
	s_waitcnt lgkmcnt(0)
	s_setprio 1
	s_barrier
	v_mfma_f32_16x16x32_bf16 v[126:129], v[130:133], v[186:189], v[126:129]
	v_mfma_f32_16x16x32_bf16 v[122:125], v[138:141], v[186:189], v[122:125]
	v_mfma_f32_16x16x32_bf16 v[118:121], v[130:133], v[194:197], v[118:121]
	v_mfma_f32_16x16x32_bf16 v[114:117], v[138:141], v[194:197], v[114:117]
	v_mfma_f32_16x16x32_bf16 v[110:113], v[130:133], v[202:205], v[110:113]
	v_mfma_f32_16x16x32_bf16 v[102:105], v[138:141], v[202:205], v[102:105]
	v_mfma_f32_16x16x32_bf16 v[78:81], v[130:133], v[214:217], v[78:81]
	v_mfma_f32_16x16x32_bf16 v[74:77], v[138:141], v[214:217], v[74:77]
	v_mfma_f32_16x16x32_bf16 v[126:129], v[134:137], v[190:193], v[126:129]
	v_mfma_f32_16x16x32_bf16 v[122:125], v[142:145], v[190:193], v[122:125]
	v_mfma_f32_16x16x32_bf16 v[118:121], v[134:137], v[198:201], v[118:121]
	v_mfma_f32_16x16x32_bf16 v[114:117], v[142:145], v[198:201], v[114:117]
	v_mfma_f32_16x16x32_bf16 v[110:113], v[134:137], v[210:213], v[110:113]
	v_mfma_f32_16x16x32_bf16 v[102:105], v[142:145], v[210:213], v[102:105]
	v_mfma_f32_16x16x32_bf16 v[78:81], v[134:137], v[218:221], v[78:81]
	v_mfma_f32_16x16x32_bf16 v[74:77], v[142:145], v[218:221], v[74:77]
	s_setprio 0
	s_setprio 1
	v_mfma_f32_16x16x32_bf16 v[106:109], v[154:157], v[186:189], v[106:109]
	v_mfma_f32_16x16x32_bf16 v[98:101], v[178:181], v[186:189], v[98:101]
	v_mfma_f32_16x16x32_bf16 v[94:97], v[154:157], v[194:197], v[94:97]
	v_mfma_f32_16x16x32_bf16 v[90:93], v[178:181], v[194:197], v[90:93]
	v_mfma_f32_16x16x32_bf16 v[86:89], v[154:157], v[202:205], v[86:89]
	v_mfma_f32_16x16x32_bf16 v[82:85], v[178:181], v[202:205], v[82:85]
	v_mfma_f32_16x16x32_bf16 v[70:73], v[154:157], v[214:217], v[70:73]
	v_mfma_f32_16x16x32_bf16 v[66:69], v[178:181], v[214:217], v[66:69]
	v_mfma_f32_16x16x32_bf16 v[106:109], v[166:169], v[190:193], v[106:109]
	v_mfma_f32_16x16x32_bf16 v[98:101], v[182:185], v[190:193], v[98:101]
	v_mfma_f32_16x16x32_bf16 v[94:97], v[166:169], v[198:201], v[94:97]
	v_mfma_f32_16x16x32_bf16 v[90:93], v[182:185], v[198:201], v[90:93]
	v_mfma_f32_16x16x32_bf16 v[86:89], v[166:169], v[210:213], v[86:89]
	v_mfma_f32_16x16x32_bf16 v[82:85], v[182:185], v[210:213], v[82:85]
	v_mfma_f32_16x16x32_bf16 v[70:73], v[166:169], v[218:221], v[70:73]
	v_mfma_f32_16x16x32_bf16 v[66:69], v[182:185], v[218:221], v[66:69]
	s_barrier
; #define PG8_STAGE(bufoff, gbase, voff) do { _Pragma("unroll") for (int _i = 0; _i < 2; ++_i) \
;         __builtin_amdgcn_global_load_lds((const unsigned*)((const char*)(gbase) + (voff)[_i]), (PG8_LAS unsigned*)(lds + (bufoff) + ldsw + _i * 8192), 16, 0, 0); } while (0)
; #define PG8_LDA(dst, b, h) do { _Pragma("unroll") for (int m = 0; m < 4; ++m) _Pragma("unroll") for (int k = 0; k < 2; ++k) dst[m][k] = *(const PG8_LAS bf16x8*)(lds + PG8_SA(b, h) + aoff + m * 2048 + k * 1024); } while (0)
; #define PG8_MMA(ai, bj, At, Bt) do { __builtin_amdgcn_s_setprio(1); _Pragma("unroll") for (int m = 0; m < 4; ++m) _Pragma("unroll") for (int n = 0; n < 2; ++n) _Pragma("unroll") for (int k = 0; k < 2; ++k) \
;         acc[ai][bj][m][n] = __builtin_amdgcn_mfma_f32_16x16x32_bf16(Bt[n][k], At[m][k], acc[ai][bj][m][n], 0, 0, 0); __builtin_amdgcn_s_setprio(0); } while (0)
; #define PG8_WAIT_V(n) asm volatile("s_waitcnt vmcnt(" #n ")" ::: "memory")
; #define PG8_WAIT_L(n) asm volatile("s_waitcnt lgkmcnt(" #n ")" ::: "memory")
; #define PG8_BAR __builtin_amdgcn_s_barrier()
; #define PG8_SCHED __builtin_amdgcn_sched_barrier(0)
;     ...
;             PG8_LDA(At, 1, 1); PG8_STAGE(PG8_SB(1, 0), b3, voffB); PG8_STAGE(PG8_SB(1, 1), b3 + hstep, voffB); PG8_STAGE(PG8_SA(1, 0), a3, voffA);
;             PG8_WAIT_V(8); PG8_WAIT_L(0); PG8_BAR; PG8_MMA(1, 0, At, B0); PG8_MMA(1, 1, At, B1); PG8_BAR; PG8_SCHED;
;         }
;         if constexpr (ALIGN_EPI) { if (wr == 0) PG8_BAR; }
;         E(acc, cur, wr, wc, fr, fq); S.done(cur);
;         if (!has_next) break;
	s_setprio 0
	s_add_i32 s18, s49, s25
	v_lshl_add_u64 v[158:159], v[158:159], 0, s[8:9]
	s_mov_b32 m0, s18
	ds_read_b128 v[186:189], v165 offset:49152
	ds_read_b128 v[190:193], v165 offset:50176
	ds_read_b128 v[194:197], v165 offset:51200
	ds_read_b128 v[198:201], v165 offset:52224
	ds_read_b128 v[202:205], v165 offset:53248
	ds_read_b128 v[210:213], v165 offset:54272
	ds_read_b128 v[214:217], v165 offset:55296
	ds_read_b128 v[218:221], v165 offset:56320
	global_load_lds_dwordx4 v[158:159], off
	s_add_i32 m0, s18, 0x2000
	s_add_u32 s16, s16, 0xb0080
	v_lshl_add_u64 v[158:159], v[206:207], 0, s[8:9]
	s_addc_u32 s17, s17, 0
	s_add_i32 s18, s50, s25
	global_load_lds_dwordx4 v[158:159], off
	v_lshl_add_u64 v[158:159], s[16:17], 0, v[172:173]
	s_mov_b32 m0, s18
	s_nop 0
	global_load_lds_dwordx4 v[158:159], off
	v_lshl_add_u64 v[158:159], s[16:17], 0, v[176:177]
	s_add_i32 m0, s18, 0x2000
	s_nop 0
	global_load_lds_dwordx4 v[158:159], off
	v_lshl_add_u64 v[158:159], v[222:223], 0, s[8:9]
	s_mov_b32 m0, s33
	s_nop 0
	global_load_lds_dwordx4 v[158:159], off
	v_lshl_add_u64 v[158:159], v[224:225], 0, s[8:9]
	s_mov_b32 m0, s34
	s_nop 0
	global_load_lds_dwordx4 v[158:159], off
	s_waitcnt vmcnt(8)
	s_waitcnt lgkmcnt(0)
	s_setprio 1
	s_barrier
	v_mfma_f32_16x16x32_bf16 v[62:65], v[130:133], v[186:189], v[62:65]
	v_mfma_f32_16x16x32_bf16 v[58:61], v[138:141], v[186:189], v[58:61]
	v_mfma_f32_16x16x32_bf16 v[54:57], v[130:133], v[194:197], v[54:57]
	v_mfma_f32_16x16x32_bf16 v[46:49], v[138:141], v[194:197], v[46:49]
	v_mfma_f32_16x16x32_bf16 v[38:41], v[130:133], v[202:205], v[38:41]
	v_mfma_f32_16x16x32_bf16 v[30:33], v[138:141], v[202:205], v[30:33]
	v_mfma_f32_16x16x32_bf16 v[22:25], v[130:133], v[214:217], v[22:25]
	v_mfma_f32_16x16x32_bf16 v[14:17], v[138:141], v[214:217], v[14:17]
	v_mfma_f32_16x16x32_bf16 v[62:65], v[134:137], v[190:193], v[62:65]
	v_mfma_f32_16x16x32_bf16 v[58:61], v[142:145], v[190:193], v[58:61]
	v_mfma_f32_16x16x32_bf16 v[54:57], v[134:137], v[198:201], v[54:57]
	v_mfma_f32_16x16x32_bf16 v[46:49], v[142:145], v[198:201], v[46:49]
	v_mfma_f32_16x16x32_bf16 v[38:41], v[134:137], v[210:213], v[38:41]
	v_mfma_f32_16x16x32_bf16 v[30:33], v[142:145], v[210:213], v[30:33]
	v_mfma_f32_16x16x32_bf16 v[22:25], v[134:137], v[218:221], v[22:25]
	v_mfma_f32_16x16x32_bf16 v[14:17], v[142:145], v[218:221], v[14:17]
	s_setprio 0
	s_setprio 1
	v_mfma_f32_16x16x32_bf16 v[50:53], v[154:157], v[186:189], v[50:53]
	v_mfma_f32_16x16x32_bf16 v[42:45], v[178:181], v[186:189], v[42:45]
	v_mfma_f32_16x16x32_bf16 v[34:37], v[154:157], v[194:197], v[34:37]
	v_mfma_f32_16x16x32_bf16 v[26:29], v[178:181], v[194:197], v[26:29]
	v_mfma_f32_16x16x32_bf16 v[18:21], v[154:157], v[202:205], v[18:21]
	v_mfma_f32_16x16x32_bf16 v[10:13], v[178:181], v[202:205], v[10:13]
	v_mfma_f32_16x16x32_bf16 v[6:9], v[154:157], v[214:217], v[6:9]
	v_mfma_f32_16x16x32_bf16 v[2:5], v[178:181], v[214:217], v[2:5]
	v_mfma_f32_16x16x32_bf16 v[50:53], v[166:169], v[190:193], v[50:53]
	v_mfma_f32_16x16x32_bf16 v[42:45], v[182:185], v[190:193], v[42:45]
	v_mfma_f32_16x16x32_bf16 v[34:37], v[166:169], v[198:201], v[34:37]
	v_mfma_f32_16x16x32_bf16 v[26:29], v[182:185], v[198:201], v[26:29]
	v_mfma_f32_16x16x32_bf16 v[18:21], v[166:169], v[210:213], v[18:21]
	v_mfma_f32_16x16x32_bf16 v[10:13], v[182:185], v[210:213], v[10:13]
	v_mfma_f32_16x16x32_bf16 v[6:9], v[166:169], v[218:221], v[6:9]
	v_mfma_f32_16x16x32_bf16 v[2:5], v[182:185], v[218:221], v[2:5]
	s_barrier
	s_setprio 0
	s_add_i32 s48, s48, 2
	s_add_u32 s14, s14, 0x100
	s_addc_u32 s15, s15, 0
	s_add_u32 s0, s0, 0x100
	s_addc_u32 s47, s47, 0
	s_cmp_gt_u32 s48, 19
	s_cbranch_scc0 .LBB0_1117
	s_and_b64 vcc, exec, s[10:11]
	s_cbranch_vccz .LBB0_1120
	s_barrier

; #define PG8_STAGE(bufoff, gbase, voff) do { _Pragma("unroll") for (int _i = 0; _i < 2; ++_i) \
;         __builtin_amdgcn_global_load_lds((const unsigned*)((const char*)(gbase) + (voff)[_i]), (PG8_LAS unsigned*)(lds + (bufoff) + ldsw + _i * 8192), 16, 0, 0); } while (0)
; #define PG8_LDA(dst, b, h) do { _Pragma("unroll") for (int m = 0; m < 4; ++m) _Pragma("unroll") for (int k = 0; k < 2; ++k) dst[m][k] = *(const PG8_LAS bf16x8*)(lds + PG8_SA(b, h) + aoff + m * 2048 + k * 1024); } while (0)
; #define PG8_LDB(dst, b, h) do { _Pragma("unroll") for (int n = 0; n < 2; ++n) _Pragma("unroll") for (int k = 0; k < 2; ++k) dst[n][k] = *(const PG8_LAS bf16x8*)(lds + PG8_SB(b, h) + boff + n * 2048 + k * 1024); } while (0)
; #define PG8_MMA(ai, bj, At, Bt) do { __builtin_amdgcn_s_setprio(1); _Pragma("unroll") for (int m = 0; m < 4; ++m) _Pragma("unroll") for (int n = 0; n < 2; ++n) _Pragma("unroll") for (int k = 0; k < 2; ++k) \
;         acc[ai][bj][m][n] = __builtin_amdgcn_mfma_f32_16x16x32_bf16(Bt[n][k], At[m][k], acc[ai][bj][m][n], 0, 0, 0); __builtin_amdgcn_s_setprio(0); } while (0)
; #define PG8_WAIT_V(n) asm volatile("s_waitcnt vmcnt(" #n ")" ::: "memory")
; #define PG8_WAIT_L(n) asm volatile("s_waitcnt lgkmcnt(" #n ")" ::: "memory")
; #define PG8_BAR __builtin_amdgcn_s_barrier()
; #define PG8_SCHED __builtin_amdgcn_sched_barrier(0)
;     ...
;         for (int t = 0; t < nt; t += 2) {
;             const bool last = (t == nt - 2);
;             const char* a1 = cA + (size_t)(t + 1) * kstep;
;             const char* a2 = last ? nA : cA + (size_t)(t + 2) * kstep; const char* b2 = last ? nB : cB + (size_t)(t + 2) * kstep;
;             const char* a3 = a2 + kstep; const char* b3 = b2 + kstep;
;             if (last && has_next) S.a_ready(nxt);
;             PG8_LDB(B0, 0, 0); PG8_LDB(B1, 0, 1); PG8_SCHED; PG8_LDA(At, 0, 0); PG8_STAGE(PG8_SA(1, 1), a1 + hstep, voffA);
;             PG8_WAIT_V(8); PG8_WAIT_L(0); PG8_BAR; PG8_MMA(0, 0, At, B0); PG8_MMA(0, 1, At, B1); PG8_BAR; PG8_SCHED;
;             PG8_LDA(At, 0, 1); PG8_STAGE(PG8_SB(0, 0), b2, voffB); PG8_STAGE(PG8_SB(0, 1), b2 + hstep, voffB); PG8_STAGE(PG8_SA(0, 0), a2, voffA);
.LBB0_1303:
	ds_read_b128 v[148:151], v144
	ds_read_b128 v[152:155], v144 offset:1024
	ds_read_b128 v[156:159], v144 offset:2048
	ds_read_b128 v[160:163], v144 offset:3072
	ds_read_b128 v[164:167], v145
	ds_read_b128 v[168:171], v145 offset:1024
	ds_read_b128 v[172:175], v145 offset:2048
	ds_read_b128 v[176:179], v145 offset:3072
	s_add_u32 s24, s22, 0xfffc0080
	s_addc_u32 s25, s23, -1
	s_cmp_eq_u32 s46, 12
	s_cselect_b32 s27, s19, s25
	s_cselect_b32 s26, s18, s24
	s_cselect_b32 s25, s0, s45
	s_cselect_b32 s24, s15, s17
	v_lshl_add_u64 v[214:215], s[22:23], 0, v[138:139]
	s_add_i32 m0, s9, 0xc000
	ds_read_b128 v[180:183], v146
	ds_read_b128 v[184:187], v146 offset:1024
	ds_read_b128 v[188:191], v146 offset:2048
	ds_read_b128 v[192:195], v146 offset:3072
	ds_read_b128 v[196:199], v146 offset:4096
	ds_read_b128 v[200:203], v146 offset:5120
	ds_read_b128 v[204:207], v146 offset:6144
	ds_read_b128 v[210:213], v146 offset:7168
	global_load_lds_dwordx4 v[214:215], off
	v_lshl_add_u64 v[214:215], s[22:23], 0, v[140:141]
	s_add_i32 m0, s9, 0xe000
	s_nop 0
	global_load_lds_dwordx4 v[214:215], off
	s_waitcnt vmcnt(8)
	s_waitcnt lgkmcnt(0)
	s_setprio 1
	s_barrier
	v_mfma_f32_16x16x32_bf16 v[126:129], v[148:151], v[180:183], v[126:129]
	v_mfma_f32_16x16x32_bf16 v[122:125], v[156:159], v[180:183], v[122:125]
	v_mfma_f32_16x16x32_bf16 v[118:121], v[148:151], v[188:191], v[118:121]
	v_mfma_f32_16x16x32_bf16 v[114:117], v[156:159], v[188:191], v[114:117]
	v_mfma_f32_16x16x32_bf16 v[102:105], v[148:151], v[196:199], v[102:105]
	v_mfma_f32_16x16x32_bf16 v[98:101], v[156:159], v[196:199], v[98:101]
	v_mfma_f32_16x16x32_bf16 v[86:89], v[148:151], v[204:207], v[86:89]
	v_mfma_f32_16x16x32_bf16 v[82:85], v[156:159], v[204:207], v[82:85]
	v_mfma_f32_16x16x32_bf16 v[126:129], v[152:155], v[184:187], v[126:129]
	v_mfma_f32_16x16x32_bf16 v[122:125], v[160:163], v[184:187], v[122:125]
	v_mfma_f32_16x16x32_bf16 v[118:121], v[152:155], v[192:195], v[118:121]
	v_mfma_f32_16x16x32_bf16 v[114:117], v[160:163], v[192:195], v[114:117]
	v_mfma_f32_16x16x32_bf16 v[102:105], v[152:155], v[200:203], v[102:105]
	v_mfma_f32_16x16x32_bf16 v[98:101], v[160:163], v[200:203], v[98:101]
	v_mfma_f32_16x16x32_bf16 v[86:89], v[152:155], v[210:213], v[86:89]
	v_mfma_f32_16x16x32_bf16 v[82:85], v[160:163], v[210:213], v[82:85]
	s_setprio 0
	s_setprio 1
	v_mfma_f32_16x16x32_bf16 v[110:113], v[164:167], v[180:183], v[110:113]
	v_mfma_f32_16x16x32_bf16 v[106:109], v[172:175], v[180:183], v[106:109]
	v_mfma_f32_16x16x32_bf16 v[94:97], v[164:167], v[188:191], v[94:97]
	v_mfma_f32_16x16x32_bf16 v[90:93], v[172:175], v[188:191], v[90:93]
	v_mfma_f32_16x16x32_bf16 v[78:81], v[164:167], v[196:199], v[78:81]
	v_mfma_f32_16x16x32_bf16 v[74:77], v[172:175], v[196:199], v[74:77]
	v_mfma_f32_16x16x32_bf16 v[70:73], v[164:167], v[204:207], v[70:73]
	v_mfma_f32_16x16x32_bf16 v[66:69], v[172:175], v[204:207], v[66:69]
	v_mfma_f32_16x16x32_bf16 v[110:113], v[168:171], v[184:187], v[110:113]
	v_mfma_f32_16x16x32_bf16 v[106:109], v[176:179], v[184:187], v[106:109]
	v_mfma_f32_16x16x32_bf16 v[94:97], v[168:171], v[192:195], v[94:97]
	v_mfma_f32_16x16x32_bf16 v[90:93], v[176:179], v[192:195], v[90:93]
	v_mfma_f32_16x16x32_bf16 v[78:81], v[168:171], v[200:203], v[78:81]
	v_mfma_f32_16x16x32_bf16 v[74:77], v[176:179], v[200:203], v[74:77]
	v_mfma_f32_16x16x32_bf16 v[70:73], v[168:171], v[210:213], v[70:73]
	v_mfma_f32_16x16x32_bf16 v[66:69], v[176:179], v[210:213], v[66:69]
	s_barrier
	s_setprio 0
	s_add_i32 s47, s38, s11
	v_lshl_add_u64 v[214:215], s[24:25], 0, v[132:133]
	s_mov_b32 m0, s47
	ds_read_b128 v[180:183], v146 offset:16384
	ds_read_b128 v[184:187], v146 offset:17408
	ds_read_b128 v[188:191], v146 offset:18432
	ds_read_b128 v[192:195], v146 offset:19456
	ds_read_b128 v[196:199], v146 offset:20480
	ds_read_b128 v[200:203], v146 offset:21504
	ds_read_b128 v[204:207], v146 offset:22528
	ds_read_b128 v[210:213], v146 offset:23552
	global_load_lds_dwordx4 v[214:215], off
	s_add_i32 m0, s47, 0x2000
	s_add_u32 s48, s24, 0x40000
	v_lshl_add_u64 v[216:217], s[24:25], 0, v[136:137]
	s_addc_u32 s49, s25, 0
	s_add_i32 s47, s39, s11
	global_load_lds_dwordx4 v[216:217], off
	v_lshl_add_u64 v[218:219], s[48:49], 0, v[132:133]
	s_mov_b32 m0, s47
	v_lshl_add_u64 v[220:221], s[26:27], 0, v[134:135]
	global_load_lds_dwordx4 v[218:219], off
	v_lshl_add_u64 v[218:219], s[48:49], 0, v[136:137]
	s_add_i32 m0, s47, 0x2000
	s_nop 0
	global_load_lds_dwordx4 v[218:219], off
	v_lshl_add_u64 v[218:219], s[26:27], 0, v[130:131]
	s_mov_b32 m0, s9
	s_nop 0
	global_load_lds_dwordx4 v[218:219], off
	s_mov_b32 m0, s33
	s_nop 0
	global_load_lds_dwordx4 v[220:221], off
	s_waitcnt vmcnt(8)
	s_waitcnt lgkmcnt(0)
	s_setprio 1
	s_barrier
; #define PG8_STAGE(bufoff, gbase, voff) do { _Pragma("unroll") for (int _i = 0; _i < 2; ++_i) \
;         __builtin_amdgcn_global_load_lds((const unsigned*)((const char*)(gbase) + (voff)[_i]), (PG8_LAS unsigned*)(lds + (bufoff) + ldsw + _i * 8192), 16, 0, 0); } while (0)
; #define PG8_LDA(dst, b, h) do { _Pragma("unroll") for (int m = 0; m < 4; ++m) _Pragma("unroll") for (int k = 0; k < 2; ++k) dst[m][k] = *(const PG8_LAS bf16x8*)(lds + PG8_SA(b, h) + aoff + m * 2048 + k * 1024); } while (0)
; #define PG8_LDB(dst, b, h) do { _Pragma("unroll") for (int n = 0; n < 2; ++n) _Pragma("unroll") for (int k = 0; k < 2; ++k) dst[n][k] = *(const PG8_LAS bf16x8*)(lds + PG8_SB(b, h) + boff + n * 2048 + k * 1024); } while (0)
; #define PG8_MMA(ai, bj, At, Bt) do { __builtin_amdgcn_s_setprio(1); _Pragma("unroll") for (int m = 0; m < 4; ++m) _Pragma("unroll") for (int n = 0; n < 2; ++n) _Pragma("unroll") for (int k = 0; k < 2; ++k) \
;         acc[ai][bj][m][n] = __builtin_amdgcn_mfma_f32_16x16x32_bf16(Bt[n][k], At[m][k], acc[ai][bj][m][n], 0, 0, 0); __builtin_amdgcn_s_setprio(0); } while (0)
; #define PG8_WAIT_V(n) asm volatile("s_waitcnt vmcnt(" #n ")" ::: "memory")
; #define PG8_WAIT_L(n) asm volatile("s_waitcnt lgkmcnt(" #n ")" ::: "memory")
; #define PG8_BAR __builtin_amdgcn_s_barrier()
; #define PG8_SCHED __builtin_amdgcn_sched_barrier(0)
;     ...
;             PG8_WAIT_V(8); PG8_WAIT_L(0); PG8_BAR; PG8_MMA(1, 0, At, B0); PG8_MMA(1, 1, At, B1); PG8_BAR; PG8_SCHED;
;             PG8_LDB(B0, 1, 0); PG8_LDB(B1, 1, 1); PG8_SCHED; PG8_LDA(At, 1, 0); PG8_STAGE(PG8_SA(0, 1), a2 + hstep, voffA);
;             PG8_WAIT_V(8); PG8_WAIT_L(0); PG8_BAR; PG8_MMA(0, 0, At, B0); PG8_MMA(0, 1, At, B1); PG8_BAR; PG8_SCHED;
	v_mfma_f32_16x16x32_bf16 v[62:65], v[148:151], v[180:183], v[62:65]
	v_mfma_f32_16x16x32_bf16 v[58:61], v[156:159], v[180:183], v[58:61]
	v_mfma_f32_16x16x32_bf16 v[54:57], v[148:151], v[188:191], v[54:57]
	v_mfma_f32_16x16x32_bf16 v[50:53], v[156:159], v[188:191], v[50:53]
	v_mfma_f32_16x16x32_bf16 v[38:41], v[148:151], v[196:199], v[38:41]
	v_mfma_f32_16x16x32_bf16 v[34:37], v[156:159], v[196:199], v[34:37]
	v_mfma_f32_16x16x32_bf16 v[22:25], v[148:151], v[204:207], v[22:25]
	v_mfma_f32_16x16x32_bf16 v[18:21], v[156:159], v[204:207], v[18:21]
	v_mfma_f32_16x16x32_bf16 v[62:65], v[152:155], v[184:187], v[62:65]
	v_mfma_f32_16x16x32_bf16 v[58:61], v[160:163], v[184:187], v[58:61]
	v_mfma_f32_16x16x32_bf16 v[54:57], v[152:155], v[192:195], v[54:57]
	v_mfma_f32_16x16x32_bf16 v[50:53], v[160:163], v[192:195], v[50:53]
	v_mfma_f32_16x16x32_bf16 v[38:41], v[152:155], v[200:203], v[38:41]
	v_mfma_f32_16x16x32_bf16 v[34:37], v[160:163], v[200:203], v[34:37]
	v_mfma_f32_16x16x32_bf16 v[22:25], v[152:155], v[210:213], v[22:25]
	v_mfma_f32_16x16x32_bf16 v[18:21], v[160:163], v[210:213], v[18:21]
	s_setprio 0
	s_setprio 1
	v_mfma_f32_16x16x32_bf16 v[46:49], v[164:167], v[180:183], v[46:49]
	v_mfma_f32_16x16x32_bf16 v[42:45], v[172:175], v[180:183], v[42:45]
	v_mfma_f32_16x16x32_bf16 v[30:33], v[164:167], v[188:191], v[30:33]
	v_mfma_f32_16x16x32_bf16 v[26:29], v[172:175], v[188:191], v[26:29]
	v_mfma_f32_16x16x32_bf16 v[14:17], v[164:167], v[196:199], v[14:17]
	v_mfma_f32_16x16x32_bf16 v[10:13], v[172:175], v[196:199], v[10:13]
	v_mfma_f32_16x16x32_bf16 v[6:9], v[164:167], v[204:207], v[6:9]
	v_mfma_f32_16x16x32_bf16 v[2:5], v[172:175], v[204:207], v[2:5]
	v_mfma_f32_16x16x32_bf16 v[46:49], v[168:171], v[184:187], v[46:49]
	v_mfma_f32_16x16x32_bf16 v[42:45], v[176:179], v[184:187], v[42:45]
	v_mfma_f32_16x16x32_bf16 v[30:33], v[168:171], v[192:195], v[30:33]
	v_mfma_f32_16x16x32_bf16 v[26:29], v[176:179], v[192:195], v[26:29]
	v_mfma_f32_16x16x32_bf16 v[14:17], v[168:171], v[200:203], v[14:17]
	v_mfma_f32_16x16x32_bf16 v[10:13], v[176:179], v[200:203], v[10:13]
	v_mfma_f32_16x16x32_bf16 v[6:9], v[168:171], v[210:213], v[6:9]
	v_mfma_f32_16x16x32_bf16 v[2:5], v[176:179], v[210:213], v[2:5]
	s_barrier
	s_setprio 0
	s_add_i32 s47, 0, 0x18000
	v_add_u32_e32 v147, s47, v142
	s_add_i32 s48, 0, 0x1c000
	ds_read_b128 v[148:151], v147
	ds_read_b128 v[152:155], v147 offset:1024
	ds_read_b128 v[156:159], v147 offset:2048
	ds_read_b128 v[160:163], v147 offset:3072
	v_add_u32_e32 v147, s48, v142
	ds_read_b128 v[164:167], v147
	ds_read_b128 v[168:171], v147 offset:1024
	ds_read_b128 v[172:175], v147 offset:2048
	ds_read_b128 v[176:179], v147 offset:3072
	s_add_u32 s26, s26, 0x40000
	s_addc_u32 s27, s27, 0
	s_mov_b32 m0, s34
	v_lshl_add_u64 v[222:223], s[26:27], 0, v[130:131]
	ds_read_b128 v[180:183], v146 offset:32768
	ds_read_b128 v[184:187], v146 offset:33792
	ds_read_b128 v[188:191], v146 offset:34816
	ds_read_b128 v[192:195], v146 offset:35840
	ds_read_b128 v[196:199], v146 offset:36864
	ds_read_b128 v[200:203], v146 offset:37888
	ds_read_b128 v[204:207], v146 offset:38912
	ds_read_b128 v[210:213], v146 offset:39936
	global_load_lds_dwordx4 v[222:223], off
	v_lshl_add_u64 v[222:223], s[26:27], 0, v[134:135]
	s_mov_b32 m0, s35
	s_nop 0
	global_load_lds_dwordx4 v[222:223], off
	s_waitcnt vmcnt(8)
	s_waitcnt lgkmcnt(0)
	s_setprio 1
	s_barrier
	v_mfma_f32_16x16x32_bf16 v[126:129], v[148:151], v[180:183], v[126:129]
	v_mfma_f32_16x16x32_bf16 v[122:125], v[156:159], v[180:183], v[122:125]
	v_mfma_f32_16x16x32_bf16 v[118:121], v[148:151], v[188:191], v[118:121]
	v_mfma_f32_16x16x32_bf16 v[114:117], v[156:159], v[188:191], v[114:117]
	v_mfma_f32_16x16x32_bf16 v[102:105], v[148:151], v[196:199], v[102:105]
	v_mfma_f32_16x16x32_bf16 v[98:101], v[156:159], v[196:199], v[98:101]
	v_mfma_f32_16x16x32_bf16 v[86:89], v[148:151], v[204:207], v[86:89]
	v_mfma_f32_16x16x32_bf16 v[82:85], v[156:159], v[204:207], v[82:85]
	v_mfma_f32_16x16x32_bf16 v[126:129], v[152:155], v[184:187], v[126:129]
	v_mfma_f32_16x16x32_bf16 v[122:125], v[160:163], v[184:187], v[122:125]
	v_mfma_f32_16x16x32_bf16 v[118:121], v[152:155], v[192:195], v[118:121]
	v_mfma_f32_16x16x32_bf16 v[114:117], v[160:163], v[192:195], v[114:117]
	v_mfma_f32_16x16x32_bf16 v[102:105], v[152:155], v[200:203], v[102:105]
	v_mfma_f32_16x16x32_bf16 v[98:101], v[160:163], v[200:203], v[98:101]
	v_mfma_f32_16x16x32_bf16 v[86:89], v[152:155], v[210:213], v[86:89]
	v_mfma_f32_16x16x32_bf16 v[82:85], v[160:163], v[210:213], v[82:85]
	s_setprio 0
	s_setprio 1
	v_mfma_f32_16x16x32_bf16 v[110:113], v[164:167], v[180:183], v[110:113]
	v_mfma_f32_16x16x32_bf16 v[106:109], v[172:175], v[180:183], v[106:109]
	v_mfma_f32_16x16x32_bf16 v[94:97], v[164:167], v[188:191], v[94:97]
	v_mfma_f32_16x16x32_bf16 v[90:93], v[172:175], v[188:191], v[90:93]
	v_mfma_f32_16x16x32_bf16 v[78:81], v[164:167], v[196:199], v[78:81]
	v_mfma_f32_16x16x32_bf16 v[74:77], v[172:175], v[196:199], v[74:77]
	v_mfma_f32_16x16x32_bf16 v[70:73], v[164:167], v[204:207], v[70:73]
	v_mfma_f32_16x16x32_bf16 v[66:69], v[172:175], v[204:207], v[66:69]
	v_mfma_f32_16x16x32_bf16 v[110:113], v[168:171], v[184:187], v[110:113]
	v_mfma_f32_16x16x32_bf16 v[106:109], v[176:179], v[184:187], v[106:109]
	v_mfma_f32_16x16x32_bf16 v[94:97], v[168:171], v[192:195], v[94:97]
	v_mfma_f32_16x16x32_bf16 v[90:93], v[176:179], v[192:195], v[90:93]
	v_mfma_f32_16x16x32_bf16 v[78:81], v[168:171], v[200:203], v[78:81]
	v_mfma_f32_16x16x32_bf16 v[74:77], v[176:179], v[200:203], v[74:77]
	v_mfma_f32_16x16x32_bf16 v[70:73], v[168:171], v[210:213], v[70:73]
	v_mfma_f32_16x16x32_bf16 v[66:69], v[176:179], v[210:213], v[66:69]
	s_barrier
; #define PG8_STAGE(bufoff, gbase, voff) do { _Pragma("unroll") for (int _i = 0; _i < 2; ++_i) \
;         __builtin_amdgcn_global_load_lds((const unsigned*)((const char*)(gbase) + (voff)[_i]), (PG8_LAS unsigned*)(lds + (bufoff) + ldsw + _i * 8192), 16, 0, 0); } while (0)
; #define PG8_LDA(dst, b, h) do { _Pragma("unroll") for (int m = 0; m < 4; ++m) _Pragma("unroll") for (int k = 0; k < 2; ++k) dst[m][k] = *(const PG8_LAS bf16x8*)(lds + PG8_SA(b, h) + aoff + m * 2048 + k * 1024); } while (0)
; #define PG8_MMA(ai, bj, At, Bt) do { __builtin_amdgcn_s_setprio(1); _Pragma("unroll") for (int m = 0; m < 4; ++m) _Pragma("unroll") for (int n = 0; n < 2; ++n) _Pragma("unroll") for (int k = 0; k < 2; ++k) \
;         acc[ai][bj][m][n] = __builtin_amdgcn_mfma_f32_16x16x32_bf16(Bt[n][k], At[m][k], acc[ai][bj][m][n], 0, 0, 0); __builtin_amdgcn_s_setprio(0); } while (0)
; #define PG8_WAIT_V(n) asm volatile("s_waitcnt vmcnt(" #n ")" ::: "memory")
; #define PG8_WAIT_L(n) asm volatile("s_waitcnt lgkmcnt(" #n ")" ::: "memory")
; #define PG8_BAR __builtin_amdgcn_s_barrier()
; #define PG8_SCHED __builtin_amdgcn_sched_barrier(0)
;     ...
;             PG8_LDA(At, 1, 1); PG8_STAGE(PG8_SB(1, 0), b3, voffB); PG8_STAGE(PG8_SB(1, 1), b3 + hstep, voffB); PG8_STAGE(PG8_SA(1, 0), a3, voffA);
;             PG8_WAIT_V(8); PG8_WAIT_L(0); PG8_BAR; PG8_MMA(1, 0, At, B0); PG8_MMA(1, 1, At, B1); PG8_BAR; PG8_SCHED;
;         }
;         if constexpr (ALIGN_EPI) { if (wr == 0) PG8_BAR; }
;         E(acc, cur, wr, wc, fr, fq); S.done(cur);
;         if (!has_next) break;
	s_setprio 0
	s_add_i32 s26, s47, s11
	v_lshl_add_u64 v[214:215], v[214:215], 0, s[6:7]
	s_mov_b32 m0, s26
	ds_read_b128 v[180:183], v146 offset:49152
	ds_read_b128 v[184:187], v146 offset:50176
	ds_read_b128 v[188:191], v146 offset:51200
	ds_read_b128 v[192:195], v146 offset:52224
	ds_read_b128 v[196:199], v146 offset:53248
	ds_read_b128 v[200:203], v146 offset:54272
	ds_read_b128 v[204:207], v146 offset:55296
	ds_read_b128 v[210:213], v146 offset:56320
	global_load_lds_dwordx4 v[214:215], off
	s_add_i32 m0, s26, 0x2000
	s_add_u32 s24, s24, 0x40080
	v_lshl_add_u64 v[214:215], v[216:217], 0, s[6:7]
	s_addc_u32 s25, s25, 0
	s_add_i32 s26, s48, s11
	global_load_lds_dwordx4 v[214:215], off
	v_lshl_add_u64 v[214:215], s[24:25], 0, v[132:133]
	s_mov_b32 m0, s26
	s_nop 0
	global_load_lds_dwordx4 v[214:215], off
	v_lshl_add_u64 v[214:215], s[24:25], 0, v[136:137]
	s_add_i32 m0, s26, 0x2000
	s_nop 0
	global_load_lds_dwordx4 v[214:215], off
	v_lshl_add_u64 v[214:215], v[218:219], 0, s[6:7]
	s_mov_b32 m0, s36
	s_nop 0
	global_load_lds_dwordx4 v[214:215], off
	v_lshl_add_u64 v[214:215], v[220:221], 0, s[6:7]
	s_mov_b32 m0, s37
	s_nop 0
	global_load_lds_dwordx4 v[214:215], off
	s_waitcnt vmcnt(8)
	s_waitcnt lgkmcnt(0)
	s_setprio 1
	s_barrier
	v_mfma_f32_16x16x32_bf16 v[62:65], v[148:151], v[180:183], v[62:65]
	v_mfma_f32_16x16x32_bf16 v[58:61], v[156:159], v[180:183], v[58:61]
	v_mfma_f32_16x16x32_bf16 v[54:57], v[148:151], v[188:191], v[54:57]
	v_mfma_f32_16x16x32_bf16 v[50:53], v[156:159], v[188:191], v[50:53]
	v_mfma_f32_16x16x32_bf16 v[38:41], v[148:151], v[196:199], v[38:41]
	v_mfma_f32_16x16x32_bf16 v[34:37], v[156:159], v[196:199], v[34:37]
	v_mfma_f32_16x16x32_bf16 v[22:25], v[148:151], v[204:207], v[22:25]
	v_mfma_f32_16x16x32_bf16 v[18:21], v[156:159], v[204:207], v[18:21]
	v_mfma_f32_16x16x32_bf16 v[62:65], v[152:155], v[184:187], v[62:65]
	v_mfma_f32_16x16x32_bf16 v[58:61], v[160:163], v[184:187], v[58:61]
	v_mfma_f32_16x16x32_bf16 v[54:57], v[152:155], v[192:195], v[54:57]
	v_mfma_f32_16x16x32_bf16 v[50:53], v[160:163], v[192:195], v[50:53]
	v_mfma_f32_16x16x32_bf16 v[38:41], v[152:155], v[200:203], v[38:41]
	v_mfma_f32_16x16x32_bf16 v[34:37], v[160:163], v[200:203], v[34:37]
	v_mfma_f32_16x16x32_bf16 v[22:25], v[152:155], v[210:213], v[22:25]
	v_mfma_f32_16x16x32_bf16 v[18:21], v[160:163], v[210:213], v[18:21]
	s_setprio 0
	s_setprio 1
	v_mfma_f32_16x16x32_bf16 v[46:49], v[164:167], v[180:183], v[46:49]
	v_mfma_f32_16x16x32_bf16 v[42:45], v[172:175], v[180:183], v[42:45]
	v_mfma_f32_16x16x32_bf16 v[30:33], v[164:167], v[188:191], v[30:33]
	v_mfma_f32_16x16x32_bf16 v[26:29], v[172:175], v[188:191], v[26:29]
	v_mfma_f32_16x16x32_bf16 v[14:17], v[164:167], v[196:199], v[14:17]
	v_mfma_f32_16x16x32_bf16 v[10:13], v[172:175], v[196:199], v[10:13]
	v_mfma_f32_16x16x32_bf16 v[6:9], v[164:167], v[204:207], v[6:9]
	v_mfma_f32_16x16x32_bf16 v[2:5], v[172:175], v[204:207], v[2:5]
	v_mfma_f32_16x16x32_bf16 v[46:49], v[168:171], v[184:187], v[46:49]
	v_mfma_f32_16x16x32_bf16 v[42:45], v[176:179], v[184:187], v[42:45]
	v_mfma_f32_16x16x32_bf16 v[30:33], v[168:171], v[192:195], v[30:33]
	v_mfma_f32_16x16x32_bf16 v[26:29], v[176:179], v[192:195], v[26:29]
	v_mfma_f32_16x16x32_bf16 v[14:17], v[168:171], v[200:203], v[14:17]
	v_mfma_f32_16x16x32_bf16 v[10:13], v[176:179], v[200:203], v[10:13]
	v_mfma_f32_16x16x32_bf16 v[6:9], v[168:171], v[210:213], v[6:9]
	v_mfma_f32_16x16x32_bf16 v[2:5], v[176:179], v[210:213], v[2:5]
	s_barrier
	s_setprio 0
	s_add_i32 s46, s46, 2
	s_add_u32 s22, s22, 0x100
	s_addc_u32 s23, s23, 0
	s_add_u32 s17, s17, 0x100
	s_addc_u32 s45, s45, 0
	s_cmp_gt_u32 s46, 13
	s_cbranch_scc0 .LBB0_1303
	s_and_b64 vcc, exec, s[12:13]
	s_cbranch_vccz .LBB0_1306
	s_barrier

; #define PG8_STAGE(bufoff, gbase, voff) do { _Pragma("unroll") for (int _i = 0; _i < 2; ++_i) \
;         __builtin_amdgcn_global_load_lds((const unsigned*)((const char*)(gbase) + (voff)[_i]), (PG8_LAS unsigned*)(lds + (bufoff) + ldsw + _i * 8192), 16, 0, 0); } while (0)
; #define PG8_LDA(dst, b, h) do { _Pragma("unroll") for (int m = 0; m < 4; ++m) _Pragma("unroll") for (int k = 0; k < 2; ++k) dst[m][k] = *(const PG8_LAS bf16x8*)(lds + PG8_SA(b, h) + aoff + m * 2048 + k * 1024); } while (0)
; #define PG8_LDB(dst, b, h) do { _Pragma("unroll") for (int n = 0; n < 2; ++n) _Pragma("unroll") for (int k = 0; k < 2; ++k) dst[n][k] = *(const PG8_LAS bf16x8*)(lds + PG8_SB(b, h) + boff + n * 2048 + k * 1024); } while (0)
; #define PG8_MMA(ai, bj, At, Bt) do { __builtin_amdgcn_s_setprio(1); _Pragma("unroll") for (int m = 0; m < 4; ++m) _Pragma("unroll") for (int n = 0; n < 2; ++n) _Pragma("unroll") for (int k = 0; k < 2; ++k) \
;         acc[ai][bj][m][n] = __builtin_amdgcn_mfma_f32_16x16x32_bf16(Bt[n][k], At[m][k], acc[ai][bj][m][n], 0, 0, 0); __builtin_amdgcn_s_setprio(0); } while (0)
; #define PG8_WAIT_V(n) asm volatile("s_waitcnt vmcnt(" #n ")" ::: "memory")
; #define PG8_WAIT_L(n) asm volatile("s_waitcnt lgkmcnt(" #n ")" ::: "memory")
; #define PG8_BAR __builtin_amdgcn_s_barrier()
; #define PG8_SCHED __builtin_amdgcn_sched_barrier(0)
;     ...
;         for (int t = 0; t < nt; t += 2) {
;             const bool last = (t == nt - 2);
;             const char* a1 = cA + (size_t)(t + 1) * kstep;
;             const char* a2 = last ? nA : cA + (size_t)(t + 2) * kstep; const char* b2 = last ? nB : cB + (size_t)(t + 2) * kstep;
;             const char* a3 = a2 + kstep; const char* b3 = b2 + kstep;
;             if (last && has_next) S.a_ready(nxt);
;             PG8_LDB(B0, 0, 0); PG8_LDB(B1, 0, 1); PG8_SCHED; PG8_LDA(At, 0, 0); PG8_STAGE(PG8_SA(1, 1), a1 + hstep, voffA);
;             PG8_WAIT_V(8); PG8_WAIT_L(0); PG8_BAR; PG8_MMA(0, 0, At, B0); PG8_MMA(0, 1, At, B1); PG8_BAR; PG8_SCHED;
;             PG8_LDA(At, 0, 1); PG8_STAGE(PG8_SB(0, 0), b2, voffB); PG8_STAGE(PG8_SB(0, 1), b2 + hstep, voffB); PG8_STAGE(PG8_SA(0, 0), a2, voffA);
.LBB0_1939:
	ds_read_b128 v[130:133], v183
	ds_read_b128 v[134:137], v183 offset:1024
	ds_read_b128 v[138:141], v183 offset:2048
	ds_read_b128 v[142:145], v183 offset:3072
	ds_read_b128 v[178:181], v184
	ds_read_b128 v[186:189], v184 offset:1024
	ds_read_b128 v[190:193], v184 offset:2048
	ds_read_b128 v[194:197], v184 offset:3072
	s_add_u32 s20, s18, 0xfffc0080
	s_addc_u32 s21, s19, -1
	s_cmp_eq_u32 s50, 12
	s_cselect_b32 s23, s11, s21
	s_cselect_b32 s22, s17, s20
	s_cselect_b32 s21, s9, s49
	s_cselect_b32 s20, s47, s48
	v_lshl_add_u64 v[206:207], s[18:19], 0, v[170:171]
	s_add_i32 m0, s31, 0xc000
	ds_read_b128 v[198:201], v185
	ds_read_b128 v[202:205], v185 offset:1024
	ds_read_b128 v[210:213], v185 offset:2048
	ds_read_b128 v[214:217], v185 offset:3072
	ds_read_b128 v[218:221], v185 offset:4096
	ds_read_b128 v[222:225], v185 offset:5120
	ds_read_b128 v[226:229], v185 offset:6144
	ds_read_b128 v[230:233], v185 offset:7168
	global_load_lds_dwordx4 v[206:207], off
	v_lshl_add_u64 v[206:207], s[18:19], 0, v[172:173]
	s_add_i32 m0, s31, 0xe000
	s_nop 0
	global_load_lds_dwordx4 v[206:207], off
	s_waitcnt vmcnt(8)
	s_waitcnt lgkmcnt(0)
	s_setprio 1
	s_barrier
	v_mfma_f32_16x16x32_bf16 v[126:129], v[130:133], v[198:201], v[126:129]
	v_mfma_f32_16x16x32_bf16 v[122:125], v[138:141], v[198:201], v[122:125]
	v_mfma_f32_16x16x32_bf16 v[118:121], v[130:133], v[210:213], v[118:121]
	v_mfma_f32_16x16x32_bf16 v[114:117], v[138:141], v[210:213], v[114:117]
	v_mfma_f32_16x16x32_bf16 v[98:101], v[130:133], v[218:221], v[98:101]
	v_mfma_f32_16x16x32_bf16 v[90:93], v[138:141], v[218:221], v[90:93]
	v_mfma_f32_16x16x32_bf16 v[82:85], v[130:133], v[226:229], v[82:85]
	v_mfma_f32_16x16x32_bf16 v[74:77], v[138:141], v[226:229], v[74:77]
	v_mfma_f32_16x16x32_bf16 v[126:129], v[134:137], v[202:205], v[126:129]
	v_mfma_f32_16x16x32_bf16 v[122:125], v[142:145], v[202:205], v[122:125]
	v_mfma_f32_16x16x32_bf16 v[118:121], v[134:137], v[214:217], v[118:121]
	v_mfma_f32_16x16x32_bf16 v[114:117], v[142:145], v[214:217], v[114:117]
	v_mfma_f32_16x16x32_bf16 v[98:101], v[134:137], v[222:225], v[98:101]
	v_mfma_f32_16x16x32_bf16 v[90:93], v[142:145], v[222:225], v[90:93]
	v_mfma_f32_16x16x32_bf16 v[82:85], v[134:137], v[230:233], v[82:85]
	v_mfma_f32_16x16x32_bf16 v[74:77], v[142:145], v[230:233], v[74:77]
	s_setprio 0
	s_setprio 1
	v_mfma_f32_16x16x32_bf16 v[110:113], v[178:181], v[198:201], v[110:113]
	v_mfma_f32_16x16x32_bf16 v[106:109], v[190:193], v[198:201], v[106:109]
	v_mfma_f32_16x16x32_bf16 v[102:105], v[178:181], v[210:213], v[102:105]
	v_mfma_f32_16x16x32_bf16 v[94:97], v[190:193], v[210:213], v[94:97]
	v_mfma_f32_16x16x32_bf16 v[86:89], v[178:181], v[218:221], v[86:89]
	v_mfma_f32_16x16x32_bf16 v[78:81], v[190:193], v[218:221], v[78:81]
	v_mfma_f32_16x16x32_bf16 v[70:73], v[178:181], v[226:229], v[70:73]
	v_mfma_f32_16x16x32_bf16 v[66:69], v[190:193], v[226:229], v[66:69]
	v_mfma_f32_16x16x32_bf16 v[110:113], v[186:189], v[202:205], v[110:113]
	v_mfma_f32_16x16x32_bf16 v[106:109], v[194:197], v[202:205], v[106:109]
	v_mfma_f32_16x16x32_bf16 v[102:105], v[186:189], v[214:217], v[102:105]
	v_mfma_f32_16x16x32_bf16 v[94:97], v[194:197], v[214:217], v[94:97]
	v_mfma_f32_16x16x32_bf16 v[86:89], v[186:189], v[222:225], v[86:89]
	v_mfma_f32_16x16x32_bf16 v[78:81], v[194:197], v[222:225], v[78:81]
	v_mfma_f32_16x16x32_bf16 v[70:73], v[186:189], v[230:233], v[70:73]
	v_mfma_f32_16x16x32_bf16 v[66:69], v[194:197], v[230:233], v[66:69]
	s_barrier
	s_setprio 0
	s_add_i32 s51, s44, s28
	v_lshl_add_u64 v[206:207], s[20:21], 0, v[150:151]
	s_mov_b32 m0, s51
	ds_read_b128 v[198:201], v185 offset:16384
	ds_read_b128 v[202:205], v185 offset:17408
	ds_read_b128 v[210:213], v185 offset:18432
	ds_read_b128 v[214:217], v185 offset:19456
	ds_read_b128 v[218:221], v185 offset:20480
	ds_read_b128 v[222:225], v185 offset:21504
	ds_read_b128 v[226:229], v185 offset:22528
	ds_read_b128 v[230:233], v185 offset:23552
	global_load_lds_dwordx4 v[206:207], off
	s_add_i32 m0, s51, 0x2000
	s_add_u32 s52, s20, 0x40000
	v_lshl_add_u64 v[234:235], s[20:21], 0, v[146:147]
	s_addc_u32 s53, s21, 0
	s_add_i32 s51, s45, s28
	global_load_lds_dwordx4 v[234:235], off
	v_lshl_add_u64 v[236:237], s[52:53], 0, v[150:151]
	s_mov_b32 m0, s51
	v_lshl_add_u64 v[238:239], s[22:23], 0, v[148:149]
	global_load_lds_dwordx4 v[236:237], off
	v_lshl_add_u64 v[236:237], s[52:53], 0, v[146:147]
	s_add_i32 m0, s51, 0x2000
	s_nop 0
	global_load_lds_dwordx4 v[236:237], off
	v_lshl_add_u64 v[236:237], s[22:23], 0, v[152:153]
	s_mov_b32 m0, s31
	s_nop 0
	global_load_lds_dwordx4 v[236:237], off
	s_mov_b32 m0, s33
	s_nop 0
	global_load_lds_dwordx4 v[238:239], off
	s_waitcnt vmcnt(8)
	s_waitcnt lgkmcnt(0)
	s_setprio 1
	s_barrier
; #define PG8_STAGE(bufoff, gbase, voff) do { _Pragma("unroll") for (int _i = 0; _i < 2; ++_i) \
;         __builtin_amdgcn_global_load_lds((const unsigned*)((const char*)(gbase) + (voff)[_i]), (PG8_LAS unsigned*)(lds + (bufoff) + ldsw + _i * 8192), 16, 0, 0); } while (0)
; #define PG8_LDA(dst, b, h) do { _Pragma("unroll") for (int m = 0; m < 4; ++m) _Pragma("unroll") for (int k = 0; k < 2; ++k) dst[m][k] = *(const PG8_LAS bf16x8*)(lds + PG8_SA(b, h) + aoff + m * 2048 + k * 1024); } while (0)
; #define PG8_LDB(dst, b, h) do { _Pragma("unroll") for (int n = 0; n < 2; ++n) _Pragma("unroll") for (int k = 0; k < 2; ++k) dst[n][k] = *(const PG8_LAS bf16x8*)(lds + PG8_SB(b, h) + boff + n * 2048 + k * 1024); } while (0)
; #define PG8_MMA(ai, bj, At, Bt) do { __builtin_amdgcn_s_setprio(1); _Pragma("unroll") for (int m = 0; m < 4; ++m) _Pragma("unroll") for (int n = 0; n < 2; ++n) _Pragma("unroll") for (int k = 0; k < 2; ++k) \
;         acc[ai][bj][m][n] = __builtin_amdgcn_mfma_f32_16x16x32_bf16(Bt[n][k], At[m][k], acc[ai][bj][m][n], 0, 0, 0); __builtin_amdgcn_s_setprio(0); } while (0)
; #define PG8_WAIT_V(n) asm volatile("s_waitcnt vmcnt(" #n ")" ::: "memory")
; #define PG8_WAIT_L(n) asm volatile("s_waitcnt lgkmcnt(" #n ")" ::: "memory")
; #define PG8_BAR __builtin_amdgcn_s_barrier()
; #define PG8_SCHED __builtin_amdgcn_sched_barrier(0)
;     ...
;             PG8_WAIT_V(8); PG8_WAIT_L(0); PG8_BAR; PG8_MMA(1, 0, At, B0); PG8_MMA(1, 1, At, B1); PG8_BAR; PG8_SCHED;
;             PG8_LDB(B0, 1, 0); PG8_LDB(B1, 1, 1); PG8_SCHED; PG8_LDA(At, 1, 0); PG8_STAGE(PG8_SA(0, 1), a2 + hstep, voffA);
;             PG8_WAIT_V(8); PG8_WAIT_L(0); PG8_BAR; PG8_MMA(0, 0, At, B0); PG8_MMA(0, 1, At, B1); PG8_BAR; PG8_SCHED;
	v_mfma_f32_16x16x32_bf16 v[62:65], v[130:133], v[198:201], v[62:65]
	v_mfma_f32_16x16x32_bf16 v[58:61], v[138:141], v[198:201], v[58:61]
	v_mfma_f32_16x16x32_bf16 v[50:53], v[130:133], v[210:213], v[50:53]
	v_mfma_f32_16x16x32_bf16 v[42:45], v[138:141], v[210:213], v[42:45]
	v_mfma_f32_16x16x32_bf16 v[34:37], v[130:133], v[218:221], v[34:37]
	v_mfma_f32_16x16x32_bf16 v[26:29], v[138:141], v[218:221], v[26:29]
	v_mfma_f32_16x16x32_bf16 v[18:21], v[130:133], v[226:229], v[18:21]
	v_mfma_f32_16x16x32_bf16 v[10:13], v[138:141], v[226:229], v[10:13]
	v_mfma_f32_16x16x32_bf16 v[62:65], v[134:137], v[202:205], v[62:65]
	v_mfma_f32_16x16x32_bf16 v[58:61], v[142:145], v[202:205], v[58:61]
	v_mfma_f32_16x16x32_bf16 v[50:53], v[134:137], v[214:217], v[50:53]
	v_mfma_f32_16x16x32_bf16 v[42:45], v[142:145], v[214:217], v[42:45]
	v_mfma_f32_16x16x32_bf16 v[34:37], v[134:137], v[222:225], v[34:37]
	v_mfma_f32_16x16x32_bf16 v[26:29], v[142:145], v[222:225], v[26:29]
	v_mfma_f32_16x16x32_bf16 v[18:21], v[134:137], v[230:233], v[18:21]
	v_mfma_f32_16x16x32_bf16 v[10:13], v[142:145], v[230:233], v[10:13]
	s_setprio 0
	s_setprio 1
	v_mfma_f32_16x16x32_bf16 v[54:57], v[178:181], v[198:201], v[54:57]
	v_mfma_f32_16x16x32_bf16 v[46:49], v[190:193], v[198:201], v[46:49]
	v_mfma_f32_16x16x32_bf16 v[38:41], v[178:181], v[210:213], v[38:41]
	v_mfma_f32_16x16x32_bf16 v[30:33], v[190:193], v[210:213], v[30:33]
	v_mfma_f32_16x16x32_bf16 v[22:25], v[178:181], v[218:221], v[22:25]
	v_mfma_f32_16x16x32_bf16 v[14:17], v[190:193], v[218:221], v[14:17]
	v_mfma_f32_16x16x32_bf16 v[6:9], v[178:181], v[226:229], v[6:9]
	v_mfma_f32_16x16x32_bf16 v[2:5], v[190:193], v[226:229], v[2:5]
	v_mfma_f32_16x16x32_bf16 v[54:57], v[186:189], v[202:205], v[54:57]
	v_mfma_f32_16x16x32_bf16 v[46:49], v[194:197], v[202:205], v[46:49]
	v_mfma_f32_16x16x32_bf16 v[38:41], v[186:189], v[214:217], v[38:41]
	v_mfma_f32_16x16x32_bf16 v[30:33], v[194:197], v[214:217], v[30:33]
	v_mfma_f32_16x16x32_bf16 v[22:25], v[186:189], v[222:225], v[22:25]
	v_mfma_f32_16x16x32_bf16 v[14:17], v[194:197], v[222:225], v[14:17]
	v_mfma_f32_16x16x32_bf16 v[6:9], v[186:189], v[230:233], v[6:9]
	v_mfma_f32_16x16x32_bf16 v[2:5], v[194:197], v[230:233], v[2:5]
	s_barrier
	s_setprio 0
	s_add_i32 s51, 0, 0x18000
	s_add_i32 s52, 0, 0x1c000
	v_add_u32_e32 v142, s51, v1
	v_add_u32_e32 v194, s52, v1
	ds_read_b128 v[130:133], v142
	ds_read_b128 v[134:137], v142 offset:1024
	ds_read_b128 v[138:141], v142 offset:2048
	ds_read_b128 v[142:145], v142 offset:3072
	ds_read_b128 v[178:181], v194
	ds_read_b128 v[186:189], v194 offset:1024
	ds_read_b128 v[190:193], v194 offset:2048
	ds_read_b128 v[194:197], v194 offset:3072
	s_add_u32 s22, s22, 0x40000
	s_addc_u32 s23, s23, 0
	s_mov_b32 m0, s34
	v_lshl_add_u64 v[240:241], s[22:23], 0, v[152:153]
	ds_read_b128 v[198:201], v185 offset:32768
	ds_read_b128 v[202:205], v185 offset:33792
	ds_read_b128 v[210:213], v185 offset:34816
	ds_read_b128 v[214:217], v185 offset:35840
	ds_read_b128 v[218:221], v185 offset:36864
	ds_read_b128 v[222:225], v185 offset:37888
	ds_read_b128 v[226:229], v185 offset:38912
	ds_read_b128 v[230:233], v185 offset:39936
	global_load_lds_dwordx4 v[240:241], off
	v_lshl_add_u64 v[240:241], s[22:23], 0, v[148:149]
	s_mov_b32 m0, s35
	s_nop 0
	global_load_lds_dwordx4 v[240:241], off
	s_waitcnt vmcnt(8)
	s_waitcnt lgkmcnt(0)
	s_setprio 1
	s_barrier
	v_mfma_f32_16x16x32_bf16 v[126:129], v[130:133], v[198:201], v[126:129]
	v_mfma_f32_16x16x32_bf16 v[122:125], v[138:141], v[198:201], v[122:125]
	v_mfma_f32_16x16x32_bf16 v[118:121], v[130:133], v[210:213], v[118:121]
	v_mfma_f32_16x16x32_bf16 v[114:117], v[138:141], v[210:213], v[114:117]
	v_mfma_f32_16x16x32_bf16 v[98:101], v[130:133], v[218:221], v[98:101]
	v_mfma_f32_16x16x32_bf16 v[90:93], v[138:141], v[218:221], v[90:93]
	v_mfma_f32_16x16x32_bf16 v[82:85], v[130:133], v[226:229], v[82:85]
	v_mfma_f32_16x16x32_bf16 v[74:77], v[138:141], v[226:229], v[74:77]
	v_mfma_f32_16x16x32_bf16 v[126:129], v[134:137], v[202:205], v[126:129]
	v_mfma_f32_16x16x32_bf16 v[122:125], v[142:145], v[202:205], v[122:125]
	v_mfma_f32_16x16x32_bf16 v[118:121], v[134:137], v[214:217], v[118:121]
	v_mfma_f32_16x16x32_bf16 v[114:117], v[142:145], v[214:217], v[114:117]
	v_mfma_f32_16x16x32_bf16 v[98:101], v[134:137], v[222:225], v[98:101]
	v_mfma_f32_16x16x32_bf16 v[90:93], v[142:145], v[222:225], v[90:93]
	v_mfma_f32_16x16x32_bf16 v[82:85], v[134:137], v[230:233], v[82:85]
	v_mfma_f32_16x16x32_bf16 v[74:77], v[142:145], v[230:233], v[74:77]
	s_setprio 0
	s_setprio 1
	v_mfma_f32_16x16x32_bf16 v[110:113], v[178:181], v[198:201], v[110:113]
	v_mfma_f32_16x16x32_bf16 v[106:109], v[190:193], v[198:201], v[106:109]
	v_mfma_f32_16x16x32_bf16 v[102:105], v[178:181], v[210:213], v[102:105]
	v_mfma_f32_16x16x32_bf16 v[94:97], v[190:193], v[210:213], v[94:97]
	v_mfma_f32_16x16x32_bf16 v[86:89], v[178:181], v[218:221], v[86:89]
	v_mfma_f32_16x16x32_bf16 v[78:81], v[190:193], v[218:221], v[78:81]
	v_mfma_f32_16x16x32_bf16 v[70:73], v[178:181], v[226:229], v[70:73]
	v_mfma_f32_16x16x32_bf16 v[66:69], v[190:193], v[226:229], v[66:69]
	v_mfma_f32_16x16x32_bf16 v[110:113], v[186:189], v[202:205], v[110:113]
	v_mfma_f32_16x16x32_bf16 v[106:109], v[194:197], v[202:205], v[106:109]
	v_mfma_f32_16x16x32_bf16 v[102:105], v[186:189], v[214:217], v[102:105]
	v_mfma_f32_16x16x32_bf16 v[94:97], v[194:197], v[214:217], v[94:97]
	v_mfma_f32_16x16x32_bf16 v[86:89], v[186:189], v[222:225], v[86:89]
	v_mfma_f32_16x16x32_bf16 v[78:81], v[194:197], v[222:225], v[78:81]
	v_mfma_f32_16x16x32_bf16 v[70:73], v[186:189], v[230:233], v[70:73]
	v_mfma_f32_16x16x32_bf16 v[66:69], v[194:197], v[230:233], v[66:69]
	s_barrier
; #define PG8_STAGE(bufoff, gbase, voff) do { _Pragma("unroll") for (int _i = 0; _i < 2; ++_i) \
;         __builtin_amdgcn_global_load_lds((const unsigned*)((const char*)(gbase) + (voff)[_i]), (PG8_LAS unsigned*)(lds + (bufoff) + ldsw + _i * 8192), 16, 0, 0); } while (0)
; #define PG8_LDA(dst, b, h) do { _Pragma("unroll") for (int m = 0; m < 4; ++m) _Pragma("unroll") for (int k = 0; k < 2; ++k) dst[m][k] = *(const PG8_LAS bf16x8*)(lds + PG8_SA(b, h) + aoff + m * 2048 + k * 1024); } while (0)
; #define PG8_MMA(ai, bj, At, Bt) do { __builtin_amdgcn_s_setprio(1); _Pragma("unroll") for (int m = 0; m < 4; ++m) _Pragma("unroll") for (int n = 0; n < 2; ++n) _Pragma("unroll") for (int k = 0; k < 2; ++k) \
;         acc[ai][bj][m][n] = __builtin_amdgcn_mfma_f32_16x16x32_bf16(Bt[n][k], At[m][k], acc[ai][bj][m][n], 0, 0, 0); __builtin_amdgcn_s_setprio(0); } while (0)
; #define PG8_WAIT_V(n) asm volatile("s_waitcnt vmcnt(" #n ")" ::: "memory")
; #define PG8_WAIT_L(n) asm volatile("s_waitcnt lgkmcnt(" #n ")" ::: "memory")
; #define PG8_BAR __builtin_amdgcn_s_barrier()
; #define PG8_SCHED __builtin_amdgcn_sched_barrier(0)
;     ...
;             PG8_LDA(At, 1, 1); PG8_STAGE(PG8_SB(1, 0), b3, voffB); PG8_STAGE(PG8_SB(1, 1), b3 + hstep, voffB); PG8_STAGE(PG8_SA(1, 0), a3, voffA);
;             PG8_WAIT_V(8); PG8_WAIT_L(0); PG8_BAR; PG8_MMA(1, 0, At, B0); PG8_MMA(1, 1, At, B1); PG8_BAR; PG8_SCHED;
;         }
;         if constexpr (ALIGN_EPI) { if (wr == 0) PG8_BAR; }
;         E(acc, cur, wr, wc, fr, fq); S.done(cur);
;         if (!has_next) break;
	s_setprio 0
	s_add_i32 s22, s51, s28
	v_lshl_add_u64 v[206:207], v[206:207], 0, s[2:3]
	s_mov_b32 m0, s22
	ds_read_b128 v[198:201], v185 offset:49152
	ds_read_b128 v[202:205], v185 offset:50176
	ds_read_b128 v[210:213], v185 offset:51200
	ds_read_b128 v[214:217], v185 offset:52224
	ds_read_b128 v[218:221], v185 offset:53248
	ds_read_b128 v[222:225], v185 offset:54272
	ds_read_b128 v[226:229], v185 offset:55296
	ds_read_b128 v[230:233], v185 offset:56320
	global_load_lds_dwordx4 v[206:207], off
	s_add_i32 m0, s22, 0x2000
	s_add_u32 s20, s20, 0x40080
	v_lshl_add_u64 v[206:207], v[234:235], 0, s[2:3]
	s_addc_u32 s21, s21, 0
	s_add_i32 s22, s52, s28
	global_load_lds_dwordx4 v[206:207], off
	v_lshl_add_u64 v[206:207], s[20:21], 0, v[150:151]
	s_mov_b32 m0, s22
	s_nop 0
	global_load_lds_dwordx4 v[206:207], off
	v_lshl_add_u64 v[206:207], s[20:21], 0, v[146:147]
	s_add_i32 m0, s22, 0x2000
	s_nop 0
	global_load_lds_dwordx4 v[206:207], off
	v_lshl_add_u64 v[206:207], v[236:237], 0, s[2:3]
	s_mov_b32 m0, s37
	s_nop 0
	global_load_lds_dwordx4 v[206:207], off
	v_lshl_add_u64 v[206:207], v[238:239], 0, s[2:3]
	s_mov_b32 m0, s38
	s_nop 0
	global_load_lds_dwordx4 v[206:207], off
	s_waitcnt vmcnt(8)
	s_waitcnt lgkmcnt(0)
	s_setprio 1
	s_barrier
	v_mfma_f32_16x16x32_bf16 v[62:65], v[130:133], v[198:201], v[62:65]
	v_mfma_f32_16x16x32_bf16 v[58:61], v[138:141], v[198:201], v[58:61]
	v_mfma_f32_16x16x32_bf16 v[50:53], v[130:133], v[210:213], v[50:53]
	v_mfma_f32_16x16x32_bf16 v[42:45], v[138:141], v[210:213], v[42:45]
	v_mfma_f32_16x16x32_bf16 v[34:37], v[130:133], v[218:221], v[34:37]
	v_mfma_f32_16x16x32_bf16 v[26:29], v[138:141], v[218:221], v[26:29]
	v_mfma_f32_16x16x32_bf16 v[18:21], v[130:133], v[226:229], v[18:21]
	v_mfma_f32_16x16x32_bf16 v[10:13], v[138:141], v[226:229], v[10:13]
	v_mfma_f32_16x16x32_bf16 v[62:65], v[134:137], v[202:205], v[62:65]
	v_mfma_f32_16x16x32_bf16 v[58:61], v[142:145], v[202:205], v[58:61]
	v_mfma_f32_16x16x32_bf16 v[50:53], v[134:137], v[214:217], v[50:53]
	v_mfma_f32_16x16x32_bf16 v[42:45], v[142:145], v[214:217], v[42:45]
	v_mfma_f32_16x16x32_bf16 v[34:37], v[134:137], v[222:225], v[34:37]
	v_mfma_f32_16x16x32_bf16 v[26:29], v[142:145], v[222:225], v[26:29]
	v_mfma_f32_16x16x32_bf16 v[18:21], v[134:137], v[230:233], v[18:21]
	v_mfma_f32_16x16x32_bf16 v[10:13], v[142:145], v[230:233], v[10:13]
	s_setprio 0
	s_setprio 1
	v_mfma_f32_16x16x32_bf16 v[54:57], v[178:181], v[198:201], v[54:57]
	v_mfma_f32_16x16x32_bf16 v[46:49], v[190:193], v[198:201], v[46:49]
	v_mfma_f32_16x16x32_bf16 v[38:41], v[178:181], v[210:213], v[38:41]
	v_mfma_f32_16x16x32_bf16 v[30:33], v[190:193], v[210:213], v[30:33]
	v_mfma_f32_16x16x32_bf16 v[22:25], v[178:181], v[218:221], v[22:25]
	v_mfma_f32_16x16x32_bf16 v[14:17], v[190:193], v[218:221], v[14:17]
	v_mfma_f32_16x16x32_bf16 v[6:9], v[178:181], v[226:229], v[6:9]
	v_mfma_f32_16x16x32_bf16 v[2:5], v[190:193], v[226:229], v[2:5]
	v_mfma_f32_16x16x32_bf16 v[54:57], v[186:189], v[202:205], v[54:57]
	v_mfma_f32_16x16x32_bf16 v[46:49], v[194:197], v[202:205], v[46:49]
	v_mfma_f32_16x16x32_bf16 v[38:41], v[186:189], v[214:217], v[38:41]
	v_mfma_f32_16x16x32_bf16 v[30:33], v[194:197], v[214:217], v[30:33]
	v_mfma_f32_16x16x32_bf16 v[22:25], v[186:189], v[222:225], v[22:25]
	v_mfma_f32_16x16x32_bf16 v[14:17], v[194:197], v[222:225], v[14:17]
	v_mfma_f32_16x16x32_bf16 v[6:9], v[186:189], v[230:233], v[6:9]
	v_mfma_f32_16x16x32_bf16 v[2:5], v[194:197], v[230:233], v[2:5]
	s_barrier
	s_setprio 0
	s_add_i32 s50, s50, 2
	s_add_u32 s18, s18, 0x100
	s_addc_u32 s19, s19, 0
	s_add_u32 s48, s48, 0x100
	s_addc_u32 s49, s49, 0
	s_cmp_gt_u32 s50, 13
	s_cbranch_scc0 .LBB0_1939
	s_and_b64 vcc, exec, s[6:7]
	s_cbranch_vccz .LBB0_1942
	s_barrier

; #define PG8_STAGE(bufoff, gbase, voff) do { _Pragma("unroll") for (int _i = 0; _i < 2; ++_i) \
;         __builtin_amdgcn_global_load_lds((const unsigned*)((const char*)(gbase) + (voff)[_i]), (PG8_LAS unsigned*)(lds + (bufoff) + ldsw + _i * 8192), 16, 0, 0); } while (0)
; #define PG8_LDA(dst, b, h) do { _Pragma("unroll") for (int m = 0; m < 4; ++m) _Pragma("unroll") for (int k = 0; k < 2; ++k) dst[m][k] = *(const PG8_LAS bf16x8*)(lds + PG8_SA(b, h) + aoff + m * 2048 + k * 1024); } while (0)
; #define PG8_LDB(dst, b, h) do { _Pragma("unroll") for (int n = 0; n < 2; ++n) _Pragma("unroll") for (int k = 0; k < 2; ++k) dst[n][k] = *(const PG8_LAS bf16x8*)(lds + PG8_SB(b, h) + boff + n * 2048 + k * 1024); } while (0)
; #define PG8_MMA(ai, bj, At, Bt) do { __builtin_amdgcn_s_setprio(1); _Pragma("unroll") for (int m = 0; m < 4; ++m) _Pragma("unroll") for (int n = 0; n < 2; ++n) _Pragma("unroll") for (int k = 0; k < 2; ++k) \
;         acc[ai][bj][m][n] = __builtin_amdgcn_mfma_f32_16x16x32_bf16(Bt[n][k], At[m][k], acc[ai][bj][m][n], 0, 0, 0); __builtin_amdgcn_s_setprio(0); } while (0)
; #define PG8_WAIT_V(n) asm volatile("s_waitcnt vmcnt(" #n ")" ::: "memory")
; #define PG8_WAIT_L(n) asm volatile("s_waitcnt lgkmcnt(" #n ")" ::: "memory")
; #define PG8_BAR __builtin_amdgcn_s_barrier()
; #define PG8_SCHED __builtin_amdgcn_sched_barrier(0)
;     ...
;         for (int t = 0; t < nt; t += 2) {
;             const bool last = (t == nt - 2);
;             const char* a1 = cA + (size_t)(t + 1) * kstep;
;             const char* a2 = last ? nA : cA + (size_t)(t + 2) * kstep; const char* b2 = last ? nB : cB + (size_t)(t + 2) * kstep;
;             const char* a3 = a2 + kstep; const char* b3 = b2 + kstep;
;             if (last && has_next) S.a_ready(nxt);
;             PG8_LDB(B0, 0, 0); PG8_LDB(B1, 0, 1); PG8_SCHED; PG8_LDA(At, 0, 0); PG8_STAGE(PG8_SA(1, 1), a1 + hstep, voffA);
;             PG8_WAIT_V(8); PG8_WAIT_L(0); PG8_BAR; PG8_MMA(0, 0, At, B0); PG8_MMA(0, 1, At, B1); PG8_BAR; PG8_SCHED;
;             PG8_LDA(At, 0, 1); PG8_STAGE(PG8_SB(0, 0), b2, voffB); PG8_STAGE(PG8_SB(0, 1), b2 + hstep, voffB); PG8_STAGE(PG8_SA(0, 0), a2, voffA);
.LBB0_2242:
	s_add_u32 s46, s74, 0xfff20080
	s_addc_u32 s47, s75, -1
	s_add_i32 s20, 0, 0x10000
	s_cmp_eq_u32 s19, 52
	s_cselect_b32 s81, s73, s47
	s_cselect_b32 s80, s72, s46
	v_add_u32_e32 v132, s20, v173
	s_cselect_b64 vcc, -1, 0
	s_add_i32 s21, 0, 0x14000
	ds_read_b128 v[176:179], v132
	ds_read_b128 v[180:183], v132 offset:1024
	ds_read_b128 v[184:187], v132 offset:2048
	ds_read_b128 v[188:191], v132 offset:3072
	v_add_u32_e32 v132, s21, v173
	ds_read_b128 v[192:195], v132
	ds_read_b128 v[196:199], v132 offset:1024
	ds_read_b128 v[200:203], v132 offset:2048
	ds_read_b128 v[204:207], v132 offset:3072
	v_cndmask_b32_e32 v243, v165, v163, vcc
	v_cndmask_b32_e32 v242, v164, v162, vcc
	v_lshl_add_u64 v[244:245], s[74:75], 0, v[154:155]
	s_add_i32 m0, s61, 0xc000
	ds_read_b128 v[210:213], v175
	ds_read_b128 v[214:217], v175 offset:1024
	ds_read_b128 v[218:221], v175 offset:2048
	ds_read_b128 v[222:225], v175 offset:3072
	ds_read_b128 v[226:229], v175 offset:4096
	ds_read_b128 v[230:233], v175 offset:5120
	ds_read_b128 v[234:237], v175 offset:6144
	ds_read_b128 v[238:241], v175 offset:7168
	global_load_lds_dwordx4 v[244:245], off
	v_lshl_add_u64 v[244:245], s[74:75], 0, v[156:157]
	s_add_i32 m0, s61, 0xe000
	s_nop 0
	global_load_lds_dwordx4 v[244:245], off
	s_waitcnt vmcnt(8)
	s_waitcnt lgkmcnt(0)
	s_setprio 1
	s_barrier
	v_mfma_f32_16x16x32_bf16 v[126:129], v[176:179], v[210:213], v[126:129]
	v_mfma_f32_16x16x32_bf16 v[122:125], v[184:187], v[210:213], v[122:125]
	v_mfma_f32_16x16x32_bf16 v[118:121], v[176:179], v[218:221], v[118:121]
	v_mfma_f32_16x16x32_bf16 v[114:117], v[184:187], v[218:221], v[114:117]
	v_mfma_f32_16x16x32_bf16 v[106:109], v[176:179], v[226:229], v[106:109]
	v_mfma_f32_16x16x32_bf16 v[98:101], v[184:187], v[226:229], v[98:101]
	v_mfma_f32_16x16x32_bf16 v[78:81], v[176:179], v[234:237], v[78:81]
	v_mfma_f32_16x16x32_bf16 v[74:77], v[184:187], v[234:237], v[74:77]
	v_mfma_f32_16x16x32_bf16 v[126:129], v[180:183], v[214:217], v[126:129]
	v_mfma_f32_16x16x32_bf16 v[122:125], v[188:191], v[214:217], v[122:125]
	v_mfma_f32_16x16x32_bf16 v[118:121], v[180:183], v[222:225], v[118:121]
	v_mfma_f32_16x16x32_bf16 v[114:117], v[188:191], v[222:225], v[114:117]
	v_mfma_f32_16x16x32_bf16 v[106:109], v[180:183], v[230:233], v[106:109]
	v_mfma_f32_16x16x32_bf16 v[98:101], v[188:191], v[230:233], v[98:101]
	v_mfma_f32_16x16x32_bf16 v[78:81], v[180:183], v[238:241], v[78:81]
	v_mfma_f32_16x16x32_bf16 v[74:77], v[188:191], v[238:241], v[74:77]
	s_setprio 0
	s_setprio 1
	v_mfma_f32_16x16x32_bf16 v[110:113], v[192:195], v[210:213], v[110:113]
	v_mfma_f32_16x16x32_bf16 v[102:105], v[200:203], v[210:213], v[102:105]
	v_mfma_f32_16x16x32_bf16 v[94:97], v[192:195], v[218:221], v[94:97]
	v_mfma_f32_16x16x32_bf16 v[90:93], v[200:203], v[218:221], v[90:93]
	v_mfma_f32_16x16x32_bf16 v[86:89], v[192:195], v[226:229], v[86:89]
	v_mfma_f32_16x16x32_bf16 v[82:85], v[200:203], v[226:229], v[82:85]
	v_mfma_f32_16x16x32_bf16 v[70:73], v[192:195], v[234:237], v[70:73]
	v_mfma_f32_16x16x32_bf16 v[66:69], v[200:203], v[234:237], v[66:69]
	v_mfma_f32_16x16x32_bf16 v[110:113], v[196:199], v[214:217], v[110:113]
	v_mfma_f32_16x16x32_bf16 v[102:105], v[204:207], v[214:217], v[102:105]
	v_mfma_f32_16x16x32_bf16 v[94:97], v[196:199], v[222:225], v[94:97]
	v_mfma_f32_16x16x32_bf16 v[90:93], v[204:207], v[222:225], v[90:93]
	v_mfma_f32_16x16x32_bf16 v[86:89], v[196:199], v[230:233], v[86:89]
	v_mfma_f32_16x16x32_bf16 v[82:85], v[204:207], v[230:233], v[82:85]
	v_mfma_f32_16x16x32_bf16 v[70:73], v[196:199], v[238:241], v[70:73]
	v_mfma_f32_16x16x32_bf16 v[66:69], v[204:207], v[238:241], v[66:69]
	s_barrier
	s_setprio 0
	s_add_i32 s20, s20, s60
	v_lshl_add_u64 v[244:245], v[242:243], 0, v[140:141]
	s_mov_b32 m0, s20
	ds_read_b128 v[210:213], v175 offset:16384
	ds_read_b128 v[214:217], v175 offset:17408
	ds_read_b128 v[218:221], v175 offset:18432
	ds_read_b128 v[222:225], v175 offset:19456
	ds_read_b128 v[226:229], v175 offset:20480
	ds_read_b128 v[230:233], v175 offset:21504
	ds_read_b128 v[234:237], v175 offset:22528
	ds_read_b128 v[238:241], v175 offset:23552
	global_load_lds_dwordx4 v[244:245], off
	v_lshl_add_u64 v[246:247], v[242:243], 0, v[144:145]
	s_add_i32 m0, s20, 0x2000
	v_lshl_add_u64 v[248:249], v[242:243], 0, s[82:83]
	s_add_i32 s20, s21, s60
	global_load_lds_dwordx4 v[246:247], off
	v_lshl_add_u64 v[250:251], v[248:249], 0, v[140:141]
	s_mov_b32 m0, s20
	v_lshl_add_u64 v[248:249], v[248:249], 0, v[144:145]
	global_load_lds_dwordx4 v[250:251], off
	s_add_i32 m0, s20, 0x2000
	v_lshl_add_u64 v[250:251], s[80:81], 0, v[142:143]
	global_load_lds_dwordx4 v[248:249], off
	v_lshl_add_u64 v[248:249], s[80:81], 0, v[138:139]
	s_mov_b32 m0, s61
	s_nop 0
	global_load_lds_dwordx4 v[248:249], off
	s_mov_b32 m0, s62
	s_nop 0
	global_load_lds_dwordx4 v[250:251], off
	s_waitcnt vmcnt(8)
	s_waitcnt lgkmcnt(0)
	s_setprio 1
	s_barrier
; #define PG8_STAGE(bufoff, gbase, voff) do { _Pragma("unroll") for (int _i = 0; _i < 2; ++_i) \
;         __builtin_amdgcn_global_load_lds((const unsigned*)((const char*)(gbase) + (voff)[_i]), (PG8_LAS unsigned*)(lds + (bufoff) + ldsw + _i * 8192), 16, 0, 0); } while (0)
; #define PG8_LDA(dst, b, h) do { _Pragma("unroll") for (int m = 0; m < 4; ++m) _Pragma("unroll") for (int k = 0; k < 2; ++k) dst[m][k] = *(const PG8_LAS bf16x8*)(lds + PG8_SA(b, h) + aoff + m * 2048 + k * 1024); } while (0)
; #define PG8_LDB(dst, b, h) do { _Pragma("unroll") for (int n = 0; n < 2; ++n) _Pragma("unroll") for (int k = 0; k < 2; ++k) dst[n][k] = *(const PG8_LAS bf16x8*)(lds + PG8_SB(b, h) + boff + n * 2048 + k * 1024); } while (0)
; #define PG8_MMA(ai, bj, At, Bt) do { __builtin_amdgcn_s_setprio(1); _Pragma("unroll") for (int m = 0; m < 4; ++m) _Pragma("unroll") for (int n = 0; n < 2; ++n) _Pragma("unroll") for (int k = 0; k < 2; ++k) \
;         acc[ai][bj][m][n] = __builtin_amdgcn_mfma_f32_16x16x32_bf16(Bt[n][k], At[m][k], acc[ai][bj][m][n], 0, 0, 0); __builtin_amdgcn_s_setprio(0); } while (0)
; #define PG8_WAIT_V(n) asm volatile("s_waitcnt vmcnt(" #n ")" ::: "memory")
; #define PG8_WAIT_L(n) asm volatile("s_waitcnt lgkmcnt(" #n ")" ::: "memory")
; #define PG8_BAR __builtin_amdgcn_s_barrier()
; #define PG8_SCHED __builtin_amdgcn_sched_barrier(0)
;     ...
;             PG8_WAIT_V(8); PG8_WAIT_L(0); PG8_BAR; PG8_MMA(1, 0, At, B0); PG8_MMA(1, 1, At, B1); PG8_BAR; PG8_SCHED;
;             PG8_LDB(B0, 1, 0); PG8_LDB(B1, 1, 1); PG8_SCHED; PG8_LDA(At, 1, 0); PG8_STAGE(PG8_SA(0, 1), a2 + hstep, voffA);
;             PG8_WAIT_V(8); PG8_WAIT_L(0); PG8_BAR; PG8_MMA(0, 0, At, B0); PG8_MMA(0, 1, At, B1); PG8_BAR; PG8_SCHED;
	v_mfma_f32_16x16x32_bf16 v[62:65], v[176:179], v[210:213], v[62:65]
	v_mfma_f32_16x16x32_bf16 v[58:61], v[184:187], v[210:213], v[58:61]
	v_mfma_f32_16x16x32_bf16 v[54:57], v[176:179], v[218:221], v[54:57]
	v_mfma_f32_16x16x32_bf16 v[46:49], v[184:187], v[218:221], v[46:49]
	v_mfma_f32_16x16x32_bf16 v[38:41], v[176:179], v[226:229], v[38:41]
	v_mfma_f32_16x16x32_bf16 v[30:33], v[184:187], v[226:229], v[30:33]
	v_mfma_f32_16x16x32_bf16 v[22:25], v[176:179], v[234:237], v[22:25]
	v_mfma_f32_16x16x32_bf16 v[14:17], v[184:187], v[234:237], v[14:17]
	v_mfma_f32_16x16x32_bf16 v[62:65], v[180:183], v[214:217], v[62:65]
	v_mfma_f32_16x16x32_bf16 v[58:61], v[188:191], v[214:217], v[58:61]
	v_mfma_f32_16x16x32_bf16 v[54:57], v[180:183], v[222:225], v[54:57]
	v_mfma_f32_16x16x32_bf16 v[46:49], v[188:191], v[222:225], v[46:49]
	v_mfma_f32_16x16x32_bf16 v[38:41], v[180:183], v[230:233], v[38:41]
	v_mfma_f32_16x16x32_bf16 v[30:33], v[188:191], v[230:233], v[30:33]
	v_mfma_f32_16x16x32_bf16 v[22:25], v[180:183], v[238:241], v[22:25]
	v_mfma_f32_16x16x32_bf16 v[14:17], v[188:191], v[238:241], v[14:17]
	s_setprio 0
	s_setprio 1
	v_mfma_f32_16x16x32_bf16 v[50:53], v[192:195], v[210:213], v[50:53]
	v_mfma_f32_16x16x32_bf16 v[42:45], v[200:203], v[210:213], v[42:45]
	v_mfma_f32_16x16x32_bf16 v[34:37], v[192:195], v[218:221], v[34:37]
	v_mfma_f32_16x16x32_bf16 v[26:29], v[200:203], v[218:221], v[26:29]
	v_mfma_f32_16x16x32_bf16 v[18:21], v[192:195], v[226:229], v[18:21]
	v_mfma_f32_16x16x32_bf16 v[10:13], v[200:203], v[226:229], v[10:13]
	v_mfma_f32_16x16x32_bf16 v[6:9], v[192:195], v[234:237], v[6:9]
	v_mfma_f32_16x16x32_bf16 v[2:5], v[200:203], v[234:237], v[2:5]
	v_mfma_f32_16x16x32_bf16 v[50:53], v[196:199], v[214:217], v[50:53]
	v_mfma_f32_16x16x32_bf16 v[42:45], v[204:207], v[214:217], v[42:45]
	v_mfma_f32_16x16x32_bf16 v[34:37], v[196:199], v[222:225], v[34:37]
	v_mfma_f32_16x16x32_bf16 v[26:29], v[204:207], v[222:225], v[26:29]
	v_mfma_f32_16x16x32_bf16 v[18:21], v[196:199], v[230:233], v[18:21]
	v_mfma_f32_16x16x32_bf16 v[10:13], v[204:207], v[230:233], v[10:13]
	v_mfma_f32_16x16x32_bf16 v[6:9], v[196:199], v[238:241], v[6:9]
	v_mfma_f32_16x16x32_bf16 v[2:5], v[204:207], v[238:241], v[2:5]
	s_barrier
	s_setprio 0
	s_add_i32 s20, 0, 0x18000
	v_add_u32_e32 v132, s20, v173
	s_add_i32 s21, 0, 0x1c000
	ds_read_b128 v[176:179], v132
	ds_read_b128 v[180:183], v132 offset:1024
	ds_read_b128 v[184:187], v132 offset:2048
	ds_read_b128 v[188:191], v132 offset:3072
	v_add_u32_e32 v132, s21, v173
	ds_read_b128 v[192:195], v132
	ds_read_b128 v[196:199], v132 offset:1024
	ds_read_b128 v[200:203], v132 offset:2048
	ds_read_b128 v[204:207], v132 offset:3072
	s_add_u32 s46, s80, 0xe0000
	s_addc_u32 s47, s81, 0
	s_mov_b32 m0, s63
	v_lshl_add_u64 v[208:209], s[46:47], 0, v[138:139]
	ds_read_b128 v[210:213], v175 offset:32768
	ds_read_b128 v[214:217], v175 offset:33792
	ds_read_b128 v[218:221], v175 offset:34816
	ds_read_b128 v[222:225], v175 offset:35840
	ds_read_b128 v[226:229], v175 offset:36864
	ds_read_b128 v[230:233], v175 offset:37888
	ds_read_b128 v[234:237], v175 offset:38912
	ds_read_b128 v[238:241], v175 offset:39936
	global_load_lds_dwordx4 v[208:209], off
	v_lshl_add_u64 v[208:209], s[46:47], 0, v[142:143]
	s_mov_b32 m0, s92
	s_nop 0
	global_load_lds_dwordx4 v[208:209], off
	s_waitcnt vmcnt(8)
	s_waitcnt lgkmcnt(0)
	s_setprio 1
	s_barrier
	v_mfma_f32_16x16x32_bf16 v[126:129], v[176:179], v[210:213], v[126:129]
	v_mfma_f32_16x16x32_bf16 v[122:125], v[184:187], v[210:213], v[122:125]
	v_mfma_f32_16x16x32_bf16 v[118:121], v[176:179], v[218:221], v[118:121]
	v_mfma_f32_16x16x32_bf16 v[114:117], v[184:187], v[218:221], v[114:117]
	v_mfma_f32_16x16x32_bf16 v[106:109], v[176:179], v[226:229], v[106:109]
	v_mfma_f32_16x16x32_bf16 v[98:101], v[184:187], v[226:229], v[98:101]
	v_mfma_f32_16x16x32_bf16 v[78:81], v[176:179], v[234:237], v[78:81]
	v_mfma_f32_16x16x32_bf16 v[74:77], v[184:187], v[234:237], v[74:77]
	v_mfma_f32_16x16x32_bf16 v[126:129], v[180:183], v[214:217], v[126:129]
	v_mfma_f32_16x16x32_bf16 v[122:125], v[188:191], v[214:217], v[122:125]
	v_mfma_f32_16x16x32_bf16 v[118:121], v[180:183], v[222:225], v[118:121]
	v_mfma_f32_16x16x32_bf16 v[114:117], v[188:191], v[222:225], v[114:117]
	v_mfma_f32_16x16x32_bf16 v[106:109], v[180:183], v[230:233], v[106:109]
	v_mfma_f32_16x16x32_bf16 v[98:101], v[188:191], v[230:233], v[98:101]
	v_mfma_f32_16x16x32_bf16 v[78:81], v[180:183], v[238:241], v[78:81]
	v_mfma_f32_16x16x32_bf16 v[74:77], v[188:191], v[238:241], v[74:77]
	s_setprio 0
	s_setprio 1
	v_mfma_f32_16x16x32_bf16 v[110:113], v[192:195], v[210:213], v[110:113]
	v_mfma_f32_16x16x32_bf16 v[102:105], v[200:203], v[210:213], v[102:105]
	v_mfma_f32_16x16x32_bf16 v[94:97], v[192:195], v[218:221], v[94:97]
	v_mfma_f32_16x16x32_bf16 v[90:93], v[200:203], v[218:221], v[90:93]
	v_mfma_f32_16x16x32_bf16 v[86:89], v[192:195], v[226:229], v[86:89]
	v_mfma_f32_16x16x32_bf16 v[82:85], v[200:203], v[226:229], v[82:85]
	v_mfma_f32_16x16x32_bf16 v[70:73], v[192:195], v[234:237], v[70:73]
	v_mfma_f32_16x16x32_bf16 v[66:69], v[200:203], v[234:237], v[66:69]
	v_mfma_f32_16x16x32_bf16 v[110:113], v[196:199], v[214:217], v[110:113]
	v_mfma_f32_16x16x32_bf16 v[102:105], v[204:207], v[214:217], v[102:105]
	v_mfma_f32_16x16x32_bf16 v[94:97], v[196:199], v[222:225], v[94:97]
	v_mfma_f32_16x16x32_bf16 v[90:93], v[204:207], v[222:225], v[90:93]
	v_mfma_f32_16x16x32_bf16 v[86:89], v[196:199], v[230:233], v[86:89]
	v_mfma_f32_16x16x32_bf16 v[82:85], v[204:207], v[230:233], v[82:85]
	v_mfma_f32_16x16x32_bf16 v[70:73], v[196:199], v[238:241], v[70:73]
	v_mfma_f32_16x16x32_bf16 v[66:69], v[204:207], v[238:241], v[66:69]
	s_barrier
; #define PG8_STAGE(bufoff, gbase, voff) do { _Pragma("unroll") for (int _i = 0; _i < 2; ++_i) \
;         __builtin_amdgcn_global_load_lds((const unsigned*)((const char*)(gbase) + (voff)[_i]), (PG8_LAS unsigned*)(lds + (bufoff) + ldsw + _i * 8192), 16, 0, 0); } while (0)
; #define PG8_LDA(dst, b, h) do { _Pragma("unroll") for (int m = 0; m < 4; ++m) _Pragma("unroll") for (int k = 0; k < 2; ++k) dst[m][k] = *(const PG8_LAS bf16x8*)(lds + PG8_SA(b, h) + aoff + m * 2048 + k * 1024); } while (0)
; #define PG8_MMA(ai, bj, At, Bt) do { __builtin_amdgcn_s_setprio(1); _Pragma("unroll") for (int m = 0; m < 4; ++m) _Pragma("unroll") for (int n = 0; n < 2; ++n) _Pragma("unroll") for (int k = 0; k < 2; ++k) \
;         acc[ai][bj][m][n] = __builtin_amdgcn_mfma_f32_16x16x32_bf16(Bt[n][k], At[m][k], acc[ai][bj][m][n], 0, 0, 0); __builtin_amdgcn_s_setprio(0); } while (0)
; #define PG8_WAIT_V(n) asm volatile("s_waitcnt vmcnt(" #n ")" ::: "memory")
; #define PG8_WAIT_L(n) asm volatile("s_waitcnt lgkmcnt(" #n ")" ::: "memory")
; #define PG8_BAR __builtin_amdgcn_s_barrier()
; #define PG8_SCHED __builtin_amdgcn_sched_barrier(0)
;     ...
;             PG8_LDA(At, 1, 1); PG8_STAGE(PG8_SB(1, 0), b3, voffB); PG8_STAGE(PG8_SB(1, 1), b3 + hstep, voffB); PG8_STAGE(PG8_SA(1, 0), a3, voffA);
;             PG8_WAIT_V(8); PG8_WAIT_L(0); PG8_BAR; PG8_MMA(1, 0, At, B0); PG8_MMA(1, 1, At, B1); PG8_BAR; PG8_SCHED;
;         }
;         if constexpr (ALIGN_EPI) { if (wr == 0) PG8_BAR; }
;         E(acc, cur, wr, wc, fr, fq); S.done(cur);
;         if (!has_next) break;
	s_setprio 0
	s_add_i32 s20, s20, s60
	v_lshl_add_u64 v[208:209], v[244:245], 0, s[84:85]
	s_mov_b32 m0, s20
	ds_read_b128 v[210:213], v175 offset:49152
	ds_read_b128 v[214:217], v175 offset:50176
	ds_read_b128 v[218:221], v175 offset:51200
	ds_read_b128 v[222:225], v175 offset:52224
	ds_read_b128 v[226:229], v175 offset:53248
	ds_read_b128 v[230:233], v175 offset:54272
	ds_read_b128 v[234:237], v175 offset:55296
	ds_read_b128 v[238:241], v175 offset:56320
	global_load_lds_dwordx4 v[208:209], off
	v_lshl_add_u64 v[208:209], v[246:247], 0, s[84:85]
	s_add_i32 m0, s20, 0x2000
	s_add_i32 s20, s21, s60
	global_load_lds_dwordx4 v[208:209], off
	v_lshl_add_u64 v[208:209], v[242:243], 0, s[86:87]
	v_lshl_add_u64 v[242:243], v[208:209], 0, v[140:141]
	s_mov_b32 m0, s20
	v_lshl_add_u64 v[208:209], v[208:209], 0, v[144:145]
	global_load_lds_dwordx4 v[242:243], off
	s_add_i32 m0, s20, 0x2000
	s_nop 0
	global_load_lds_dwordx4 v[208:209], off
	v_lshl_add_u64 v[208:209], v[248:249], 0, s[84:85]
	s_mov_b32 m0, s93
	s_nop 0
	global_load_lds_dwordx4 v[208:209], off
	v_lshl_add_u64 v[208:209], v[250:251], 0, s[84:85]
	s_mov_b32 m0, s57
	s_nop 0
	global_load_lds_dwordx4 v[208:209], off
	s_waitcnt vmcnt(8)
	s_waitcnt lgkmcnt(0)
	s_setprio 1
	s_barrier
	v_mfma_f32_16x16x32_bf16 v[62:65], v[176:179], v[210:213], v[62:65]
	v_mfma_f32_16x16x32_bf16 v[58:61], v[184:187], v[210:213], v[58:61]
	v_mfma_f32_16x16x32_bf16 v[54:57], v[176:179], v[218:221], v[54:57]
	v_mfma_f32_16x16x32_bf16 v[46:49], v[184:187], v[218:221], v[46:49]
	v_mfma_f32_16x16x32_bf16 v[38:41], v[176:179], v[226:229], v[38:41]
	v_mfma_f32_16x16x32_bf16 v[30:33], v[184:187], v[226:229], v[30:33]
	v_mfma_f32_16x16x32_bf16 v[22:25], v[176:179], v[234:237], v[22:25]
	v_mfma_f32_16x16x32_bf16 v[14:17], v[184:187], v[234:237], v[14:17]
	v_mfma_f32_16x16x32_bf16 v[62:65], v[180:183], v[214:217], v[62:65]
	v_mfma_f32_16x16x32_bf16 v[58:61], v[188:191], v[214:217], v[58:61]
	v_mfma_f32_16x16x32_bf16 v[54:57], v[180:183], v[222:225], v[54:57]
	v_mfma_f32_16x16x32_bf16 v[46:49], v[188:191], v[222:225], v[46:49]
	v_mfma_f32_16x16x32_bf16 v[38:41], v[180:183], v[230:233], v[38:41]
	v_mfma_f32_16x16x32_bf16 v[30:33], v[188:191], v[230:233], v[30:33]
	v_mfma_f32_16x16x32_bf16 v[22:25], v[180:183], v[238:241], v[22:25]
	v_mfma_f32_16x16x32_bf16 v[14:17], v[188:191], v[238:241], v[14:17]
	s_setprio 0
	s_setprio 1
	v_mfma_f32_16x16x32_bf16 v[50:53], v[192:195], v[210:213], v[50:53]
	v_mfma_f32_16x16x32_bf16 v[42:45], v[200:203], v[210:213], v[42:45]
	v_mfma_f32_16x16x32_bf16 v[34:37], v[192:195], v[218:221], v[34:37]
	v_mfma_f32_16x16x32_bf16 v[26:29], v[200:203], v[218:221], v[26:29]
	v_mfma_f32_16x16x32_bf16 v[18:21], v[192:195], v[226:229], v[18:21]
	v_mfma_f32_16x16x32_bf16 v[10:13], v[200:203], v[226:229], v[10:13]
	v_mfma_f32_16x16x32_bf16 v[6:9], v[192:195], v[234:237], v[6:9]
	v_mfma_f32_16x16x32_bf16 v[2:5], v[200:203], v[234:237], v[2:5]
	v_mfma_f32_16x16x32_bf16 v[50:53], v[196:199], v[214:217], v[50:53]
	v_mfma_f32_16x16x32_bf16 v[42:45], v[204:207], v[214:217], v[42:45]
	v_mfma_f32_16x16x32_bf16 v[34:37], v[196:199], v[222:225], v[34:37]
	v_mfma_f32_16x16x32_bf16 v[26:29], v[204:207], v[222:225], v[26:29]
	v_mfma_f32_16x16x32_bf16 v[18:21], v[196:199], v[230:233], v[18:21]
	v_mfma_f32_16x16x32_bf16 v[10:13], v[204:207], v[230:233], v[10:13]
	v_mfma_f32_16x16x32_bf16 v[6:9], v[196:199], v[238:241], v[6:9]
	v_mfma_f32_16x16x32_bf16 v[2:5], v[204:207], v[238:241], v[2:5]
	s_barrier
	s_setprio 0
	s_add_i32 s19, s19, 2
	s_add_u32 s74, s74, 0x100
	s_addc_u32 s75, s75, 0
	s_cmp_gt_u32 s19, 53
	v_lshl_add_u64 v[164:165], v[164:165], 0, s[88:89]
	s_cbranch_scc0 .LBB0_2242
	s_and_b64 vcc, exec, s[70:71]
	s_cbranch_vccz .LBB0_2245
	s_barrier

; #define PG8_STAGE(bufoff, gbase, voff) do { _Pragma("unroll") for (int _i = 0; _i < 2; ++_i) \
;         __builtin_amdgcn_global_load_lds((const unsigned*)((const char*)(gbase) + (voff)[_i]), (PG8_LAS unsigned*)(lds + (bufoff) + ldsw + _i * 8192), 16, 0, 0); } while (0)
; #define PG8_LDA(dst, b, h) do { _Pragma("unroll") for (int m = 0; m < 4; ++m) _Pragma("unroll") for (int k = 0; k < 2; ++k) dst[m][k] = *(const PG8_LAS bf16x8*)(lds + PG8_SA(b, h) + aoff + m * 2048 + k * 1024); } while (0)
; #define PG8_LDB(dst, b, h) do { _Pragma("unroll") for (int n = 0; n < 2; ++n) _Pragma("unroll") for (int k = 0; k < 2; ++k) dst[n][k] = *(const PG8_LAS bf16x8*)(lds + PG8_SB(b, h) + boff + n * 2048 + k * 1024); } while (0)
; #define PG8_MMA(ai, bj, At, Bt) do { __builtin_amdgcn_s_setprio(1); _Pragma("unroll") for (int m = 0; m < 4; ++m) _Pragma("unroll") for (int n = 0; n < 2; ++n) _Pragma("unroll") for (int k = 0; k < 2; ++k) \
;         acc[ai][bj][m][n] = __builtin_amdgcn_mfma_f32_16x16x32_bf16(Bt[n][k], At[m][k], acc[ai][bj][m][n], 0, 0, 0); __builtin_amdgcn_s_setprio(0); } while (0)
; #define PG8_WAIT_V(n) asm volatile("s_waitcnt vmcnt(" #n ")" ::: "memory")
; #define PG8_WAIT_L(n) asm volatile("s_waitcnt lgkmcnt(" #n ")" ::: "memory")
; #define PG8_BAR __builtin_amdgcn_s_barrier()
; #define PG8_SCHED __builtin_amdgcn_sched_barrier(0)
;     ...
;         for (int t = 0; t < nt; t += 2) {
;             const bool last = (t == nt - 2);
;             const char* a1 = cA + (size_t)(t + 1) * kstep;
;             const char* a2 = last ? nA : cA + (size_t)(t + 2) * kstep; const char* b2 = last ? nB : cB + (size_t)(t + 2) * kstep;
;             const char* a3 = a2 + kstep; const char* b3 = b2 + kstep;
;             if (last && has_next) S.a_ready(nxt);
;             PG8_LDB(B0, 0, 0); PG8_LDB(B1, 0, 1); PG8_SCHED; PG8_LDA(At, 0, 0); PG8_STAGE(PG8_SA(1, 1), a1 + hstep, voffA);
;             PG8_WAIT_V(8); PG8_WAIT_L(0); PG8_BAR; PG8_MMA(0, 0, At, B0); PG8_MMA(0, 1, At, B1); PG8_BAR; PG8_SCHED;
;             PG8_LDA(At, 0, 1); PG8_STAGE(PG8_SB(0, 0), b2, voffB); PG8_STAGE(PG8_SB(0, 1), b2 + hstep, voffB); PG8_STAGE(PG8_SA(0, 0), a2, voffA);
.LBB0_2271:
	s_add_u32 s18, s92, 0xfffc0080
	s_addc_u32 s19, s93, -1
	s_add_i32 s20, 0, 0x10000
	s_cmp_eq_u32 s17, 12
	s_cselect_b32 s47, s15, s19
	s_cselect_b32 s46, s16, s18
	v_add_u32_e32 v132, s20, v173
	s_cselect_b64 vcc, -1, 0
	s_add_i32 s18, 0, 0x14000
	ds_read_b128 v[176:179], v132
	ds_read_b128 v[180:183], v132 offset:1024
	ds_read_b128 v[184:187], v132 offset:2048
	ds_read_b128 v[188:191], v132 offset:3072
	v_add_u32_e32 v132, s18, v173
	ds_read_b128 v[192:195], v132
	ds_read_b128 v[196:199], v132 offset:1024
	ds_read_b128 v[200:203], v132 offset:2048
	ds_read_b128 v[204:207], v132 offset:3072
	v_cndmask_b32_e32 v209, v165, v163, vcc
	v_cndmask_b32_e32 v208, v164, v162, vcc
	v_lshl_add_u64 v[242:243], s[92:93], 0, v[158:159]
	s_add_i32 m0, s58, 0xc000
	ds_read_b128 v[210:213], v175
	ds_read_b128 v[214:217], v175 offset:1024
	ds_read_b128 v[218:221], v175 offset:2048
	ds_read_b128 v[222:225], v175 offset:3072
	ds_read_b128 v[226:229], v175 offset:4096
	ds_read_b128 v[230:233], v175 offset:5120
	ds_read_b128 v[234:237], v175 offset:6144
	ds_read_b128 v[238:241], v175 offset:7168
	global_load_lds_dwordx4 v[242:243], off
	v_lshl_add_u64 v[242:243], s[92:93], 0, v[160:161]
	s_add_i32 m0, s58, 0xe000
	s_nop 0
	global_load_lds_dwordx4 v[242:243], off
	s_waitcnt vmcnt(8)
	s_waitcnt lgkmcnt(0)
	s_setprio 1
	s_barrier
	v_mfma_f32_16x16x32_bf16 v[126:129], v[176:179], v[210:213], v[126:129]
	v_mfma_f32_16x16x32_bf16 v[122:125], v[184:187], v[210:213], v[122:125]
	v_mfma_f32_16x16x32_bf16 v[110:113], v[176:179], v[218:221], v[110:113]
	v_mfma_f32_16x16x32_bf16 v[106:109], v[184:187], v[218:221], v[106:109]
	v_mfma_f32_16x16x32_bf16 v[94:97], v[176:179], v[226:229], v[94:97]
	v_mfma_f32_16x16x32_bf16 v[90:93], v[184:187], v[226:229], v[90:93]
	v_mfma_f32_16x16x32_bf16 v[78:81], v[176:179], v[234:237], v[78:81]
	v_mfma_f32_16x16x32_bf16 v[74:77], v[184:187], v[234:237], v[74:77]
	v_mfma_f32_16x16x32_bf16 v[126:129], v[180:183], v[214:217], v[126:129]
	v_mfma_f32_16x16x32_bf16 v[122:125], v[188:191], v[214:217], v[122:125]
	v_mfma_f32_16x16x32_bf16 v[110:113], v[180:183], v[222:225], v[110:113]
	v_mfma_f32_16x16x32_bf16 v[106:109], v[188:191], v[222:225], v[106:109]
	v_mfma_f32_16x16x32_bf16 v[94:97], v[180:183], v[230:233], v[94:97]
	v_mfma_f32_16x16x32_bf16 v[90:93], v[188:191], v[230:233], v[90:93]
	v_mfma_f32_16x16x32_bf16 v[78:81], v[180:183], v[238:241], v[78:81]
	v_mfma_f32_16x16x32_bf16 v[74:77], v[188:191], v[238:241], v[74:77]
	s_setprio 0
	s_setprio 1
	v_mfma_f32_16x16x32_bf16 v[118:121], v[192:195], v[210:213], v[118:121]
	v_mfma_f32_16x16x32_bf16 v[114:117], v[200:203], v[210:213], v[114:117]
	v_mfma_f32_16x16x32_bf16 v[102:105], v[192:195], v[218:221], v[102:105]
	v_mfma_f32_16x16x32_bf16 v[98:101], v[200:203], v[218:221], v[98:101]
	v_mfma_f32_16x16x32_bf16 v[86:89], v[192:195], v[226:229], v[86:89]
	v_mfma_f32_16x16x32_bf16 v[82:85], v[200:203], v[226:229], v[82:85]
	v_mfma_f32_16x16x32_bf16 v[70:73], v[192:195], v[234:237], v[70:73]
	v_mfma_f32_16x16x32_bf16 v[66:69], v[200:203], v[234:237], v[66:69]
	v_mfma_f32_16x16x32_bf16 v[118:121], v[196:199], v[214:217], v[118:121]
	v_mfma_f32_16x16x32_bf16 v[114:117], v[204:207], v[214:217], v[114:117]
	v_mfma_f32_16x16x32_bf16 v[102:105], v[196:199], v[222:225], v[102:105]
	v_mfma_f32_16x16x32_bf16 v[98:101], v[204:207], v[222:225], v[98:101]
	v_mfma_f32_16x16x32_bf16 v[86:89], v[196:199], v[230:233], v[86:89]
	v_mfma_f32_16x16x32_bf16 v[82:85], v[204:207], v[230:233], v[82:85]
	v_mfma_f32_16x16x32_bf16 v[70:73], v[196:199], v[238:241], v[70:73]
	v_mfma_f32_16x16x32_bf16 v[66:69], v[204:207], v[238:241], v[66:69]
	s_barrier
	s_setprio 0
	s_add_i32 s19, s20, s57
	v_lshl_add_u64 v[242:243], v[208:209], 0, v[148:149]
	s_mov_b32 m0, s19
	ds_read_b128 v[210:213], v175 offset:16384
	ds_read_b128 v[214:217], v175 offset:17408
	ds_read_b128 v[218:221], v175 offset:18432
	ds_read_b128 v[222:225], v175 offset:19456
	ds_read_b128 v[226:229], v175 offset:20480
	ds_read_b128 v[230:233], v175 offset:21504
	ds_read_b128 v[234:237], v175 offset:22528
	ds_read_b128 v[238:241], v175 offset:23552
	global_load_lds_dwordx4 v[242:243], off
	v_lshl_add_u64 v[244:245], v[208:209], 0, v[152:153]
	s_add_i32 m0, s19, 0x2000
	v_lshl_add_u64 v[246:247], v[208:209], 0, s[90:91]
	s_add_i32 s18, s18, s57
	global_load_lds_dwordx4 v[244:245], off
	v_lshl_add_u64 v[248:249], v[246:247], 0, v[148:149]
	s_mov_b32 m0, s18
	v_lshl_add_u64 v[246:247], v[246:247], 0, v[152:153]
	global_load_lds_dwordx4 v[248:249], off
	s_add_i32 m0, s18, 0x2000
	v_lshl_add_u64 v[248:249], s[46:47], 0, v[150:151]
	global_load_lds_dwordx4 v[246:247], off
	v_lshl_add_u64 v[246:247], s[46:47], 0, v[146:147]
	s_mov_b32 m0, s58
	s_nop 0
	global_load_lds_dwordx4 v[246:247], off
	s_mov_b32 m0, s59
	s_nop 0
	global_load_lds_dwordx4 v[248:249], off
	s_waitcnt vmcnt(8)
	s_waitcnt lgkmcnt(0)
	s_setprio 1
	s_barrier
; #define PG8_STAGE(bufoff, gbase, voff) do { _Pragma("unroll") for (int _i = 0; _i < 2; ++_i) \
;         __builtin_amdgcn_global_load_lds((const unsigned*)((const char*)(gbase) + (voff)[_i]), (PG8_LAS unsigned*)(lds + (bufoff) + ldsw + _i * 8192), 16, 0, 0); } while (0)
; #define PG8_LDA(dst, b, h) do { _Pragma("unroll") for (int m = 0; m < 4; ++m) _Pragma("unroll") for (int k = 0; k < 2; ++k) dst[m][k] = *(const PG8_LAS bf16x8*)(lds + PG8_SA(b, h) + aoff + m * 2048 + k * 1024); } while (0)
; #define PG8_LDB(dst, b, h) do { _Pragma("unroll") for (int n = 0; n < 2; ++n) _Pragma("unroll") for (int k = 0; k < 2; ++k) dst[n][k] = *(const PG8_LAS bf16x8*)(lds + PG8_SB(b, h) + boff + n * 2048 + k * 1024); } while (0)
; #define PG8_MMA(ai, bj, At, Bt) do { __builtin_amdgcn_s_setprio(1); _Pragma("unroll") for (int m = 0; m < 4; ++m) _Pragma("unroll") for (int n = 0; n < 2; ++n) _Pragma("unroll") for (int k = 0; k < 2; ++k) \
;         acc[ai][bj][m][n] = __builtin_amdgcn_mfma_f32_16x16x32_bf16(Bt[n][k], At[m][k], acc[ai][bj][m][n], 0, 0, 0); __builtin_amdgcn_s_setprio(0); } while (0)
; #define PG8_WAIT_V(n) asm volatile("s_waitcnt vmcnt(" #n ")" ::: "memory")
; #define PG8_WAIT_L(n) asm volatile("s_waitcnt lgkmcnt(" #n ")" ::: "memory")
; #define PG8_BAR __builtin_amdgcn_s_barrier()
; #define PG8_SCHED __builtin_amdgcn_sched_barrier(0)
;     ...
;             PG8_WAIT_V(8); PG8_WAIT_L(0); PG8_BAR; PG8_MMA(1, 0, At, B0); PG8_MMA(1, 1, At, B1); PG8_BAR; PG8_SCHED;
;             PG8_LDB(B0, 1, 0); PG8_LDB(B1, 1, 1); PG8_SCHED; PG8_LDA(At, 1, 0); PG8_STAGE(PG8_SA(0, 1), a2 + hstep, voffA);
;             PG8_WAIT_V(8); PG8_WAIT_L(0); PG8_BAR; PG8_MMA(0, 0, At, B0); PG8_MMA(0, 1, At, B1); PG8_BAR; PG8_SCHED;
	v_mfma_f32_16x16x32_bf16 v[62:65], v[176:179], v[210:213], v[62:65]
	v_mfma_f32_16x16x32_bf16 v[58:61], v[184:187], v[210:213], v[58:61]
	v_mfma_f32_16x16x32_bf16 v[46:49], v[176:179], v[218:221], v[46:49]
	v_mfma_f32_16x16x32_bf16 v[42:45], v[184:187], v[218:221], v[42:45]
	v_mfma_f32_16x16x32_bf16 v[30:33], v[176:179], v[226:229], v[30:33]
	v_mfma_f32_16x16x32_bf16 v[26:29], v[184:187], v[226:229], v[26:29]
	v_mfma_f32_16x16x32_bf16 v[14:17], v[176:179], v[234:237], v[14:17]
	v_mfma_f32_16x16x32_bf16 v[10:13], v[184:187], v[234:237], v[10:13]
	v_mfma_f32_16x16x32_bf16 v[62:65], v[180:183], v[214:217], v[62:65]
	v_mfma_f32_16x16x32_bf16 v[58:61], v[188:191], v[214:217], v[58:61]
	v_mfma_f32_16x16x32_bf16 v[46:49], v[180:183], v[222:225], v[46:49]
	v_mfma_f32_16x16x32_bf16 v[42:45], v[188:191], v[222:225], v[42:45]
	v_mfma_f32_16x16x32_bf16 v[30:33], v[180:183], v[230:233], v[30:33]
	v_mfma_f32_16x16x32_bf16 v[26:29], v[188:191], v[230:233], v[26:29]
	v_mfma_f32_16x16x32_bf16 v[14:17], v[180:183], v[238:241], v[14:17]
	v_mfma_f32_16x16x32_bf16 v[10:13], v[188:191], v[238:241], v[10:13]
	s_setprio 0
	s_setprio 1
	v_mfma_f32_16x16x32_bf16 v[54:57], v[192:195], v[210:213], v[54:57]
	v_mfma_f32_16x16x32_bf16 v[50:53], v[200:203], v[210:213], v[50:53]
	v_mfma_f32_16x16x32_bf16 v[38:41], v[192:195], v[218:221], v[38:41]
	v_mfma_f32_16x16x32_bf16 v[34:37], v[200:203], v[218:221], v[34:37]
	v_mfma_f32_16x16x32_bf16 v[22:25], v[192:195], v[226:229], v[22:25]
	v_mfma_f32_16x16x32_bf16 v[18:21], v[200:203], v[226:229], v[18:21]
	v_mfma_f32_16x16x32_bf16 v[6:9], v[192:195], v[234:237], v[6:9]
	v_mfma_f32_16x16x32_bf16 v[2:5], v[200:203], v[234:237], v[2:5]
	v_mfma_f32_16x16x32_bf16 v[54:57], v[196:199], v[214:217], v[54:57]
	v_mfma_f32_16x16x32_bf16 v[50:53], v[204:207], v[214:217], v[50:53]
	v_mfma_f32_16x16x32_bf16 v[38:41], v[196:199], v[222:225], v[38:41]
	v_mfma_f32_16x16x32_bf16 v[34:37], v[204:207], v[222:225], v[34:37]
	v_mfma_f32_16x16x32_bf16 v[22:25], v[196:199], v[230:233], v[22:25]
	v_mfma_f32_16x16x32_bf16 v[18:21], v[204:207], v[230:233], v[18:21]
	v_mfma_f32_16x16x32_bf16 v[6:9], v[196:199], v[238:241], v[6:9]
	v_mfma_f32_16x16x32_bf16 v[2:5], v[204:207], v[238:241], v[2:5]
	s_barrier
	s_setprio 0
	s_add_i32 s20, 0, 0x18000
	v_add_u32_e32 v132, s20, v173
	s_add_i32 s21, 0, 0x1c000
	ds_read_b128 v[176:179], v132
	ds_read_b128 v[180:183], v132 offset:1024
	ds_read_b128 v[184:187], v132 offset:2048
	ds_read_b128 v[188:191], v132 offset:3072
	v_add_u32_e32 v132, s21, v173
	ds_read_b128 v[192:195], v132
	ds_read_b128 v[196:199], v132 offset:1024
	ds_read_b128 v[200:203], v132 offset:2048
	ds_read_b128 v[204:207], v132 offset:3072
	s_add_u32 s18, s46, 0x40000
	s_addc_u32 s19, s47, 0
	s_mov_b32 m0, s60
	v_lshl_add_u64 v[250:251], s[18:19], 0, v[146:147]
	ds_read_b128 v[210:213], v175 offset:32768
	ds_read_b128 v[214:217], v175 offset:33792
	ds_read_b128 v[218:221], v175 offset:34816
	ds_read_b128 v[222:225], v175 offset:35840
	ds_read_b128 v[226:229], v175 offset:36864
	ds_read_b128 v[230:233], v175 offset:37888
	ds_read_b128 v[234:237], v175 offset:38912
	ds_read_b128 v[238:241], v175 offset:39936
	global_load_lds_dwordx4 v[250:251], off
	v_lshl_add_u64 v[250:251], s[18:19], 0, v[150:151]
	s_mov_b32 m0, s61
	s_nop 0
	global_load_lds_dwordx4 v[250:251], off
	s_waitcnt vmcnt(8)
	s_waitcnt lgkmcnt(0)
	s_setprio 1
	s_barrier
	v_mfma_f32_16x16x32_bf16 v[126:129], v[176:179], v[210:213], v[126:129]
	v_mfma_f32_16x16x32_bf16 v[122:125], v[184:187], v[210:213], v[122:125]
	v_mfma_f32_16x16x32_bf16 v[110:113], v[176:179], v[218:221], v[110:113]
	v_mfma_f32_16x16x32_bf16 v[106:109], v[184:187], v[218:221], v[106:109]
	v_mfma_f32_16x16x32_bf16 v[94:97], v[176:179], v[226:229], v[94:97]
	v_mfma_f32_16x16x32_bf16 v[90:93], v[184:187], v[226:229], v[90:93]
	v_mfma_f32_16x16x32_bf16 v[78:81], v[176:179], v[234:237], v[78:81]
	v_mfma_f32_16x16x32_bf16 v[74:77], v[184:187], v[234:237], v[74:77]
	v_mfma_f32_16x16x32_bf16 v[126:129], v[180:183], v[214:217], v[126:129]
	v_mfma_f32_16x16x32_bf16 v[122:125], v[188:191], v[214:217], v[122:125]
	v_mfma_f32_16x16x32_bf16 v[110:113], v[180:183], v[222:225], v[110:113]
	v_mfma_f32_16x16x32_bf16 v[106:109], v[188:191], v[222:225], v[106:109]
	v_mfma_f32_16x16x32_bf16 v[94:97], v[180:183], v[230:233], v[94:97]
	v_mfma_f32_16x16x32_bf16 v[90:93], v[188:191], v[230:233], v[90:93]
	v_mfma_f32_16x16x32_bf16 v[78:81], v[180:183], v[238:241], v[78:81]
	v_mfma_f32_16x16x32_bf16 v[74:77], v[188:191], v[238:241], v[74:77]
	s_setprio 0
	s_setprio 1
	v_mfma_f32_16x16x32_bf16 v[118:121], v[192:195], v[210:213], v[118:121]
	v_mfma_f32_16x16x32_bf16 v[114:117], v[200:203], v[210:213], v[114:117]
	v_mfma_f32_16x16x32_bf16 v[102:105], v[192:195], v[218:221], v[102:105]
	v_mfma_f32_16x16x32_bf16 v[98:101], v[200:203], v[218:221], v[98:101]
	v_mfma_f32_16x16x32_bf16 v[86:89], v[192:195], v[226:229], v[86:89]
	v_mfma_f32_16x16x32_bf16 v[82:85], v[200:203], v[226:229], v[82:85]
	v_mfma_f32_16x16x32_bf16 v[70:73], v[192:195], v[234:237], v[70:73]
	v_mfma_f32_16x16x32_bf16 v[66:69], v[200:203], v[234:237], v[66:69]
	v_mfma_f32_16x16x32_bf16 v[118:121], v[196:199], v[214:217], v[118:121]
	v_mfma_f32_16x16x32_bf16 v[114:117], v[204:207], v[214:217], v[114:117]
	v_mfma_f32_16x16x32_bf16 v[102:105], v[196:199], v[222:225], v[102:105]
	v_mfma_f32_16x16x32_bf16 v[98:101], v[204:207], v[222:225], v[98:101]
	v_mfma_f32_16x16x32_bf16 v[86:89], v[196:199], v[230:233], v[86:89]
	v_mfma_f32_16x16x32_bf16 v[82:85], v[204:207], v[230:233], v[82:85]
	v_mfma_f32_16x16x32_bf16 v[70:73], v[196:199], v[238:241], v[70:73]
	v_mfma_f32_16x16x32_bf16 v[66:69], v[204:207], v[238:241], v[66:69]
	s_barrier
; #define PG8_STAGE(bufoff, gbase, voff) do { _Pragma("unroll") for (int _i = 0; _i < 2; ++_i) \
;         __builtin_amdgcn_global_load_lds((const unsigned*)((const char*)(gbase) + (voff)[_i]), (PG8_LAS unsigned*)(lds + (bufoff) + ldsw + _i * 8192), 16, 0, 0); } while (0)
; #define PG8_LDA(dst, b, h) do { _Pragma("unroll") for (int m = 0; m < 4; ++m) _Pragma("unroll") for (int k = 0; k < 2; ++k) dst[m][k] = *(const PG8_LAS bf16x8*)(lds + PG8_SA(b, h) + aoff + m * 2048 + k * 1024); } while (0)
; #define PG8_MMA(ai, bj, At, Bt) do { __builtin_amdgcn_s_setprio(1); _Pragma("unroll") for (int m = 0; m < 4; ++m) _Pragma("unroll") for (int n = 0; n < 2; ++n) _Pragma("unroll") for (int k = 0; k < 2; ++k) \
;         acc[ai][bj][m][n] = __builtin_amdgcn_mfma_f32_16x16x32_bf16(Bt[n][k], At[m][k], acc[ai][bj][m][n], 0, 0, 0); __builtin_amdgcn_s_setprio(0); } while (0)
; #define PG8_WAIT_V(n) asm volatile("s_waitcnt vmcnt(" #n ")" ::: "memory")
; #define PG8_WAIT_L(n) asm volatile("s_waitcnt lgkmcnt(" #n ")" ::: "memory")
; #define PG8_BAR __builtin_amdgcn_s_barrier()
; #define PG8_SCHED __builtin_amdgcn_sched_barrier(0)
;     ...
;             PG8_LDA(At, 1, 1); PG8_STAGE(PG8_SB(1, 0), b3, voffB); PG8_STAGE(PG8_SB(1, 1), b3 + hstep, voffB); PG8_STAGE(PG8_SA(1, 0), a3, voffA);
;             PG8_WAIT_V(8); PG8_WAIT_L(0); PG8_BAR; PG8_MMA(1, 0, At, B0); PG8_MMA(1, 1, At, B1); PG8_BAR; PG8_SCHED;
;         }
;         if constexpr (ALIGN_EPI) { if (wr == 0) PG8_BAR; }
;         E(acc, cur, wr, wc, fr, fq); S.done(cur);
;         if (!has_next) break;
	s_setprio 0
	s_add_i32 s18, s20, s57
	v_lshl_add_u64 v[242:243], v[242:243], 0, s[84:85]
	s_mov_b32 m0, s18
	ds_read_b128 v[210:213], v175 offset:49152
	ds_read_b128 v[214:217], v175 offset:50176
	ds_read_b128 v[218:221], v175 offset:51200
	ds_read_b128 v[222:225], v175 offset:52224
	ds_read_b128 v[226:229], v175 offset:53248
	ds_read_b128 v[230:233], v175 offset:54272
	ds_read_b128 v[234:237], v175 offset:55296
	ds_read_b128 v[238:241], v175 offset:56320
	global_load_lds_dwordx4 v[242:243], off
	v_lshl_add_u64 v[242:243], v[244:245], 0, s[84:85]
	s_add_i32 m0, s18, 0x2000
	v_lshl_add_u64 v[208:209], v[208:209], 0, s[94:95]
	s_add_i32 s18, s21, s57
	global_load_lds_dwordx4 v[242:243], off
	v_lshl_add_u64 v[242:243], v[208:209], 0, v[148:149]
	s_mov_b32 m0, s18
	v_lshl_add_u64 v[208:209], v[208:209], 0, v[152:153]
	global_load_lds_dwordx4 v[242:243], off
	s_add_i32 m0, s18, 0x2000
	s_nop 0
	global_load_lds_dwordx4 v[208:209], off
	v_lshl_add_u64 v[208:209], v[246:247], 0, s[84:85]
	s_mov_b32 m0, s63
	s_nop 0
	global_load_lds_dwordx4 v[208:209], off
	v_lshl_add_u64 v[208:209], v[248:249], 0, s[84:85]
	s_mov_b32 m0, s81
	s_nop 0
	global_load_lds_dwordx4 v[208:209], off
	s_waitcnt vmcnt(8)
	s_waitcnt lgkmcnt(0)
	s_setprio 1
	s_barrier
	v_mfma_f32_16x16x32_bf16 v[62:65], v[176:179], v[210:213], v[62:65]
	v_mfma_f32_16x16x32_bf16 v[58:61], v[184:187], v[210:213], v[58:61]
	v_mfma_f32_16x16x32_bf16 v[46:49], v[176:179], v[218:221], v[46:49]
	v_mfma_f32_16x16x32_bf16 v[42:45], v[184:187], v[218:221], v[42:45]
	v_mfma_f32_16x16x32_bf16 v[30:33], v[176:179], v[226:229], v[30:33]
	v_mfma_f32_16x16x32_bf16 v[26:29], v[184:187], v[226:229], v[26:29]
	v_mfma_f32_16x16x32_bf16 v[14:17], v[176:179], v[234:237], v[14:17]
	v_mfma_f32_16x16x32_bf16 v[10:13], v[184:187], v[234:237], v[10:13]
	v_mfma_f32_16x16x32_bf16 v[62:65], v[180:183], v[214:217], v[62:65]
	v_mfma_f32_16x16x32_bf16 v[58:61], v[188:191], v[214:217], v[58:61]
	v_mfma_f32_16x16x32_bf16 v[46:49], v[180:183], v[222:225], v[46:49]
	v_mfma_f32_16x16x32_bf16 v[42:45], v[188:191], v[222:225], v[42:45]
	v_mfma_f32_16x16x32_bf16 v[30:33], v[180:183], v[230:233], v[30:33]
	v_mfma_f32_16x16x32_bf16 v[26:29], v[188:191], v[230:233], v[26:29]
	v_mfma_f32_16x16x32_bf16 v[14:17], v[180:183], v[238:241], v[14:17]
	v_mfma_f32_16x16x32_bf16 v[10:13], v[188:191], v[238:241], v[10:13]
	s_setprio 0
	s_setprio 1
	v_mfma_f32_16x16x32_bf16 v[54:57], v[192:195], v[210:213], v[54:57]
	v_mfma_f32_16x16x32_bf16 v[50:53], v[200:203], v[210:213], v[50:53]
	v_mfma_f32_16x16x32_bf16 v[38:41], v[192:195], v[218:221], v[38:41]
	v_mfma_f32_16x16x32_bf16 v[34:37], v[200:203], v[218:221], v[34:37]
	v_mfma_f32_16x16x32_bf16 v[22:25], v[192:195], v[226:229], v[22:25]
	v_mfma_f32_16x16x32_bf16 v[18:21], v[200:203], v[226:229], v[18:21]
	v_mfma_f32_16x16x32_bf16 v[6:9], v[192:195], v[234:237], v[6:9]
	v_mfma_f32_16x16x32_bf16 v[2:5], v[200:203], v[234:237], v[2:5]
	v_mfma_f32_16x16x32_bf16 v[54:57], v[196:199], v[214:217], v[54:57]
	v_mfma_f32_16x16x32_bf16 v[50:53], v[204:207], v[214:217], v[50:53]
	v_mfma_f32_16x16x32_bf16 v[38:41], v[196:199], v[222:225], v[38:41]
	v_mfma_f32_16x16x32_bf16 v[34:37], v[204:207], v[222:225], v[34:37]
	v_mfma_f32_16x16x32_bf16 v[22:25], v[196:199], v[230:233], v[22:25]
	v_mfma_f32_16x16x32_bf16 v[18:21], v[204:207], v[230:233], v[18:21]
	v_mfma_f32_16x16x32_bf16 v[6:9], v[196:199], v[238:241], v[6:9]
	v_mfma_f32_16x16x32_bf16 v[2:5], v[204:207], v[238:241], v[2:5]
	s_barrier
	s_setprio 0
	s_add_i32 s17, s17, 2
	s_add_u32 s92, s92, 0x100
	s_addc_u32 s93, s93, 0
	s_cmp_gt_u32 s17, 13
	v_lshl_add_u64 v[164:165], v[164:165], 0, s[88:89]
	s_cbranch_scc0 .LBB0_2271
	s_and_b64 vcc, exec, s[70:71]
	s_cbranch_vccz .LBB0_2274
	s_barrier

; #define PG8_STAGE(bufoff, gbase, voff) do { _Pragma("unroll") for (int _i = 0; _i < 2; ++_i) \
;         __builtin_amdgcn_global_load_lds((const unsigned*)((const char*)(gbase) + (voff)[_i]), (PG8_LAS unsigned*)(lds + (bufoff) + ldsw + _i * 8192), 16, 0, 0); } while (0)
; #define PG8_LDA(dst, b, h) do { _Pragma("unroll") for (int m = 0; m < 4; ++m) _Pragma("unroll") for (int k = 0; k < 2; ++k) dst[m][k] = *(const PG8_LAS bf16x8*)(lds + PG8_SA(b, h) + aoff + m * 2048 + k * 1024); } while (0)
; #define PG8_LDB(dst, b, h) do { _Pragma("unroll") for (int n = 0; n < 2; ++n) _Pragma("unroll") for (int k = 0; k < 2; ++k) dst[n][k] = *(const PG8_LAS bf16x8*)(lds + PG8_SB(b, h) + boff + n * 2048 + k * 1024); } while (0)
; #define PG8_MMA(ai, bj, At, Bt) do { __builtin_amdgcn_s_setprio(1); _Pragma("unroll") for (int m = 0; m < 4; ++m) _Pragma("unroll") for (int n = 0; n < 2; ++n) _Pragma("unroll") for (int k = 0; k < 2; ++k) \
;         acc[ai][bj][m][n] = __builtin_amdgcn_mfma_f32_16x16x32_bf16(Bt[n][k], At[m][k], acc[ai][bj][m][n], 0, 0, 0); __builtin_amdgcn_s_setprio(0); } while (0)
; #define PG8_WAIT_V(n) asm volatile("s_waitcnt vmcnt(" #n ")" ::: "memory")
; #define PG8_WAIT_L(n) asm volatile("s_waitcnt lgkmcnt(" #n ")" ::: "memory")
; #define PG8_BAR __builtin_amdgcn_s_barrier()
; #define PG8_SCHED __builtin_amdgcn_sched_barrier(0)
;     ...
;         for (int t = 0; t < nt; t += 2) {
;             const bool last = (t == nt - 2);
;             const char* a1 = cA + (size_t)(t + 1) * kstep;
;             const char* a2 = last ? nA : cA + (size_t)(t + 2) * kstep; const char* b2 = last ? nB : cB + (size_t)(t + 2) * kstep;
;             const char* a3 = a2 + kstep; const char* b3 = b2 + kstep;
;             if (last && has_next) S.a_ready(nxt);
;             PG8_LDB(B0, 0, 0); PG8_LDB(B1, 0, 1); PG8_SCHED; PG8_LDA(At, 0, 0); PG8_STAGE(PG8_SA(1, 1), a1 + hstep, voffA);
;             PG8_WAIT_V(8); PG8_WAIT_L(0); PG8_BAR; PG8_MMA(0, 0, At, B0); PG8_MMA(0, 1, At, B1); PG8_BAR; PG8_SCHED;
;             PG8_LDA(At, 0, 1); PG8_STAGE(PG8_SB(0, 0), b2, voffB); PG8_STAGE(PG8_SB(0, 1), b2 + hstep, voffB); PG8_STAGE(PG8_SA(0, 0), a2, voffA);
.LBB0_2443:
	ds_read_b128 v[148:151], v145
	ds_read_b128 v[152:155], v145 offset:1024
	ds_read_b128 v[156:159], v145 offset:2048
	ds_read_b128 v[160:163], v145 offset:3072
	ds_read_b128 v[164:167], v146
	ds_read_b128 v[172:175], v146 offset:1024
	ds_read_b128 v[176:179], v146 offset:2048
	ds_read_b128 v[180:183], v146 offset:3072
	s_add_u32 s24, s22, 0xfffc0080
	s_addc_u32 s25, s23, -1
	s_cmp_eq_u32 s46, 12
	s_cselect_b32 s27, s19, s25
	s_cselect_b32 s26, s18, s24
	s_cselect_b32 s25, s0, s45
	s_cselect_b32 s24, s15, s17
	v_lshl_add_u64 v[168:169], s[22:23], 0, v[138:139]
	s_add_i32 m0, s9, 0xc000
	ds_read_b128 v[184:187], v147
	ds_read_b128 v[188:191], v147 offset:1024
	ds_read_b128 v[192:195], v147 offset:2048
	ds_read_b128 v[196:199], v147 offset:3072
	ds_read_b128 v[200:203], v147 offset:4096
	ds_read_b128 v[204:207], v147 offset:5120
	ds_read_b128 v[210:213], v147 offset:6144
	ds_read_b128 v[214:217], v147 offset:7168
	global_load_lds_dwordx4 v[168:169], off
	v_lshl_add_u64 v[168:169], s[22:23], 0, v[140:141]
	s_add_i32 m0, s9, 0xe000
	s_nop 0
	global_load_lds_dwordx4 v[168:169], off
	s_waitcnt vmcnt(8)
	s_waitcnt lgkmcnt(0)
	s_setprio 1
	s_barrier
	v_mfma_f32_16x16x32_bf16 v[126:129], v[148:151], v[184:187], v[126:129]
	v_mfma_f32_16x16x32_bf16 v[122:125], v[156:159], v[184:187], v[122:125]
	v_mfma_f32_16x16x32_bf16 v[118:121], v[148:151], v[192:195], v[118:121]
	v_mfma_f32_16x16x32_bf16 v[114:117], v[156:159], v[192:195], v[114:117]
	v_mfma_f32_16x16x32_bf16 v[102:105], v[148:151], v[200:203], v[102:105]
	v_mfma_f32_16x16x32_bf16 v[98:101], v[156:159], v[200:203], v[98:101]
	v_mfma_f32_16x16x32_bf16 v[86:89], v[148:151], v[210:213], v[86:89]
	v_mfma_f32_16x16x32_bf16 v[82:85], v[156:159], v[210:213], v[82:85]
	v_mfma_f32_16x16x32_bf16 v[126:129], v[152:155], v[188:191], v[126:129]
	v_mfma_f32_16x16x32_bf16 v[122:125], v[160:163], v[188:191], v[122:125]
	v_mfma_f32_16x16x32_bf16 v[118:121], v[152:155], v[196:199], v[118:121]
	v_mfma_f32_16x16x32_bf16 v[114:117], v[160:163], v[196:199], v[114:117]
	v_mfma_f32_16x16x32_bf16 v[102:105], v[152:155], v[204:207], v[102:105]
	v_mfma_f32_16x16x32_bf16 v[98:101], v[160:163], v[204:207], v[98:101]
	v_mfma_f32_16x16x32_bf16 v[86:89], v[152:155], v[214:217], v[86:89]
	v_mfma_f32_16x16x32_bf16 v[82:85], v[160:163], v[214:217], v[82:85]
	s_setprio 0
	s_setprio 1
	v_mfma_f32_16x16x32_bf16 v[110:113], v[164:167], v[184:187], v[110:113]
	v_mfma_f32_16x16x32_bf16 v[106:109], v[176:179], v[184:187], v[106:109]
	v_mfma_f32_16x16x32_bf16 v[94:97], v[164:167], v[192:195], v[94:97]
	v_mfma_f32_16x16x32_bf16 v[90:93], v[176:179], v[192:195], v[90:93]
	v_mfma_f32_16x16x32_bf16 v[78:81], v[164:167], v[200:203], v[78:81]
	v_mfma_f32_16x16x32_bf16 v[74:77], v[176:179], v[200:203], v[74:77]
	v_mfma_f32_16x16x32_bf16 v[70:73], v[164:167], v[210:213], v[70:73]
	v_mfma_f32_16x16x32_bf16 v[66:69], v[176:179], v[210:213], v[66:69]
	v_mfma_f32_16x16x32_bf16 v[110:113], v[172:175], v[188:191], v[110:113]
	v_mfma_f32_16x16x32_bf16 v[106:109], v[180:183], v[188:191], v[106:109]
	v_mfma_f32_16x16x32_bf16 v[94:97], v[172:175], v[196:199], v[94:97]
	v_mfma_f32_16x16x32_bf16 v[90:93], v[180:183], v[196:199], v[90:93]
	v_mfma_f32_16x16x32_bf16 v[78:81], v[172:175], v[204:207], v[78:81]
	v_mfma_f32_16x16x32_bf16 v[74:77], v[180:183], v[204:207], v[74:77]
	v_mfma_f32_16x16x32_bf16 v[70:73], v[172:175], v[214:217], v[70:73]
	v_mfma_f32_16x16x32_bf16 v[66:69], v[180:183], v[214:217], v[66:69]
	s_barrier
	s_setprio 0
	s_add_i32 s47, s38, s11
	v_lshl_add_u64 v[168:169], s[24:25], 0, v[132:133]
	s_mov_b32 m0, s47
	ds_read_b128 v[184:187], v147 offset:16384
	ds_read_b128 v[188:191], v147 offset:17408
	ds_read_b128 v[192:195], v147 offset:18432
	ds_read_b128 v[196:199], v147 offset:19456
	ds_read_b128 v[200:203], v147 offset:20480
	ds_read_b128 v[204:207], v147 offset:21504
	ds_read_b128 v[210:213], v147 offset:22528
	ds_read_b128 v[214:217], v147 offset:23552
	global_load_lds_dwordx4 v[168:169], off
	s_add_i32 m0, s47, 0x2000
	s_add_u32 s50, s24, 0x40000
	v_lshl_add_u64 v[208:209], s[24:25], 0, v[136:137]
	s_addc_u32 s51, s25, 0
	s_add_i32 s47, s39, s11
	global_load_lds_dwordx4 v[208:209], off
	v_lshl_add_u64 v[218:219], s[50:51], 0, v[132:133]
	s_mov_b32 m0, s47
	v_lshl_add_u64 v[220:221], s[26:27], 0, v[134:135]
	global_load_lds_dwordx4 v[218:219], off
	v_lshl_add_u64 v[218:219], s[50:51], 0, v[136:137]
	s_add_i32 m0, s47, 0x2000
	s_nop 0
	global_load_lds_dwordx4 v[218:219], off
	v_lshl_add_u64 v[218:219], s[26:27], 0, v[130:131]
	s_mov_b32 m0, s9
	s_nop 0
	global_load_lds_dwordx4 v[218:219], off
	s_mov_b32 m0, s33
	s_nop 0
	global_load_lds_dwordx4 v[220:221], off
	s_waitcnt vmcnt(8)
	s_waitcnt lgkmcnt(0)
	s_setprio 1
	s_barrier
; #define PG8_STAGE(bufoff, gbase, voff) do { _Pragma("unroll") for (int _i = 0; _i < 2; ++_i) \
;         __builtin_amdgcn_global_load_lds((const unsigned*)((const char*)(gbase) + (voff)[_i]), (PG8_LAS unsigned*)(lds + (bufoff) + ldsw + _i * 8192), 16, 0, 0); } while (0)
; #define PG8_LDA(dst, b, h) do { _Pragma("unroll") for (int m = 0; m < 4; ++m) _Pragma("unroll") for (int k = 0; k < 2; ++k) dst[m][k] = *(const PG8_LAS bf16x8*)(lds + PG8_SA(b, h) + aoff + m * 2048 + k * 1024); } while (0)
; #define PG8_LDB(dst, b, h) do { _Pragma("unroll") for (int n = 0; n < 2; ++n) _Pragma("unroll") for (int k = 0; k < 2; ++k) dst[n][k] = *(const PG8_LAS bf16x8*)(lds + PG8_SB(b, h) + boff + n * 2048 + k * 1024); } while (0)
; #define PG8_MMA(ai, bj, At, Bt) do { __builtin_amdgcn_s_setprio(1); _Pragma("unroll") for (int m = 0; m < 4; ++m) _Pragma("unroll") for (int n = 0; n < 2; ++n) _Pragma("unroll") for (int k = 0; k < 2; ++k) \
;         acc[ai][bj][m][n] = __builtin_amdgcn_mfma_f32_16x16x32_bf16(Bt[n][k], At[m][k], acc[ai][bj][m][n], 0, 0, 0); __builtin_amdgcn_s_setprio(0); } while (0)
; #define PG8_WAIT_V(n) asm volatile("s_waitcnt vmcnt(" #n ")" ::: "memory")
; #define PG8_WAIT_L(n) asm volatile("s_waitcnt lgkmcnt(" #n ")" ::: "memory")
; #define PG8_BAR __builtin_amdgcn_s_barrier()
; #define PG8_SCHED __builtin_amdgcn_sched_barrier(0)
;     ...
;             PG8_WAIT_V(8); PG8_WAIT_L(0); PG8_BAR; PG8_MMA(1, 0, At, B0); PG8_MMA(1, 1, At, B1); PG8_BAR; PG8_SCHED;
;             PG8_LDB(B0, 1, 0); PG8_LDB(B1, 1, 1); PG8_SCHED; PG8_LDA(At, 1, 0); PG8_STAGE(PG8_SA(0, 1), a2 + hstep, voffA);
;             PG8_WAIT_V(8); PG8_WAIT_L(0); PG8_BAR; PG8_MMA(0, 0, At, B0); PG8_MMA(0, 1, At, B1); PG8_BAR; PG8_SCHED;
	v_mfma_f32_16x16x32_bf16 v[62:65], v[148:151], v[184:187], v[62:65]
	v_mfma_f32_16x16x32_bf16 v[58:61], v[156:159], v[184:187], v[58:61]
	v_mfma_f32_16x16x32_bf16 v[54:57], v[148:151], v[192:195], v[54:57]
	v_mfma_f32_16x16x32_bf16 v[50:53], v[156:159], v[192:195], v[50:53]
	v_mfma_f32_16x16x32_bf16 v[38:41], v[148:151], v[200:203], v[38:41]
	v_mfma_f32_16x16x32_bf16 v[34:37], v[156:159], v[200:203], v[34:37]
	v_mfma_f32_16x16x32_bf16 v[22:25], v[148:151], v[210:213], v[22:25]
	v_mfma_f32_16x16x32_bf16 v[18:21], v[156:159], v[210:213], v[18:21]
	v_mfma_f32_16x16x32_bf16 v[62:65], v[152:155], v[188:191], v[62:65]
	v_mfma_f32_16x16x32_bf16 v[58:61], v[160:163], v[188:191], v[58:61]
	v_mfma_f32_16x16x32_bf16 v[54:57], v[152:155], v[196:199], v[54:57]
	v_mfma_f32_16x16x32_bf16 v[50:53], v[160:163], v[196:199], v[50:53]
	v_mfma_f32_16x16x32_bf16 v[38:41], v[152:155], v[204:207], v[38:41]
	v_mfma_f32_16x16x32_bf16 v[34:37], v[160:163], v[204:207], v[34:37]
	v_mfma_f32_16x16x32_bf16 v[22:25], v[152:155], v[214:217], v[22:25]
	v_mfma_f32_16x16x32_bf16 v[18:21], v[160:163], v[214:217], v[18:21]
	s_setprio 0
	s_setprio 1
	v_mfma_f32_16x16x32_bf16 v[46:49], v[164:167], v[184:187], v[46:49]
	v_mfma_f32_16x16x32_bf16 v[42:45], v[176:179], v[184:187], v[42:45]
	v_mfma_f32_16x16x32_bf16 v[30:33], v[164:167], v[192:195], v[30:33]
	v_mfma_f32_16x16x32_bf16 v[26:29], v[176:179], v[192:195], v[26:29]
	v_mfma_f32_16x16x32_bf16 v[14:17], v[164:167], v[200:203], v[14:17]
	v_mfma_f32_16x16x32_bf16 v[10:13], v[176:179], v[200:203], v[10:13]
	v_mfma_f32_16x16x32_bf16 v[6:9], v[164:167], v[210:213], v[6:9]
	v_mfma_f32_16x16x32_bf16 v[2:5], v[176:179], v[210:213], v[2:5]
	v_mfma_f32_16x16x32_bf16 v[46:49], v[172:175], v[188:191], v[46:49]
	v_mfma_f32_16x16x32_bf16 v[42:45], v[180:183], v[188:191], v[42:45]
	v_mfma_f32_16x16x32_bf16 v[30:33], v[172:175], v[196:199], v[30:33]
	v_mfma_f32_16x16x32_bf16 v[26:29], v[180:183], v[196:199], v[26:29]
	v_mfma_f32_16x16x32_bf16 v[14:17], v[172:175], v[204:207], v[14:17]
	v_mfma_f32_16x16x32_bf16 v[10:13], v[180:183], v[204:207], v[10:13]
	v_mfma_f32_16x16x32_bf16 v[6:9], v[172:175], v[214:217], v[6:9]
	v_mfma_f32_16x16x32_bf16 v[2:5], v[180:183], v[214:217], v[2:5]
	s_barrier
	s_setprio 0
	s_add_i32 s47, 0, 0x18000
	s_add_i32 s50, 0, 0x1c000
	v_add_u32_e32 v160, s47, v143
	v_add_u32_e32 v180, s50, v143
	ds_read_b128 v[148:151], v160
	ds_read_b128 v[152:155], v160 offset:1024
	ds_read_b128 v[156:159], v160 offset:2048
	ds_read_b128 v[160:163], v160 offset:3072
	ds_read_b128 v[164:167], v180
	ds_read_b128 v[172:175], v180 offset:1024
	ds_read_b128 v[176:179], v180 offset:2048
	ds_read_b128 v[180:183], v180 offset:3072
	s_add_u32 s26, s26, 0x40000
	s_addc_u32 s27, s27, 0
	s_mov_b32 m0, s34
	v_lshl_add_u64 v[222:223], s[26:27], 0, v[130:131]
	ds_read_b128 v[184:187], v147 offset:32768
	ds_read_b128 v[188:191], v147 offset:33792
	ds_read_b128 v[192:195], v147 offset:34816
	ds_read_b128 v[196:199], v147 offset:35840
	ds_read_b128 v[200:203], v147 offset:36864
	ds_read_b128 v[204:207], v147 offset:37888
	ds_read_b128 v[210:213], v147 offset:38912
	ds_read_b128 v[214:217], v147 offset:39936
	global_load_lds_dwordx4 v[222:223], off
	v_lshl_add_u64 v[222:223], s[26:27], 0, v[134:135]
	s_mov_b32 m0, s35
	s_nop 0
	global_load_lds_dwordx4 v[222:223], off
	s_waitcnt vmcnt(8)
	s_waitcnt lgkmcnt(0)
	s_setprio 1
	s_barrier
	v_mfma_f32_16x16x32_bf16 v[126:129], v[148:151], v[184:187], v[126:129]
	v_mfma_f32_16x16x32_bf16 v[122:125], v[156:159], v[184:187], v[122:125]
	v_mfma_f32_16x16x32_bf16 v[118:121], v[148:151], v[192:195], v[118:121]
	v_mfma_f32_16x16x32_bf16 v[114:117], v[156:159], v[192:195], v[114:117]
	v_mfma_f32_16x16x32_bf16 v[102:105], v[148:151], v[200:203], v[102:105]
	v_mfma_f32_16x16x32_bf16 v[98:101], v[156:159], v[200:203], v[98:101]
	v_mfma_f32_16x16x32_bf16 v[86:89], v[148:151], v[210:213], v[86:89]
	v_mfma_f32_16x16x32_bf16 v[82:85], v[156:159], v[210:213], v[82:85]
	v_mfma_f32_16x16x32_bf16 v[126:129], v[152:155], v[188:191], v[126:129]
	v_mfma_f32_16x16x32_bf16 v[122:125], v[160:163], v[188:191], v[122:125]
	v_mfma_f32_16x16x32_bf16 v[118:121], v[152:155], v[196:199], v[118:121]
	v_mfma_f32_16x16x32_bf16 v[114:117], v[160:163], v[196:199], v[114:117]
	v_mfma_f32_16x16x32_bf16 v[102:105], v[152:155], v[204:207], v[102:105]
	v_mfma_f32_16x16x32_bf16 v[98:101], v[160:163], v[204:207], v[98:101]
	v_mfma_f32_16x16x32_bf16 v[86:89], v[152:155], v[214:217], v[86:89]
	v_mfma_f32_16x16x32_bf16 v[82:85], v[160:163], v[214:217], v[82:85]
	s_setprio 0
	s_setprio 1
	v_mfma_f32_16x16x32_bf16 v[110:113], v[164:167], v[184:187], v[110:113]
	v_mfma_f32_16x16x32_bf16 v[106:109], v[176:179], v[184:187], v[106:109]
	v_mfma_f32_16x16x32_bf16 v[94:97], v[164:167], v[192:195], v[94:97]
	v_mfma_f32_16x16x32_bf16 v[90:93], v[176:179], v[192:195], v[90:93]
	v_mfma_f32_16x16x32_bf16 v[78:81], v[164:167], v[200:203], v[78:81]
	v_mfma_f32_16x16x32_bf16 v[74:77], v[176:179], v[200:203], v[74:77]
	v_mfma_f32_16x16x32_bf16 v[70:73], v[164:167], v[210:213], v[70:73]
	v_mfma_f32_16x16x32_bf16 v[66:69], v[176:179], v[210:213], v[66:69]
	v_mfma_f32_16x16x32_bf16 v[110:113], v[172:175], v[188:191], v[110:113]
	v_mfma_f32_16x16x32_bf16 v[106:109], v[180:183], v[188:191], v[106:109]
	v_mfma_f32_16x16x32_bf16 v[94:97], v[172:175], v[196:199], v[94:97]
	v_mfma_f32_16x16x32_bf16 v[90:93], v[180:183], v[196:199], v[90:93]
	v_mfma_f32_16x16x32_bf16 v[78:81], v[172:175], v[204:207], v[78:81]
	v_mfma_f32_16x16x32_bf16 v[74:77], v[180:183], v[204:207], v[74:77]
	v_mfma_f32_16x16x32_bf16 v[70:73], v[172:175], v[214:217], v[70:73]
	v_mfma_f32_16x16x32_bf16 v[66:69], v[180:183], v[214:217], v[66:69]
	s_barrier
; #define PG8_STAGE(bufoff, gbase, voff) do { _Pragma("unroll") for (int _i = 0; _i < 2; ++_i) \
;         __builtin_amdgcn_global_load_lds((const unsigned*)((const char*)(gbase) + (voff)[_i]), (PG8_LAS unsigned*)(lds + (bufoff) + ldsw + _i * 8192), 16, 0, 0); } while (0)
; #define PG8_LDA(dst, b, h) do { _Pragma("unroll") for (int m = 0; m < 4; ++m) _Pragma("unroll") for (int k = 0; k < 2; ++k) dst[m][k] = *(const PG8_LAS bf16x8*)(lds + PG8_SA(b, h) + aoff + m * 2048 + k * 1024); } while (0)
; #define PG8_MMA(ai, bj, At, Bt) do { __builtin_amdgcn_s_setprio(1); _Pragma("unroll") for (int m = 0; m < 4; ++m) _Pragma("unroll") for (int n = 0; n < 2; ++n) _Pragma("unroll") for (int k = 0; k < 2; ++k) \
;         acc[ai][bj][m][n] = __builtin_amdgcn_mfma_f32_16x16x32_bf16(Bt[n][k], At[m][k], acc[ai][bj][m][n], 0, 0, 0); __builtin_amdgcn_s_setprio(0); } while (0)
; #define PG8_WAIT_V(n) asm volatile("s_waitcnt vmcnt(" #n ")" ::: "memory")
; #define PG8_WAIT_L(n) asm volatile("s_waitcnt lgkmcnt(" #n ")" ::: "memory")
; #define PG8_BAR __builtin_amdgcn_s_barrier()
; #define PG8_SCHED __builtin_amdgcn_sched_barrier(0)
;     ...
;             PG8_LDA(At, 1, 1); PG8_STAGE(PG8_SB(1, 0), b3, voffB); PG8_STAGE(PG8_SB(1, 1), b3 + hstep, voffB); PG8_STAGE(PG8_SA(1, 0), a3, voffA);
;             PG8_WAIT_V(8); PG8_WAIT_L(0); PG8_BAR; PG8_MMA(1, 0, At, B0); PG8_MMA(1, 1, At, B1); PG8_BAR; PG8_SCHED;
;         }
;         if constexpr (ALIGN_EPI) { if (wr == 0) PG8_BAR; }
	s_setprio 0
	s_add_i32 s26, s47, s11
	v_lshl_add_u64 v[168:169], v[168:169], 0, s[6:7]
	s_mov_b32 m0, s26
	ds_read_b128 v[184:187], v147 offset:49152
	ds_read_b128 v[188:191], v147 offset:50176
	ds_read_b128 v[192:195], v147 offset:51200
	ds_read_b128 v[196:199], v147 offset:52224
	ds_read_b128 v[200:203], v147 offset:53248
	ds_read_b128 v[204:207], v147 offset:54272
	ds_read_b128 v[210:213], v147 offset:55296
	ds_read_b128 v[214:217], v147 offset:56320
	global_load_lds_dwordx4 v[168:169], off
	s_add_i32 m0, s26, 0x2000
	s_add_u32 s24, s24, 0x40080
	v_lshl_add_u64 v[168:169], v[208:209], 0, s[6:7]
	s_addc_u32 s25, s25, 0
	s_add_i32 s26, s50, s11
	global_load_lds_dwordx4 v[168:169], off
	v_lshl_add_u64 v[168:169], s[24:25], 0, v[132:133]
	s_mov_b32 m0, s26
	s_nop 0
	global_load_lds_dwordx4 v[168:169], off
	v_lshl_add_u64 v[168:169], s[24:25], 0, v[136:137]
	s_add_i32 m0, s26, 0x2000
	s_nop 0
	global_load_lds_dwordx4 v[168:169], off
	v_lshl_add_u64 v[168:169], v[218:219], 0, s[6:7]
	s_mov_b32 m0, s36
	s_nop 0
	global_load_lds_dwordx4 v[168:169], off
	v_lshl_add_u64 v[168:169], v[220:221], 0, s[6:7]
	s_mov_b32 m0, s37
	s_nop 0
	global_load_lds_dwordx4 v[168:169], off
	s_waitcnt vmcnt(8)
	s_waitcnt lgkmcnt(0)
	s_setprio 1
	s_barrier
	v_mfma_f32_16x16x32_bf16 v[62:65], v[148:151], v[184:187], v[62:65]
	v_mfma_f32_16x16x32_bf16 v[58:61], v[156:159], v[184:187], v[58:61]
	v_mfma_f32_16x16x32_bf16 v[54:57], v[148:151], v[192:195], v[54:57]
	v_mfma_f32_16x16x32_bf16 v[50:53], v[156:159], v[192:195], v[50:53]
	v_mfma_f32_16x16x32_bf16 v[38:41], v[148:151], v[200:203], v[38:41]
	v_mfma_f32_16x16x32_bf16 v[34:37], v[156:159], v[200:203], v[34:37]
	v_mfma_f32_16x16x32_bf16 v[22:25], v[148:151], v[210:213], v[22:25]
	v_mfma_f32_16x16x32_bf16 v[18:21], v[156:159], v[210:213], v[18:21]
	v_mfma_f32_16x16x32_bf16 v[62:65], v[152:155], v[188:191], v[62:65]
	v_mfma_f32_16x16x32_bf16 v[58:61], v[160:163], v[188:191], v[58:61]
	v_mfma_f32_16x16x32_bf16 v[54:57], v[152:155], v[196:199], v[54:57]
	v_mfma_f32_16x16x32_bf16 v[50:53], v[160:163], v[196:199], v[50:53]
	v_mfma_f32_16x16x32_bf16 v[38:41], v[152:155], v[204:207], v[38:41]
	v_mfma_f32_16x16x32_bf16 v[34:37], v[160:163], v[204:207], v[34:37]
	v_mfma_f32_16x16x32_bf16 v[22:25], v[152:155], v[214:217], v[22:25]
	v_mfma_f32_16x16x32_bf16 v[18:21], v[160:163], v[214:217], v[18:21]
	s_setprio 0
	s_setprio 1
	v_mfma_f32_16x16x32_bf16 v[46:49], v[164:167], v[184:187], v[46:49]
	v_mfma_f32_16x16x32_bf16 v[42:45], v[176:179], v[184:187], v[42:45]
	v_mfma_f32_16x16x32_bf16 v[30:33], v[164:167], v[192:195], v[30:33]
	v_mfma_f32_16x16x32_bf16 v[26:29], v[176:179], v[192:195], v[26:29]
	v_mfma_f32_16x16x32_bf16 v[14:17], v[164:167], v[200:203], v[14:17]
	v_mfma_f32_16x16x32_bf16 v[10:13], v[176:179], v[200:203], v[10:13]
	v_mfma_f32_16x16x32_bf16 v[6:9], v[164:167], v[210:213], v[6:9]
	v_mfma_f32_16x16x32_bf16 v[2:5], v[176:179], v[210:213], v[2:5]
	v_mfma_f32_16x16x32_bf16 v[46:49], v[172:175], v[188:191], v[46:49]
	v_mfma_f32_16x16x32_bf16 v[42:45], v[180:183], v[188:191], v[42:45]
	v_mfma_f32_16x16x32_bf16 v[30:33], v[172:175], v[196:199], v[30:33]
	v_mfma_f32_16x16x32_bf16 v[26:29], v[180:183], v[196:199], v[26:29]
	v_mfma_f32_16x16x32_bf16 v[14:17], v[172:175], v[204:207], v[14:17]
	v_mfma_f32_16x16x32_bf16 v[10:13], v[180:183], v[204:207], v[10:13]
	v_mfma_f32_16x16x32_bf16 v[6:9], v[172:175], v[214:217], v[6:9]
	v_mfma_f32_16x16x32_bf16 v[2:5], v[180:183], v[214:217], v[2:5]
	s_barrier
	s_setprio 0
	s_add_i32 s46, s46, 2
	s_add_u32 s22, s22, 0x100
	s_addc_u32 s23, s23, 0
	s_add_u32 s17, s17, 0x100
	s_addc_u32 s45, s45, 0
	s_cmp_gt_u32 s46, 13
	s_cbranch_scc0 .LBB0_2443
	s_and_b64 vcc, exec, s[12:13]
	s_cbranch_vccz .LBB0_2446
	s_barrier

; #define PG8_STAGE(bufoff, gbase, voff) do { _Pragma("unroll") for (int _i = 0; _i < 2; ++_i) \
;         __builtin_amdgcn_global_load_lds((const unsigned*)((const char*)(gbase) + (voff)[_i]), (PG8_LAS unsigned*)(lds + (bufoff) + ldsw + _i * 8192), 16, 0, 0); } while (0)
; #define PG8_LDA(dst, b, h) do { _Pragma("unroll") for (int m = 0; m < 4; ++m) _Pragma("unroll") for (int k = 0; k < 2; ++k) dst[m][k] = *(const PG8_LAS bf16x8*)(lds + PG8_SA(b, h) + aoff + m * 2048 + k * 1024); } while (0)
; #define PG8_LDB(dst, b, h) do { _Pragma("unroll") for (int n = 0; n < 2; ++n) _Pragma("unroll") for (int k = 0; k < 2; ++k) dst[n][k] = *(const PG8_LAS bf16x8*)(lds + PG8_SB(b, h) + boff + n * 2048 + k * 1024); } while (0)
; #define PG8_MMA(ai, bj, At, Bt) do { __builtin_amdgcn_s_setprio(1); _Pragma("unroll") for (int m = 0; m < 4; ++m) _Pragma("unroll") for (int n = 0; n < 2; ++n) _Pragma("unroll") for (int k = 0; k < 2; ++k) \
;         acc[ai][bj][m][n] = __builtin_amdgcn_mfma_f32_16x16x32_bf16(Bt[n][k], At[m][k], acc[ai][bj][m][n], 0, 0, 0); __builtin_amdgcn_s_setprio(0); } while (0)
; #define PG8_WAIT_V(n) asm volatile("s_waitcnt vmcnt(" #n ")" ::: "memory")
; #define PG8_WAIT_L(n) asm volatile("s_waitcnt lgkmcnt(" #n ")" ::: "memory")
; #define PG8_BAR __builtin_amdgcn_s_barrier()
; #define PG8_SCHED __builtin_amdgcn_sched_barrier(0)
;     ...
;             const bool last = (t == nt - 2);
;             const char* a1 = cA + (size_t)(t + 1) * kstep;
;             const char* a2 = last ? nA : cA + (size_t)(t + 2) * kstep; const char* b2 = last ? nB : cB + (size_t)(t + 2) * kstep;
;             const char* a3 = a2 + kstep; const char* b3 = b2 + kstep;
;             if (last && has_next) S.a_ready(nxt);
;             PG8_LDB(B0, 0, 0); PG8_LDB(B1, 0, 1); PG8_SCHED; PG8_LDA(At, 0, 0); PG8_STAGE(PG8_SA(1, 1), a1 + hstep, voffA);
;             PG8_WAIT_V(8); PG8_WAIT_L(0); PG8_BAR; PG8_MMA(0, 0, At, B0); PG8_MMA(0, 1, At, B1); PG8_BAR; PG8_SCHED;
;             PG8_LDA(At, 0, 1); PG8_STAGE(PG8_SB(0, 0), b2, voffB); PG8_STAGE(PG8_SB(0, 1), b2 + hstep, voffB); PG8_STAGE(PG8_SA(0, 0), a2, voffA);
.LBB0_3094:
	ds_read_b128 v[114:117], v211
	ds_read_b128 v[118:121], v211 offset:1024
	ds_read_b128 v[122:125], v211 offset:2048
	ds_read_b128 v[126:129], v211 offset:3072
	ds_read_b128 v[146:149], v212
	ds_read_b128 v[150:153], v212 offset:1024
	ds_read_b128 v[154:157], v212 offset:2048
	ds_read_b128 v[158:161], v212 offset:3072
	s_add_u32 s20, s18, 0xfffc0080
	s_addc_u32 s21, s19, -1
	s_cmp_eq_u32 s52, 12
	s_cselect_b32 s23, s11, s21
	s_cselect_b32 s22, s17, s20
	s_cselect_b32 s21, s9, s51
	s_cselect_b32 s20, s47, s50
	v_lshl_add_u64 v[234:235], s[18:19], 0, v[196:197]
	s_add_i32 m0, s31, 0xc000
	ds_read_b128 v[162:165], v213
	ds_read_b128 v[166:169], v213 offset:1024
	ds_read_b128 v[204:207], v213 offset:2048
	ds_read_b128 v[214:217], v213 offset:3072
	ds_read_b128 v[218:221], v213 offset:4096
	ds_read_b128 v[222:225], v213 offset:5120
	ds_read_b128 v[226:229], v213 offset:6144
	ds_read_b128 v[230:233], v213 offset:7168
	global_load_lds_dwordx4 v[234:235], off
	v_lshl_add_u64 v[234:235], s[18:19], 0, v[198:199]
	s_add_i32 m0, s31, 0xe000
	s_nop 0
	global_load_lds_dwordx4 v[234:235], off
	s_waitcnt vmcnt(8)
	s_waitcnt lgkmcnt(0)
	s_setprio 1
	s_barrier
	v_mfma_f32_16x16x32_bf16 v[142:145], v[114:117], v[162:165], v[142:145]
	v_mfma_f32_16x16x32_bf16 v[138:141], v[122:125], v[162:165], v[138:141]
	v_mfma_f32_16x16x32_bf16 v[110:113], v[114:117], v[204:207], v[110:113]
	v_mfma_f32_16x16x32_bf16 v[106:109], v[122:125], v[204:207], v[106:109]
	v_mfma_f32_16x16x32_bf16 v[98:101], v[114:117], v[218:221], v[98:101]
	v_mfma_f32_16x16x32_bf16 v[90:93], v[122:125], v[218:221], v[90:93]
	v_mfma_f32_16x16x32_bf16 v[82:85], v[114:117], v[226:229], v[82:85]
	v_mfma_f32_16x16x32_bf16 v[74:77], v[122:125], v[226:229], v[74:77]
	v_mfma_f32_16x16x32_bf16 v[142:145], v[118:121], v[166:169], v[142:145]
	v_mfma_f32_16x16x32_bf16 v[138:141], v[126:129], v[166:169], v[138:141]
	v_mfma_f32_16x16x32_bf16 v[110:113], v[118:121], v[214:217], v[110:113]
	v_mfma_f32_16x16x32_bf16 v[106:109], v[126:129], v[214:217], v[106:109]
	v_mfma_f32_16x16x32_bf16 v[98:101], v[118:121], v[222:225], v[98:101]
	v_mfma_f32_16x16x32_bf16 v[90:93], v[126:129], v[222:225], v[90:93]
	v_mfma_f32_16x16x32_bf16 v[82:85], v[118:121], v[230:233], v[82:85]
	v_mfma_f32_16x16x32_bf16 v[74:77], v[126:129], v[230:233], v[74:77]
	s_setprio 0
	s_setprio 1
	v_mfma_f32_16x16x32_bf16 v[134:137], v[146:149], v[162:165], v[134:137]
	v_mfma_f32_16x16x32_bf16 v[130:133], v[154:157], v[162:165], v[130:133]
	v_mfma_f32_16x16x32_bf16 v[102:105], v[146:149], v[204:207], v[102:105]
	v_mfma_f32_16x16x32_bf16 v[94:97], v[154:157], v[204:207], v[94:97]
	v_mfma_f32_16x16x32_bf16 v[86:89], v[146:149], v[218:221], v[86:89]
	v_mfma_f32_16x16x32_bf16 v[78:81], v[154:157], v[218:221], v[78:81]
	v_mfma_f32_16x16x32_bf16 v[70:73], v[146:149], v[226:229], v[70:73]
	v_mfma_f32_16x16x32_bf16 v[66:69], v[154:157], v[226:229], v[66:69]
	v_mfma_f32_16x16x32_bf16 v[134:137], v[150:153], v[166:169], v[134:137]
	v_mfma_f32_16x16x32_bf16 v[130:133], v[158:161], v[166:169], v[130:133]
	v_mfma_f32_16x16x32_bf16 v[102:105], v[150:153], v[214:217], v[102:105]
	v_mfma_f32_16x16x32_bf16 v[94:97], v[158:161], v[214:217], v[94:97]
	v_mfma_f32_16x16x32_bf16 v[86:89], v[150:153], v[222:225], v[86:89]
	v_mfma_f32_16x16x32_bf16 v[78:81], v[158:161], v[222:225], v[78:81]
	v_mfma_f32_16x16x32_bf16 v[70:73], v[150:153], v[230:233], v[70:73]
	v_mfma_f32_16x16x32_bf16 v[66:69], v[158:161], v[230:233], v[66:69]
	s_barrier
	s_setprio 0
	s_add_i32 s53, s44, s28
	v_lshl_add_u64 v[234:235], s[20:21], 0, v[176:177]
	s_mov_b32 m0, s53
	ds_read_b128 v[162:165], v213 offset:16384
	ds_read_b128 v[166:169], v213 offset:17408
	ds_read_b128 v[204:207], v213 offset:18432
	ds_read_b128 v[214:217], v213 offset:19456
	ds_read_b128 v[218:221], v213 offset:20480
	ds_read_b128 v[222:225], v213 offset:21504
	ds_read_b128 v[226:229], v213 offset:22528
	ds_read_b128 v[230:233], v213 offset:23552
	global_load_lds_dwordx4 v[234:235], off
	s_add_i32 m0, s53, 0x2000
	s_add_u32 s54, s20, 0x40000
	v_lshl_add_u64 v[236:237], s[20:21], 0, v[172:173]
	s_addc_u32 s55, s21, 0
	s_add_i32 s53, s45, s28
	global_load_lds_dwordx4 v[236:237], off
	v_lshl_add_u64 v[238:239], s[54:55], 0, v[176:177]
	s_mov_b32 m0, s53
	v_lshl_add_u64 v[240:241], s[22:23], 0, v[174:175]
	global_load_lds_dwordx4 v[238:239], off
	v_lshl_add_u64 v[238:239], s[54:55], 0, v[172:173]
	s_add_i32 m0, s53, 0x2000
	s_nop 0
	global_load_lds_dwordx4 v[238:239], off
	v_lshl_add_u64 v[238:239], s[22:23], 0, v[178:179]
	s_mov_b32 m0, s31
	s_nop 0
	global_load_lds_dwordx4 v[238:239], off
	s_mov_b32 m0, s33
	s_nop 0
	global_load_lds_dwordx4 v[240:241], off
	s_waitcnt vmcnt(8)
	s_waitcnt lgkmcnt(0)
	s_setprio 1
	s_barrier
; #define PG8_STAGE(bufoff, gbase, voff) do { _Pragma("unroll") for (int _i = 0; _i < 2; ++_i) \
;         __builtin_amdgcn_global_load_lds((const unsigned*)((const char*)(gbase) + (voff)[_i]), (PG8_LAS unsigned*)(lds + (bufoff) + ldsw + _i * 8192), 16, 0, 0); } while (0)
; #define PG8_LDA(dst, b, h) do { _Pragma("unroll") for (int m = 0; m < 4; ++m) _Pragma("unroll") for (int k = 0; k < 2; ++k) dst[m][k] = *(const PG8_LAS bf16x8*)(lds + PG8_SA(b, h) + aoff + m * 2048 + k * 1024); } while (0)
; #define PG8_LDB(dst, b, h) do { _Pragma("unroll") for (int n = 0; n < 2; ++n) _Pragma("unroll") for (int k = 0; k < 2; ++k) dst[n][k] = *(const PG8_LAS bf16x8*)(lds + PG8_SB(b, h) + boff + n * 2048 + k * 1024); } while (0)
; #define PG8_MMA(ai, bj, At, Bt) do { __builtin_amdgcn_s_setprio(1); _Pragma("unroll") for (int m = 0; m < 4; ++m) _Pragma("unroll") for (int n = 0; n < 2; ++n) _Pragma("unroll") for (int k = 0; k < 2; ++k) \
;         acc[ai][bj][m][n] = __builtin_amdgcn_mfma_f32_16x16x32_bf16(Bt[n][k], At[m][k], acc[ai][bj][m][n], 0, 0, 0); __builtin_amdgcn_s_setprio(0); } while (0)
; #define PG8_WAIT_V(n) asm volatile("s_waitcnt vmcnt(" #n ")" ::: "memory")
; #define PG8_WAIT_L(n) asm volatile("s_waitcnt lgkmcnt(" #n ")" ::: "memory")
; #define PG8_BAR __builtin_amdgcn_s_barrier()
; #define PG8_SCHED __builtin_amdgcn_sched_barrier(0)
;     ...
;             PG8_WAIT_V(8); PG8_WAIT_L(0); PG8_BAR; PG8_MMA(1, 0, At, B0); PG8_MMA(1, 1, At, B1); PG8_BAR; PG8_SCHED;
;             PG8_LDB(B0, 1, 0); PG8_LDB(B1, 1, 1); PG8_SCHED; PG8_LDA(At, 1, 0); PG8_STAGE(PG8_SA(0, 1), a2 + hstep, voffA);
;             PG8_WAIT_V(8); PG8_WAIT_L(0); PG8_BAR; PG8_MMA(0, 0, At, B0); PG8_MMA(0, 1, At, B1); PG8_BAR; PG8_SCHED;
	v_mfma_f32_16x16x32_bf16 v[62:65], v[114:117], v[162:165], v[62:65]
	v_mfma_f32_16x16x32_bf16 v[58:61], v[122:125], v[162:165], v[58:61]
	v_mfma_f32_16x16x32_bf16 v[50:53], v[114:117], v[204:207], v[50:53]
	v_mfma_f32_16x16x32_bf16 v[42:45], v[122:125], v[204:207], v[42:45]
	v_mfma_f32_16x16x32_bf16 v[34:37], v[114:117], v[218:221], v[34:37]
	v_mfma_f32_16x16x32_bf16 v[26:29], v[122:125], v[218:221], v[26:29]
	v_mfma_f32_16x16x32_bf16 v[18:21], v[114:117], v[226:229], v[18:21]
	v_mfma_f32_16x16x32_bf16 v[10:13], v[122:125], v[226:229], v[10:13]
	v_mfma_f32_16x16x32_bf16 v[62:65], v[118:121], v[166:169], v[62:65]
	v_mfma_f32_16x16x32_bf16 v[58:61], v[126:129], v[166:169], v[58:61]
	v_mfma_f32_16x16x32_bf16 v[50:53], v[118:121], v[214:217], v[50:53]
	v_mfma_f32_16x16x32_bf16 v[42:45], v[126:129], v[214:217], v[42:45]
	v_mfma_f32_16x16x32_bf16 v[34:37], v[118:121], v[222:225], v[34:37]
	v_mfma_f32_16x16x32_bf16 v[26:29], v[126:129], v[222:225], v[26:29]
	v_mfma_f32_16x16x32_bf16 v[18:21], v[118:121], v[230:233], v[18:21]
	v_mfma_f32_16x16x32_bf16 v[10:13], v[126:129], v[230:233], v[10:13]
	s_setprio 0
	s_setprio 1
	v_mfma_f32_16x16x32_bf16 v[54:57], v[146:149], v[162:165], v[54:57]
	v_mfma_f32_16x16x32_bf16 v[46:49], v[154:157], v[162:165], v[46:49]
	v_mfma_f32_16x16x32_bf16 v[38:41], v[146:149], v[204:207], v[38:41]
	v_mfma_f32_16x16x32_bf16 v[30:33], v[154:157], v[204:207], v[30:33]
	v_mfma_f32_16x16x32_bf16 v[22:25], v[146:149], v[218:221], v[22:25]
	v_mfma_f32_16x16x32_bf16 v[14:17], v[154:157], v[218:221], v[14:17]
	v_mfma_f32_16x16x32_bf16 v[6:9], v[146:149], v[226:229], v[6:9]
	v_mfma_f32_16x16x32_bf16 v[2:5], v[154:157], v[226:229], v[2:5]
	v_mfma_f32_16x16x32_bf16 v[54:57], v[150:153], v[166:169], v[54:57]
	v_mfma_f32_16x16x32_bf16 v[46:49], v[158:161], v[166:169], v[46:49]
	v_mfma_f32_16x16x32_bf16 v[38:41], v[150:153], v[214:217], v[38:41]
	v_mfma_f32_16x16x32_bf16 v[30:33], v[158:161], v[214:217], v[30:33]
	v_mfma_f32_16x16x32_bf16 v[22:25], v[150:153], v[222:225], v[22:25]
	v_mfma_f32_16x16x32_bf16 v[14:17], v[158:161], v[222:225], v[14:17]
	v_mfma_f32_16x16x32_bf16 v[6:9], v[150:153], v[230:233], v[6:9]
	v_mfma_f32_16x16x32_bf16 v[2:5], v[158:161], v[230:233], v[2:5]
	s_barrier
	s_setprio 0
	s_add_i32 s53, 0, 0x18000
	s_add_i32 s54, 0, 0x1c000
	v_add_u32_e32 v126, s53, v209
	v_add_u32_e32 v158, s54, v209
	ds_read_b128 v[114:117], v126
	ds_read_b128 v[118:121], v126 offset:1024
	ds_read_b128 v[122:125], v126 offset:2048
	ds_read_b128 v[126:129], v126 offset:3072
	ds_read_b128 v[146:149], v158
	ds_read_b128 v[150:153], v158 offset:1024
	ds_read_b128 v[154:157], v158 offset:2048
	ds_read_b128 v[158:161], v158 offset:3072
	s_add_u32 s22, s22, 0x40000
	s_addc_u32 s23, s23, 0
	s_mov_b32 m0, s34
	v_lshl_add_u64 v[242:243], s[22:23], 0, v[178:179]
	ds_read_b128 v[162:165], v213 offset:32768
	ds_read_b128 v[166:169], v213 offset:33792
	ds_read_b128 v[204:207], v213 offset:34816
	ds_read_b128 v[214:217], v213 offset:35840
	ds_read_b128 v[218:221], v213 offset:36864
	ds_read_b128 v[222:225], v213 offset:37888
	ds_read_b128 v[226:229], v213 offset:38912
	ds_read_b128 v[230:233], v213 offset:39936
	global_load_lds_dwordx4 v[242:243], off
	v_lshl_add_u64 v[242:243], s[22:23], 0, v[174:175]
	s_mov_b32 m0, s35
	s_nop 0
	global_load_lds_dwordx4 v[242:243], off
	s_waitcnt vmcnt(8)
	s_waitcnt lgkmcnt(0)
	s_setprio 1
	s_barrier
	v_mfma_f32_16x16x32_bf16 v[142:145], v[114:117], v[162:165], v[142:145]
	v_mfma_f32_16x16x32_bf16 v[138:141], v[122:125], v[162:165], v[138:141]
	v_mfma_f32_16x16x32_bf16 v[110:113], v[114:117], v[204:207], v[110:113]
	v_mfma_f32_16x16x32_bf16 v[106:109], v[122:125], v[204:207], v[106:109]
	v_mfma_f32_16x16x32_bf16 v[98:101], v[114:117], v[218:221], v[98:101]
	v_mfma_f32_16x16x32_bf16 v[90:93], v[122:125], v[218:221], v[90:93]
	v_mfma_f32_16x16x32_bf16 v[82:85], v[114:117], v[226:229], v[82:85]
	v_mfma_f32_16x16x32_bf16 v[74:77], v[122:125], v[226:229], v[74:77]
	v_mfma_f32_16x16x32_bf16 v[142:145], v[118:121], v[166:169], v[142:145]
	v_mfma_f32_16x16x32_bf16 v[138:141], v[126:129], v[166:169], v[138:141]
	v_mfma_f32_16x16x32_bf16 v[110:113], v[118:121], v[214:217], v[110:113]
	v_mfma_f32_16x16x32_bf16 v[106:109], v[126:129], v[214:217], v[106:109]
	v_mfma_f32_16x16x32_bf16 v[98:101], v[118:121], v[222:225], v[98:101]
	v_mfma_f32_16x16x32_bf16 v[90:93], v[126:129], v[222:225], v[90:93]
	v_mfma_f32_16x16x32_bf16 v[82:85], v[118:121], v[230:233], v[82:85]
	v_mfma_f32_16x16x32_bf16 v[74:77], v[126:129], v[230:233], v[74:77]
	s_setprio 0
	s_setprio 1
	v_mfma_f32_16x16x32_bf16 v[134:137], v[146:149], v[162:165], v[134:137]
	v_mfma_f32_16x16x32_bf16 v[130:133], v[154:157], v[162:165], v[130:133]
	v_mfma_f32_16x16x32_bf16 v[102:105], v[146:149], v[204:207], v[102:105]
	v_mfma_f32_16x16x32_bf16 v[94:97], v[154:157], v[204:207], v[94:97]
	v_mfma_f32_16x16x32_bf16 v[86:89], v[146:149], v[218:221], v[86:89]
	v_mfma_f32_16x16x32_bf16 v[78:81], v[154:157], v[218:221], v[78:81]
	v_mfma_f32_16x16x32_bf16 v[70:73], v[146:149], v[226:229], v[70:73]
	v_mfma_f32_16x16x32_bf16 v[66:69], v[154:157], v[226:229], v[66:69]
	v_mfma_f32_16x16x32_bf16 v[134:137], v[150:153], v[166:169], v[134:137]
	v_mfma_f32_16x16x32_bf16 v[130:133], v[158:161], v[166:169], v[130:133]
	v_mfma_f32_16x16x32_bf16 v[102:105], v[150:153], v[214:217], v[102:105]
	v_mfma_f32_16x16x32_bf16 v[94:97], v[158:161], v[214:217], v[94:97]
	v_mfma_f32_16x16x32_bf16 v[86:89], v[150:153], v[222:225], v[86:89]
	v_mfma_f32_16x16x32_bf16 v[78:81], v[158:161], v[222:225], v[78:81]
	v_mfma_f32_16x16x32_bf16 v[70:73], v[150:153], v[230:233], v[70:73]
	v_mfma_f32_16x16x32_bf16 v[66:69], v[158:161], v[230:233], v[66:69]
	s_barrier
; #define PG8_STAGE(bufoff, gbase, voff) do { _Pragma("unroll") for (int _i = 0; _i < 2; ++_i) \
;         __builtin_amdgcn_global_load_lds((const unsigned*)((const char*)(gbase) + (voff)[_i]), (PG8_LAS unsigned*)(lds + (bufoff) + ldsw + _i * 8192), 16, 0, 0); } while (0)
; #define PG8_LDA(dst, b, h) do { _Pragma("unroll") for (int m = 0; m < 4; ++m) _Pragma("unroll") for (int k = 0; k < 2; ++k) dst[m][k] = *(const PG8_LAS bf16x8*)(lds + PG8_SA(b, h) + aoff + m * 2048 + k * 1024); } while (0)
; #define PG8_MMA(ai, bj, At, Bt) do { __builtin_amdgcn_s_setprio(1); _Pragma("unroll") for (int m = 0; m < 4; ++m) _Pragma("unroll") for (int n = 0; n < 2; ++n) _Pragma("unroll") for (int k = 0; k < 2; ++k) \
;         acc[ai][bj][m][n] = __builtin_amdgcn_mfma_f32_16x16x32_bf16(Bt[n][k], At[m][k], acc[ai][bj][m][n], 0, 0, 0); __builtin_amdgcn_s_setprio(0); } while (0)
; #define PG8_WAIT_V(n) asm volatile("s_waitcnt vmcnt(" #n ")" ::: "memory")
; #define PG8_WAIT_L(n) asm volatile("s_waitcnt lgkmcnt(" #n ")" ::: "memory")
; #define PG8_BAR __builtin_amdgcn_s_barrier()
; #define PG8_SCHED __builtin_amdgcn_sched_barrier(0)
;     ...
;             PG8_LDA(At, 1, 1); PG8_STAGE(PG8_SB(1, 0), b3, voffB); PG8_STAGE(PG8_SB(1, 1), b3 + hstep, voffB); PG8_STAGE(PG8_SA(1, 0), a3, voffA);
;             PG8_WAIT_V(8); PG8_WAIT_L(0); PG8_BAR; PG8_MMA(1, 0, At, B0); PG8_MMA(1, 1, At, B1); PG8_BAR; PG8_SCHED;
;         }
;         if constexpr (ALIGN_EPI) { if (wr == 0) PG8_BAR; }
	s_setprio 0
	s_add_i32 s22, s53, s28
	v_lshl_add_u64 v[234:235], v[234:235], 0, s[2:3]
	s_mov_b32 m0, s22
	ds_read_b128 v[162:165], v213 offset:49152
	ds_read_b128 v[166:169], v213 offset:50176
	ds_read_b128 v[204:207], v213 offset:51200
	ds_read_b128 v[214:217], v213 offset:52224
	ds_read_b128 v[218:221], v213 offset:53248
	ds_read_b128 v[222:225], v213 offset:54272
	ds_read_b128 v[226:229], v213 offset:55296
	ds_read_b128 v[230:233], v213 offset:56320
	global_load_lds_dwordx4 v[234:235], off
	s_add_i32 m0, s22, 0x2000
	s_add_u32 s20, s20, 0x40080
	v_lshl_add_u64 v[234:235], v[236:237], 0, s[2:3]
	s_addc_u32 s21, s21, 0
	s_add_i32 s22, s54, s28
	global_load_lds_dwordx4 v[234:235], off
	v_lshl_add_u64 v[234:235], s[20:21], 0, v[176:177]
	s_mov_b32 m0, s22
	s_nop 0
	global_load_lds_dwordx4 v[234:235], off
	v_lshl_add_u64 v[234:235], s[20:21], 0, v[172:173]
	s_add_i32 m0, s22, 0x2000
	s_nop 0
	global_load_lds_dwordx4 v[234:235], off
	v_lshl_add_u64 v[234:235], v[238:239], 0, s[2:3]
	s_mov_b32 m0, s37
	s_nop 0
	global_load_lds_dwordx4 v[234:235], off
	v_lshl_add_u64 v[234:235], v[240:241], 0, s[2:3]
	s_mov_b32 m0, s38
	s_nop 0
	global_load_lds_dwordx4 v[234:235], off
	s_waitcnt vmcnt(8)
	s_waitcnt lgkmcnt(0)
	s_setprio 1
	s_barrier
	v_mfma_f32_16x16x32_bf16 v[62:65], v[114:117], v[162:165], v[62:65]
	v_mfma_f32_16x16x32_bf16 v[58:61], v[122:125], v[162:165], v[58:61]
	v_mfma_f32_16x16x32_bf16 v[50:53], v[114:117], v[204:207], v[50:53]
	v_mfma_f32_16x16x32_bf16 v[42:45], v[122:125], v[204:207], v[42:45]
	v_mfma_f32_16x16x32_bf16 v[34:37], v[114:117], v[218:221], v[34:37]
	v_mfma_f32_16x16x32_bf16 v[26:29], v[122:125], v[218:221], v[26:29]
	v_mfma_f32_16x16x32_bf16 v[18:21], v[114:117], v[226:229], v[18:21]
	v_mfma_f32_16x16x32_bf16 v[10:13], v[122:125], v[226:229], v[10:13]
	v_mfma_f32_16x16x32_bf16 v[62:65], v[118:121], v[166:169], v[62:65]
	v_mfma_f32_16x16x32_bf16 v[58:61], v[126:129], v[166:169], v[58:61]
	v_mfma_f32_16x16x32_bf16 v[50:53], v[118:121], v[214:217], v[50:53]
	v_mfma_f32_16x16x32_bf16 v[42:45], v[126:129], v[214:217], v[42:45]
	v_mfma_f32_16x16x32_bf16 v[34:37], v[118:121], v[222:225], v[34:37]
	v_mfma_f32_16x16x32_bf16 v[26:29], v[126:129], v[222:225], v[26:29]
	v_mfma_f32_16x16x32_bf16 v[18:21], v[118:121], v[230:233], v[18:21]
	v_mfma_f32_16x16x32_bf16 v[10:13], v[126:129], v[230:233], v[10:13]
	s_setprio 0
	s_setprio 1
	v_mfma_f32_16x16x32_bf16 v[54:57], v[146:149], v[162:165], v[54:57]
	v_mfma_f32_16x16x32_bf16 v[46:49], v[154:157], v[162:165], v[46:49]
	v_mfma_f32_16x16x32_bf16 v[38:41], v[146:149], v[204:207], v[38:41]
	v_mfma_f32_16x16x32_bf16 v[30:33], v[154:157], v[204:207], v[30:33]
	v_mfma_f32_16x16x32_bf16 v[22:25], v[146:149], v[218:221], v[22:25]
	v_mfma_f32_16x16x32_bf16 v[14:17], v[154:157], v[218:221], v[14:17]
	v_mfma_f32_16x16x32_bf16 v[6:9], v[146:149], v[226:229], v[6:9]
	v_mfma_f32_16x16x32_bf16 v[2:5], v[154:157], v[226:229], v[2:5]
	v_mfma_f32_16x16x32_bf16 v[54:57], v[150:153], v[166:169], v[54:57]
	v_mfma_f32_16x16x32_bf16 v[46:49], v[158:161], v[166:169], v[46:49]
	v_mfma_f32_16x16x32_bf16 v[38:41], v[150:153], v[214:217], v[38:41]
	v_mfma_f32_16x16x32_bf16 v[30:33], v[158:161], v[214:217], v[30:33]
	v_mfma_f32_16x16x32_bf16 v[22:25], v[150:153], v[222:225], v[22:25]
	v_mfma_f32_16x16x32_bf16 v[14:17], v[158:161], v[222:225], v[14:17]
	v_mfma_f32_16x16x32_bf16 v[6:9], v[150:153], v[230:233], v[6:9]
	v_mfma_f32_16x16x32_bf16 v[2:5], v[158:161], v[230:233], v[2:5]
	s_barrier
	s_setprio 0
	s_add_i32 s52, s52, 2
	s_add_u32 s18, s18, 0x100
	s_addc_u32 s19, s19, 0
	s_add_u32 s50, s50, 0x100
	s_addc_u32 s51, s51, 0
	s_cmp_gt_u32 s52, 13
	s_cbranch_scc0 .LBB0_3094
	s_and_b64 vcc, exec, s[6:7]
	s_cbranch_vccz .LBB0_3097
	s_barrier

; #define PG8_STAGE(bufoff, gbase, voff) do { _Pragma("unroll") for (int _i = 0; _i < 2; ++_i) \
;         __builtin_amdgcn_global_load_lds((const unsigned*)((const char*)(gbase) + (voff)[_i]), (PG8_LAS unsigned*)(lds + (bufoff) + ldsw + _i * 8192), 16, 0, 0); } while (0)
; #define PG8_LDA(dst, b, h) do { _Pragma("unroll") for (int m = 0; m < 4; ++m) _Pragma("unroll") for (int k = 0; k < 2; ++k) dst[m][k] = *(const PG8_LAS bf16x8*)(lds + PG8_SA(b, h) + aoff + m * 2048 + k * 1024); } while (0)
; #define PG8_LDB(dst, b, h) do { _Pragma("unroll") for (int n = 0; n < 2; ++n) _Pragma("unroll") for (int k = 0; k < 2; ++k) dst[n][k] = *(const PG8_LAS bf16x8*)(lds + PG8_SB(b, h) + boff + n * 2048 + k * 1024); } while (0)
; #define PG8_MMA(ai, bj, At, Bt) do { __builtin_amdgcn_s_setprio(1); _Pragma("unroll") for (int m = 0; m < 4; ++m) _Pragma("unroll") for (int n = 0; n < 2; ++n) _Pragma("unroll") for (int k = 0; k < 2; ++k) \
;         acc[ai][bj][m][n] = __builtin_amdgcn_mfma_f32_16x16x32_bf16(Bt[n][k], At[m][k], acc[ai][bj][m][n], 0, 0, 0); __builtin_amdgcn_s_setprio(0); } while (0)
; #define PG8_WAIT_V(n) asm volatile("s_waitcnt vmcnt(" #n ")" ::: "memory")
; #define PG8_WAIT_L(n) asm volatile("s_waitcnt lgkmcnt(" #n ")" ::: "memory")
; #define PG8_BAR __builtin_amdgcn_s_barrier()
; #define PG8_SCHED __builtin_amdgcn_sched_barrier(0)
;     ...
;             const bool last = (t == nt - 2);
;             const char* a1 = cA + (size_t)(t + 1) * kstep;
;             const char* a2 = last ? nA : cA + (size_t)(t + 2) * kstep; const char* b2 = last ? nB : cB + (size_t)(t + 2) * kstep;
;             const char* a3 = a2 + kstep; const char* b3 = b2 + kstep;
;             if (last && has_next) S.a_ready(nxt);
;             PG8_LDB(B0, 0, 0); PG8_LDB(B1, 0, 1); PG8_SCHED; PG8_LDA(At, 0, 0); PG8_STAGE(PG8_SA(1, 1), a1 + hstep, voffA);
;             PG8_WAIT_V(8); PG8_WAIT_L(0); PG8_BAR; PG8_MMA(0, 0, At, B0); PG8_MMA(0, 1, At, B1); PG8_BAR; PG8_SCHED;
;             PG8_LDA(At, 0, 1); PG8_STAGE(PG8_SB(0, 0), b2, voffB); PG8_STAGE(PG8_SB(0, 1), b2 + hstep, voffB); PG8_STAGE(PG8_SA(0, 0), a2, voffA);
.LBB0_3248:
	ds_read_b128 v[154:157], v151
	ds_read_b128 v[158:161], v151 offset:1024
	ds_read_b128 v[162:165], v151 offset:2048
	ds_read_b128 v[166:169], v151 offset:3072
	ds_read_b128 v[170:173], v152
	ds_read_b128 v[174:177], v152 offset:1024
	ds_read_b128 v[178:181], v152 offset:2048
	ds_read_b128 v[182:185], v152 offset:3072
	s_add_u32 s22, s20, 0xfffc0080
	s_addc_u32 s23, s21, -1
	s_cmp_eq_u32 s55, 12
	s_cselect_b32 s25, s13, s23
	s_cselect_b32 s24, s51, s22
	s_cselect_b32 s23, s11, s54
	s_cselect_b32 s22, s52, s53
	v_lshl_add_u64 v[146:147], s[20:21], 0, v[138:139]
	s_add_i32 m0, s19, 0xc000
	ds_read_b128 v[186:189], v153
	ds_read_b128 v[190:193], v153 offset:1024
	ds_read_b128 v[194:197], v153 offset:2048
	ds_read_b128 v[198:201], v153 offset:3072
	ds_read_b128 v[202:205], v153 offset:4096
	ds_read_b128 v[210:213], v153 offset:5120
	ds_read_b128 v[214:217], v153 offset:6144
	ds_read_b128 v[218:221], v153 offset:7168
	global_load_lds_dwordx4 v[146:147], off
	v_lshl_add_u64 v[146:147], s[20:21], 0, v[140:141]
	s_add_i32 m0, s19, 0xe000
	s_nop 0
	global_load_lds_dwordx4 v[146:147], off
	s_waitcnt vmcnt(8)
	s_waitcnt lgkmcnt(0)
	s_setprio 1
	s_barrier
	v_mfma_f32_16x16x32_bf16 v[126:129], v[154:157], v[186:189], v[126:129]
	v_mfma_f32_16x16x32_bf16 v[122:125], v[162:165], v[186:189], v[122:125]
	v_mfma_f32_16x16x32_bf16 v[110:113], v[154:157], v[194:197], v[110:113]
	v_mfma_f32_16x16x32_bf16 v[106:109], v[162:165], v[194:197], v[106:109]
	v_mfma_f32_16x16x32_bf16 v[94:97], v[154:157], v[202:205], v[94:97]
	v_mfma_f32_16x16x32_bf16 v[90:93], v[162:165], v[202:205], v[90:93]
	v_mfma_f32_16x16x32_bf16 v[78:81], v[154:157], v[214:217], v[78:81]
	v_mfma_f32_16x16x32_bf16 v[74:77], v[162:165], v[214:217], v[74:77]
	v_mfma_f32_16x16x32_bf16 v[126:129], v[158:161], v[190:193], v[126:129]
	v_mfma_f32_16x16x32_bf16 v[122:125], v[166:169], v[190:193], v[122:125]
	v_mfma_f32_16x16x32_bf16 v[110:113], v[158:161], v[198:201], v[110:113]
	v_mfma_f32_16x16x32_bf16 v[106:109], v[166:169], v[198:201], v[106:109]
	v_mfma_f32_16x16x32_bf16 v[94:97], v[158:161], v[210:213], v[94:97]
	v_mfma_f32_16x16x32_bf16 v[90:93], v[166:169], v[210:213], v[90:93]
	v_mfma_f32_16x16x32_bf16 v[78:81], v[158:161], v[218:221], v[78:81]
	v_mfma_f32_16x16x32_bf16 v[74:77], v[166:169], v[218:221], v[74:77]
	s_setprio 0
	s_setprio 1
	v_mfma_f32_16x16x32_bf16 v[118:121], v[170:173], v[186:189], v[118:121]
	v_mfma_f32_16x16x32_bf16 v[114:117], v[178:181], v[186:189], v[114:117]
	v_mfma_f32_16x16x32_bf16 v[102:105], v[170:173], v[194:197], v[102:105]
	v_mfma_f32_16x16x32_bf16 v[98:101], v[178:181], v[194:197], v[98:101]
	v_mfma_f32_16x16x32_bf16 v[86:89], v[170:173], v[202:205], v[86:89]
	v_mfma_f32_16x16x32_bf16 v[82:85], v[178:181], v[202:205], v[82:85]
	v_mfma_f32_16x16x32_bf16 v[70:73], v[170:173], v[214:217], v[70:73]
	v_mfma_f32_16x16x32_bf16 v[66:69], v[178:181], v[214:217], v[66:69]
	v_mfma_f32_16x16x32_bf16 v[118:121], v[174:177], v[190:193], v[118:121]
	v_mfma_f32_16x16x32_bf16 v[114:117], v[182:185], v[190:193], v[114:117]
	v_mfma_f32_16x16x32_bf16 v[102:105], v[174:177], v[198:201], v[102:105]
	v_mfma_f32_16x16x32_bf16 v[98:101], v[182:185], v[198:201], v[98:101]
	v_mfma_f32_16x16x32_bf16 v[86:89], v[174:177], v[210:213], v[86:89]
	v_mfma_f32_16x16x32_bf16 v[82:85], v[182:185], v[210:213], v[82:85]
	v_mfma_f32_16x16x32_bf16 v[70:73], v[174:177], v[218:221], v[70:73]
	v_mfma_f32_16x16x32_bf16 v[66:69], v[182:185], v[218:221], v[66:69]
	s_barrier
	s_setprio 0
	s_add_i32 s56, s45, s30
	v_lshl_add_u64 v[146:147], s[22:23], 0, v[134:135]
	s_mov_b32 m0, s56
	ds_read_b128 v[186:189], v153 offset:16384
	ds_read_b128 v[190:193], v153 offset:17408
	ds_read_b128 v[194:197], v153 offset:18432
	ds_read_b128 v[198:201], v153 offset:19456
	ds_read_b128 v[202:205], v153 offset:20480
	ds_read_b128 v[210:213], v153 offset:21504
	ds_read_b128 v[214:217], v153 offset:22528
	ds_read_b128 v[218:221], v153 offset:23552
	global_load_lds_dwordx4 v[146:147], off
	s_add_i32 m0, s56, 0x2000
	s_add_u32 s56, s22, 0x40000
	v_lshl_add_u64 v[206:207], s[22:23], 0, v[130:131]
	s_addc_u32 s57, s23, 0
	s_add_i32 s58, s46, s30
	global_load_lds_dwordx4 v[206:207], off
	v_lshl_add_u64 v[208:209], s[56:57], 0, v[134:135]
	s_mov_b32 m0, s58
	v_lshl_add_u64 v[222:223], s[24:25], 0, v[132:133]
	global_load_lds_dwordx4 v[208:209], off
	v_lshl_add_u64 v[208:209], s[56:57], 0, v[130:131]
	s_add_i32 m0, s58, 0x2000
	s_nop 0
	global_load_lds_dwordx4 v[208:209], off
	v_lshl_add_u64 v[208:209], s[24:25], 0, v[136:137]
	s_mov_b32 m0, s19
	s_nop 0
	global_load_lds_dwordx4 v[208:209], off
	s_mov_b32 m0, s34
	s_nop 0
	global_load_lds_dwordx4 v[222:223], off
	s_waitcnt vmcnt(8)
	s_waitcnt lgkmcnt(0)
	s_setprio 1
	s_barrier
; #define PG8_STAGE(bufoff, gbase, voff) do { _Pragma("unroll") for (int _i = 0; _i < 2; ++_i) \
;         __builtin_amdgcn_global_load_lds((const unsigned*)((const char*)(gbase) + (voff)[_i]), (PG8_LAS unsigned*)(lds + (bufoff) + ldsw + _i * 8192), 16, 0, 0); } while (0)
; #define PG8_LDA(dst, b, h) do { _Pragma("unroll") for (int m = 0; m < 4; ++m) _Pragma("unroll") for (int k = 0; k < 2; ++k) dst[m][k] = *(const PG8_LAS bf16x8*)(lds + PG8_SA(b, h) + aoff + m * 2048 + k * 1024); } while (0)
; #define PG8_LDB(dst, b, h) do { _Pragma("unroll") for (int n = 0; n < 2; ++n) _Pragma("unroll") for (int k = 0; k < 2; ++k) dst[n][k] = *(const PG8_LAS bf16x8*)(lds + PG8_SB(b, h) + boff + n * 2048 + k * 1024); } while (0)
; #define PG8_MMA(ai, bj, At, Bt) do { __builtin_amdgcn_s_setprio(1); _Pragma("unroll") for (int m = 0; m < 4; ++m) _Pragma("unroll") for (int n = 0; n < 2; ++n) _Pragma("unroll") for (int k = 0; k < 2; ++k) \
;         acc[ai][bj][m][n] = __builtin_amdgcn_mfma_f32_16x16x32_bf16(Bt[n][k], At[m][k], acc[ai][bj][m][n], 0, 0, 0); __builtin_amdgcn_s_setprio(0); } while (0)
; #define PG8_WAIT_V(n) asm volatile("s_waitcnt vmcnt(" #n ")" ::: "memory")
; #define PG8_WAIT_L(n) asm volatile("s_waitcnt lgkmcnt(" #n ")" ::: "memory")
; #define PG8_BAR __builtin_amdgcn_s_barrier()
; #define PG8_SCHED __builtin_amdgcn_sched_barrier(0)
;     ...
;             PG8_WAIT_V(8); PG8_WAIT_L(0); PG8_BAR; PG8_MMA(1, 0, At, B0); PG8_MMA(1, 1, At, B1); PG8_BAR; PG8_SCHED;
;             PG8_LDB(B0, 1, 0); PG8_LDB(B1, 1, 1); PG8_SCHED; PG8_LDA(At, 1, 0); PG8_STAGE(PG8_SA(0, 1), a2 + hstep, voffA);
;             PG8_WAIT_V(8); PG8_WAIT_L(0); PG8_BAR; PG8_MMA(0, 0, At, B0); PG8_MMA(0, 1, At, B1); PG8_BAR; PG8_SCHED;
	v_mfma_f32_16x16x32_bf16 v[62:65], v[154:157], v[186:189], v[62:65]
	v_mfma_f32_16x16x32_bf16 v[58:61], v[162:165], v[186:189], v[58:61]
	v_mfma_f32_16x16x32_bf16 v[46:49], v[154:157], v[194:197], v[46:49]
	v_mfma_f32_16x16x32_bf16 v[42:45], v[162:165], v[194:197], v[42:45]
	v_mfma_f32_16x16x32_bf16 v[30:33], v[154:157], v[202:205], v[30:33]
	v_mfma_f32_16x16x32_bf16 v[26:29], v[162:165], v[202:205], v[26:29]
	v_mfma_f32_16x16x32_bf16 v[14:17], v[154:157], v[214:217], v[14:17]
	v_mfma_f32_16x16x32_bf16 v[10:13], v[162:165], v[214:217], v[10:13]
	v_mfma_f32_16x16x32_bf16 v[62:65], v[158:161], v[190:193], v[62:65]
	v_mfma_f32_16x16x32_bf16 v[58:61], v[166:169], v[190:193], v[58:61]
	v_mfma_f32_16x16x32_bf16 v[46:49], v[158:161], v[198:201], v[46:49]
	v_mfma_f32_16x16x32_bf16 v[42:45], v[166:169], v[198:201], v[42:45]
	v_mfma_f32_16x16x32_bf16 v[30:33], v[158:161], v[210:213], v[30:33]
	v_mfma_f32_16x16x32_bf16 v[26:29], v[166:169], v[210:213], v[26:29]
	v_mfma_f32_16x16x32_bf16 v[14:17], v[158:161], v[218:221], v[14:17]
	v_mfma_f32_16x16x32_bf16 v[10:13], v[166:169], v[218:221], v[10:13]
	s_setprio 0
	s_setprio 1
	v_mfma_f32_16x16x32_bf16 v[54:57], v[170:173], v[186:189], v[54:57]
	v_mfma_f32_16x16x32_bf16 v[50:53], v[178:181], v[186:189], v[50:53]
	v_mfma_f32_16x16x32_bf16 v[38:41], v[170:173], v[194:197], v[38:41]
	v_mfma_f32_16x16x32_bf16 v[34:37], v[178:181], v[194:197], v[34:37]
	v_mfma_f32_16x16x32_bf16 v[22:25], v[170:173], v[202:205], v[22:25]
	v_mfma_f32_16x16x32_bf16 v[18:21], v[178:181], v[202:205], v[18:21]
	v_mfma_f32_16x16x32_bf16 v[6:9], v[170:173], v[214:217], v[6:9]
	v_mfma_f32_16x16x32_bf16 v[2:5], v[178:181], v[214:217], v[2:5]
	v_mfma_f32_16x16x32_bf16 v[54:57], v[174:177], v[190:193], v[54:57]
	v_mfma_f32_16x16x32_bf16 v[50:53], v[182:185], v[190:193], v[50:53]
	v_mfma_f32_16x16x32_bf16 v[38:41], v[174:177], v[198:201], v[38:41]
	v_mfma_f32_16x16x32_bf16 v[34:37], v[182:185], v[198:201], v[34:37]
	v_mfma_f32_16x16x32_bf16 v[22:25], v[174:177], v[210:213], v[22:25]
	v_mfma_f32_16x16x32_bf16 v[18:21], v[182:185], v[210:213], v[18:21]
	v_mfma_f32_16x16x32_bf16 v[6:9], v[174:177], v[218:221], v[6:9]
	v_mfma_f32_16x16x32_bf16 v[2:5], v[182:185], v[218:221], v[2:5]
	s_barrier
	s_setprio 0
	s_add_i32 s56, 0, 0x18000
	s_add_i32 s57, 0, 0x1c000
	v_add_u32_e32 v166, s56, v149
	v_add_u32_e32 v182, s57, v149
	ds_read_b128 v[154:157], v166
	ds_read_b128 v[158:161], v166 offset:1024
	ds_read_b128 v[162:165], v166 offset:2048
	ds_read_b128 v[166:169], v166 offset:3072
	ds_read_b128 v[170:173], v182
	ds_read_b128 v[174:177], v182 offset:1024
	ds_read_b128 v[178:181], v182 offset:2048
	ds_read_b128 v[182:185], v182 offset:3072
	s_add_u32 s24, s24, 0x40000
	s_addc_u32 s25, s25, 0
	s_mov_b32 m0, s35
	v_lshl_add_u64 v[224:225], s[24:25], 0, v[136:137]
	ds_read_b128 v[186:189], v153 offset:32768
	ds_read_b128 v[190:193], v153 offset:33792
	ds_read_b128 v[194:197], v153 offset:34816
	ds_read_b128 v[198:201], v153 offset:35840
	ds_read_b128 v[202:205], v153 offset:36864
	ds_read_b128 v[210:213], v153 offset:37888
	ds_read_b128 v[214:217], v153 offset:38912
	ds_read_b128 v[218:221], v153 offset:39936
	global_load_lds_dwordx4 v[224:225], off
	v_lshl_add_u64 v[224:225], s[24:25], 0, v[132:133]
	s_mov_b32 m0, s36
	s_nop 0
	global_load_lds_dwordx4 v[224:225], off
	s_waitcnt vmcnt(8)
	s_waitcnt lgkmcnt(0)
	s_setprio 1
	s_barrier
	v_mfma_f32_16x16x32_bf16 v[126:129], v[154:157], v[186:189], v[126:129]
	v_mfma_f32_16x16x32_bf16 v[122:125], v[162:165], v[186:189], v[122:125]
	v_mfma_f32_16x16x32_bf16 v[110:113], v[154:157], v[194:197], v[110:113]
	v_mfma_f32_16x16x32_bf16 v[106:109], v[162:165], v[194:197], v[106:109]
	v_mfma_f32_16x16x32_bf16 v[94:97], v[154:157], v[202:205], v[94:97]
	v_mfma_f32_16x16x32_bf16 v[90:93], v[162:165], v[202:205], v[90:93]
	v_mfma_f32_16x16x32_bf16 v[78:81], v[154:157], v[214:217], v[78:81]
	v_mfma_f32_16x16x32_bf16 v[74:77], v[162:165], v[214:217], v[74:77]
	v_mfma_f32_16x16x32_bf16 v[126:129], v[158:161], v[190:193], v[126:129]
	v_mfma_f32_16x16x32_bf16 v[122:125], v[166:169], v[190:193], v[122:125]
	v_mfma_f32_16x16x32_bf16 v[110:113], v[158:161], v[198:201], v[110:113]
	v_mfma_f32_16x16x32_bf16 v[106:109], v[166:169], v[198:201], v[106:109]
	v_mfma_f32_16x16x32_bf16 v[94:97], v[158:161], v[210:213], v[94:97]
	v_mfma_f32_16x16x32_bf16 v[90:93], v[166:169], v[210:213], v[90:93]
	v_mfma_f32_16x16x32_bf16 v[78:81], v[158:161], v[218:221], v[78:81]
	v_mfma_f32_16x16x32_bf16 v[74:77], v[166:169], v[218:221], v[74:77]
	s_setprio 0
	s_setprio 1
	v_mfma_f32_16x16x32_bf16 v[118:121], v[170:173], v[186:189], v[118:121]
	v_mfma_f32_16x16x32_bf16 v[114:117], v[178:181], v[186:189], v[114:117]
	v_mfma_f32_16x16x32_bf16 v[102:105], v[170:173], v[194:197], v[102:105]
	v_mfma_f32_16x16x32_bf16 v[98:101], v[178:181], v[194:197], v[98:101]
	v_mfma_f32_16x16x32_bf16 v[86:89], v[170:173], v[202:205], v[86:89]
	v_mfma_f32_16x16x32_bf16 v[82:85], v[178:181], v[202:205], v[82:85]
	v_mfma_f32_16x16x32_bf16 v[70:73], v[170:173], v[214:217], v[70:73]
	v_mfma_f32_16x16x32_bf16 v[66:69], v[178:181], v[214:217], v[66:69]
	v_mfma_f32_16x16x32_bf16 v[118:121], v[174:177], v[190:193], v[118:121]
	v_mfma_f32_16x16x32_bf16 v[114:117], v[182:185], v[190:193], v[114:117]
	v_mfma_f32_16x16x32_bf16 v[102:105], v[174:177], v[198:201], v[102:105]
	v_mfma_f32_16x16x32_bf16 v[98:101], v[182:185], v[198:201], v[98:101]
	v_mfma_f32_16x16x32_bf16 v[86:89], v[174:177], v[210:213], v[86:89]
	v_mfma_f32_16x16x32_bf16 v[82:85], v[182:185], v[210:213], v[82:85]
	v_mfma_f32_16x16x32_bf16 v[70:73], v[174:177], v[218:221], v[70:73]
	v_mfma_f32_16x16x32_bf16 v[66:69], v[182:185], v[218:221], v[66:69]
	s_barrier
; #define PG8_STAGE(bufoff, gbase, voff) do { _Pragma("unroll") for (int _i = 0; _i < 2; ++_i) \
;         __builtin_amdgcn_global_load_lds((const unsigned*)((const char*)(gbase) + (voff)[_i]), (PG8_LAS unsigned*)(lds + (bufoff) + ldsw + _i * 8192), 16, 0, 0); } while (0)
; #define PG8_LDA(dst, b, h) do { _Pragma("unroll") for (int m = 0; m < 4; ++m) _Pragma("unroll") for (int k = 0; k < 2; ++k) dst[m][k] = *(const PG8_LAS bf16x8*)(lds + PG8_SA(b, h) + aoff + m * 2048 + k * 1024); } while (0)
; #define PG8_MMA(ai, bj, At, Bt) do { __builtin_amdgcn_s_setprio(1); _Pragma("unroll") for (int m = 0; m < 4; ++m) _Pragma("unroll") for (int n = 0; n < 2; ++n) _Pragma("unroll") for (int k = 0; k < 2; ++k) \
;         acc[ai][bj][m][n] = __builtin_amdgcn_mfma_f32_16x16x32_bf16(Bt[n][k], At[m][k], acc[ai][bj][m][n], 0, 0, 0); __builtin_amdgcn_s_setprio(0); } while (0)
; #define PG8_WAIT_V(n) asm volatile("s_waitcnt vmcnt(" #n ")" ::: "memory")
; #define PG8_WAIT_L(n) asm volatile("s_waitcnt lgkmcnt(" #n ")" ::: "memory")
; #define PG8_BAR __builtin_amdgcn_s_barrier()
; #define PG8_SCHED __builtin_amdgcn_sched_barrier(0)
;     ...
;             PG8_LDA(At, 1, 1); PG8_STAGE(PG8_SB(1, 0), b3, voffB); PG8_STAGE(PG8_SB(1, 1), b3 + hstep, voffB); PG8_STAGE(PG8_SA(1, 0), a3, voffA);
;             PG8_WAIT_V(8); PG8_WAIT_L(0); PG8_BAR; PG8_MMA(1, 0, At, B0); PG8_MMA(1, 1, At, B1); PG8_BAR; PG8_SCHED;
;         }
;         if constexpr (ALIGN_EPI) { if (wr == 0) PG8_BAR; }
	s_setprio 0
	s_add_i32 s24, s56, s30
	v_lshl_add_u64 v[146:147], v[146:147], 0, s[6:7]
	s_mov_b32 m0, s24
	ds_read_b128 v[186:189], v153 offset:49152
	ds_read_b128 v[190:193], v153 offset:50176
	ds_read_b128 v[194:197], v153 offset:51200
	ds_read_b128 v[198:201], v153 offset:52224
	ds_read_b128 v[202:205], v153 offset:53248
	ds_read_b128 v[210:213], v153 offset:54272
	ds_read_b128 v[214:217], v153 offset:55296
	ds_read_b128 v[218:221], v153 offset:56320
	global_load_lds_dwordx4 v[146:147], off
	s_add_i32 m0, s24, 0x2000
	s_add_u32 s22, s22, 0x40080
	v_lshl_add_u64 v[146:147], v[206:207], 0, s[6:7]
	s_addc_u32 s23, s23, 0
	s_add_i32 s24, s57, s30
	global_load_lds_dwordx4 v[146:147], off
	v_lshl_add_u64 v[146:147], s[22:23], 0, v[134:135]
	s_mov_b32 m0, s24
	s_nop 0
	global_load_lds_dwordx4 v[146:147], off
	v_lshl_add_u64 v[146:147], s[22:23], 0, v[130:131]
	s_add_i32 m0, s24, 0x2000
	s_nop 0
	global_load_lds_dwordx4 v[146:147], off
	v_lshl_add_u64 v[146:147], v[208:209], 0, s[6:7]
	s_mov_b32 m0, s38
	s_nop 0
	global_load_lds_dwordx4 v[146:147], off
	v_lshl_add_u64 v[146:147], v[222:223], 0, s[6:7]
	s_mov_b32 m0, s39
	s_nop 0
	global_load_lds_dwordx4 v[146:147], off
	s_waitcnt vmcnt(8)
	s_waitcnt lgkmcnt(0)
	s_setprio 1
	s_barrier
	v_mfma_f32_16x16x32_bf16 v[62:65], v[154:157], v[186:189], v[62:65]
	v_mfma_f32_16x16x32_bf16 v[58:61], v[162:165], v[186:189], v[58:61]
	v_mfma_f32_16x16x32_bf16 v[46:49], v[154:157], v[194:197], v[46:49]
	v_mfma_f32_16x16x32_bf16 v[42:45], v[162:165], v[194:197], v[42:45]
	v_mfma_f32_16x16x32_bf16 v[30:33], v[154:157], v[202:205], v[30:33]
	v_mfma_f32_16x16x32_bf16 v[26:29], v[162:165], v[202:205], v[26:29]
	v_mfma_f32_16x16x32_bf16 v[14:17], v[154:157], v[214:217], v[14:17]
	v_mfma_f32_16x16x32_bf16 v[10:13], v[162:165], v[214:217], v[10:13]
	v_mfma_f32_16x16x32_bf16 v[62:65], v[158:161], v[190:193], v[62:65]
	v_mfma_f32_16x16x32_bf16 v[58:61], v[166:169], v[190:193], v[58:61]
	v_mfma_f32_16x16x32_bf16 v[46:49], v[158:161], v[198:201], v[46:49]
	v_mfma_f32_16x16x32_bf16 v[42:45], v[166:169], v[198:201], v[42:45]
	v_mfma_f32_16x16x32_bf16 v[30:33], v[158:161], v[210:213], v[30:33]
	v_mfma_f32_16x16x32_bf16 v[26:29], v[166:169], v[210:213], v[26:29]
	v_mfma_f32_16x16x32_bf16 v[14:17], v[158:161], v[218:221], v[14:17]
	v_mfma_f32_16x16x32_bf16 v[10:13], v[166:169], v[218:221], v[10:13]
	s_setprio 0
	s_setprio 1
	v_mfma_f32_16x16x32_bf16 v[54:57], v[170:173], v[186:189], v[54:57]
	v_mfma_f32_16x16x32_bf16 v[50:53], v[178:181], v[186:189], v[50:53]
	v_mfma_f32_16x16x32_bf16 v[38:41], v[170:173], v[194:197], v[38:41]
	v_mfma_f32_16x16x32_bf16 v[34:37], v[178:181], v[194:197], v[34:37]
	v_mfma_f32_16x16x32_bf16 v[22:25], v[170:173], v[202:205], v[22:25]
	v_mfma_f32_16x16x32_bf16 v[18:21], v[178:181], v[202:205], v[18:21]
	v_mfma_f32_16x16x32_bf16 v[6:9], v[170:173], v[214:217], v[6:9]
	v_mfma_f32_16x16x32_bf16 v[2:5], v[178:181], v[214:217], v[2:5]
	v_mfma_f32_16x16x32_bf16 v[54:57], v[174:177], v[190:193], v[54:57]
	v_mfma_f32_16x16x32_bf16 v[50:53], v[182:185], v[190:193], v[50:53]
	v_mfma_f32_16x16x32_bf16 v[38:41], v[174:177], v[198:201], v[38:41]
	v_mfma_f32_16x16x32_bf16 v[34:37], v[182:185], v[198:201], v[34:37]
	v_mfma_f32_16x16x32_bf16 v[22:25], v[174:177], v[210:213], v[22:25]
	v_mfma_f32_16x16x32_bf16 v[18:21], v[182:185], v[210:213], v[18:21]
	v_mfma_f32_16x16x32_bf16 v[6:9], v[174:177], v[218:221], v[6:9]
	v_mfma_f32_16x16x32_bf16 v[2:5], v[182:185], v[218:221], v[2:5]
	s_barrier
	s_setprio 0
	s_add_i32 s55, s55, 2
	s_add_u32 s20, s20, 0x100
	s_addc_u32 s21, s21, 0
	s_add_u32 s53, s53, 0x100
	s_addc_u32 s54, s54, 0
	s_cmp_gt_u32 s55, 13
	s_cbranch_scc0 .LBB0_3248
	s_and_b64 vcc, exec, s[8:9]
	s_cbranch_vccz .LBB0_3251
	s_barrier

; #define PG8_STAGE(bufoff, gbase, voff) do { _Pragma("unroll") for (int _i = 0; _i < 2; ++_i) \
;         __builtin_amdgcn_global_load_lds((const unsigned*)((const char*)(gbase) + (voff)[_i]), (PG8_LAS unsigned*)(lds + (bufoff) + ldsw + _i * 8192), 16, 0, 0); } while (0)
; #define PG8_LDA(dst, b, h) do { _Pragma("unroll") for (int m = 0; m < 4; ++m) _Pragma("unroll") for (int k = 0; k < 2; ++k) dst[m][k] = *(const PG8_LAS bf16x8*)(lds + PG8_SA(b, h) + aoff + m * 2048 + k * 1024); } while (0)
; #define PG8_LDB(dst, b, h) do { _Pragma("unroll") for (int n = 0; n < 2; ++n) _Pragma("unroll") for (int k = 0; k < 2; ++k) dst[n][k] = *(const PG8_LAS bf16x8*)(lds + PG8_SB(b, h) + boff + n * 2048 + k * 1024); } while (0)
; #define PG8_MMA(ai, bj, At, Bt) do { __builtin_amdgcn_s_setprio(1); _Pragma("unroll") for (int m = 0; m < 4; ++m) _Pragma("unroll") for (int n = 0; n < 2; ++n) _Pragma("unroll") for (int k = 0; k < 2; ++k) \
;         acc[ai][bj][m][n] = __builtin_amdgcn_mfma_f32_16x16x32_bf16(Bt[n][k], At[m][k], acc[ai][bj][m][n], 0, 0, 0); __builtin_amdgcn_s_setprio(0); } while (0)
; #define PG8_WAIT_V(n) asm volatile("s_waitcnt vmcnt(" #n ")" ::: "memory")
; #define PG8_WAIT_L(n) asm volatile("s_waitcnt lgkmcnt(" #n ")" ::: "memory")
; #define PG8_BAR __builtin_amdgcn_s_barrier()
; #define PG8_SCHED __builtin_amdgcn_sched_barrier(0)
;     ...
;             const bool last = (t == nt - 2);
;             const char* a1 = cA + (size_t)(t + 1) * kstep;
;             const char* a2 = last ? nA : cA + (size_t)(t + 2) * kstep; const char* b2 = last ? nB : cB + (size_t)(t + 2) * kstep;
;             const char* a3 = a2 + kstep; const char* b3 = b2 + kstep;
;             if (last && has_next) S.a_ready(nxt);
;             PG8_LDB(B0, 0, 0); PG8_LDB(B1, 0, 1); PG8_SCHED; PG8_LDA(At, 0, 0); PG8_STAGE(PG8_SA(1, 1), a1 + hstep, voffA);
;             PG8_WAIT_V(8); PG8_WAIT_L(0); PG8_BAR; PG8_MMA(0, 0, At, B0); PG8_MMA(0, 1, At, B1); PG8_BAR; PG8_SCHED;
;             PG8_LDA(At, 0, 1); PG8_STAGE(PG8_SB(0, 0), b2, voffB); PG8_STAGE(PG8_SB(0, 1), b2 + hstep, voffB); PG8_STAGE(PG8_SA(0, 0), a2, voffA);
.LBB0_3342:
	ds_read_b128 v[114:117], v217
	ds_read_b128 v[118:121], v217 offset:1024
	ds_read_b128 v[122:125], v217 offset:2048
	ds_read_b128 v[126:129], v217 offset:3072
	ds_read_b128 v[146:149], v218
	ds_read_b128 v[150:153], v218 offset:1024
	ds_read_b128 v[154:157], v218 offset:2048
	ds_read_b128 v[158:161], v218 offset:3072
	s_add_u32 s16, s14, 0xfff50080
	s_addc_u32 s17, s15, -1
	s_cmp_eq_u32 s45, 40
	s_cselect_b32 s19, s7, s17
	s_cselect_b32 s18, s6, s16
	s_cselect_b32 s17, s11, s44
	s_cselect_b32 s16, s10, s13
	v_lshl_add_u64 v[240:241], s[14:15], 0, v[194:195]
	s_add_i32 m0, s26, 0xc000
	ds_read_b128 v[162:165], v219
	ds_read_b128 v[166:169], v219 offset:1024
	ds_read_b128 v[202:205], v219 offset:2048
	ds_read_b128 v[220:223], v219 offset:3072
	ds_read_b128 v[224:227], v219 offset:4096
	ds_read_b128 v[228:231], v219 offset:5120
	ds_read_b128 v[232:235], v219 offset:6144
	ds_read_b128 v[236:239], v219 offset:7168
	global_load_lds_dwordx4 v[240:241], off
	v_lshl_add_u64 v[240:241], s[14:15], 0, v[196:197]
	s_add_i32 m0, s26, 0xe000
	s_nop 0
	global_load_lds_dwordx4 v[240:241], off
	s_waitcnt vmcnt(8)
	s_waitcnt lgkmcnt(0)
	s_setprio 1
	s_barrier
	v_mfma_f32_16x16x32_bf16 v[142:145], v[114:117], v[162:165], v[142:145]
	v_mfma_f32_16x16x32_bf16 v[138:141], v[122:125], v[162:165], v[138:141]
	v_mfma_f32_16x16x32_bf16 v[110:113], v[114:117], v[202:205], v[110:113]
	v_mfma_f32_16x16x32_bf16 v[106:109], v[122:125], v[202:205], v[106:109]
	v_mfma_f32_16x16x32_bf16 v[98:101], v[114:117], v[224:227], v[98:101]
	v_mfma_f32_16x16x32_bf16 v[90:93], v[122:125], v[224:227], v[90:93]
	v_mfma_f32_16x16x32_bf16 v[82:85], v[114:117], v[232:235], v[82:85]
	v_mfma_f32_16x16x32_bf16 v[74:77], v[122:125], v[232:235], v[74:77]
	v_mfma_f32_16x16x32_bf16 v[142:145], v[118:121], v[166:169], v[142:145]
	v_mfma_f32_16x16x32_bf16 v[138:141], v[126:129], v[166:169], v[138:141]
	v_mfma_f32_16x16x32_bf16 v[110:113], v[118:121], v[220:223], v[110:113]
	v_mfma_f32_16x16x32_bf16 v[106:109], v[126:129], v[220:223], v[106:109]
	v_mfma_f32_16x16x32_bf16 v[98:101], v[118:121], v[228:231], v[98:101]
	v_mfma_f32_16x16x32_bf16 v[90:93], v[126:129], v[228:231], v[90:93]
	v_mfma_f32_16x16x32_bf16 v[82:85], v[118:121], v[236:239], v[82:85]
	v_mfma_f32_16x16x32_bf16 v[74:77], v[126:129], v[236:239], v[74:77]
	s_setprio 0
	s_setprio 1
	v_mfma_f32_16x16x32_bf16 v[134:137], v[146:149], v[162:165], v[134:137]
	v_mfma_f32_16x16x32_bf16 v[130:133], v[154:157], v[162:165], v[130:133]
	v_mfma_f32_16x16x32_bf16 v[102:105], v[146:149], v[202:205], v[102:105]
	v_mfma_f32_16x16x32_bf16 v[94:97], v[154:157], v[202:205], v[94:97]
	v_mfma_f32_16x16x32_bf16 v[86:89], v[146:149], v[224:227], v[86:89]
	v_mfma_f32_16x16x32_bf16 v[78:81], v[154:157], v[224:227], v[78:81]
	v_mfma_f32_16x16x32_bf16 v[70:73], v[146:149], v[232:235], v[70:73]
	v_mfma_f32_16x16x32_bf16 v[66:69], v[154:157], v[232:235], v[66:69]
	v_mfma_f32_16x16x32_bf16 v[134:137], v[150:153], v[166:169], v[134:137]
	v_mfma_f32_16x16x32_bf16 v[130:133], v[158:161], v[166:169], v[130:133]
	v_mfma_f32_16x16x32_bf16 v[102:105], v[150:153], v[220:223], v[102:105]
	v_mfma_f32_16x16x32_bf16 v[94:97], v[158:161], v[220:223], v[94:97]
	v_mfma_f32_16x16x32_bf16 v[86:89], v[150:153], v[228:231], v[86:89]
	v_mfma_f32_16x16x32_bf16 v[78:81], v[158:161], v[228:231], v[78:81]
	v_mfma_f32_16x16x32_bf16 v[70:73], v[150:153], v[236:239], v[70:73]
	v_mfma_f32_16x16x32_bf16 v[66:69], v[158:161], v[236:239], v[66:69]
	s_barrier
	s_setprio 0
	s_add_i32 s46, s35, s25
	v_lshl_add_u64 v[240:241], s[16:17], 0, v[172:173]
	s_mov_b32 m0, s46
	ds_read_b128 v[162:165], v219 offset:16384
	ds_read_b128 v[166:169], v219 offset:17408
	ds_read_b128 v[202:205], v219 offset:18432
	ds_read_b128 v[220:223], v219 offset:19456
	ds_read_b128 v[224:227], v219 offset:20480
	ds_read_b128 v[228:231], v219 offset:21504
	ds_read_b128 v[232:235], v219 offset:22528
	ds_read_b128 v[236:239], v219 offset:23552
	global_load_lds_dwordx4 v[240:241], off
	s_add_i32 m0, s46, 0x2000
	s_add_u32 s46, s16, 0xb0000
	v_lshl_add_u64 v[242:243], s[16:17], 0, v[176:177]
	s_addc_u32 s47, s17, 0
	s_add_i32 s50, s36, s25
	global_load_lds_dwordx4 v[242:243], off
	v_lshl_add_u64 v[244:245], s[46:47], 0, v[172:173]
	s_mov_b32 m0, s50
	v_lshl_add_u64 v[246:247], s[18:19], 0, v[174:175]
	global_load_lds_dwordx4 v[244:245], off
	v_lshl_add_u64 v[244:245], s[46:47], 0, v[176:177]
	s_add_i32 m0, s50, 0x2000
	s_nop 0
	global_load_lds_dwordx4 v[244:245], off
	v_lshl_add_u64 v[244:245], s[18:19], 0, v[170:171]
	s_mov_b32 m0, s26
	s_nop 0
	global_load_lds_dwordx4 v[244:245], off
	s_mov_b32 m0, s27
	s_nop 0
	global_load_lds_dwordx4 v[246:247], off
	s_waitcnt vmcnt(8)
	s_waitcnt lgkmcnt(0)
	s_setprio 1
	s_barrier
; #define PG8_STAGE(bufoff, gbase, voff) do { _Pragma("unroll") for (int _i = 0; _i < 2; ++_i) \
;         __builtin_amdgcn_global_load_lds((const unsigned*)((const char*)(gbase) + (voff)[_i]), (PG8_LAS unsigned*)(lds + (bufoff) + ldsw + _i * 8192), 16, 0, 0); } while (0)
; #define PG8_LDA(dst, b, h) do { _Pragma("unroll") for (int m = 0; m < 4; ++m) _Pragma("unroll") for (int k = 0; k < 2; ++k) dst[m][k] = *(const PG8_LAS bf16x8*)(lds + PG8_SA(b, h) + aoff + m * 2048 + k * 1024); } while (0)
; #define PG8_LDB(dst, b, h) do { _Pragma("unroll") for (int n = 0; n < 2; ++n) _Pragma("unroll") for (int k = 0; k < 2; ++k) dst[n][k] = *(const PG8_LAS bf16x8*)(lds + PG8_SB(b, h) + boff + n * 2048 + k * 1024); } while (0)
; #define PG8_MMA(ai, bj, At, Bt) do { __builtin_amdgcn_s_setprio(1); _Pragma("unroll") for (int m = 0; m < 4; ++m) _Pragma("unroll") for (int n = 0; n < 2; ++n) _Pragma("unroll") for (int k = 0; k < 2; ++k) \
;         acc[ai][bj][m][n] = __builtin_amdgcn_mfma_f32_16x16x32_bf16(Bt[n][k], At[m][k], acc[ai][bj][m][n], 0, 0, 0); __builtin_amdgcn_s_setprio(0); } while (0)
; #define PG8_WAIT_V(n) asm volatile("s_waitcnt vmcnt(" #n ")" ::: "memory")
; #define PG8_WAIT_L(n) asm volatile("s_waitcnt lgkmcnt(" #n ")" ::: "memory")
; #define PG8_BAR __builtin_amdgcn_s_barrier()
; #define PG8_SCHED __builtin_amdgcn_sched_barrier(0)
;     ...
;             PG8_WAIT_V(8); PG8_WAIT_L(0); PG8_BAR; PG8_MMA(1, 0, At, B0); PG8_MMA(1, 1, At, B1); PG8_BAR; PG8_SCHED;
;             PG8_LDB(B0, 1, 0); PG8_LDB(B1, 1, 1); PG8_SCHED; PG8_LDA(At, 1, 0); PG8_STAGE(PG8_SA(0, 1), a2 + hstep, voffA);
;             PG8_WAIT_V(8); PG8_WAIT_L(0); PG8_BAR; PG8_MMA(0, 0, At, B0); PG8_MMA(0, 1, At, B1); PG8_BAR; PG8_SCHED;
	v_mfma_f32_16x16x32_bf16 v[62:65], v[114:117], v[162:165], v[62:65]
	v_mfma_f32_16x16x32_bf16 v[58:61], v[122:125], v[162:165], v[58:61]
	v_mfma_f32_16x16x32_bf16 v[50:53], v[114:117], v[202:205], v[50:53]
	v_mfma_f32_16x16x32_bf16 v[42:45], v[122:125], v[202:205], v[42:45]
	v_mfma_f32_16x16x32_bf16 v[34:37], v[114:117], v[224:227], v[34:37]
	v_mfma_f32_16x16x32_bf16 v[26:29], v[122:125], v[224:227], v[26:29]
	v_mfma_f32_16x16x32_bf16 v[18:21], v[114:117], v[232:235], v[18:21]
	v_mfma_f32_16x16x32_bf16 v[10:13], v[122:125], v[232:235], v[10:13]
	v_mfma_f32_16x16x32_bf16 v[62:65], v[118:121], v[166:169], v[62:65]
	v_mfma_f32_16x16x32_bf16 v[58:61], v[126:129], v[166:169], v[58:61]
	v_mfma_f32_16x16x32_bf16 v[50:53], v[118:121], v[220:223], v[50:53]
	v_mfma_f32_16x16x32_bf16 v[42:45], v[126:129], v[220:223], v[42:45]
	v_mfma_f32_16x16x32_bf16 v[34:37], v[118:121], v[228:231], v[34:37]
	v_mfma_f32_16x16x32_bf16 v[26:29], v[126:129], v[228:231], v[26:29]
	v_mfma_f32_16x16x32_bf16 v[18:21], v[118:121], v[236:239], v[18:21]
	v_mfma_f32_16x16x32_bf16 v[10:13], v[126:129], v[236:239], v[10:13]
	s_setprio 0
	s_setprio 1
	v_mfma_f32_16x16x32_bf16 v[54:57], v[146:149], v[162:165], v[54:57]
	v_mfma_f32_16x16x32_bf16 v[46:49], v[154:157], v[162:165], v[46:49]
	v_mfma_f32_16x16x32_bf16 v[38:41], v[146:149], v[202:205], v[38:41]
	v_mfma_f32_16x16x32_bf16 v[30:33], v[154:157], v[202:205], v[30:33]
	v_mfma_f32_16x16x32_bf16 v[22:25], v[146:149], v[224:227], v[22:25]
	v_mfma_f32_16x16x32_bf16 v[14:17], v[154:157], v[224:227], v[14:17]
	v_mfma_f32_16x16x32_bf16 v[6:9], v[146:149], v[232:235], v[6:9]
	v_mfma_f32_16x16x32_bf16 v[2:5], v[154:157], v[232:235], v[2:5]
	v_mfma_f32_16x16x32_bf16 v[54:57], v[150:153], v[166:169], v[54:57]
	v_mfma_f32_16x16x32_bf16 v[46:49], v[158:161], v[166:169], v[46:49]
	v_mfma_f32_16x16x32_bf16 v[38:41], v[150:153], v[220:223], v[38:41]
	v_mfma_f32_16x16x32_bf16 v[30:33], v[158:161], v[220:223], v[30:33]
	v_mfma_f32_16x16x32_bf16 v[22:25], v[150:153], v[228:231], v[22:25]
	v_mfma_f32_16x16x32_bf16 v[14:17], v[158:161], v[228:231], v[14:17]
	v_mfma_f32_16x16x32_bf16 v[6:9], v[150:153], v[236:239], v[6:9]
	v_mfma_f32_16x16x32_bf16 v[2:5], v[158:161], v[236:239], v[2:5]
	s_barrier
	s_setprio 0
	s_add_i32 s46, 0, 0x18000
	s_add_i32 s47, 0, 0x1c000
	v_add_u32_e32 v126, s46, v215
	v_add_u32_e32 v158, s47, v215
	ds_read_b128 v[114:117], v126
	ds_read_b128 v[118:121], v126 offset:1024
	ds_read_b128 v[122:125], v126 offset:2048
	ds_read_b128 v[126:129], v126 offset:3072
	ds_read_b128 v[146:149], v158
	ds_read_b128 v[150:153], v158 offset:1024
	ds_read_b128 v[154:157], v158 offset:2048
	ds_read_b128 v[158:161], v158 offset:3072
	s_add_u32 s18, s18, 0xb0000
	s_addc_u32 s19, s19, 0
	s_mov_b32 m0, s28
	v_lshl_add_u64 v[248:249], s[18:19], 0, v[170:171]
	ds_read_b128 v[162:165], v219 offset:32768
	ds_read_b128 v[166:169], v219 offset:33792
	ds_read_b128 v[202:205], v219 offset:34816
	ds_read_b128 v[220:223], v219 offset:35840
	ds_read_b128 v[224:227], v219 offset:36864
	ds_read_b128 v[228:231], v219 offset:37888
	ds_read_b128 v[232:235], v219 offset:38912
	ds_read_b128 v[236:239], v219 offset:39936
	global_load_lds_dwordx4 v[248:249], off
	v_lshl_add_u64 v[248:249], s[18:19], 0, v[174:175]
	s_mov_b32 m0, s29
	s_nop 0
	global_load_lds_dwordx4 v[248:249], off
	s_waitcnt vmcnt(8)
	s_waitcnt lgkmcnt(0)
	s_setprio 1
	s_barrier
	v_mfma_f32_16x16x32_bf16 v[142:145], v[114:117], v[162:165], v[142:145]
	v_mfma_f32_16x16x32_bf16 v[138:141], v[122:125], v[162:165], v[138:141]
	v_mfma_f32_16x16x32_bf16 v[110:113], v[114:117], v[202:205], v[110:113]
	v_mfma_f32_16x16x32_bf16 v[106:109], v[122:125], v[202:205], v[106:109]
	v_mfma_f32_16x16x32_bf16 v[98:101], v[114:117], v[224:227], v[98:101]
	v_mfma_f32_16x16x32_bf16 v[90:93], v[122:125], v[224:227], v[90:93]
	v_mfma_f32_16x16x32_bf16 v[82:85], v[114:117], v[232:235], v[82:85]
	v_mfma_f32_16x16x32_bf16 v[74:77], v[122:125], v[232:235], v[74:77]
	v_mfma_f32_16x16x32_bf16 v[142:145], v[118:121], v[166:169], v[142:145]
	v_mfma_f32_16x16x32_bf16 v[138:141], v[126:129], v[166:169], v[138:141]
	v_mfma_f32_16x16x32_bf16 v[110:113], v[118:121], v[220:223], v[110:113]
	v_mfma_f32_16x16x32_bf16 v[106:109], v[126:129], v[220:223], v[106:109]
	v_mfma_f32_16x16x32_bf16 v[98:101], v[118:121], v[228:231], v[98:101]
	v_mfma_f32_16x16x32_bf16 v[90:93], v[126:129], v[228:231], v[90:93]
	v_mfma_f32_16x16x32_bf16 v[82:85], v[118:121], v[236:239], v[82:85]
	v_mfma_f32_16x16x32_bf16 v[74:77], v[126:129], v[236:239], v[74:77]
	s_setprio 0
	s_setprio 1
	v_mfma_f32_16x16x32_bf16 v[134:137], v[146:149], v[162:165], v[134:137]
	v_mfma_f32_16x16x32_bf16 v[130:133], v[154:157], v[162:165], v[130:133]
	v_mfma_f32_16x16x32_bf16 v[102:105], v[146:149], v[202:205], v[102:105]
	v_mfma_f32_16x16x32_bf16 v[94:97], v[154:157], v[202:205], v[94:97]
	v_mfma_f32_16x16x32_bf16 v[86:89], v[146:149], v[224:227], v[86:89]
	v_mfma_f32_16x16x32_bf16 v[78:81], v[154:157], v[224:227], v[78:81]
	v_mfma_f32_16x16x32_bf16 v[70:73], v[146:149], v[232:235], v[70:73]
	v_mfma_f32_16x16x32_bf16 v[66:69], v[154:157], v[232:235], v[66:69]
	v_mfma_f32_16x16x32_bf16 v[134:137], v[150:153], v[166:169], v[134:137]
	v_mfma_f32_16x16x32_bf16 v[130:133], v[158:161], v[166:169], v[130:133]
	v_mfma_f32_16x16x32_bf16 v[102:105], v[150:153], v[220:223], v[102:105]
	v_mfma_f32_16x16x32_bf16 v[94:97], v[158:161], v[220:223], v[94:97]
	v_mfma_f32_16x16x32_bf16 v[86:89], v[150:153], v[228:231], v[86:89]
	v_mfma_f32_16x16x32_bf16 v[78:81], v[158:161], v[228:231], v[78:81]
	v_mfma_f32_16x16x32_bf16 v[70:73], v[150:153], v[236:239], v[70:73]
	v_mfma_f32_16x16x32_bf16 v[66:69], v[158:161], v[236:239], v[66:69]
	s_barrier
; #define PG8_STAGE(bufoff, gbase, voff) do { _Pragma("unroll") for (int _i = 0; _i < 2; ++_i) \
;         __builtin_amdgcn_global_load_lds((const unsigned*)((const char*)(gbase) + (voff)[_i]), (PG8_LAS unsigned*)(lds + (bufoff) + ldsw + _i * 8192), 16, 0, 0); } while (0)
; #define PG8_LDA(dst, b, h) do { _Pragma("unroll") for (int m = 0; m < 4; ++m) _Pragma("unroll") for (int k = 0; k < 2; ++k) dst[m][k] = *(const PG8_LAS bf16x8*)(lds + PG8_SA(b, h) + aoff + m * 2048 + k * 1024); } while (0)
; #define PG8_MMA(ai, bj, At, Bt) do { __builtin_amdgcn_s_setprio(1); _Pragma("unroll") for (int m = 0; m < 4; ++m) _Pragma("unroll") for (int n = 0; n < 2; ++n) _Pragma("unroll") for (int k = 0; k < 2; ++k) \
;         acc[ai][bj][m][n] = __builtin_amdgcn_mfma_f32_16x16x32_bf16(Bt[n][k], At[m][k], acc[ai][bj][m][n], 0, 0, 0); __builtin_amdgcn_s_setprio(0); } while (0)
; #define PG8_WAIT_V(n) asm volatile("s_waitcnt vmcnt(" #n ")" ::: "memory")
; #define PG8_WAIT_L(n) asm volatile("s_waitcnt lgkmcnt(" #n ")" ::: "memory")
; #define PG8_BAR __builtin_amdgcn_s_barrier()
; #define PG8_SCHED __builtin_amdgcn_sched_barrier(0)
;     ...
;             PG8_LDA(At, 1, 1); PG8_STAGE(PG8_SB(1, 0), b3, voffB); PG8_STAGE(PG8_SB(1, 1), b3 + hstep, voffB); PG8_STAGE(PG8_SA(1, 0), a3, voffA);
;             PG8_WAIT_V(8); PG8_WAIT_L(0); PG8_BAR; PG8_MMA(1, 0, At, B0); PG8_MMA(1, 1, At, B1); PG8_BAR; PG8_SCHED;
;         }
;         if constexpr (ALIGN_EPI) { if (wr == 0) PG8_BAR; }
	s_setprio 0
	s_add_i32 s18, s46, s25
	v_lshl_add_u64 v[240:241], v[240:241], 0, s[2:3]
	s_mov_b32 m0, s18
	ds_read_b128 v[162:165], v219 offset:49152
	ds_read_b128 v[166:169], v219 offset:50176
	ds_read_b128 v[202:205], v219 offset:51200
	ds_read_b128 v[220:223], v219 offset:52224
	ds_read_b128 v[224:227], v219 offset:53248
	ds_read_b128 v[228:231], v219 offset:54272
	ds_read_b128 v[232:235], v219 offset:55296
	ds_read_b128 v[236:239], v219 offset:56320
	global_load_lds_dwordx4 v[240:241], off
	s_add_i32 m0, s18, 0x2000
	s_add_u32 s16, s16, 0xb0080
	v_lshl_add_u64 v[240:241], v[242:243], 0, s[2:3]
	s_addc_u32 s17, s17, 0
	s_add_i32 s18, s47, s25
	global_load_lds_dwordx4 v[240:241], off
	v_lshl_add_u64 v[240:241], s[16:17], 0, v[172:173]
	s_mov_b32 m0, s18
	s_nop 0
	global_load_lds_dwordx4 v[240:241], off
	v_lshl_add_u64 v[240:241], s[16:17], 0, v[176:177]
	s_add_i32 m0, s18, 0x2000
	s_nop 0
	global_load_lds_dwordx4 v[240:241], off
	v_lshl_add_u64 v[240:241], v[244:245], 0, s[2:3]
	s_mov_b32 m0, s31
	s_nop 0
	global_load_lds_dwordx4 v[240:241], off
	v_lshl_add_u64 v[240:241], v[246:247], 0, s[2:3]
	s_mov_b32 m0, s33
	s_nop 0
	global_load_lds_dwordx4 v[240:241], off
	s_waitcnt vmcnt(8)
	s_waitcnt lgkmcnt(0)
	s_setprio 1
	s_barrier
	v_mfma_f32_16x16x32_bf16 v[62:65], v[114:117], v[162:165], v[62:65]
	v_mfma_f32_16x16x32_bf16 v[58:61], v[122:125], v[162:165], v[58:61]
	v_mfma_f32_16x16x32_bf16 v[50:53], v[114:117], v[202:205], v[50:53]
	v_mfma_f32_16x16x32_bf16 v[42:45], v[122:125], v[202:205], v[42:45]
	v_mfma_f32_16x16x32_bf16 v[34:37], v[114:117], v[224:227], v[34:37]
	v_mfma_f32_16x16x32_bf16 v[26:29], v[122:125], v[224:227], v[26:29]
	v_mfma_f32_16x16x32_bf16 v[18:21], v[114:117], v[232:235], v[18:21]
	v_mfma_f32_16x16x32_bf16 v[10:13], v[122:125], v[232:235], v[10:13]
	v_mfma_f32_16x16x32_bf16 v[62:65], v[118:121], v[166:169], v[62:65]
	v_mfma_f32_16x16x32_bf16 v[58:61], v[126:129], v[166:169], v[58:61]
	v_mfma_f32_16x16x32_bf16 v[50:53], v[118:121], v[220:223], v[50:53]
	v_mfma_f32_16x16x32_bf16 v[42:45], v[126:129], v[220:223], v[42:45]
	v_mfma_f32_16x16x32_bf16 v[34:37], v[118:121], v[228:231], v[34:37]
	v_mfma_f32_16x16x32_bf16 v[26:29], v[126:129], v[228:231], v[26:29]
	v_mfma_f32_16x16x32_bf16 v[18:21], v[118:121], v[236:239], v[18:21]
	v_mfma_f32_16x16x32_bf16 v[10:13], v[126:129], v[236:239], v[10:13]
	s_setprio 0
	s_setprio 1
	v_mfma_f32_16x16x32_bf16 v[54:57], v[146:149], v[162:165], v[54:57]
	v_mfma_f32_16x16x32_bf16 v[46:49], v[154:157], v[162:165], v[46:49]
	v_mfma_f32_16x16x32_bf16 v[38:41], v[146:149], v[202:205], v[38:41]
	v_mfma_f32_16x16x32_bf16 v[30:33], v[154:157], v[202:205], v[30:33]
	v_mfma_f32_16x16x32_bf16 v[22:25], v[146:149], v[224:227], v[22:25]
	v_mfma_f32_16x16x32_bf16 v[14:17], v[154:157], v[224:227], v[14:17]
	v_mfma_f32_16x16x32_bf16 v[6:9], v[146:149], v[232:235], v[6:9]
	v_mfma_f32_16x16x32_bf16 v[2:5], v[154:157], v[232:235], v[2:5]
	v_mfma_f32_16x16x32_bf16 v[54:57], v[150:153], v[166:169], v[54:57]
	v_mfma_f32_16x16x32_bf16 v[46:49], v[158:161], v[166:169], v[46:49]
	v_mfma_f32_16x16x32_bf16 v[38:41], v[150:153], v[220:223], v[38:41]
	v_mfma_f32_16x16x32_bf16 v[30:33], v[158:161], v[220:223], v[30:33]
	v_mfma_f32_16x16x32_bf16 v[22:25], v[150:153], v[228:231], v[22:25]
	v_mfma_f32_16x16x32_bf16 v[14:17], v[158:161], v[228:231], v[14:17]
	v_mfma_f32_16x16x32_bf16 v[6:9], v[150:153], v[236:239], v[6:9]
	v_mfma_f32_16x16x32_bf16 v[2:5], v[158:161], v[236:239], v[2:5]
	s_barrier
	s_setprio 0
	s_add_i32 s45, s45, 2
	s_add_u32 s14, s14, 0x100
	s_addc_u32 s15, s15, 0
	s_add_u32 s13, s13, 0x100
	s_addc_u32 s44, s44, 0
	s_cmp_gt_u32 s45, 41
	s_cbranch_scc0 .LBB0_3342
	s_and_b64 vcc, exec, s[8:9]
	s_cbranch_vccz .LBB0_3345
	s_barrier

; #define PG8_STAGE(bufoff, gbase, voff) do { _Pragma("unroll") for (int _i = 0; _i < 2; ++_i) \
;         __builtin_amdgcn_global_load_lds((const unsigned*)((const char*)(gbase) + (voff)[_i]), (PG8_LAS unsigned*)(lds + (bufoff) + ldsw + _i * 8192), 16, 0, 0); } while (0)
; #define PG8_LDA(dst, b, h) do { _Pragma("unroll") for (int m = 0; m < 4; ++m) _Pragma("unroll") for (int k = 0; k < 2; ++k) dst[m][k] = *(const PG8_LAS bf16x8*)(lds + PG8_SA(b, h) + aoff + m * 2048 + k * 1024); } while (0)
; #define PG8_LDB(dst, b, h) do { _Pragma("unroll") for (int n = 0; n < 2; ++n) _Pragma("unroll") for (int k = 0; k < 2; ++k) dst[n][k] = *(const PG8_LAS bf16x8*)(lds + PG8_SB(b, h) + boff + n * 2048 + k * 1024); } while (0)
; #define PG8_MMA(ai, bj, At, Bt) do { __builtin_amdgcn_s_setprio(1); _Pragma("unroll") for (int m = 0; m < 4; ++m) _Pragma("unroll") for (int n = 0; n < 2; ++n) _Pragma("unroll") for (int k = 0; k < 2; ++k) \
;         acc[ai][bj][m][n] = __builtin_amdgcn_mfma_f32_16x16x32_bf16(Bt[n][k], At[m][k], acc[ai][bj][m][n], 0, 0, 0); __builtin_amdgcn_s_setprio(0); } while (0)
; #define PG8_WAIT_V(n) asm volatile("s_waitcnt vmcnt(" #n ")" ::: "memory")
; #define PG8_WAIT_L(n) asm volatile("s_waitcnt lgkmcnt(" #n ")" ::: "memory")
; #define PG8_BAR __builtin_amdgcn_s_barrier()
; #define PG8_SCHED __builtin_amdgcn_sched_barrier(0)
;     ...
;             const bool last = (t == nt - 2);
;             const char* a1 = cA + (size_t)(t + 1) * kstep;
;             const char* a2 = last ? nA : cA + (size_t)(t + 2) * kstep; const char* b2 = last ? nB : cB + (size_t)(t + 2) * kstep;
;             const char* a3 = a2 + kstep; const char* b3 = b2 + kstep;
;             if (last && has_next) S.a_ready(nxt);
;             PG8_LDB(B0, 0, 0); PG8_LDB(B1, 0, 1); PG8_SCHED; PG8_LDA(At, 0, 0); PG8_STAGE(PG8_SA(1, 1), a1 + hstep, voffA);
;             PG8_WAIT_V(8); PG8_WAIT_L(0); PG8_BAR; PG8_MMA(0, 0, At, B0); PG8_MMA(0, 1, At, B1); PG8_BAR; PG8_SCHED;
;             PG8_LDA(At, 0, 1); PG8_STAGE(PG8_SB(0, 0), b2, voffB); PG8_STAGE(PG8_SB(0, 1), b2 + hstep, voffB); PG8_STAGE(PG8_SA(0, 0), a2, voffA);
.LBB0_3370:
	ds_read_b128 v[130:133], v163
	ds_read_b128 v[134:137], v163 offset:1024
	ds_read_b128 v[138:141], v163 offset:2048
	ds_read_b128 v[142:145], v163 offset:3072
	ds_read_b128 v[154:157], v164
	ds_read_b128 v[166:169], v164 offset:1024
	ds_read_b128 v[178:181], v164 offset:2048
	ds_read_b128 v[182:185], v164 offset:3072
	s_add_u32 s16, s14, 0xfff50080
	s_addc_u32 s17, s15, -1
	s_cmp_eq_u32 s46, 18
	s_cselect_b32 s19, s7, s17
	s_cselect_b32 s18, s6, s16
	s_cselect_b32 s17, s13, s45
	s_cselect_b32 s16, s12, s0
	v_lshl_add_u64 v[158:159], s[14:15], 0, v[146:147]
	s_add_i32 m0, s26, 0xc000
	ds_read_b128 v[186:189], v165
	ds_read_b128 v[190:193], v165 offset:1024
	ds_read_b128 v[194:197], v165 offset:2048
	ds_read_b128 v[198:201], v165 offset:3072
	ds_read_b128 v[202:205], v165 offset:4096
	ds_read_b128 v[210:213], v165 offset:5120
	ds_read_b128 v[214:217], v165 offset:6144
	ds_read_b128 v[218:221], v165 offset:7168
	global_load_lds_dwordx4 v[158:159], off
	v_lshl_add_u64 v[158:159], s[14:15], 0, v[148:149]
	s_add_i32 m0, s26, 0xe000
	s_nop 0
	global_load_lds_dwordx4 v[158:159], off
	s_waitcnt vmcnt(8)
	s_waitcnt lgkmcnt(0)
	s_setprio 1
	s_barrier
	v_mfma_f32_16x16x32_bf16 v[126:129], v[130:133], v[186:189], v[126:129]
	v_mfma_f32_16x16x32_bf16 v[122:125], v[138:141], v[186:189], v[122:125]
	v_mfma_f32_16x16x32_bf16 v[118:121], v[130:133], v[194:197], v[118:121]
	v_mfma_f32_16x16x32_bf16 v[114:117], v[138:141], v[194:197], v[114:117]
	v_mfma_f32_16x16x32_bf16 v[110:113], v[130:133], v[202:205], v[110:113]
	v_mfma_f32_16x16x32_bf16 v[102:105], v[138:141], v[202:205], v[102:105]
	v_mfma_f32_16x16x32_bf16 v[78:81], v[130:133], v[214:217], v[78:81]
	v_mfma_f32_16x16x32_bf16 v[74:77], v[138:141], v[214:217], v[74:77]
	v_mfma_f32_16x16x32_bf16 v[126:129], v[134:137], v[190:193], v[126:129]
	v_mfma_f32_16x16x32_bf16 v[122:125], v[142:145], v[190:193], v[122:125]
	v_mfma_f32_16x16x32_bf16 v[118:121], v[134:137], v[198:201], v[118:121]
	v_mfma_f32_16x16x32_bf16 v[114:117], v[142:145], v[198:201], v[114:117]
	v_mfma_f32_16x16x32_bf16 v[110:113], v[134:137], v[210:213], v[110:113]
	v_mfma_f32_16x16x32_bf16 v[102:105], v[142:145], v[210:213], v[102:105]
	v_mfma_f32_16x16x32_bf16 v[78:81], v[134:137], v[218:221], v[78:81]
	v_mfma_f32_16x16x32_bf16 v[74:77], v[142:145], v[218:221], v[74:77]
	s_setprio 0
	s_setprio 1
	v_mfma_f32_16x16x32_bf16 v[106:109], v[154:157], v[186:189], v[106:109]
	v_mfma_f32_16x16x32_bf16 v[98:101], v[178:181], v[186:189], v[98:101]
	v_mfma_f32_16x16x32_bf16 v[94:97], v[154:157], v[194:197], v[94:97]
	v_mfma_f32_16x16x32_bf16 v[90:93], v[178:181], v[194:197], v[90:93]
	v_mfma_f32_16x16x32_bf16 v[86:89], v[154:157], v[202:205], v[86:89]
	v_mfma_f32_16x16x32_bf16 v[82:85], v[178:181], v[202:205], v[82:85]
	v_mfma_f32_16x16x32_bf16 v[70:73], v[154:157], v[214:217], v[70:73]
	v_mfma_f32_16x16x32_bf16 v[66:69], v[178:181], v[214:217], v[66:69]
	v_mfma_f32_16x16x32_bf16 v[106:109], v[166:169], v[190:193], v[106:109]
	v_mfma_f32_16x16x32_bf16 v[98:101], v[182:185], v[190:193], v[98:101]
	v_mfma_f32_16x16x32_bf16 v[94:97], v[166:169], v[198:201], v[94:97]
	v_mfma_f32_16x16x32_bf16 v[90:93], v[182:185], v[198:201], v[90:93]
	v_mfma_f32_16x16x32_bf16 v[86:89], v[166:169], v[210:213], v[86:89]
	v_mfma_f32_16x16x32_bf16 v[82:85], v[182:185], v[210:213], v[82:85]
	v_mfma_f32_16x16x32_bf16 v[70:73], v[166:169], v[218:221], v[70:73]
	v_mfma_f32_16x16x32_bf16 v[66:69], v[182:185], v[218:221], v[66:69]
	s_barrier
	s_setprio 0
	s_add_i32 s47, s36, s25
	v_lshl_add_u64 v[158:159], s[16:17], 0, v[172:173]
	s_mov_b32 m0, s47
	ds_read_b128 v[186:189], v165 offset:16384
	ds_read_b128 v[190:193], v165 offset:17408
	ds_read_b128 v[194:197], v165 offset:18432
	ds_read_b128 v[198:201], v165 offset:19456
	ds_read_b128 v[202:205], v165 offset:20480
	ds_read_b128 v[210:213], v165 offset:21504
	ds_read_b128 v[214:217], v165 offset:22528
	ds_read_b128 v[218:221], v165 offset:23552
	global_load_lds_dwordx4 v[158:159], off
	s_add_i32 m0, s47, 0x2000
	s_add_u32 s50, s16, 0xb0000
	v_lshl_add_u64 v[206:207], s[16:17], 0, v[176:177]
	s_addc_u32 s51, s17, 0
	s_add_i32 s47, s37, s25
	global_load_lds_dwordx4 v[206:207], off
	v_lshl_add_u64 v[208:209], s[50:51], 0, v[172:173]
	s_mov_b32 m0, s47
	v_lshl_add_u64 v[222:223], s[18:19], 0, v[174:175]
	global_load_lds_dwordx4 v[208:209], off
	v_lshl_add_u64 v[208:209], s[50:51], 0, v[176:177]
	s_add_i32 m0, s47, 0x2000
	s_nop 0
	global_load_lds_dwordx4 v[208:209], off
	v_lshl_add_u64 v[208:209], s[18:19], 0, v[170:171]
	s_mov_b32 m0, s26
	s_nop 0
	global_load_lds_dwordx4 v[208:209], off
	s_mov_b32 m0, s27
	s_nop 0
	global_load_lds_dwordx4 v[222:223], off
	s_waitcnt vmcnt(8)
	s_waitcnt lgkmcnt(0)
	s_setprio 1
	s_barrier
; #define PG8_STAGE(bufoff, gbase, voff) do { _Pragma("unroll") for (int _i = 0; _i < 2; ++_i) \
;         __builtin_amdgcn_global_load_lds((const unsigned*)((const char*)(gbase) + (voff)[_i]), (PG8_LAS unsigned*)(lds + (bufoff) + ldsw + _i * 8192), 16, 0, 0); } while (0)
; #define PG8_LDA(dst, b, h) do { _Pragma("unroll") for (int m = 0; m < 4; ++m) _Pragma("unroll") for (int k = 0; k < 2; ++k) dst[m][k] = *(const PG8_LAS bf16x8*)(lds + PG8_SA(b, h) + aoff + m * 2048 + k * 1024); } while (0)
; #define PG8_LDB(dst, b, h) do { _Pragma("unroll") for (int n = 0; n < 2; ++n) _Pragma("unroll") for (int k = 0; k < 2; ++k) dst[n][k] = *(const PG8_LAS bf16x8*)(lds + PG8_SB(b, h) + boff + n * 2048 + k * 1024); } while (0)
; #define PG8_MMA(ai, bj, At, Bt) do { __builtin_amdgcn_s_setprio(1); _Pragma("unroll") for (int m = 0; m < 4; ++m) _Pragma("unroll") for (int n = 0; n < 2; ++n) _Pragma("unroll") for (int k = 0; k < 2; ++k) \
;         acc[ai][bj][m][n] = __builtin_amdgcn_mfma_f32_16x16x32_bf16(Bt[n][k], At[m][k], acc[ai][bj][m][n], 0, 0, 0); __builtin_amdgcn_s_setprio(0); } while (0)
; #define PG8_WAIT_V(n) asm volatile("s_waitcnt vmcnt(" #n ")" ::: "memory")
; #define PG8_WAIT_L(n) asm volatile("s_waitcnt lgkmcnt(" #n ")" ::: "memory")
; #define PG8_BAR __builtin_amdgcn_s_barrier()
; #define PG8_SCHED __builtin_amdgcn_sched_barrier(0)
;     ...
;             PG8_WAIT_V(8); PG8_WAIT_L(0); PG8_BAR; PG8_MMA(1, 0, At, B0); PG8_MMA(1, 1, At, B1); PG8_BAR; PG8_SCHED;
;             PG8_LDB(B0, 1, 0); PG8_LDB(B1, 1, 1); PG8_SCHED; PG8_LDA(At, 1, 0); PG8_STAGE(PG8_SA(0, 1), a2 + hstep, voffA);
;             PG8_WAIT_V(8); PG8_WAIT_L(0); PG8_BAR; PG8_MMA(0, 0, At, B0); PG8_MMA(0, 1, At, B1); PG8_BAR; PG8_SCHED;
	v_mfma_f32_16x16x32_bf16 v[62:65], v[130:133], v[186:189], v[62:65]
	v_mfma_f32_16x16x32_bf16 v[58:61], v[138:141], v[186:189], v[58:61]
	v_mfma_f32_16x16x32_bf16 v[54:57], v[130:133], v[194:197], v[54:57]
	v_mfma_f32_16x16x32_bf16 v[46:49], v[138:141], v[194:197], v[46:49]
	v_mfma_f32_16x16x32_bf16 v[38:41], v[130:133], v[202:205], v[38:41]
	v_mfma_f32_16x16x32_bf16 v[30:33], v[138:141], v[202:205], v[30:33]
	v_mfma_f32_16x16x32_bf16 v[22:25], v[130:133], v[214:217], v[22:25]
	v_mfma_f32_16x16x32_bf16 v[14:17], v[138:141], v[214:217], v[14:17]
	v_mfma_f32_16x16x32_bf16 v[62:65], v[134:137], v[190:193], v[62:65]
	v_mfma_f32_16x16x32_bf16 v[58:61], v[142:145], v[190:193], v[58:61]
	v_mfma_f32_16x16x32_bf16 v[54:57], v[134:137], v[198:201], v[54:57]
	v_mfma_f32_16x16x32_bf16 v[46:49], v[142:145], v[198:201], v[46:49]
	v_mfma_f32_16x16x32_bf16 v[38:41], v[134:137], v[210:213], v[38:41]
	v_mfma_f32_16x16x32_bf16 v[30:33], v[142:145], v[210:213], v[30:33]
	v_mfma_f32_16x16x32_bf16 v[22:25], v[134:137], v[218:221], v[22:25]
	v_mfma_f32_16x16x32_bf16 v[14:17], v[142:145], v[218:221], v[14:17]
	s_setprio 0
	s_setprio 1
	v_mfma_f32_16x16x32_bf16 v[50:53], v[154:157], v[186:189], v[50:53]
	v_mfma_f32_16x16x32_bf16 v[42:45], v[178:181], v[186:189], v[42:45]
	v_mfma_f32_16x16x32_bf16 v[34:37], v[154:157], v[194:197], v[34:37]
	v_mfma_f32_16x16x32_bf16 v[26:29], v[178:181], v[194:197], v[26:29]
	v_mfma_f32_16x16x32_bf16 v[18:21], v[154:157], v[202:205], v[18:21]
	v_mfma_f32_16x16x32_bf16 v[10:13], v[178:181], v[202:205], v[10:13]
	v_mfma_f32_16x16x32_bf16 v[6:9], v[154:157], v[214:217], v[6:9]
	v_mfma_f32_16x16x32_bf16 v[2:5], v[178:181], v[214:217], v[2:5]
	v_mfma_f32_16x16x32_bf16 v[50:53], v[166:169], v[190:193], v[50:53]
	v_mfma_f32_16x16x32_bf16 v[42:45], v[182:185], v[190:193], v[42:45]
	v_mfma_f32_16x16x32_bf16 v[34:37], v[166:169], v[198:201], v[34:37]
	v_mfma_f32_16x16x32_bf16 v[26:29], v[182:185], v[198:201], v[26:29]
	v_mfma_f32_16x16x32_bf16 v[18:21], v[166:169], v[210:213], v[18:21]
	v_mfma_f32_16x16x32_bf16 v[10:13], v[182:185], v[210:213], v[10:13]
	v_mfma_f32_16x16x32_bf16 v[6:9], v[166:169], v[218:221], v[6:9]
	v_mfma_f32_16x16x32_bf16 v[2:5], v[182:185], v[218:221], v[2:5]
	s_barrier
	s_setprio 0
	s_add_i32 s47, 0, 0x18000
	s_add_i32 s50, 0, 0x1c000
	v_add_u32_e32 v142, s47, v161
	v_add_u32_e32 v182, s50, v161
	ds_read_b128 v[130:133], v142
	ds_read_b128 v[134:137], v142 offset:1024
	ds_read_b128 v[138:141], v142 offset:2048
	ds_read_b128 v[142:145], v142 offset:3072
	ds_read_b128 v[154:157], v182
	ds_read_b128 v[166:169], v182 offset:1024
	ds_read_b128 v[178:181], v182 offset:2048
	ds_read_b128 v[182:185], v182 offset:3072
	s_add_u32 s18, s18, 0xb0000
	s_addc_u32 s19, s19, 0
	s_mov_b32 m0, s28
	v_lshl_add_u64 v[224:225], s[18:19], 0, v[170:171]
	ds_read_b128 v[186:189], v165 offset:32768
	ds_read_b128 v[190:193], v165 offset:33792
	ds_read_b128 v[194:197], v165 offset:34816
	ds_read_b128 v[198:201], v165 offset:35840
	ds_read_b128 v[202:205], v165 offset:36864
	ds_read_b128 v[210:213], v165 offset:37888
	ds_read_b128 v[214:217], v165 offset:38912
	ds_read_b128 v[218:221], v165 offset:39936
	global_load_lds_dwordx4 v[224:225], off
	v_lshl_add_u64 v[224:225], s[18:19], 0, v[174:175]
	s_mov_b32 m0, s29
	s_nop 0
	global_load_lds_dwordx4 v[224:225], off
	s_waitcnt vmcnt(8)
	s_waitcnt lgkmcnt(0)
	s_setprio 1
	s_barrier
	v_mfma_f32_16x16x32_bf16 v[126:129], v[130:133], v[186:189], v[126:129]
	v_mfma_f32_16x16x32_bf16 v[122:125], v[138:141], v[186:189], v[122:125]
	v_mfma_f32_16x16x32_bf16 v[118:121], v[130:133], v[194:197], v[118:121]
	v_mfma_f32_16x16x32_bf16 v[114:117], v[138:141], v[194:197], v[114:117]
	v_mfma_f32_16x16x32_bf16 v[110:113], v[130:133], v[202:205], v[110:113]
	v_mfma_f32_16x16x32_bf16 v[102:105], v[138:141], v[202:205], v[102:105]
	v_mfma_f32_16x16x32_bf16 v[78:81], v[130:133], v[214:217], v[78:81]
	v_mfma_f32_16x16x32_bf16 v[74:77], v[138:141], v[214:217], v[74:77]
	v_mfma_f32_16x16x32_bf16 v[126:129], v[134:137], v[190:193], v[126:129]
	v_mfma_f32_16x16x32_bf16 v[122:125], v[142:145], v[190:193], v[122:125]
	v_mfma_f32_16x16x32_bf16 v[118:121], v[134:137], v[198:201], v[118:121]
	v_mfma_f32_16x16x32_bf16 v[114:117], v[142:145], v[198:201], v[114:117]
	v_mfma_f32_16x16x32_bf16 v[110:113], v[134:137], v[210:213], v[110:113]
	v_mfma_f32_16x16x32_bf16 v[102:105], v[142:145], v[210:213], v[102:105]
	v_mfma_f32_16x16x32_bf16 v[78:81], v[134:137], v[218:221], v[78:81]
	v_mfma_f32_16x16x32_bf16 v[74:77], v[142:145], v[218:221], v[74:77]
	s_setprio 0
	s_setprio 1
	v_mfma_f32_16x16x32_bf16 v[106:109], v[154:157], v[186:189], v[106:109]
	v_mfma_f32_16x16x32_bf16 v[98:101], v[178:181], v[186:189], v[98:101]
	v_mfma_f32_16x16x32_bf16 v[94:97], v[154:157], v[194:197], v[94:97]
	v_mfma_f32_16x16x32_bf16 v[90:93], v[178:181], v[194:197], v[90:93]
	v_mfma_f32_16x16x32_bf16 v[86:89], v[154:157], v[202:205], v[86:89]
	v_mfma_f32_16x16x32_bf16 v[82:85], v[178:181], v[202:205], v[82:85]
	v_mfma_f32_16x16x32_bf16 v[70:73], v[154:157], v[214:217], v[70:73]
	v_mfma_f32_16x16x32_bf16 v[66:69], v[178:181], v[214:217], v[66:69]
	v_mfma_f32_16x16x32_bf16 v[106:109], v[166:169], v[190:193], v[106:109]
	v_mfma_f32_16x16x32_bf16 v[98:101], v[182:185], v[190:193], v[98:101]
	v_mfma_f32_16x16x32_bf16 v[94:97], v[166:169], v[198:201], v[94:97]
	v_mfma_f32_16x16x32_bf16 v[90:93], v[182:185], v[198:201], v[90:93]
	v_mfma_f32_16x16x32_bf16 v[86:89], v[166:169], v[210:213], v[86:89]
	v_mfma_f32_16x16x32_bf16 v[82:85], v[182:185], v[210:213], v[82:85]
	v_mfma_f32_16x16x32_bf16 v[70:73], v[166:169], v[218:221], v[70:73]
	v_mfma_f32_16x16x32_bf16 v[66:69], v[182:185], v[218:221], v[66:69]
	s_barrier
; #define PG8_STAGE(bufoff, gbase, voff) do { _Pragma("unroll") for (int _i = 0; _i < 2; ++_i) \
;         __builtin_amdgcn_global_load_lds((const unsigned*)((const char*)(gbase) + (voff)[_i]), (PG8_LAS unsigned*)(lds + (bufoff) + ldsw + _i * 8192), 16, 0, 0); } while (0)
; #define PG8_LDA(dst, b, h) do { _Pragma("unroll") for (int m = 0; m < 4; ++m) _Pragma("unroll") for (int k = 0; k < 2; ++k) dst[m][k] = *(const PG8_LAS bf16x8*)(lds + PG8_SA(b, h) + aoff + m * 2048 + k * 1024); } while (0)
; #define PG8_MMA(ai, bj, At, Bt) do { __builtin_amdgcn_s_setprio(1); _Pragma("unroll") for (int m = 0; m < 4; ++m) _Pragma("unroll") for (int n = 0; n < 2; ++n) _Pragma("unroll") for (int k = 0; k < 2; ++k) \
;         acc[ai][bj][m][n] = __builtin_amdgcn_mfma_f32_16x16x32_bf16(Bt[n][k], At[m][k], acc[ai][bj][m][n], 0, 0, 0); __builtin_amdgcn_s_setprio(0); } while (0)
; #define PG8_WAIT_V(n) asm volatile("s_waitcnt vmcnt(" #n ")" ::: "memory")
; #define PG8_WAIT_L(n) asm volatile("s_waitcnt lgkmcnt(" #n ")" ::: "memory")
; #define PG8_BAR __builtin_amdgcn_s_barrier()
; #define PG8_SCHED __builtin_amdgcn_sched_barrier(0)
;     ...
;             PG8_LDA(At, 1, 1); PG8_STAGE(PG8_SB(1, 0), b3, voffB); PG8_STAGE(PG8_SB(1, 1), b3 + hstep, voffB); PG8_STAGE(PG8_SA(1, 0), a3, voffA);
;             PG8_WAIT_V(8); PG8_WAIT_L(0); PG8_BAR; PG8_MMA(1, 0, At, B0); PG8_MMA(1, 1, At, B1); PG8_BAR; PG8_SCHED;
;         }
;         if constexpr (ALIGN_EPI) { if (wr == 0) PG8_BAR; }
	s_setprio 0
	s_add_i32 s18, s47, s25
	v_lshl_add_u64 v[158:159], v[158:159], 0, s[8:9]
	s_mov_b32 m0, s18
	ds_read_b128 v[186:189], v165 offset:49152
	ds_read_b128 v[190:193], v165 offset:50176
	ds_read_b128 v[194:197], v165 offset:51200
	ds_read_b128 v[198:201], v165 offset:52224
	ds_read_b128 v[202:205], v165 offset:53248
	ds_read_b128 v[210:213], v165 offset:54272
	ds_read_b128 v[214:217], v165 offset:55296
	ds_read_b128 v[218:221], v165 offset:56320
	global_load_lds_dwordx4 v[158:159], off
	s_add_i32 m0, s18, 0x2000
	s_add_u32 s16, s16, 0xb0080
	v_lshl_add_u64 v[158:159], v[206:207], 0, s[8:9]
	s_addc_u32 s17, s17, 0
	s_add_i32 s18, s50, s25
	global_load_lds_dwordx4 v[158:159], off
	v_lshl_add_u64 v[158:159], s[16:17], 0, v[172:173]
	s_mov_b32 m0, s18
	s_nop 0
	global_load_lds_dwordx4 v[158:159], off
	v_lshl_add_u64 v[158:159], s[16:17], 0, v[176:177]
	s_add_i32 m0, s18, 0x2000
	s_nop 0
	global_load_lds_dwordx4 v[158:159], off
	v_lshl_add_u64 v[158:159], v[208:209], 0, s[8:9]
	s_mov_b32 m0, s33
	s_nop 0
	global_load_lds_dwordx4 v[158:159], off
	v_lshl_add_u64 v[158:159], v[222:223], 0, s[8:9]
	s_mov_b32 m0, s34
	s_nop 0
	global_load_lds_dwordx4 v[158:159], off
	s_waitcnt vmcnt(8)
	s_waitcnt lgkmcnt(0)
	s_setprio 1
	s_barrier
	v_mfma_f32_16x16x32_bf16 v[62:65], v[130:133], v[186:189], v[62:65]
	v_mfma_f32_16x16x32_bf16 v[58:61], v[138:141], v[186:189], v[58:61]
	v_mfma_f32_16x16x32_bf16 v[54:57], v[130:133], v[194:197], v[54:57]
	v_mfma_f32_16x16x32_bf16 v[46:49], v[138:141], v[194:197], v[46:49]
	v_mfma_f32_16x16x32_bf16 v[38:41], v[130:133], v[202:205], v[38:41]
	v_mfma_f32_16x16x32_bf16 v[30:33], v[138:141], v[202:205], v[30:33]
	v_mfma_f32_16x16x32_bf16 v[22:25], v[130:133], v[214:217], v[22:25]
	v_mfma_f32_16x16x32_bf16 v[14:17], v[138:141], v[214:217], v[14:17]
	v_mfma_f32_16x16x32_bf16 v[62:65], v[134:137], v[190:193], v[62:65]
	v_mfma_f32_16x16x32_bf16 v[58:61], v[142:145], v[190:193], v[58:61]
	v_mfma_f32_16x16x32_bf16 v[54:57], v[134:137], v[198:201], v[54:57]
	v_mfma_f32_16x16x32_bf16 v[46:49], v[142:145], v[198:201], v[46:49]
	v_mfma_f32_16x16x32_bf16 v[38:41], v[134:137], v[210:213], v[38:41]
	v_mfma_f32_16x16x32_bf16 v[30:33], v[142:145], v[210:213], v[30:33]
	v_mfma_f32_16x16x32_bf16 v[22:25], v[134:137], v[218:221], v[22:25]
	v_mfma_f32_16x16x32_bf16 v[14:17], v[142:145], v[218:221], v[14:17]
	s_setprio 0
	s_setprio 1
	v_mfma_f32_16x16x32_bf16 v[50:53], v[154:157], v[186:189], v[50:53]
	v_mfma_f32_16x16x32_bf16 v[42:45], v[178:181], v[186:189], v[42:45]
	v_mfma_f32_16x16x32_bf16 v[34:37], v[154:157], v[194:197], v[34:37]
	v_mfma_f32_16x16x32_bf16 v[26:29], v[178:181], v[194:197], v[26:29]
	v_mfma_f32_16x16x32_bf16 v[18:21], v[154:157], v[202:205], v[18:21]
	v_mfma_f32_16x16x32_bf16 v[10:13], v[178:181], v[202:205], v[10:13]
	v_mfma_f32_16x16x32_bf16 v[6:9], v[154:157], v[214:217], v[6:9]
	v_mfma_f32_16x16x32_bf16 v[2:5], v[178:181], v[214:217], v[2:5]
	v_mfma_f32_16x16x32_bf16 v[50:53], v[166:169], v[190:193], v[50:53]
	v_mfma_f32_16x16x32_bf16 v[42:45], v[182:185], v[190:193], v[42:45]
	v_mfma_f32_16x16x32_bf16 v[34:37], v[166:169], v[198:201], v[34:37]
	v_mfma_f32_16x16x32_bf16 v[26:29], v[182:185], v[198:201], v[26:29]
	v_mfma_f32_16x16x32_bf16 v[18:21], v[166:169], v[210:213], v[18:21]
	v_mfma_f32_16x16x32_bf16 v[10:13], v[182:185], v[210:213], v[10:13]
	v_mfma_f32_16x16x32_bf16 v[6:9], v[166:169], v[218:221], v[6:9]
	v_mfma_f32_16x16x32_bf16 v[2:5], v[182:185], v[218:221], v[2:5]
	s_barrier
	s_setprio 0
	s_add_i32 s46, s46, 2
	s_add_u32 s14, s14, 0x100
	s_addc_u32 s15, s15, 0
	s_add_u32 s0, s0, 0x100
	s_addc_u32 s45, s45, 0
	s_cmp_gt_u32 s46, 19
	s_cbranch_scc0 .LBB0_3370
	s_and_b64 vcc, exec, s[10:11]
	s_cbranch_vccz .LBB0_3373
	s_barrier

; #define PG8_STAGE(bufoff, gbase, voff) do { _Pragma("unroll") for (int _i = 0; _i < 2; ++_i) \
;         __builtin_amdgcn_global_load_lds((const unsigned*)((const char*)(gbase) + (voff)[_i]), (PG8_LAS unsigned*)(lds + (bufoff) + ldsw + _i * 8192), 16, 0, 0); } while (0)
; #define PG8_LDA(dst, b, h) do { _Pragma("unroll") for (int m = 0; m < 4; ++m) _Pragma("unroll") for (int k = 0; k < 2; ++k) dst[m][k] = *(const PG8_LAS bf16x8*)(lds + PG8_SA(b, h) + aoff + m * 2048 + k * 1024); } while (0)
; #define PG8_LDB(dst, b, h) do { _Pragma("unroll") for (int n = 0; n < 2; ++n) _Pragma("unroll") for (int k = 0; k < 2; ++k) dst[n][k] = *(const PG8_LAS bf16x8*)(lds + PG8_SB(b, h) + boff + n * 2048 + k * 1024); } while (0)
; #define PG8_MMA(ai, bj, At, Bt) do { __builtin_amdgcn_s_setprio(1); _Pragma("unroll") for (int m = 0; m < 4; ++m) _Pragma("unroll") for (int n = 0; n < 2; ++n) _Pragma("unroll") for (int k = 0; k < 2; ++k) \
;         acc[ai][bj][m][n] = __builtin_amdgcn_mfma_f32_16x16x32_bf16(Bt[n][k], At[m][k], acc[ai][bj][m][n], 0, 0, 0); __builtin_amdgcn_s_setprio(0); } while (0)
; #define PG8_WAIT_V(n) asm volatile("s_waitcnt vmcnt(" #n ")" ::: "memory")
; #define PG8_WAIT_L(n) asm volatile("s_waitcnt lgkmcnt(" #n ")" ::: "memory")
; #define PG8_BAR __builtin_amdgcn_s_barrier()
; #define PG8_SCHED __builtin_amdgcn_sched_barrier(0)
;     ...
;             const bool last = (t == nt - 2);
;             const char* a1 = cA + (size_t)(t + 1) * kstep;
;             const char* a2 = last ? nA : cA + (size_t)(t + 2) * kstep; const char* b2 = last ? nB : cB + (size_t)(t + 2) * kstep;
;             const char* a3 = a2 + kstep; const char* b3 = b2 + kstep;
;             if (last && has_next) S.a_ready(nxt);
;             PG8_LDB(B0, 0, 0); PG8_LDB(B1, 0, 1); PG8_SCHED; PG8_LDA(At, 0, 0); PG8_STAGE(PG8_SA(1, 1), a1 + hstep, voffA);
;             PG8_WAIT_V(8); PG8_WAIT_L(0); PG8_BAR; PG8_MMA(0, 0, At, B0); PG8_MMA(0, 1, At, B1); PG8_BAR; PG8_SCHED;
;             PG8_LDA(At, 0, 1); PG8_STAGE(PG8_SB(0, 0), b2, voffB); PG8_STAGE(PG8_SB(0, 1), b2 + hstep, voffB); PG8_STAGE(PG8_SA(0, 0), a2, voffA);
.LBB0_3556:
	ds_read_b128 v[148:151], v144
	ds_read_b128 v[152:155], v144 offset:1024
	ds_read_b128 v[156:159], v144 offset:2048
	ds_read_b128 v[160:163], v144 offset:3072
	ds_read_b128 v[164:167], v145
	ds_read_b128 v[168:171], v145 offset:1024
	ds_read_b128 v[172:175], v145 offset:2048
	ds_read_b128 v[176:179], v145 offset:3072
	s_add_u32 s24, s22, 0xfffc0080
	s_addc_u32 s25, s23, -1
	s_cmp_eq_u32 s48, 12
	s_cselect_b32 s27, s19, s25
	s_cselect_b32 s26, s18, s24
	s_cselect_b32 s25, s0, s47
	s_cselect_b32 s24, s15, s17
	v_lshl_add_u64 v[208:209], s[22:23], 0, v[138:139]
	s_add_i32 m0, s9, 0xc000
	ds_read_b128 v[180:183], v146
	ds_read_b128 v[184:187], v146 offset:1024
	ds_read_b128 v[188:191], v146 offset:2048
	ds_read_b128 v[192:195], v146 offset:3072
	ds_read_b128 v[196:199], v146 offset:4096
	ds_read_b128 v[200:203], v146 offset:5120
	ds_read_b128 v[204:207], v146 offset:6144
	ds_read_b128 v[210:213], v146 offset:7168
	global_load_lds_dwordx4 v[208:209], off
	v_lshl_add_u64 v[208:209], s[22:23], 0, v[140:141]
	s_add_i32 m0, s9, 0xe000
	s_nop 0
	global_load_lds_dwordx4 v[208:209], off
	s_waitcnt vmcnt(8)
	s_waitcnt lgkmcnt(0)
	s_setprio 1
	s_barrier
	v_mfma_f32_16x16x32_bf16 v[126:129], v[148:151], v[180:183], v[126:129]
	v_mfma_f32_16x16x32_bf16 v[122:125], v[156:159], v[180:183], v[122:125]
	v_mfma_f32_16x16x32_bf16 v[118:121], v[148:151], v[188:191], v[118:121]
	v_mfma_f32_16x16x32_bf16 v[114:117], v[156:159], v[188:191], v[114:117]
	v_mfma_f32_16x16x32_bf16 v[102:105], v[148:151], v[196:199], v[102:105]
	v_mfma_f32_16x16x32_bf16 v[98:101], v[156:159], v[196:199], v[98:101]
	v_mfma_f32_16x16x32_bf16 v[86:89], v[148:151], v[204:207], v[86:89]
	v_mfma_f32_16x16x32_bf16 v[82:85], v[156:159], v[204:207], v[82:85]
	v_mfma_f32_16x16x32_bf16 v[126:129], v[152:155], v[184:187], v[126:129]
	v_mfma_f32_16x16x32_bf16 v[122:125], v[160:163], v[184:187], v[122:125]
	v_mfma_f32_16x16x32_bf16 v[118:121], v[152:155], v[192:195], v[118:121]
	v_mfma_f32_16x16x32_bf16 v[114:117], v[160:163], v[192:195], v[114:117]
	v_mfma_f32_16x16x32_bf16 v[102:105], v[152:155], v[200:203], v[102:105]
	v_mfma_f32_16x16x32_bf16 v[98:101], v[160:163], v[200:203], v[98:101]
	v_mfma_f32_16x16x32_bf16 v[86:89], v[152:155], v[210:213], v[86:89]
	v_mfma_f32_16x16x32_bf16 v[82:85], v[160:163], v[210:213], v[82:85]
	s_setprio 0
	s_setprio 1
	v_mfma_f32_16x16x32_bf16 v[110:113], v[164:167], v[180:183], v[110:113]
	v_mfma_f32_16x16x32_bf16 v[106:109], v[172:175], v[180:183], v[106:109]
	v_mfma_f32_16x16x32_bf16 v[94:97], v[164:167], v[188:191], v[94:97]
	v_mfma_f32_16x16x32_bf16 v[90:93], v[172:175], v[188:191], v[90:93]
	v_mfma_f32_16x16x32_bf16 v[78:81], v[164:167], v[196:199], v[78:81]
	v_mfma_f32_16x16x32_bf16 v[74:77], v[172:175], v[196:199], v[74:77]
	v_mfma_f32_16x16x32_bf16 v[70:73], v[164:167], v[204:207], v[70:73]
	v_mfma_f32_16x16x32_bf16 v[66:69], v[172:175], v[204:207], v[66:69]
	v_mfma_f32_16x16x32_bf16 v[110:113], v[168:171], v[184:187], v[110:113]
	v_mfma_f32_16x16x32_bf16 v[106:109], v[176:179], v[184:187], v[106:109]
	v_mfma_f32_16x16x32_bf16 v[94:97], v[168:171], v[192:195], v[94:97]
	v_mfma_f32_16x16x32_bf16 v[90:93], v[176:179], v[192:195], v[90:93]
	v_mfma_f32_16x16x32_bf16 v[78:81], v[168:171], v[200:203], v[78:81]
	v_mfma_f32_16x16x32_bf16 v[74:77], v[176:179], v[200:203], v[74:77]
	v_mfma_f32_16x16x32_bf16 v[70:73], v[168:171], v[210:213], v[70:73]
	v_mfma_f32_16x16x32_bf16 v[66:69], v[176:179], v[210:213], v[66:69]
	s_barrier
	s_setprio 0
	s_add_i32 s49, s38, s11
	v_lshl_add_u64 v[208:209], s[24:25], 0, v[132:133]
	s_mov_b32 m0, s49
	ds_read_b128 v[180:183], v146 offset:16384
	ds_read_b128 v[184:187], v146 offset:17408
	ds_read_b128 v[188:191], v146 offset:18432
	ds_read_b128 v[192:195], v146 offset:19456
	ds_read_b128 v[196:199], v146 offset:20480
	ds_read_b128 v[200:203], v146 offset:21504
	ds_read_b128 v[204:207], v146 offset:22528
	ds_read_b128 v[210:213], v146 offset:23552
	global_load_lds_dwordx4 v[208:209], off
	s_add_i32 m0, s49, 0x2000
	s_add_u32 s50, s24, 0x40000
	v_lshl_add_u64 v[214:215], s[24:25], 0, v[136:137]
	s_addc_u32 s51, s25, 0
	s_add_i32 s49, s39, s11
	global_load_lds_dwordx4 v[214:215], off
	v_lshl_add_u64 v[216:217], s[50:51], 0, v[132:133]
	s_mov_b32 m0, s49
	v_lshl_add_u64 v[218:219], s[26:27], 0, v[134:135]
	global_load_lds_dwordx4 v[216:217], off
	v_lshl_add_u64 v[216:217], s[50:51], 0, v[136:137]
	s_add_i32 m0, s49, 0x2000
	s_nop 0
	global_load_lds_dwordx4 v[216:217], off
	v_lshl_add_u64 v[216:217], s[26:27], 0, v[130:131]
	s_mov_b32 m0, s9
	s_nop 0
	global_load_lds_dwordx4 v[216:217], off
	s_mov_b32 m0, s33
	s_nop 0
	global_load_lds_dwordx4 v[218:219], off
	s_waitcnt vmcnt(8)
	s_waitcnt lgkmcnt(0)
	s_setprio 1
	s_barrier
; #define PG8_STAGE(bufoff, gbase, voff) do { _Pragma("unroll") for (int _i = 0; _i < 2; ++_i) \
;         __builtin_amdgcn_global_load_lds((const unsigned*)((const char*)(gbase) + (voff)[_i]), (PG8_LAS unsigned*)(lds + (bufoff) + ldsw + _i * 8192), 16, 0, 0); } while (0)
; #define PG8_LDA(dst, b, h) do { _Pragma("unroll") for (int m = 0; m < 4; ++m) _Pragma("unroll") for (int k = 0; k < 2; ++k) dst[m][k] = *(const PG8_LAS bf16x8*)(lds + PG8_SA(b, h) + aoff + m * 2048 + k * 1024); } while (0)
; #define PG8_LDB(dst, b, h) do { _Pragma("unroll") for (int n = 0; n < 2; ++n) _Pragma("unroll") for (int k = 0; k < 2; ++k) dst[n][k] = *(const PG8_LAS bf16x8*)(lds + PG8_SB(b, h) + boff + n * 2048 + k * 1024); } while (0)
; #define PG8_MMA(ai, bj, At, Bt) do { __builtin_amdgcn_s_setprio(1); _Pragma("unroll") for (int m = 0; m < 4; ++m) _Pragma("unroll") for (int n = 0; n < 2; ++n) _Pragma("unroll") for (int k = 0; k < 2; ++k) \
;         acc[ai][bj][m][n] = __builtin_amdgcn_mfma_f32_16x16x32_bf16(Bt[n][k], At[m][k], acc[ai][bj][m][n], 0, 0, 0); __builtin_amdgcn_s_setprio(0); } while (0)
; #define PG8_WAIT_V(n) asm volatile("s_waitcnt vmcnt(" #n ")" ::: "memory")
; #define PG8_WAIT_L(n) asm volatile("s_waitcnt lgkmcnt(" #n ")" ::: "memory")
; #define PG8_BAR __builtin_amdgcn_s_barrier()
; #define PG8_SCHED __builtin_amdgcn_sched_barrier(0)
;     ...
;             PG8_WAIT_V(8); PG8_WAIT_L(0); PG8_BAR; PG8_MMA(1, 0, At, B0); PG8_MMA(1, 1, At, B1); PG8_BAR; PG8_SCHED;
;             PG8_LDB(B0, 1, 0); PG8_LDB(B1, 1, 1); PG8_SCHED; PG8_LDA(At, 1, 0); PG8_STAGE(PG8_SA(0, 1), a2 + hstep, voffA);
;             PG8_WAIT_V(8); PG8_WAIT_L(0); PG8_BAR; PG8_MMA(0, 0, At, B0); PG8_MMA(0, 1, At, B1); PG8_BAR; PG8_SCHED;
	v_mfma_f32_16x16x32_bf16 v[62:65], v[148:151], v[180:183], v[62:65]
	v_mfma_f32_16x16x32_bf16 v[58:61], v[156:159], v[180:183], v[58:61]
	v_mfma_f32_16x16x32_bf16 v[54:57], v[148:151], v[188:191], v[54:57]
	v_mfma_f32_16x16x32_bf16 v[50:53], v[156:159], v[188:191], v[50:53]
	v_mfma_f32_16x16x32_bf16 v[38:41], v[148:151], v[196:199], v[38:41]
	v_mfma_f32_16x16x32_bf16 v[34:37], v[156:159], v[196:199], v[34:37]
	v_mfma_f32_16x16x32_bf16 v[22:25], v[148:151], v[204:207], v[22:25]
	v_mfma_f32_16x16x32_bf16 v[18:21], v[156:159], v[204:207], v[18:21]
	v_mfma_f32_16x16x32_bf16 v[62:65], v[152:155], v[184:187], v[62:65]
	v_mfma_f32_16x16x32_bf16 v[58:61], v[160:163], v[184:187], v[58:61]
	v_mfma_f32_16x16x32_bf16 v[54:57], v[152:155], v[192:195], v[54:57]
	v_mfma_f32_16x16x32_bf16 v[50:53], v[160:163], v[192:195], v[50:53]
	v_mfma_f32_16x16x32_bf16 v[38:41], v[152:155], v[200:203], v[38:41]
	v_mfma_f32_16x16x32_bf16 v[34:37], v[160:163], v[200:203], v[34:37]
	v_mfma_f32_16x16x32_bf16 v[22:25], v[152:155], v[210:213], v[22:25]
	v_mfma_f32_16x16x32_bf16 v[18:21], v[160:163], v[210:213], v[18:21]
	s_setprio 0
	s_setprio 1
	v_mfma_f32_16x16x32_bf16 v[46:49], v[164:167], v[180:183], v[46:49]
	v_mfma_f32_16x16x32_bf16 v[42:45], v[172:175], v[180:183], v[42:45]
	v_mfma_f32_16x16x32_bf16 v[30:33], v[164:167], v[188:191], v[30:33]
	v_mfma_f32_16x16x32_bf16 v[26:29], v[172:175], v[188:191], v[26:29]
	v_mfma_f32_16x16x32_bf16 v[14:17], v[164:167], v[196:199], v[14:17]
	v_mfma_f32_16x16x32_bf16 v[10:13], v[172:175], v[196:199], v[10:13]
	v_mfma_f32_16x16x32_bf16 v[6:9], v[164:167], v[204:207], v[6:9]
	v_mfma_f32_16x16x32_bf16 v[2:5], v[172:175], v[204:207], v[2:5]
	v_mfma_f32_16x16x32_bf16 v[46:49], v[168:171], v[184:187], v[46:49]
	v_mfma_f32_16x16x32_bf16 v[42:45], v[176:179], v[184:187], v[42:45]
	v_mfma_f32_16x16x32_bf16 v[30:33], v[168:171], v[192:195], v[30:33]
	v_mfma_f32_16x16x32_bf16 v[26:29], v[176:179], v[192:195], v[26:29]
	v_mfma_f32_16x16x32_bf16 v[14:17], v[168:171], v[200:203], v[14:17]
	v_mfma_f32_16x16x32_bf16 v[10:13], v[176:179], v[200:203], v[10:13]
	v_mfma_f32_16x16x32_bf16 v[6:9], v[168:171], v[210:213], v[6:9]
	v_mfma_f32_16x16x32_bf16 v[2:5], v[176:179], v[210:213], v[2:5]
	s_barrier
	s_setprio 0
	s_add_i32 s49, 0, 0x18000
	v_add_u32_e32 v147, s49, v142
	s_add_i32 s50, 0, 0x1c000
	ds_read_b128 v[148:151], v147
	ds_read_b128 v[152:155], v147 offset:1024
	ds_read_b128 v[156:159], v147 offset:2048
	ds_read_b128 v[160:163], v147 offset:3072
	v_add_u32_e32 v147, s50, v142
	ds_read_b128 v[164:167], v147
	ds_read_b128 v[168:171], v147 offset:1024
	ds_read_b128 v[172:175], v147 offset:2048
	ds_read_b128 v[176:179], v147 offset:3072
	s_add_u32 s26, s26, 0x40000
	s_addc_u32 s27, s27, 0
	s_mov_b32 m0, s34
	v_lshl_add_u64 v[220:221], s[26:27], 0, v[130:131]
	ds_read_b128 v[180:183], v146 offset:32768
	ds_read_b128 v[184:187], v146 offset:33792
	ds_read_b128 v[188:191], v146 offset:34816
	ds_read_b128 v[192:195], v146 offset:35840
	ds_read_b128 v[196:199], v146 offset:36864
	ds_read_b128 v[200:203], v146 offset:37888
	ds_read_b128 v[204:207], v146 offset:38912
	ds_read_b128 v[210:213], v146 offset:39936
	global_load_lds_dwordx4 v[220:221], off
	v_lshl_add_u64 v[220:221], s[26:27], 0, v[134:135]
	s_mov_b32 m0, s35
	s_nop 0
	global_load_lds_dwordx4 v[220:221], off
	s_waitcnt vmcnt(8)
	s_waitcnt lgkmcnt(0)
	s_setprio 1
	s_barrier
	v_mfma_f32_16x16x32_bf16 v[126:129], v[148:151], v[180:183], v[126:129]
	v_mfma_f32_16x16x32_bf16 v[122:125], v[156:159], v[180:183], v[122:125]
	v_mfma_f32_16x16x32_bf16 v[118:121], v[148:151], v[188:191], v[118:121]
	v_mfma_f32_16x16x32_bf16 v[114:117], v[156:159], v[188:191], v[114:117]
	v_mfma_f32_16x16x32_bf16 v[102:105], v[148:151], v[196:199], v[102:105]
	v_mfma_f32_16x16x32_bf16 v[98:101], v[156:159], v[196:199], v[98:101]
	v_mfma_f32_16x16x32_bf16 v[86:89], v[148:151], v[204:207], v[86:89]
	v_mfma_f32_16x16x32_bf16 v[82:85], v[156:159], v[204:207], v[82:85]
	v_mfma_f32_16x16x32_bf16 v[126:129], v[152:155], v[184:187], v[126:129]
	v_mfma_f32_16x16x32_bf16 v[122:125], v[160:163], v[184:187], v[122:125]
	v_mfma_f32_16x16x32_bf16 v[118:121], v[152:155], v[192:195], v[118:121]
	v_mfma_f32_16x16x32_bf16 v[114:117], v[160:163], v[192:195], v[114:117]
	v_mfma_f32_16x16x32_bf16 v[102:105], v[152:155], v[200:203], v[102:105]
	v_mfma_f32_16x16x32_bf16 v[98:101], v[160:163], v[200:203], v[98:101]
	v_mfma_f32_16x16x32_bf16 v[86:89], v[152:155], v[210:213], v[86:89]
	v_mfma_f32_16x16x32_bf16 v[82:85], v[160:163], v[210:213], v[82:85]
	s_setprio 0
	s_setprio 1
	v_mfma_f32_16x16x32_bf16 v[110:113], v[164:167], v[180:183], v[110:113]
	v_mfma_f32_16x16x32_bf16 v[106:109], v[172:175], v[180:183], v[106:109]
	v_mfma_f32_16x16x32_bf16 v[94:97], v[164:167], v[188:191], v[94:97]
	v_mfma_f32_16x16x32_bf16 v[90:93], v[172:175], v[188:191], v[90:93]
	v_mfma_f32_16x16x32_bf16 v[78:81], v[164:167], v[196:199], v[78:81]
	v_mfma_f32_16x16x32_bf16 v[74:77], v[172:175], v[196:199], v[74:77]
	v_mfma_f32_16x16x32_bf16 v[70:73], v[164:167], v[204:207], v[70:73]
	v_mfma_f32_16x16x32_bf16 v[66:69], v[172:175], v[204:207], v[66:69]
	v_mfma_f32_16x16x32_bf16 v[110:113], v[168:171], v[184:187], v[110:113]
	v_mfma_f32_16x16x32_bf16 v[106:109], v[176:179], v[184:187], v[106:109]
	v_mfma_f32_16x16x32_bf16 v[94:97], v[168:171], v[192:195], v[94:97]
	v_mfma_f32_16x16x32_bf16 v[90:93], v[176:179], v[192:195], v[90:93]
	v_mfma_f32_16x16x32_bf16 v[78:81], v[168:171], v[200:203], v[78:81]
	v_mfma_f32_16x16x32_bf16 v[74:77], v[176:179], v[200:203], v[74:77]
	v_mfma_f32_16x16x32_bf16 v[70:73], v[168:171], v[210:213], v[70:73]
	v_mfma_f32_16x16x32_bf16 v[66:69], v[176:179], v[210:213], v[66:69]
	s_barrier
; #define PG8_STAGE(bufoff, gbase, voff) do { _Pragma("unroll") for (int _i = 0; _i < 2; ++_i) \
;         __builtin_amdgcn_global_load_lds((const unsigned*)((const char*)(gbase) + (voff)[_i]), (PG8_LAS unsigned*)(lds + (bufoff) + ldsw + _i * 8192), 16, 0, 0); } while (0)
; #define PG8_LDA(dst, b, h) do { _Pragma("unroll") for (int m = 0; m < 4; ++m) _Pragma("unroll") for (int k = 0; k < 2; ++k) dst[m][k] = *(const PG8_LAS bf16x8*)(lds + PG8_SA(b, h) + aoff + m * 2048 + k * 1024); } while (0)
; #define PG8_MMA(ai, bj, At, Bt) do { __builtin_amdgcn_s_setprio(1); _Pragma("unroll") for (int m = 0; m < 4; ++m) _Pragma("unroll") for (int n = 0; n < 2; ++n) _Pragma("unroll") for (int k = 0; k < 2; ++k) \
;         acc[ai][bj][m][n] = __builtin_amdgcn_mfma_f32_16x16x32_bf16(Bt[n][k], At[m][k], acc[ai][bj][m][n], 0, 0, 0); __builtin_amdgcn_s_setprio(0); } while (0)
; #define PG8_WAIT_V(n) asm volatile("s_waitcnt vmcnt(" #n ")" ::: "memory")
; #define PG8_WAIT_L(n) asm volatile("s_waitcnt lgkmcnt(" #n ")" ::: "memory")
; #define PG8_BAR __builtin_amdgcn_s_barrier()
; #define PG8_SCHED __builtin_amdgcn_sched_barrier(0)
;     ...
;             PG8_LDA(At, 1, 1); PG8_STAGE(PG8_SB(1, 0), b3, voffB); PG8_STAGE(PG8_SB(1, 1), b3 + hstep, voffB); PG8_STAGE(PG8_SA(1, 0), a3, voffA);
;             PG8_WAIT_V(8); PG8_WAIT_L(0); PG8_BAR; PG8_MMA(1, 0, At, B0); PG8_MMA(1, 1, At, B1); PG8_BAR; PG8_SCHED;
;         }
;         if constexpr (ALIGN_EPI) { if (wr == 0) PG8_BAR; }
	s_setprio 0
	s_add_i32 s26, s49, s11
	v_lshl_add_u64 v[208:209], v[208:209], 0, s[6:7]
	s_mov_b32 m0, s26
	ds_read_b128 v[180:183], v146 offset:49152
	ds_read_b128 v[184:187], v146 offset:50176
	ds_read_b128 v[188:191], v146 offset:51200
	ds_read_b128 v[192:195], v146 offset:52224
	ds_read_b128 v[196:199], v146 offset:53248
	ds_read_b128 v[200:203], v146 offset:54272
	ds_read_b128 v[204:207], v146 offset:55296
	ds_read_b128 v[210:213], v146 offset:56320
	global_load_lds_dwordx4 v[208:209], off
	s_add_i32 m0, s26, 0x2000
	s_add_u32 s24, s24, 0x40080
	v_lshl_add_u64 v[208:209], v[214:215], 0, s[6:7]
	s_addc_u32 s25, s25, 0
	s_add_i32 s26, s50, s11
	global_load_lds_dwordx4 v[208:209], off
	v_lshl_add_u64 v[208:209], s[24:25], 0, v[132:133]
	s_mov_b32 m0, s26
	s_nop 0
	global_load_lds_dwordx4 v[208:209], off
	v_lshl_add_u64 v[208:209], s[24:25], 0, v[136:137]
	s_add_i32 m0, s26, 0x2000
	s_nop 0
	global_load_lds_dwordx4 v[208:209], off
	v_lshl_add_u64 v[208:209], v[216:217], 0, s[6:7]
	s_mov_b32 m0, s36
	s_nop 0
	global_load_lds_dwordx4 v[208:209], off
	v_lshl_add_u64 v[208:209], v[218:219], 0, s[6:7]
	s_mov_b32 m0, s37
	s_nop 0
	global_load_lds_dwordx4 v[208:209], off
	s_waitcnt vmcnt(8)
	s_waitcnt lgkmcnt(0)
	s_setprio 1
	s_barrier
	v_mfma_f32_16x16x32_bf16 v[62:65], v[148:151], v[180:183], v[62:65]
	v_mfma_f32_16x16x32_bf16 v[58:61], v[156:159], v[180:183], v[58:61]
	v_mfma_f32_16x16x32_bf16 v[54:57], v[148:151], v[188:191], v[54:57]
	v_mfma_f32_16x16x32_bf16 v[50:53], v[156:159], v[188:191], v[50:53]
	v_mfma_f32_16x16x32_bf16 v[38:41], v[148:151], v[196:199], v[38:41]
	v_mfma_f32_16x16x32_bf16 v[34:37], v[156:159], v[196:199], v[34:37]
	v_mfma_f32_16x16x32_bf16 v[22:25], v[148:151], v[204:207], v[22:25]
	v_mfma_f32_16x16x32_bf16 v[18:21], v[156:159], v[204:207], v[18:21]
	v_mfma_f32_16x16x32_bf16 v[62:65], v[152:155], v[184:187], v[62:65]
	v_mfma_f32_16x16x32_bf16 v[58:61], v[160:163], v[184:187], v[58:61]
	v_mfma_f32_16x16x32_bf16 v[54:57], v[152:155], v[192:195], v[54:57]
	v_mfma_f32_16x16x32_bf16 v[50:53], v[160:163], v[192:195], v[50:53]
	v_mfma_f32_16x16x32_bf16 v[38:41], v[152:155], v[200:203], v[38:41]
	v_mfma_f32_16x16x32_bf16 v[34:37], v[160:163], v[200:203], v[34:37]
	v_mfma_f32_16x16x32_bf16 v[22:25], v[152:155], v[210:213], v[22:25]
	v_mfma_f32_16x16x32_bf16 v[18:21], v[160:163], v[210:213], v[18:21]
	s_setprio 0
	s_setprio 1
	v_mfma_f32_16x16x32_bf16 v[46:49], v[164:167], v[180:183], v[46:49]
	v_mfma_f32_16x16x32_bf16 v[42:45], v[172:175], v[180:183], v[42:45]
	v_mfma_f32_16x16x32_bf16 v[30:33], v[164:167], v[188:191], v[30:33]
	v_mfma_f32_16x16x32_bf16 v[26:29], v[172:175], v[188:191], v[26:29]
	v_mfma_f32_16x16x32_bf16 v[14:17], v[164:167], v[196:199], v[14:17]
	v_mfma_f32_16x16x32_bf16 v[10:13], v[172:175], v[196:199], v[10:13]
	v_mfma_f32_16x16x32_bf16 v[6:9], v[164:167], v[204:207], v[6:9]
	v_mfma_f32_16x16x32_bf16 v[2:5], v[172:175], v[204:207], v[2:5]
	v_mfma_f32_16x16x32_bf16 v[46:49], v[168:171], v[184:187], v[46:49]
	v_mfma_f32_16x16x32_bf16 v[42:45], v[176:179], v[184:187], v[42:45]
	v_mfma_f32_16x16x32_bf16 v[30:33], v[168:171], v[192:195], v[30:33]
	v_mfma_f32_16x16x32_bf16 v[26:29], v[176:179], v[192:195], v[26:29]
	v_mfma_f32_16x16x32_bf16 v[14:17], v[168:171], v[200:203], v[14:17]
	v_mfma_f32_16x16x32_bf16 v[10:13], v[176:179], v[200:203], v[10:13]
	v_mfma_f32_16x16x32_bf16 v[6:9], v[168:171], v[210:213], v[6:9]
	v_mfma_f32_16x16x32_bf16 v[2:5], v[176:179], v[210:213], v[2:5]
	s_barrier
	s_setprio 0
	s_add_i32 s48, s48, 2
	s_add_u32 s22, s22, 0x100
	s_addc_u32 s23, s23, 0
	s_add_u32 s17, s17, 0x100
	s_addc_u32 s47, s47, 0
	s_cmp_gt_u32 s48, 13
	s_cbranch_scc0 .LBB0_3556
	s_and_b64 vcc, exec, s[12:13]
	s_cbranch_vccz .LBB0_3559
	s_barrier

; #define PG8_STAGE(bufoff, gbase, voff) do { _Pragma("unroll") for (int _i = 0; _i < 2; ++_i) \
;         __builtin_amdgcn_global_load_lds((const unsigned*)((const char*)(gbase) + (voff)[_i]), (PG8_LAS unsigned*)(lds + (bufoff) + ldsw + _i * 8192), 16, 0, 0); } while (0)
; #define PG8_LDA(dst, b, h) do { _Pragma("unroll") for (int m = 0; m < 4; ++m) _Pragma("unroll") for (int k = 0; k < 2; ++k) dst[m][k] = *(const PG8_LAS bf16x8*)(lds + PG8_SA(b, h) + aoff + m * 2048 + k * 1024); } while (0)
; #define PG8_LDB(dst, b, h) do { _Pragma("unroll") for (int n = 0; n < 2; ++n) _Pragma("unroll") for (int k = 0; k < 2; ++k) dst[n][k] = *(const PG8_LAS bf16x8*)(lds + PG8_SB(b, h) + boff + n * 2048 + k * 1024); } while (0)
; #define PG8_MMA(ai, bj, At, Bt) do { __builtin_amdgcn_s_setprio(1); _Pragma("unroll") for (int m = 0; m < 4; ++m) _Pragma("unroll") for (int n = 0; n < 2; ++n) _Pragma("unroll") for (int k = 0; k < 2; ++k) \
;         acc[ai][bj][m][n] = __builtin_amdgcn_mfma_f32_16x16x32_bf16(Bt[n][k], At[m][k], acc[ai][bj][m][n], 0, 0, 0); __builtin_amdgcn_s_setprio(0); } while (0)
; #define PG8_WAIT_V(n) asm volatile("s_waitcnt vmcnt(" #n ")" ::: "memory")
; #define PG8_WAIT_L(n) asm volatile("s_waitcnt lgkmcnt(" #n ")" ::: "memory")
; #define PG8_BAR __builtin_amdgcn_s_barrier()
; #define PG8_SCHED __builtin_amdgcn_sched_barrier(0)
;     ...
;             const bool last = (t == nt - 2);
;             const char* a1 = cA + (size_t)(t + 1) * kstep;
;             const char* a2 = last ? nA : cA + (size_t)(t + 2) * kstep; const char* b2 = last ? nB : cB + (size_t)(t + 2) * kstep;
;             const char* a3 = a2 + kstep; const char* b3 = b2 + kstep;
;             if (last && has_next) S.a_ready(nxt);
;             PG8_LDB(B0, 0, 0); PG8_LDB(B1, 0, 1); PG8_SCHED; PG8_LDA(At, 0, 0); PG8_STAGE(PG8_SA(1, 1), a1 + hstep, voffA);
;             PG8_WAIT_V(8); PG8_WAIT_L(0); PG8_BAR; PG8_MMA(0, 0, At, B0); PG8_MMA(0, 1, At, B1); PG8_BAR; PG8_SCHED;
;             PG8_LDA(At, 0, 1); PG8_STAGE(PG8_SB(0, 0), b2, voffB); PG8_STAGE(PG8_SB(0, 1), b2 + hstep, voffB); PG8_STAGE(PG8_SA(0, 0), a2, voffA);
.LBB0_4202:
	ds_read_b128 v[130:133], v183
	ds_read_b128 v[134:137], v183 offset:1024
	ds_read_b128 v[138:141], v183 offset:2048
	ds_read_b128 v[142:145], v183 offset:3072
	ds_read_b128 v[178:181], v184
	ds_read_b128 v[186:189], v184 offset:1024
	ds_read_b128 v[190:193], v184 offset:2048
	ds_read_b128 v[194:197], v184 offset:3072
	s_add_u32 s22, s20, 0xfffc0080
	s_addc_u32 s23, s21, -1
	s_cmp_eq_u32 s52, 12
	s_cselect_b32 s25, s13, s23
	s_cselect_b32 s24, s19, s22
	s_cselect_b32 s23, s11, s51
	s_cselect_b32 s22, s49, s50
	v_lshl_add_u64 v[206:207], s[20:21], 0, v[170:171]
	s_add_i32 m0, s33, 0xc000
	ds_read_b128 v[198:201], v185
	ds_read_b128 v[202:205], v185 offset:1024
	ds_read_b128 v[210:213], v185 offset:2048
	ds_read_b128 v[214:217], v185 offset:3072
	ds_read_b128 v[218:221], v185 offset:4096
	ds_read_b128 v[222:225], v185 offset:5120
	ds_read_b128 v[226:229], v185 offset:6144
	ds_read_b128 v[230:233], v185 offset:7168
	global_load_lds_dwordx4 v[206:207], off
	v_lshl_add_u64 v[206:207], s[20:21], 0, v[172:173]
	s_add_i32 m0, s33, 0xe000
	s_nop 0
	global_load_lds_dwordx4 v[206:207], off
	s_waitcnt vmcnt(8)
	s_waitcnt lgkmcnt(0)
	s_setprio 1
	s_barrier
	v_mfma_f32_16x16x32_bf16 v[126:129], v[130:133], v[198:201], v[126:129]
	v_mfma_f32_16x16x32_bf16 v[122:125], v[138:141], v[198:201], v[122:125]
	v_mfma_f32_16x16x32_bf16 v[118:121], v[130:133], v[210:213], v[118:121]
	v_mfma_f32_16x16x32_bf16 v[114:117], v[138:141], v[210:213], v[114:117]
	v_mfma_f32_16x16x32_bf16 v[98:101], v[130:133], v[218:221], v[98:101]
	v_mfma_f32_16x16x32_bf16 v[90:93], v[138:141], v[218:221], v[90:93]
	v_mfma_f32_16x16x32_bf16 v[82:85], v[130:133], v[226:229], v[82:85]
	v_mfma_f32_16x16x32_bf16 v[74:77], v[138:141], v[226:229], v[74:77]
	v_mfma_f32_16x16x32_bf16 v[126:129], v[134:137], v[202:205], v[126:129]
	v_mfma_f32_16x16x32_bf16 v[122:125], v[142:145], v[202:205], v[122:125]
	v_mfma_f32_16x16x32_bf16 v[118:121], v[134:137], v[214:217], v[118:121]
	v_mfma_f32_16x16x32_bf16 v[114:117], v[142:145], v[214:217], v[114:117]
	v_mfma_f32_16x16x32_bf16 v[98:101], v[134:137], v[222:225], v[98:101]
	v_mfma_f32_16x16x32_bf16 v[90:93], v[142:145], v[222:225], v[90:93]
	v_mfma_f32_16x16x32_bf16 v[82:85], v[134:137], v[230:233], v[82:85]
	v_mfma_f32_16x16x32_bf16 v[74:77], v[142:145], v[230:233], v[74:77]
	s_setprio 0
	s_setprio 1
	v_mfma_f32_16x16x32_bf16 v[110:113], v[178:181], v[198:201], v[110:113]
	v_mfma_f32_16x16x32_bf16 v[106:109], v[190:193], v[198:201], v[106:109]
	v_mfma_f32_16x16x32_bf16 v[102:105], v[178:181], v[210:213], v[102:105]
	v_mfma_f32_16x16x32_bf16 v[94:97], v[190:193], v[210:213], v[94:97]
	v_mfma_f32_16x16x32_bf16 v[86:89], v[178:181], v[218:221], v[86:89]
	v_mfma_f32_16x16x32_bf16 v[78:81], v[190:193], v[218:221], v[78:81]
	v_mfma_f32_16x16x32_bf16 v[70:73], v[178:181], v[226:229], v[70:73]
	v_mfma_f32_16x16x32_bf16 v[66:69], v[190:193], v[226:229], v[66:69]
	v_mfma_f32_16x16x32_bf16 v[110:113], v[186:189], v[202:205], v[110:113]
	v_mfma_f32_16x16x32_bf16 v[106:109], v[194:197], v[202:205], v[106:109]
	v_mfma_f32_16x16x32_bf16 v[102:105], v[186:189], v[214:217], v[102:105]
	v_mfma_f32_16x16x32_bf16 v[94:97], v[194:197], v[214:217], v[94:97]
	v_mfma_f32_16x16x32_bf16 v[86:89], v[186:189], v[222:225], v[86:89]
	v_mfma_f32_16x16x32_bf16 v[78:81], v[194:197], v[222:225], v[78:81]
	v_mfma_f32_16x16x32_bf16 v[70:73], v[186:189], v[230:233], v[70:73]
	v_mfma_f32_16x16x32_bf16 v[66:69], v[194:197], v[230:233], v[66:69]
	s_barrier
	s_setprio 0
	s_add_i32 s53, s46, s31
	v_lshl_add_u64 v[206:207], s[22:23], 0, v[148:149]
	s_mov_b32 m0, s53
	ds_read_b128 v[198:201], v185 offset:16384
	ds_read_b128 v[202:205], v185 offset:17408
	ds_read_b128 v[210:213], v185 offset:18432
	ds_read_b128 v[214:217], v185 offset:19456
	ds_read_b128 v[218:221], v185 offset:20480
	ds_read_b128 v[222:225], v185 offset:21504
	ds_read_b128 v[226:229], v185 offset:22528
	ds_read_b128 v[230:233], v185 offset:23552
	global_load_lds_dwordx4 v[206:207], off
	s_add_i32 m0, s53, 0x2000
	s_add_u32 s54, s22, 0x40000
	v_lshl_add_u64 v[208:209], s[22:23], 0, v[152:153]
	s_addc_u32 s55, s23, 0
	s_add_i32 s53, s47, s31
	global_load_lds_dwordx4 v[208:209], off
	v_lshl_add_u64 v[234:235], s[54:55], 0, v[148:149]
	s_mov_b32 m0, s53
	v_lshl_add_u64 v[236:237], s[24:25], 0, v[150:151]
	global_load_lds_dwordx4 v[234:235], off
	v_lshl_add_u64 v[234:235], s[54:55], 0, v[152:153]
	s_add_i32 m0, s53, 0x2000
	s_nop 0
	global_load_lds_dwordx4 v[234:235], off
	v_lshl_add_u64 v[234:235], s[24:25], 0, v[146:147]
	s_mov_b32 m0, s33
	s_nop 0
	global_load_lds_dwordx4 v[234:235], off
	s_mov_b32 m0, s34
	s_nop 0
	global_load_lds_dwordx4 v[236:237], off
	s_waitcnt vmcnt(8)
	s_waitcnt lgkmcnt(0)
	s_setprio 1
	s_barrier
; #define PG8_STAGE(bufoff, gbase, voff) do { _Pragma("unroll") for (int _i = 0; _i < 2; ++_i) \
;         __builtin_amdgcn_global_load_lds((const unsigned*)((const char*)(gbase) + (voff)[_i]), (PG8_LAS unsigned*)(lds + (bufoff) + ldsw + _i * 8192), 16, 0, 0); } while (0)
; #define PG8_LDA(dst, b, h) do { _Pragma("unroll") for (int m = 0; m < 4; ++m) _Pragma("unroll") for (int k = 0; k < 2; ++k) dst[m][k] = *(const PG8_LAS bf16x8*)(lds + PG8_SA(b, h) + aoff + m * 2048 + k * 1024); } while (0)
; #define PG8_LDB(dst, b, h) do { _Pragma("unroll") for (int n = 0; n < 2; ++n) _Pragma("unroll") for (int k = 0; k < 2; ++k) dst[n][k] = *(const PG8_LAS bf16x8*)(lds + PG8_SB(b, h) + boff + n * 2048 + k * 1024); } while (0)
; #define PG8_MMA(ai, bj, At, Bt) do { __builtin_amdgcn_s_setprio(1); _Pragma("unroll") for (int m = 0; m < 4; ++m) _Pragma("unroll") for (int n = 0; n < 2; ++n) _Pragma("unroll") for (int k = 0; k < 2; ++k) \
;         acc[ai][bj][m][n] = __builtin_amdgcn_mfma_f32_16x16x32_bf16(Bt[n][k], At[m][k], acc[ai][bj][m][n], 0, 0, 0); __builtin_amdgcn_s_setprio(0); } while (0)
; #define PG8_WAIT_V(n) asm volatile("s_waitcnt vmcnt(" #n ")" ::: "memory")
; #define PG8_WAIT_L(n) asm volatile("s_waitcnt lgkmcnt(" #n ")" ::: "memory")
; #define PG8_BAR __builtin_amdgcn_s_barrier()
; #define PG8_SCHED __builtin_amdgcn_sched_barrier(0)
;     ...
;             PG8_WAIT_V(8); PG8_WAIT_L(0); PG8_BAR; PG8_MMA(1, 0, At, B0); PG8_MMA(1, 1, At, B1); PG8_BAR; PG8_SCHED;
;             PG8_LDB(B0, 1, 0); PG8_LDB(B1, 1, 1); PG8_SCHED; PG8_LDA(At, 1, 0); PG8_STAGE(PG8_SA(0, 1), a2 + hstep, voffA);
;             PG8_WAIT_V(8); PG8_WAIT_L(0); PG8_BAR; PG8_MMA(0, 0, At, B0); PG8_MMA(0, 1, At, B1); PG8_BAR; PG8_SCHED;
	v_mfma_f32_16x16x32_bf16 v[62:65], v[130:133], v[198:201], v[62:65]
	v_mfma_f32_16x16x32_bf16 v[58:61], v[138:141], v[198:201], v[58:61]
	v_mfma_f32_16x16x32_bf16 v[50:53], v[130:133], v[210:213], v[50:53]
	v_mfma_f32_16x16x32_bf16 v[42:45], v[138:141], v[210:213], v[42:45]
	v_mfma_f32_16x16x32_bf16 v[34:37], v[130:133], v[218:221], v[34:37]
	v_mfma_f32_16x16x32_bf16 v[26:29], v[138:141], v[218:221], v[26:29]
	v_mfma_f32_16x16x32_bf16 v[18:21], v[130:133], v[226:229], v[18:21]
	v_mfma_f32_16x16x32_bf16 v[10:13], v[138:141], v[226:229], v[10:13]
	v_mfma_f32_16x16x32_bf16 v[62:65], v[134:137], v[202:205], v[62:65]
	v_mfma_f32_16x16x32_bf16 v[58:61], v[142:145], v[202:205], v[58:61]
	v_mfma_f32_16x16x32_bf16 v[50:53], v[134:137], v[214:217], v[50:53]
	v_mfma_f32_16x16x32_bf16 v[42:45], v[142:145], v[214:217], v[42:45]
	v_mfma_f32_16x16x32_bf16 v[34:37], v[134:137], v[222:225], v[34:37]
	v_mfma_f32_16x16x32_bf16 v[26:29], v[142:145], v[222:225], v[26:29]
	v_mfma_f32_16x16x32_bf16 v[18:21], v[134:137], v[230:233], v[18:21]
	v_mfma_f32_16x16x32_bf16 v[10:13], v[142:145], v[230:233], v[10:13]
	s_setprio 0
	s_setprio 1
	v_mfma_f32_16x16x32_bf16 v[54:57], v[178:181], v[198:201], v[54:57]
	v_mfma_f32_16x16x32_bf16 v[46:49], v[190:193], v[198:201], v[46:49]
	v_mfma_f32_16x16x32_bf16 v[38:41], v[178:181], v[210:213], v[38:41]
	v_mfma_f32_16x16x32_bf16 v[30:33], v[190:193], v[210:213], v[30:33]
	v_mfma_f32_16x16x32_bf16 v[22:25], v[178:181], v[218:221], v[22:25]
	v_mfma_f32_16x16x32_bf16 v[14:17], v[190:193], v[218:221], v[14:17]
	v_mfma_f32_16x16x32_bf16 v[6:9], v[178:181], v[226:229], v[6:9]
	v_mfma_f32_16x16x32_bf16 v[2:5], v[190:193], v[226:229], v[2:5]
	v_mfma_f32_16x16x32_bf16 v[54:57], v[186:189], v[202:205], v[54:57]
	v_mfma_f32_16x16x32_bf16 v[46:49], v[194:197], v[202:205], v[46:49]
	v_mfma_f32_16x16x32_bf16 v[38:41], v[186:189], v[214:217], v[38:41]
	v_mfma_f32_16x16x32_bf16 v[30:33], v[194:197], v[214:217], v[30:33]
	v_mfma_f32_16x16x32_bf16 v[22:25], v[186:189], v[222:225], v[22:25]
	v_mfma_f32_16x16x32_bf16 v[14:17], v[194:197], v[222:225], v[14:17]
	v_mfma_f32_16x16x32_bf16 v[6:9], v[186:189], v[230:233], v[6:9]
	v_mfma_f32_16x16x32_bf16 v[2:5], v[194:197], v[230:233], v[2:5]
	s_barrier
	s_setprio 0
	s_add_i32 s53, 0, 0x18000
	s_add_i32 s54, 0, 0x1c000
	v_add_u32_e32 v142, s53, v1
	v_add_u32_e32 v194, s54, v1
	ds_read_b128 v[130:133], v142
	ds_read_b128 v[134:137], v142 offset:1024
	ds_read_b128 v[138:141], v142 offset:2048
	ds_read_b128 v[142:145], v142 offset:3072
	ds_read_b128 v[178:181], v194
	ds_read_b128 v[186:189], v194 offset:1024
	ds_read_b128 v[190:193], v194 offset:2048
	ds_read_b128 v[194:197], v194 offset:3072
	s_add_u32 s24, s24, 0x40000
	s_addc_u32 s25, s25, 0
	s_mov_b32 m0, s35
	v_lshl_add_u64 v[238:239], s[24:25], 0, v[146:147]
	ds_read_b128 v[198:201], v185 offset:32768
	ds_read_b128 v[202:205], v185 offset:33792
	ds_read_b128 v[210:213], v185 offset:34816
	ds_read_b128 v[214:217], v185 offset:35840
	ds_read_b128 v[218:221], v185 offset:36864
	ds_read_b128 v[222:225], v185 offset:37888
	ds_read_b128 v[226:229], v185 offset:38912
	ds_read_b128 v[230:233], v185 offset:39936
	global_load_lds_dwordx4 v[238:239], off
	v_lshl_add_u64 v[238:239], s[24:25], 0, v[150:151]
	s_mov_b32 m0, s36
	s_nop 0
	global_load_lds_dwordx4 v[238:239], off
	s_waitcnt vmcnt(8)
	s_waitcnt lgkmcnt(0)
	s_setprio 1
	s_barrier
	v_mfma_f32_16x16x32_bf16 v[126:129], v[130:133], v[198:201], v[126:129]
	v_mfma_f32_16x16x32_bf16 v[122:125], v[138:141], v[198:201], v[122:125]
	v_mfma_f32_16x16x32_bf16 v[118:121], v[130:133], v[210:213], v[118:121]
	v_mfma_f32_16x16x32_bf16 v[114:117], v[138:141], v[210:213], v[114:117]
	v_mfma_f32_16x16x32_bf16 v[98:101], v[130:133], v[218:221], v[98:101]
	v_mfma_f32_16x16x32_bf16 v[90:93], v[138:141], v[218:221], v[90:93]
	v_mfma_f32_16x16x32_bf16 v[82:85], v[130:133], v[226:229], v[82:85]
	v_mfma_f32_16x16x32_bf16 v[74:77], v[138:141], v[226:229], v[74:77]
	v_mfma_f32_16x16x32_bf16 v[126:129], v[134:137], v[202:205], v[126:129]
	v_mfma_f32_16x16x32_bf16 v[122:125], v[142:145], v[202:205], v[122:125]
	v_mfma_f32_16x16x32_bf16 v[118:121], v[134:137], v[214:217], v[118:121]
	v_mfma_f32_16x16x32_bf16 v[114:117], v[142:145], v[214:217], v[114:117]
	v_mfma_f32_16x16x32_bf16 v[98:101], v[134:137], v[222:225], v[98:101]
	v_mfma_f32_16x16x32_bf16 v[90:93], v[142:145], v[222:225], v[90:93]
	v_mfma_f32_16x16x32_bf16 v[82:85], v[134:137], v[230:233], v[82:85]
	v_mfma_f32_16x16x32_bf16 v[74:77], v[142:145], v[230:233], v[74:77]
	s_setprio 0
	s_setprio 1
	v_mfma_f32_16x16x32_bf16 v[110:113], v[178:181], v[198:201], v[110:113]
	v_mfma_f32_16x16x32_bf16 v[106:109], v[190:193], v[198:201], v[106:109]
	v_mfma_f32_16x16x32_bf16 v[102:105], v[178:181], v[210:213], v[102:105]
	v_mfma_f32_16x16x32_bf16 v[94:97], v[190:193], v[210:213], v[94:97]
	v_mfma_f32_16x16x32_bf16 v[86:89], v[178:181], v[218:221], v[86:89]
	v_mfma_f32_16x16x32_bf16 v[78:81], v[190:193], v[218:221], v[78:81]
	v_mfma_f32_16x16x32_bf16 v[70:73], v[178:181], v[226:229], v[70:73]
	v_mfma_f32_16x16x32_bf16 v[66:69], v[190:193], v[226:229], v[66:69]
	v_mfma_f32_16x16x32_bf16 v[110:113], v[186:189], v[202:205], v[110:113]
	v_mfma_f32_16x16x32_bf16 v[106:109], v[194:197], v[202:205], v[106:109]
	v_mfma_f32_16x16x32_bf16 v[102:105], v[186:189], v[214:217], v[102:105]
	v_mfma_f32_16x16x32_bf16 v[94:97], v[194:197], v[214:217], v[94:97]
	v_mfma_f32_16x16x32_bf16 v[86:89], v[186:189], v[222:225], v[86:89]
	v_mfma_f32_16x16x32_bf16 v[78:81], v[194:197], v[222:225], v[78:81]
	v_mfma_f32_16x16x32_bf16 v[70:73], v[186:189], v[230:233], v[70:73]
	v_mfma_f32_16x16x32_bf16 v[66:69], v[194:197], v[230:233], v[66:69]
	s_barrier
; #define PG8_STAGE(bufoff, gbase, voff) do { _Pragma("unroll") for (int _i = 0; _i < 2; ++_i) \
;         __builtin_amdgcn_global_load_lds((const unsigned*)((const char*)(gbase) + (voff)[_i]), (PG8_LAS unsigned*)(lds + (bufoff) + ldsw + _i * 8192), 16, 0, 0); } while (0)
; #define PG8_LDA(dst, b, h) do { _Pragma("unroll") for (int m = 0; m < 4; ++m) _Pragma("unroll") for (int k = 0; k < 2; ++k) dst[m][k] = *(const PG8_LAS bf16x8*)(lds + PG8_SA(b, h) + aoff + m * 2048 + k * 1024); } while (0)
; #define PG8_MMA(ai, bj, At, Bt) do { __builtin_amdgcn_s_setprio(1); _Pragma("unroll") for (int m = 0; m < 4; ++m) _Pragma("unroll") for (int n = 0; n < 2; ++n) _Pragma("unroll") for (int k = 0; k < 2; ++k) \
;         acc[ai][bj][m][n] = __builtin_amdgcn_mfma_f32_16x16x32_bf16(Bt[n][k], At[m][k], acc[ai][bj][m][n], 0, 0, 0); __builtin_amdgcn_s_setprio(0); } while (0)
; #define PG8_WAIT_V(n) asm volatile("s_waitcnt vmcnt(" #n ")" ::: "memory")
; #define PG8_WAIT_L(n) asm volatile("s_waitcnt lgkmcnt(" #n ")" ::: "memory")
; #define PG8_BAR __builtin_amdgcn_s_barrier()
; #define PG8_SCHED __builtin_amdgcn_sched_barrier(0)
;     ...
;             PG8_LDA(At, 1, 1); PG8_STAGE(PG8_SB(1, 0), b3, voffB); PG8_STAGE(PG8_SB(1, 1), b3 + hstep, voffB); PG8_STAGE(PG8_SA(1, 0), a3, voffA);
;             PG8_WAIT_V(8); PG8_WAIT_L(0); PG8_BAR; PG8_MMA(1, 0, At, B0); PG8_MMA(1, 1, At, B1); PG8_BAR; PG8_SCHED;
;         }
;         if constexpr (ALIGN_EPI) { if (wr == 0) PG8_BAR; }
	s_setprio 0
	s_add_i32 s24, s53, s31
	v_lshl_add_u64 v[206:207], v[206:207], 0, s[4:5]
	s_mov_b32 m0, s24
	ds_read_b128 v[198:201], v185 offset:49152
	ds_read_b128 v[202:205], v185 offset:50176
	ds_read_b128 v[210:213], v185 offset:51200
	ds_read_b128 v[214:217], v185 offset:52224
	ds_read_b128 v[218:221], v185 offset:53248
	ds_read_b128 v[222:225], v185 offset:54272
	ds_read_b128 v[226:229], v185 offset:55296
	ds_read_b128 v[230:233], v185 offset:56320
	global_load_lds_dwordx4 v[206:207], off
	s_add_i32 m0, s24, 0x2000
	s_add_u32 s22, s22, 0x40080
	v_lshl_add_u64 v[206:207], v[208:209], 0, s[4:5]
	s_addc_u32 s23, s23, 0
	s_add_i32 s24, s54, s31
	global_load_lds_dwordx4 v[206:207], off
	v_lshl_add_u64 v[206:207], s[22:23], 0, v[148:149]
	s_mov_b32 m0, s24
	s_nop 0
	global_load_lds_dwordx4 v[206:207], off
	v_lshl_add_u64 v[206:207], s[22:23], 0, v[152:153]
	s_add_i32 m0, s24, 0x2000
	s_nop 0
	global_load_lds_dwordx4 v[206:207], off
	v_lshl_add_u64 v[206:207], v[234:235], 0, s[4:5]
	s_mov_b32 m0, s39
	s_nop 0
	global_load_lds_dwordx4 v[206:207], off
	v_lshl_add_u64 v[206:207], v[236:237], 0, s[4:5]
	s_mov_b32 m0, s44
	s_nop 0
	global_load_lds_dwordx4 v[206:207], off
	s_waitcnt vmcnt(8)
	s_waitcnt lgkmcnt(0)
	s_setprio 1
	s_barrier
	v_mfma_f32_16x16x32_bf16 v[62:65], v[130:133], v[198:201], v[62:65]
	v_mfma_f32_16x16x32_bf16 v[58:61], v[138:141], v[198:201], v[58:61]
	v_mfma_f32_16x16x32_bf16 v[50:53], v[130:133], v[210:213], v[50:53]
	v_mfma_f32_16x16x32_bf16 v[42:45], v[138:141], v[210:213], v[42:45]
	v_mfma_f32_16x16x32_bf16 v[34:37], v[130:133], v[218:221], v[34:37]
	v_mfma_f32_16x16x32_bf16 v[26:29], v[138:141], v[218:221], v[26:29]
	v_mfma_f32_16x16x32_bf16 v[18:21], v[130:133], v[226:229], v[18:21]
	v_mfma_f32_16x16x32_bf16 v[10:13], v[138:141], v[226:229], v[10:13]
	v_mfma_f32_16x16x32_bf16 v[62:65], v[134:137], v[202:205], v[62:65]
	v_mfma_f32_16x16x32_bf16 v[58:61], v[142:145], v[202:205], v[58:61]
	v_mfma_f32_16x16x32_bf16 v[50:53], v[134:137], v[214:217], v[50:53]
	v_mfma_f32_16x16x32_bf16 v[42:45], v[142:145], v[214:217], v[42:45]
	v_mfma_f32_16x16x32_bf16 v[34:37], v[134:137], v[222:225], v[34:37]
	v_mfma_f32_16x16x32_bf16 v[26:29], v[142:145], v[222:225], v[26:29]
	v_mfma_f32_16x16x32_bf16 v[18:21], v[134:137], v[230:233], v[18:21]
	v_mfma_f32_16x16x32_bf16 v[10:13], v[142:145], v[230:233], v[10:13]
	s_setprio 0
	s_setprio 1
	v_mfma_f32_16x16x32_bf16 v[54:57], v[178:181], v[198:201], v[54:57]
	v_mfma_f32_16x16x32_bf16 v[46:49], v[190:193], v[198:201], v[46:49]
	v_mfma_f32_16x16x32_bf16 v[38:41], v[178:181], v[210:213], v[38:41]
	v_mfma_f32_16x16x32_bf16 v[30:33], v[190:193], v[210:213], v[30:33]
	v_mfma_f32_16x16x32_bf16 v[22:25], v[178:181], v[218:221], v[22:25]
	v_mfma_f32_16x16x32_bf16 v[14:17], v[190:193], v[218:221], v[14:17]
	v_mfma_f32_16x16x32_bf16 v[6:9], v[178:181], v[226:229], v[6:9]
	v_mfma_f32_16x16x32_bf16 v[2:5], v[190:193], v[226:229], v[2:5]
	v_mfma_f32_16x16x32_bf16 v[54:57], v[186:189], v[202:205], v[54:57]
	v_mfma_f32_16x16x32_bf16 v[46:49], v[194:197], v[202:205], v[46:49]
	v_mfma_f32_16x16x32_bf16 v[38:41], v[186:189], v[214:217], v[38:41]
	v_mfma_f32_16x16x32_bf16 v[30:33], v[194:197], v[214:217], v[30:33]
	v_mfma_f32_16x16x32_bf16 v[22:25], v[186:189], v[222:225], v[22:25]
	v_mfma_f32_16x16x32_bf16 v[14:17], v[194:197], v[222:225], v[14:17]
	v_mfma_f32_16x16x32_bf16 v[6:9], v[186:189], v[230:233], v[6:9]
	v_mfma_f32_16x16x32_bf16 v[2:5], v[194:197], v[230:233], v[2:5]
	s_barrier
	s_setprio 0
	s_add_i32 s52, s52, 2
	s_add_u32 s20, s20, 0x100
	s_addc_u32 s21, s21, 0
	s_add_u32 s50, s50, 0x100
	s_addc_u32 s51, s51, 0
	s_cmp_gt_u32 s52, 13
	s_cbranch_scc0 .LBB0_4202
	s_and_b64 vcc, exec, s[6:7]
	s_cbranch_vccz .LBB0_4205
	s_barrier

; #define PG8_STAGE(bufoff, gbase, voff) do { _Pragma("unroll") for (int _i = 0; _i < 2; ++_i) \
;         __builtin_amdgcn_global_load_lds((const unsigned*)((const char*)(gbase) + (voff)[_i]), (PG8_LAS unsigned*)(lds + (bufoff) + ldsw + _i * 8192), 16, 0, 0); } while (0)
; #define PG8_LDA(dst, b, h) do { _Pragma("unroll") for (int m = 0; m < 4; ++m) _Pragma("unroll") for (int k = 0; k < 2; ++k) dst[m][k] = *(const PG8_LAS bf16x8*)(lds + PG8_SA(b, h) + aoff + m * 2048 + k * 1024); } while (0)
; #define PG8_LDB(dst, b, h) do { _Pragma("unroll") for (int n = 0; n < 2; ++n) _Pragma("unroll") for (int k = 0; k < 2; ++k) dst[n][k] = *(const PG8_LAS bf16x8*)(lds + PG8_SB(b, h) + boff + n * 2048 + k * 1024); } while (0)
; #define PG8_MMA(ai, bj, At, Bt) do { __builtin_amdgcn_s_setprio(1); _Pragma("unroll") for (int m = 0; m < 4; ++m) _Pragma("unroll") for (int n = 0; n < 2; ++n) _Pragma("unroll") for (int k = 0; k < 2; ++k) \
;         acc[ai][bj][m][n] = __builtin_amdgcn_mfma_f32_16x16x32_bf16(Bt[n][k], At[m][k], acc[ai][bj][m][n], 0, 0, 0); __builtin_amdgcn_s_setprio(0); } while (0)
; #define PG8_WAIT_V(n) asm volatile("s_waitcnt vmcnt(" #n ")" ::: "memory")
; #define PG8_WAIT_L(n) asm volatile("s_waitcnt lgkmcnt(" #n ")" ::: "memory")
; #define PG8_BAR __builtin_amdgcn_s_barrier()
; #define PG8_SCHED __builtin_amdgcn_sched_barrier(0)
;     ...
;             const bool last = (t == nt - 2);
;             const char* a1 = cA + (size_t)(t + 1) * kstep;
;             const char* a2 = last ? nA : cA + (size_t)(t + 2) * kstep; const char* b2 = last ? nB : cB + (size_t)(t + 2) * kstep;
;             const char* a3 = a2 + kstep; const char* b3 = b2 + kstep;
;             if (last && has_next) S.a_ready(nxt);
;             PG8_LDB(B0, 0, 0); PG8_LDB(B1, 0, 1); PG8_SCHED; PG8_LDA(At, 0, 0); PG8_STAGE(PG8_SA(1, 1), a1 + hstep, voffA);
;             PG8_WAIT_V(8); PG8_WAIT_L(0); PG8_BAR; PG8_MMA(0, 0, At, B0); PG8_MMA(0, 1, At, B1); PG8_BAR; PG8_SCHED;
;             PG8_LDA(At, 0, 1); PG8_STAGE(PG8_SB(0, 0), b2, voffB); PG8_STAGE(PG8_SB(0, 1), b2 + hstep, voffB); PG8_STAGE(PG8_SA(0, 0), a2, voffA);
.LBB0_4505:
	s_add_u32 s52, s50, 0xfff20080
	s_addc_u32 s53, s51, -1
	s_add_i32 s84, 0, 0x10000
	s_cmp_eq_u32 s83, 52
	s_cselect_b32 s53, s45, s53
	s_cselect_b32 s52, s44, s52
	v_add_u32_e32 v132, s84, v173
	s_cselect_b64 vcc, -1, 0
	s_add_i32 s85, 0, 0x14000
	ds_read_b128 v[176:179], v132
	ds_read_b128 v[180:183], v132 offset:1024
	ds_read_b128 v[184:187], v132 offset:2048
	ds_read_b128 v[188:191], v132 offset:3072
	v_add_u32_e32 v132, s85, v173
	ds_read_b128 v[192:195], v132
	ds_read_b128 v[196:199], v132 offset:1024
	ds_read_b128 v[200:203], v132 offset:2048
	ds_read_b128 v[204:207], v132 offset:3072
	v_cndmask_b32_e32 v209, v165, v163, vcc
	v_cndmask_b32_e32 v208, v164, v162, vcc
	v_lshl_add_u64 v[242:243], s[50:51], 0, v[154:155]
	s_add_i32 m0, s61, 0xc000
	ds_read_b128 v[210:213], v175
	ds_read_b128 v[214:217], v175 offset:1024
	ds_read_b128 v[218:221], v175 offset:2048
	ds_read_b128 v[222:225], v175 offset:3072
	ds_read_b128 v[226:229], v175 offset:4096
	ds_read_b128 v[230:233], v175 offset:5120
	ds_read_b128 v[234:237], v175 offset:6144
	ds_read_b128 v[238:241], v175 offset:7168
	global_load_lds_dwordx4 v[242:243], off
	v_lshl_add_u64 v[242:243], s[50:51], 0, v[156:157]
	s_add_i32 m0, s61, 0xe000
	s_nop 0
	global_load_lds_dwordx4 v[242:243], off
	s_waitcnt vmcnt(8)
	s_waitcnt lgkmcnt(0)
	s_setprio 1
	s_barrier
	v_mfma_f32_16x16x32_bf16 v[126:129], v[176:179], v[210:213], v[126:129]
	v_mfma_f32_16x16x32_bf16 v[122:125], v[184:187], v[210:213], v[122:125]
	v_mfma_f32_16x16x32_bf16 v[118:121], v[176:179], v[218:221], v[118:121]
	v_mfma_f32_16x16x32_bf16 v[114:117], v[184:187], v[218:221], v[114:117]
	v_mfma_f32_16x16x32_bf16 v[106:109], v[176:179], v[226:229], v[106:109]
	v_mfma_f32_16x16x32_bf16 v[98:101], v[184:187], v[226:229], v[98:101]
	v_mfma_f32_16x16x32_bf16 v[78:81], v[176:179], v[234:237], v[78:81]
	v_mfma_f32_16x16x32_bf16 v[74:77], v[184:187], v[234:237], v[74:77]
	v_mfma_f32_16x16x32_bf16 v[126:129], v[180:183], v[214:217], v[126:129]
	v_mfma_f32_16x16x32_bf16 v[122:125], v[188:191], v[214:217], v[122:125]
	v_mfma_f32_16x16x32_bf16 v[118:121], v[180:183], v[222:225], v[118:121]
	v_mfma_f32_16x16x32_bf16 v[114:117], v[188:191], v[222:225], v[114:117]
	v_mfma_f32_16x16x32_bf16 v[106:109], v[180:183], v[230:233], v[106:109]
	v_mfma_f32_16x16x32_bf16 v[98:101], v[188:191], v[230:233], v[98:101]
	v_mfma_f32_16x16x32_bf16 v[78:81], v[180:183], v[238:241], v[78:81]
	v_mfma_f32_16x16x32_bf16 v[74:77], v[188:191], v[238:241], v[74:77]
	s_setprio 0
	s_setprio 1
	v_mfma_f32_16x16x32_bf16 v[110:113], v[192:195], v[210:213], v[110:113]
	v_mfma_f32_16x16x32_bf16 v[102:105], v[200:203], v[210:213], v[102:105]
	v_mfma_f32_16x16x32_bf16 v[94:97], v[192:195], v[218:221], v[94:97]
	v_mfma_f32_16x16x32_bf16 v[90:93], v[200:203], v[218:221], v[90:93]
	v_mfma_f32_16x16x32_bf16 v[86:89], v[192:195], v[226:229], v[86:89]
	v_mfma_f32_16x16x32_bf16 v[82:85], v[200:203], v[226:229], v[82:85]
	v_mfma_f32_16x16x32_bf16 v[70:73], v[192:195], v[234:237], v[70:73]
	v_mfma_f32_16x16x32_bf16 v[66:69], v[200:203], v[234:237], v[66:69]
	v_mfma_f32_16x16x32_bf16 v[110:113], v[196:199], v[214:217], v[110:113]
	v_mfma_f32_16x16x32_bf16 v[102:105], v[204:207], v[214:217], v[102:105]
	v_mfma_f32_16x16x32_bf16 v[94:97], v[196:199], v[222:225], v[94:97]
	v_mfma_f32_16x16x32_bf16 v[90:93], v[204:207], v[222:225], v[90:93]
	v_mfma_f32_16x16x32_bf16 v[86:89], v[196:199], v[230:233], v[86:89]
	v_mfma_f32_16x16x32_bf16 v[82:85], v[204:207], v[230:233], v[82:85]
	v_mfma_f32_16x16x32_bf16 v[70:73], v[196:199], v[238:241], v[70:73]
	v_mfma_f32_16x16x32_bf16 v[66:69], v[204:207], v[238:241], v[66:69]
	s_barrier
	s_setprio 0
	s_add_i32 s84, s84, s60
	v_lshl_add_u64 v[242:243], v[208:209], 0, v[140:141]
	s_mov_b32 m0, s84
	ds_read_b128 v[210:213], v175 offset:16384
	ds_read_b128 v[214:217], v175 offset:17408
	ds_read_b128 v[218:221], v175 offset:18432
	ds_read_b128 v[222:225], v175 offset:19456
	ds_read_b128 v[226:229], v175 offset:20480
	ds_read_b128 v[230:233], v175 offset:21504
	ds_read_b128 v[234:237], v175 offset:22528
	ds_read_b128 v[238:241], v175 offset:23552
	global_load_lds_dwordx4 v[242:243], off
	v_lshl_add_u64 v[244:245], v[208:209], 0, v[144:145]
	s_add_i32 m0, s84, 0x2000
	v_lshl_add_u64 v[246:247], v[208:209], 0, s[24:25]
	s_add_i32 s84, s85, s60
	global_load_lds_dwordx4 v[244:245], off
	v_lshl_add_u64 v[248:249], v[246:247], 0, v[140:141]
	s_mov_b32 m0, s84
	v_lshl_add_u64 v[246:247], v[246:247], 0, v[144:145]
	global_load_lds_dwordx4 v[248:249], off
	s_add_i32 m0, s84, 0x2000
	v_lshl_add_u64 v[248:249], s[52:53], 0, v[142:143]
	global_load_lds_dwordx4 v[246:247], off
	v_lshl_add_u64 v[246:247], s[52:53], 0, v[138:139]
	s_mov_b32 m0, s61
	s_nop 0
	global_load_lds_dwordx4 v[246:247], off
	s_mov_b32 m0, s62
	s_nop 0
	global_load_lds_dwordx4 v[248:249], off
	s_waitcnt vmcnt(8)
	s_waitcnt lgkmcnt(0)
	s_setprio 1
	s_barrier
; #define PG8_STAGE(bufoff, gbase, voff) do { _Pragma("unroll") for (int _i = 0; _i < 2; ++_i) \
;         __builtin_amdgcn_global_load_lds((const unsigned*)((const char*)(gbase) + (voff)[_i]), (PG8_LAS unsigned*)(lds + (bufoff) + ldsw + _i * 8192), 16, 0, 0); } while (0)
; #define PG8_LDA(dst, b, h) do { _Pragma("unroll") for (int m = 0; m < 4; ++m) _Pragma("unroll") for (int k = 0; k < 2; ++k) dst[m][k] = *(const PG8_LAS bf16x8*)(lds + PG8_SA(b, h) + aoff + m * 2048 + k * 1024); } while (0)
; #define PG8_LDB(dst, b, h) do { _Pragma("unroll") for (int n = 0; n < 2; ++n) _Pragma("unroll") for (int k = 0; k < 2; ++k) dst[n][k] = *(const PG8_LAS bf16x8*)(lds + PG8_SB(b, h) + boff + n * 2048 + k * 1024); } while (0)
; #define PG8_MMA(ai, bj, At, Bt) do { __builtin_amdgcn_s_setprio(1); _Pragma("unroll") for (int m = 0; m < 4; ++m) _Pragma("unroll") for (int n = 0; n < 2; ++n) _Pragma("unroll") for (int k = 0; k < 2; ++k) \
;         acc[ai][bj][m][n] = __builtin_amdgcn_mfma_f32_16x16x32_bf16(Bt[n][k], At[m][k], acc[ai][bj][m][n], 0, 0, 0); __builtin_amdgcn_s_setprio(0); } while (0)
; #define PG8_WAIT_V(n) asm volatile("s_waitcnt vmcnt(" #n ")" ::: "memory")
; #define PG8_WAIT_L(n) asm volatile("s_waitcnt lgkmcnt(" #n ")" ::: "memory")
; #define PG8_BAR __builtin_amdgcn_s_barrier()
; #define PG8_SCHED __builtin_amdgcn_sched_barrier(0)
;     ...
;             PG8_WAIT_V(8); PG8_WAIT_L(0); PG8_BAR; PG8_MMA(1, 0, At, B0); PG8_MMA(1, 1, At, B1); PG8_BAR; PG8_SCHED;
;             PG8_LDB(B0, 1, 0); PG8_LDB(B1, 1, 1); PG8_SCHED; PG8_LDA(At, 1, 0); PG8_STAGE(PG8_SA(0, 1), a2 + hstep, voffA);
;             PG8_WAIT_V(8); PG8_WAIT_L(0); PG8_BAR; PG8_MMA(0, 0, At, B0); PG8_MMA(0, 1, At, B1); PG8_BAR; PG8_SCHED;
	v_mfma_f32_16x16x32_bf16 v[62:65], v[176:179], v[210:213], v[62:65]
	v_mfma_f32_16x16x32_bf16 v[58:61], v[184:187], v[210:213], v[58:61]
	v_mfma_f32_16x16x32_bf16 v[54:57], v[176:179], v[218:221], v[54:57]
	v_mfma_f32_16x16x32_bf16 v[46:49], v[184:187], v[218:221], v[46:49]
	v_mfma_f32_16x16x32_bf16 v[38:41], v[176:179], v[226:229], v[38:41]
	v_mfma_f32_16x16x32_bf16 v[30:33], v[184:187], v[226:229], v[30:33]
	v_mfma_f32_16x16x32_bf16 v[22:25], v[176:179], v[234:237], v[22:25]
	v_mfma_f32_16x16x32_bf16 v[14:17], v[184:187], v[234:237], v[14:17]
	v_mfma_f32_16x16x32_bf16 v[62:65], v[180:183], v[214:217], v[62:65]
	v_mfma_f32_16x16x32_bf16 v[58:61], v[188:191], v[214:217], v[58:61]
	v_mfma_f32_16x16x32_bf16 v[54:57], v[180:183], v[222:225], v[54:57]
	v_mfma_f32_16x16x32_bf16 v[46:49], v[188:191], v[222:225], v[46:49]
	v_mfma_f32_16x16x32_bf16 v[38:41], v[180:183], v[230:233], v[38:41]
	v_mfma_f32_16x16x32_bf16 v[30:33], v[188:191], v[230:233], v[30:33]
	v_mfma_f32_16x16x32_bf16 v[22:25], v[180:183], v[238:241], v[22:25]
	v_mfma_f32_16x16x32_bf16 v[14:17], v[188:191], v[238:241], v[14:17]
	s_setprio 0
	s_setprio 1
	v_mfma_f32_16x16x32_bf16 v[50:53], v[192:195], v[210:213], v[50:53]
	v_mfma_f32_16x16x32_bf16 v[42:45], v[200:203], v[210:213], v[42:45]
	v_mfma_f32_16x16x32_bf16 v[34:37], v[192:195], v[218:221], v[34:37]
	v_mfma_f32_16x16x32_bf16 v[26:29], v[200:203], v[218:221], v[26:29]
	v_mfma_f32_16x16x32_bf16 v[18:21], v[192:195], v[226:229], v[18:21]
	v_mfma_f32_16x16x32_bf16 v[10:13], v[200:203], v[226:229], v[10:13]
	v_mfma_f32_16x16x32_bf16 v[6:9], v[192:195], v[234:237], v[6:9]
	v_mfma_f32_16x16x32_bf16 v[2:5], v[200:203], v[234:237], v[2:5]
	v_mfma_f32_16x16x32_bf16 v[50:53], v[196:199], v[214:217], v[50:53]
	v_mfma_f32_16x16x32_bf16 v[42:45], v[204:207], v[214:217], v[42:45]
	v_mfma_f32_16x16x32_bf16 v[34:37], v[196:199], v[222:225], v[34:37]
	v_mfma_f32_16x16x32_bf16 v[26:29], v[204:207], v[222:225], v[26:29]
	v_mfma_f32_16x16x32_bf16 v[18:21], v[196:199], v[230:233], v[18:21]
	v_mfma_f32_16x16x32_bf16 v[10:13], v[204:207], v[230:233], v[10:13]
	v_mfma_f32_16x16x32_bf16 v[6:9], v[196:199], v[238:241], v[6:9]
	v_mfma_f32_16x16x32_bf16 v[2:5], v[204:207], v[238:241], v[2:5]
	s_barrier
	s_setprio 0
	s_add_i32 s84, 0, 0x18000
	v_add_u32_e32 v132, s84, v173
	s_add_i32 s85, 0, 0x1c000
	ds_read_b128 v[176:179], v132
	ds_read_b128 v[180:183], v132 offset:1024
	ds_read_b128 v[184:187], v132 offset:2048
	ds_read_b128 v[188:191], v132 offset:3072
	v_add_u32_e32 v132, s85, v173
	ds_read_b128 v[192:195], v132
	ds_read_b128 v[196:199], v132 offset:1024
	ds_read_b128 v[200:203], v132 offset:2048
	ds_read_b128 v[204:207], v132 offset:3072
	s_add_u32 s52, s52, 0xe0000
	s_addc_u32 s53, s53, 0
	s_mov_b32 m0, s63
	v_lshl_add_u64 v[250:251], s[52:53], 0, v[138:139]
	ds_read_b128 v[210:213], v175 offset:32768
	ds_read_b128 v[214:217], v175 offset:33792
	ds_read_b128 v[218:221], v175 offset:34816
	ds_read_b128 v[222:225], v175 offset:35840
	ds_read_b128 v[226:229], v175 offset:36864
	ds_read_b128 v[230:233], v175 offset:37888
	ds_read_b128 v[234:237], v175 offset:38912
	ds_read_b128 v[238:241], v175 offset:39936
	global_load_lds_dwordx4 v[250:251], off
	v_lshl_add_u64 v[250:251], s[52:53], 0, v[142:143]
	s_mov_b32 m0, s65
	s_nop 0
	global_load_lds_dwordx4 v[250:251], off
	s_waitcnt vmcnt(8)
	s_waitcnt lgkmcnt(0)
	s_setprio 1
	s_barrier
	v_mfma_f32_16x16x32_bf16 v[126:129], v[176:179], v[210:213], v[126:129]
	v_mfma_f32_16x16x32_bf16 v[122:125], v[184:187], v[210:213], v[122:125]
	v_mfma_f32_16x16x32_bf16 v[118:121], v[176:179], v[218:221], v[118:121]
	v_mfma_f32_16x16x32_bf16 v[114:117], v[184:187], v[218:221], v[114:117]
	v_mfma_f32_16x16x32_bf16 v[106:109], v[176:179], v[226:229], v[106:109]
	v_mfma_f32_16x16x32_bf16 v[98:101], v[184:187], v[226:229], v[98:101]
	v_mfma_f32_16x16x32_bf16 v[78:81], v[176:179], v[234:237], v[78:81]
	v_mfma_f32_16x16x32_bf16 v[74:77], v[184:187], v[234:237], v[74:77]
	v_mfma_f32_16x16x32_bf16 v[126:129], v[180:183], v[214:217], v[126:129]
	v_mfma_f32_16x16x32_bf16 v[122:125], v[188:191], v[214:217], v[122:125]
	v_mfma_f32_16x16x32_bf16 v[118:121], v[180:183], v[222:225], v[118:121]
	v_mfma_f32_16x16x32_bf16 v[114:117], v[188:191], v[222:225], v[114:117]
	v_mfma_f32_16x16x32_bf16 v[106:109], v[180:183], v[230:233], v[106:109]
	v_mfma_f32_16x16x32_bf16 v[98:101], v[188:191], v[230:233], v[98:101]
	v_mfma_f32_16x16x32_bf16 v[78:81], v[180:183], v[238:241], v[78:81]
	v_mfma_f32_16x16x32_bf16 v[74:77], v[188:191], v[238:241], v[74:77]
	s_setprio 0
	s_setprio 1
	v_mfma_f32_16x16x32_bf16 v[110:113], v[192:195], v[210:213], v[110:113]
	v_mfma_f32_16x16x32_bf16 v[102:105], v[200:203], v[210:213], v[102:105]
	v_mfma_f32_16x16x32_bf16 v[94:97], v[192:195], v[218:221], v[94:97]
	v_mfma_f32_16x16x32_bf16 v[90:93], v[200:203], v[218:221], v[90:93]
	v_mfma_f32_16x16x32_bf16 v[86:89], v[192:195], v[226:229], v[86:89]
	v_mfma_f32_16x16x32_bf16 v[82:85], v[200:203], v[226:229], v[82:85]
	v_mfma_f32_16x16x32_bf16 v[70:73], v[192:195], v[234:237], v[70:73]
	v_mfma_f32_16x16x32_bf16 v[66:69], v[200:203], v[234:237], v[66:69]
	v_mfma_f32_16x16x32_bf16 v[110:113], v[196:199], v[214:217], v[110:113]
	v_mfma_f32_16x16x32_bf16 v[102:105], v[204:207], v[214:217], v[102:105]
	v_mfma_f32_16x16x32_bf16 v[94:97], v[196:199], v[222:225], v[94:97]
	v_mfma_f32_16x16x32_bf16 v[90:93], v[204:207], v[222:225], v[90:93]
	v_mfma_f32_16x16x32_bf16 v[86:89], v[196:199], v[230:233], v[86:89]
	v_mfma_f32_16x16x32_bf16 v[82:85], v[204:207], v[230:233], v[82:85]
	v_mfma_f32_16x16x32_bf16 v[70:73], v[196:199], v[238:241], v[70:73]
	v_mfma_f32_16x16x32_bf16 v[66:69], v[204:207], v[238:241], v[66:69]
	s_barrier
; #define PG8_STAGE(bufoff, gbase, voff) do { _Pragma("unroll") for (int _i = 0; _i < 2; ++_i) \
;         __builtin_amdgcn_global_load_lds((const unsigned*)((const char*)(gbase) + (voff)[_i]), (PG8_LAS unsigned*)(lds + (bufoff) + ldsw + _i * 8192), 16, 0, 0); } while (0)
; #define PG8_LDA(dst, b, h) do { _Pragma("unroll") for (int m = 0; m < 4; ++m) _Pragma("unroll") for (int k = 0; k < 2; ++k) dst[m][k] = *(const PG8_LAS bf16x8*)(lds + PG8_SA(b, h) + aoff + m * 2048 + k * 1024); } while (0)
; #define PG8_MMA(ai, bj, At, Bt) do { __builtin_amdgcn_s_setprio(1); _Pragma("unroll") for (int m = 0; m < 4; ++m) _Pragma("unroll") for (int n = 0; n < 2; ++n) _Pragma("unroll") for (int k = 0; k < 2; ++k) \
;         acc[ai][bj][m][n] = __builtin_amdgcn_mfma_f32_16x16x32_bf16(Bt[n][k], At[m][k], acc[ai][bj][m][n], 0, 0, 0); __builtin_amdgcn_s_setprio(0); } while (0)
; #define PG8_WAIT_V(n) asm volatile("s_waitcnt vmcnt(" #n ")" ::: "memory")
; #define PG8_WAIT_L(n) asm volatile("s_waitcnt lgkmcnt(" #n ")" ::: "memory")
; #define PG8_BAR __builtin_amdgcn_s_barrier()
; #define PG8_SCHED __builtin_amdgcn_sched_barrier(0)
;     ...
;             PG8_LDA(At, 1, 1); PG8_STAGE(PG8_SB(1, 0), b3, voffB); PG8_STAGE(PG8_SB(1, 1), b3 + hstep, voffB); PG8_STAGE(PG8_SA(1, 0), a3, voffA);
;             PG8_WAIT_V(8); PG8_WAIT_L(0); PG8_BAR; PG8_MMA(1, 0, At, B0); PG8_MMA(1, 1, At, B1); PG8_BAR; PG8_SCHED;
;         }
;         if constexpr (ALIGN_EPI) { if (wr == 0) PG8_BAR; }
	s_setprio 0
	s_add_i32 s52, s84, s60
	v_lshl_add_u64 v[242:243], v[242:243], 0, s[26:27]
	s_mov_b32 m0, s52
	ds_read_b128 v[210:213], v175 offset:49152
	ds_read_b128 v[214:217], v175 offset:50176
	ds_read_b128 v[218:221], v175 offset:51200
	ds_read_b128 v[222:225], v175 offset:52224
	ds_read_b128 v[226:229], v175 offset:53248
	ds_read_b128 v[230:233], v175 offset:54272
	ds_read_b128 v[234:237], v175 offset:55296
	ds_read_b128 v[238:241], v175 offset:56320
	global_load_lds_dwordx4 v[242:243], off
	v_lshl_add_u64 v[242:243], v[244:245], 0, s[26:27]
	s_add_i32 m0, s52, 0x2000
	v_lshl_add_u64 v[208:209], v[208:209], 0, s[28:29]
	s_add_i32 s52, s85, s60
	global_load_lds_dwordx4 v[242:243], off
	v_lshl_add_u64 v[242:243], v[208:209], 0, v[140:141]
	s_mov_b32 m0, s52
	v_lshl_add_u64 v[208:209], v[208:209], 0, v[144:145]
	global_load_lds_dwordx4 v[242:243], off
	s_add_i32 m0, s52, 0x2000
	s_nop 0
	global_load_lds_dwordx4 v[208:209], off
	v_lshl_add_u64 v[208:209], v[246:247], 0, s[26:27]
	s_mov_b32 m0, s78
	s_nop 0
	global_load_lds_dwordx4 v[208:209], off
	v_lshl_add_u64 v[208:209], v[248:249], 0, s[26:27]
	s_mov_b32 m0, s79
	s_nop 0
	global_load_lds_dwordx4 v[208:209], off
	s_waitcnt vmcnt(8)
	s_waitcnt lgkmcnt(0)
	s_setprio 1
	s_barrier
	v_mfma_f32_16x16x32_bf16 v[62:65], v[176:179], v[210:213], v[62:65]
	v_mfma_f32_16x16x32_bf16 v[58:61], v[184:187], v[210:213], v[58:61]
	v_mfma_f32_16x16x32_bf16 v[54:57], v[176:179], v[218:221], v[54:57]
	v_mfma_f32_16x16x32_bf16 v[46:49], v[184:187], v[218:221], v[46:49]
	v_mfma_f32_16x16x32_bf16 v[38:41], v[176:179], v[226:229], v[38:41]
	v_mfma_f32_16x16x32_bf16 v[30:33], v[184:187], v[226:229], v[30:33]
	v_mfma_f32_16x16x32_bf16 v[22:25], v[176:179], v[234:237], v[22:25]
	v_mfma_f32_16x16x32_bf16 v[14:17], v[184:187], v[234:237], v[14:17]
	v_mfma_f32_16x16x32_bf16 v[62:65], v[180:183], v[214:217], v[62:65]
	v_mfma_f32_16x16x32_bf16 v[58:61], v[188:191], v[214:217], v[58:61]
	v_mfma_f32_16x16x32_bf16 v[54:57], v[180:183], v[222:225], v[54:57]
	v_mfma_f32_16x16x32_bf16 v[46:49], v[188:191], v[222:225], v[46:49]
	v_mfma_f32_16x16x32_bf16 v[38:41], v[180:183], v[230:233], v[38:41]
	v_mfma_f32_16x16x32_bf16 v[30:33], v[188:191], v[230:233], v[30:33]
	v_mfma_f32_16x16x32_bf16 v[22:25], v[180:183], v[238:241], v[22:25]
	v_mfma_f32_16x16x32_bf16 v[14:17], v[188:191], v[238:241], v[14:17]
	s_setprio 0
	s_setprio 1
	v_mfma_f32_16x16x32_bf16 v[50:53], v[192:195], v[210:213], v[50:53]
	v_mfma_f32_16x16x32_bf16 v[42:45], v[200:203], v[210:213], v[42:45]
	v_mfma_f32_16x16x32_bf16 v[34:37], v[192:195], v[218:221], v[34:37]
	v_mfma_f32_16x16x32_bf16 v[26:29], v[200:203], v[218:221], v[26:29]
	v_mfma_f32_16x16x32_bf16 v[18:21], v[192:195], v[226:229], v[18:21]
	v_mfma_f32_16x16x32_bf16 v[10:13], v[200:203], v[226:229], v[10:13]
	v_mfma_f32_16x16x32_bf16 v[6:9], v[192:195], v[234:237], v[6:9]
	v_mfma_f32_16x16x32_bf16 v[2:5], v[200:203], v[234:237], v[2:5]
	v_mfma_f32_16x16x32_bf16 v[50:53], v[196:199], v[214:217], v[50:53]
	v_mfma_f32_16x16x32_bf16 v[42:45], v[204:207], v[214:217], v[42:45]
	v_mfma_f32_16x16x32_bf16 v[34:37], v[196:199], v[222:225], v[34:37]
	v_mfma_f32_16x16x32_bf16 v[26:29], v[204:207], v[222:225], v[26:29]
	v_mfma_f32_16x16x32_bf16 v[18:21], v[196:199], v[230:233], v[18:21]
	v_mfma_f32_16x16x32_bf16 v[10:13], v[204:207], v[230:233], v[10:13]
	v_mfma_f32_16x16x32_bf16 v[6:9], v[196:199], v[238:241], v[6:9]
	v_mfma_f32_16x16x32_bf16 v[2:5], v[204:207], v[238:241], v[2:5]
	s_barrier
	s_setprio 0
	s_add_i32 s83, s83, 2
	s_add_u32 s50, s50, 0x100
	s_addc_u32 s51, s51, 0
	s_cmp_gt_u32 s83, 53
	v_lshl_add_u64 v[164:165], v[164:165], 0, s[30:31]
	s_cbranch_scc0 .LBB0_4505
	s_and_b64 vcc, exec, s[22:23]
	s_cbranch_vccz .LBB0_4508
	s_barrier

; #define PG8_STAGE(bufoff, gbase, voff) do { _Pragma("unroll") for (int _i = 0; _i < 2; ++_i) \
;         __builtin_amdgcn_global_load_lds((const unsigned*)((const char*)(gbase) + (voff)[_i]), (PG8_LAS unsigned*)(lds + (bufoff) + ldsw + _i * 8192), 16, 0, 0); } while (0)
; #define PG8_LDA(dst, b, h) do { _Pragma("unroll") for (int m = 0; m < 4; ++m) _Pragma("unroll") for (int k = 0; k < 2; ++k) dst[m][k] = *(const PG8_LAS bf16x8*)(lds + PG8_SA(b, h) + aoff + m * 2048 + k * 1024); } while (0)
; #define PG8_LDB(dst, b, h) do { _Pragma("unroll") for (int n = 0; n < 2; ++n) _Pragma("unroll") for (int k = 0; k < 2; ++k) dst[n][k] = *(const PG8_LAS bf16x8*)(lds + PG8_SB(b, h) + boff + n * 2048 + k * 1024); } while (0)
; #define PG8_MMA(ai, bj, At, Bt) do { __builtin_amdgcn_s_setprio(1); _Pragma("unroll") for (int m = 0; m < 4; ++m) _Pragma("unroll") for (int n = 0; n < 2; ++n) _Pragma("unroll") for (int k = 0; k < 2; ++k) \
;         acc[ai][bj][m][n] = __builtin_amdgcn_mfma_f32_16x16x32_bf16(Bt[n][k], At[m][k], acc[ai][bj][m][n], 0, 0, 0); __builtin_amdgcn_s_setprio(0); } while (0)
; #define PG8_WAIT_V(n) asm volatile("s_waitcnt vmcnt(" #n ")" ::: "memory")
; #define PG8_WAIT_L(n) asm volatile("s_waitcnt lgkmcnt(" #n ")" ::: "memory")
; #define PG8_BAR __builtin_amdgcn_s_barrier()
; #define PG8_SCHED __builtin_amdgcn_sched_barrier(0)
;     ...
;             const bool last = (t == nt - 2);
;             const char* a1 = cA + (size_t)(t + 1) * kstep;
;             const char* a2 = last ? nA : cA + (size_t)(t + 2) * kstep; const char* b2 = last ? nB : cB + (size_t)(t + 2) * kstep;
;             const char* a3 = a2 + kstep; const char* b3 = b2 + kstep;
;             if (last && has_next) S.a_ready(nxt);
;             PG8_LDB(B0, 0, 0); PG8_LDB(B1, 0, 1); PG8_SCHED; PG8_LDA(At, 0, 0); PG8_STAGE(PG8_SA(1, 1), a1 + hstep, voffA);
;             PG8_WAIT_V(8); PG8_WAIT_L(0); PG8_BAR; PG8_MMA(0, 0, At, B0); PG8_MMA(0, 1, At, B1); PG8_BAR; PG8_SCHED;
;             PG8_LDA(At, 0, 1); PG8_STAGE(PG8_SB(0, 0), b2, voffB); PG8_STAGE(PG8_SB(0, 1), b2 + hstep, voffB); PG8_STAGE(PG8_SA(0, 0), a2, voffA);
.LBB0_4534:
	s_add_u32 s56, s54, 0xfffc0080
	s_addc_u32 s57, s55, -1
	s_add_i32 s81, 0, 0x10000
	s_cmp_eq_u32 s80, 12
	s_cselect_b32 s57, s3, s57
	s_cselect_b32 s56, s51, s56
	v_add_u32_e32 v132, s81, v173
	s_cselect_b64 vcc, -1, 0
	s_add_i32 s82, 0, 0x14000
	ds_read_b128 v[176:179], v132
	ds_read_b128 v[180:183], v132 offset:1024
	ds_read_b128 v[184:187], v132 offset:2048
	ds_read_b128 v[188:191], v132 offset:3072
	v_add_u32_e32 v132, s82, v173
	ds_read_b128 v[192:195], v132
	ds_read_b128 v[196:199], v132 offset:1024
	ds_read_b128 v[200:203], v132 offset:2048
	ds_read_b128 v[204:207], v132 offset:3072
	v_cndmask_b32_e32 v209, v165, v163, vcc
	v_cndmask_b32_e32 v208, v164, v162, vcc
	v_lshl_add_u64 v[242:243], s[54:55], 0, v[158:159]
	s_add_i32 m0, s1, 0xc000
	ds_read_b128 v[210:213], v175
	ds_read_b128 v[214:217], v175 offset:1024
	ds_read_b128 v[218:221], v175 offset:2048
	ds_read_b128 v[222:225], v175 offset:3072
	ds_read_b128 v[226:229], v175 offset:4096
	ds_read_b128 v[230:233], v175 offset:5120
	ds_read_b128 v[234:237], v175 offset:6144
	ds_read_b128 v[238:241], v175 offset:7168
	global_load_lds_dwordx4 v[242:243], off
	v_lshl_add_u64 v[242:243], s[54:55], 0, v[160:161]
	s_add_i32 m0, s1, 0xe000
	s_nop 0
	global_load_lds_dwordx4 v[242:243], off
	s_waitcnt vmcnt(8)
	s_waitcnt lgkmcnt(0)
	s_setprio 1
	s_barrier
	v_mfma_f32_16x16x32_bf16 v[126:129], v[176:179], v[210:213], v[126:129]
	v_mfma_f32_16x16x32_bf16 v[122:125], v[184:187], v[210:213], v[122:125]
	v_mfma_f32_16x16x32_bf16 v[110:113], v[176:179], v[218:221], v[110:113]
	v_mfma_f32_16x16x32_bf16 v[106:109], v[184:187], v[218:221], v[106:109]
	v_mfma_f32_16x16x32_bf16 v[94:97], v[176:179], v[226:229], v[94:97]
	v_mfma_f32_16x16x32_bf16 v[90:93], v[184:187], v[226:229], v[90:93]
	v_mfma_f32_16x16x32_bf16 v[78:81], v[176:179], v[234:237], v[78:81]
	v_mfma_f32_16x16x32_bf16 v[74:77], v[184:187], v[234:237], v[74:77]
	v_mfma_f32_16x16x32_bf16 v[126:129], v[180:183], v[214:217], v[126:129]
	v_mfma_f32_16x16x32_bf16 v[122:125], v[188:191], v[214:217], v[122:125]
	v_mfma_f32_16x16x32_bf16 v[110:113], v[180:183], v[222:225], v[110:113]
	v_mfma_f32_16x16x32_bf16 v[106:109], v[188:191], v[222:225], v[106:109]
	v_mfma_f32_16x16x32_bf16 v[94:97], v[180:183], v[230:233], v[94:97]
	v_mfma_f32_16x16x32_bf16 v[90:93], v[188:191], v[230:233], v[90:93]
	v_mfma_f32_16x16x32_bf16 v[78:81], v[180:183], v[238:241], v[78:81]
	v_mfma_f32_16x16x32_bf16 v[74:77], v[188:191], v[238:241], v[74:77]
	s_setprio 0
	s_setprio 1
	v_mfma_f32_16x16x32_bf16 v[118:121], v[192:195], v[210:213], v[118:121]
	v_mfma_f32_16x16x32_bf16 v[114:117], v[200:203], v[210:213], v[114:117]
	v_mfma_f32_16x16x32_bf16 v[102:105], v[192:195], v[218:221], v[102:105]
	v_mfma_f32_16x16x32_bf16 v[98:101], v[200:203], v[218:221], v[98:101]
	v_mfma_f32_16x16x32_bf16 v[86:89], v[192:195], v[226:229], v[86:89]
	v_mfma_f32_16x16x32_bf16 v[82:85], v[200:203], v[226:229], v[82:85]
	v_mfma_f32_16x16x32_bf16 v[70:73], v[192:195], v[234:237], v[70:73]
	v_mfma_f32_16x16x32_bf16 v[66:69], v[200:203], v[234:237], v[66:69]
	v_mfma_f32_16x16x32_bf16 v[118:121], v[196:199], v[214:217], v[118:121]
	v_mfma_f32_16x16x32_bf16 v[114:117], v[204:207], v[214:217], v[114:117]
	v_mfma_f32_16x16x32_bf16 v[102:105], v[196:199], v[222:225], v[102:105]
	v_mfma_f32_16x16x32_bf16 v[98:101], v[204:207], v[222:225], v[98:101]
	v_mfma_f32_16x16x32_bf16 v[86:89], v[196:199], v[230:233], v[86:89]
	v_mfma_f32_16x16x32_bf16 v[82:85], v[204:207], v[230:233], v[82:85]
	v_mfma_f32_16x16x32_bf16 v[70:73], v[196:199], v[238:241], v[70:73]
	v_mfma_f32_16x16x32_bf16 v[66:69], v[204:207], v[238:241], v[66:69]
	s_barrier
	s_setprio 0
	s_add_i32 s81, s81, s0
	v_lshl_add_u64 v[242:243], v[208:209], 0, v[148:149]
	s_mov_b32 m0, s81
	ds_read_b128 v[210:213], v175 offset:16384
	ds_read_b128 v[214:217], v175 offset:17408
	ds_read_b128 v[218:221], v175 offset:18432
	ds_read_b128 v[222:225], v175 offset:19456
	ds_read_b128 v[226:229], v175 offset:20480
	ds_read_b128 v[230:233], v175 offset:21504
	ds_read_b128 v[234:237], v175 offset:22528
	ds_read_b128 v[238:241], v175 offset:23552
	global_load_lds_dwordx4 v[242:243], off
	v_lshl_add_u64 v[244:245], v[208:209], 0, v[152:153]
	s_add_i32 m0, s81, 0x2000
	v_lshl_add_u64 v[246:247], v[208:209], 0, s[34:35]
	s_add_i32 s81, s82, s0
	global_load_lds_dwordx4 v[244:245], off
	v_lshl_add_u64 v[248:249], v[246:247], 0, v[148:149]
	s_mov_b32 m0, s81
	v_lshl_add_u64 v[246:247], v[246:247], 0, v[152:153]
	global_load_lds_dwordx4 v[248:249], off
	s_add_i32 m0, s81, 0x2000
	v_lshl_add_u64 v[248:249], s[56:57], 0, v[150:151]
	global_load_lds_dwordx4 v[246:247], off
	v_lshl_add_u64 v[246:247], s[56:57], 0, v[146:147]
	s_mov_b32 m0, s1
	s_nop 0
	global_load_lds_dwordx4 v[246:247], off
	s_mov_b32 m0, s53
	s_nop 0
	global_load_lds_dwordx4 v[248:249], off
	s_waitcnt vmcnt(8)
	s_waitcnt lgkmcnt(0)
	s_setprio 1
	s_barrier
; #define PG8_STAGE(bufoff, gbase, voff) do { _Pragma("unroll") for (int _i = 0; _i < 2; ++_i) \
;         __builtin_amdgcn_global_load_lds((const unsigned*)((const char*)(gbase) + (voff)[_i]), (PG8_LAS unsigned*)(lds + (bufoff) + ldsw + _i * 8192), 16, 0, 0); } while (0)
; #define PG8_LDA(dst, b, h) do { _Pragma("unroll") for (int m = 0; m < 4; ++m) _Pragma("unroll") for (int k = 0; k < 2; ++k) dst[m][k] = *(const PG8_LAS bf16x8*)(lds + PG8_SA(b, h) + aoff + m * 2048 + k * 1024); } while (0)
; #define PG8_LDB(dst, b, h) do { _Pragma("unroll") for (int n = 0; n < 2; ++n) _Pragma("unroll") for (int k = 0; k < 2; ++k) dst[n][k] = *(const PG8_LAS bf16x8*)(lds + PG8_SB(b, h) + boff + n * 2048 + k * 1024); } while (0)
; #define PG8_MMA(ai, bj, At, Bt) do { __builtin_amdgcn_s_setprio(1); _Pragma("unroll") for (int m = 0; m < 4; ++m) _Pragma("unroll") for (int n = 0; n < 2; ++n) _Pragma("unroll") for (int k = 0; k < 2; ++k) \
;         acc[ai][bj][m][n] = __builtin_amdgcn_mfma_f32_16x16x32_bf16(Bt[n][k], At[m][k], acc[ai][bj][m][n], 0, 0, 0); __builtin_amdgcn_s_setprio(0); } while (0)
; #define PG8_WAIT_V(n) asm volatile("s_waitcnt vmcnt(" #n ")" ::: "memory")
; #define PG8_WAIT_L(n) asm volatile("s_waitcnt lgkmcnt(" #n ")" ::: "memory")
; #define PG8_BAR __builtin_amdgcn_s_barrier()
; #define PG8_SCHED __builtin_amdgcn_sched_barrier(0)
;     ...
;             PG8_WAIT_V(8); PG8_WAIT_L(0); PG8_BAR; PG8_MMA(1, 0, At, B0); PG8_MMA(1, 1, At, B1); PG8_BAR; PG8_SCHED;
;             PG8_LDB(B0, 1, 0); PG8_LDB(B1, 1, 1); PG8_SCHED; PG8_LDA(At, 1, 0); PG8_STAGE(PG8_SA(0, 1), a2 + hstep, voffA);
;             PG8_WAIT_V(8); PG8_WAIT_L(0); PG8_BAR; PG8_MMA(0, 0, At, B0); PG8_MMA(0, 1, At, B1); PG8_BAR; PG8_SCHED;
	v_mfma_f32_16x16x32_bf16 v[62:65], v[176:179], v[210:213], v[62:65]
	v_mfma_f32_16x16x32_bf16 v[58:61], v[184:187], v[210:213], v[58:61]
	v_mfma_f32_16x16x32_bf16 v[46:49], v[176:179], v[218:221], v[46:49]
	v_mfma_f32_16x16x32_bf16 v[42:45], v[184:187], v[218:221], v[42:45]
	v_mfma_f32_16x16x32_bf16 v[30:33], v[176:179], v[226:229], v[30:33]
	v_mfma_f32_16x16x32_bf16 v[26:29], v[184:187], v[226:229], v[26:29]
	v_mfma_f32_16x16x32_bf16 v[14:17], v[176:179], v[234:237], v[14:17]
	v_mfma_f32_16x16x32_bf16 v[10:13], v[184:187], v[234:237], v[10:13]
	v_mfma_f32_16x16x32_bf16 v[62:65], v[180:183], v[214:217], v[62:65]
	v_mfma_f32_16x16x32_bf16 v[58:61], v[188:191], v[214:217], v[58:61]
	v_mfma_f32_16x16x32_bf16 v[46:49], v[180:183], v[222:225], v[46:49]
	v_mfma_f32_16x16x32_bf16 v[42:45], v[188:191], v[222:225], v[42:45]
	v_mfma_f32_16x16x32_bf16 v[30:33], v[180:183], v[230:233], v[30:33]
	v_mfma_f32_16x16x32_bf16 v[26:29], v[188:191], v[230:233], v[26:29]
	v_mfma_f32_16x16x32_bf16 v[14:17], v[180:183], v[238:241], v[14:17]
	v_mfma_f32_16x16x32_bf16 v[10:13], v[188:191], v[238:241], v[10:13]
	s_setprio 0
	s_setprio 1
	v_mfma_f32_16x16x32_bf16 v[54:57], v[192:195], v[210:213], v[54:57]
	v_mfma_f32_16x16x32_bf16 v[50:53], v[200:203], v[210:213], v[50:53]
	v_mfma_f32_16x16x32_bf16 v[38:41], v[192:195], v[218:221], v[38:41]
	v_mfma_f32_16x16x32_bf16 v[34:37], v[200:203], v[218:221], v[34:37]
	v_mfma_f32_16x16x32_bf16 v[22:25], v[192:195], v[226:229], v[22:25]
	v_mfma_f32_16x16x32_bf16 v[18:21], v[200:203], v[226:229], v[18:21]
	v_mfma_f32_16x16x32_bf16 v[6:9], v[192:195], v[234:237], v[6:9]
	v_mfma_f32_16x16x32_bf16 v[2:5], v[200:203], v[234:237], v[2:5]
	v_mfma_f32_16x16x32_bf16 v[54:57], v[196:199], v[214:217], v[54:57]
	v_mfma_f32_16x16x32_bf16 v[50:53], v[204:207], v[214:217], v[50:53]
	v_mfma_f32_16x16x32_bf16 v[38:41], v[196:199], v[222:225], v[38:41]
	v_mfma_f32_16x16x32_bf16 v[34:37], v[204:207], v[222:225], v[34:37]
	v_mfma_f32_16x16x32_bf16 v[22:25], v[196:199], v[230:233], v[22:25]
	v_mfma_f32_16x16x32_bf16 v[18:21], v[204:207], v[230:233], v[18:21]
	v_mfma_f32_16x16x32_bf16 v[6:9], v[196:199], v[238:241], v[6:9]
	v_mfma_f32_16x16x32_bf16 v[2:5], v[204:207], v[238:241], v[2:5]
	s_barrier
	s_setprio 0
	s_add_i32 s81, 0, 0x18000
	v_add_u32_e32 v132, s81, v173
	s_add_i32 s82, 0, 0x1c000
	ds_read_b128 v[176:179], v132
	ds_read_b128 v[180:183], v132 offset:1024
	ds_read_b128 v[184:187], v132 offset:2048
	ds_read_b128 v[188:191], v132 offset:3072
	v_add_u32_e32 v132, s82, v173
	ds_read_b128 v[192:195], v132
	ds_read_b128 v[196:199], v132 offset:1024
	ds_read_b128 v[200:203], v132 offset:2048
	ds_read_b128 v[204:207], v132 offset:3072
	s_add_u32 s56, s56, 0x40000
	s_addc_u32 s57, s57, 0
	s_mov_b32 m0, s33
	v_lshl_add_u64 v[250:251], s[56:57], 0, v[146:147]
	ds_read_b128 v[210:213], v175 offset:32768
	ds_read_b128 v[214:217], v175 offset:33792
	ds_read_b128 v[218:221], v175 offset:34816
	ds_read_b128 v[222:225], v175 offset:35840
	ds_read_b128 v[226:229], v175 offset:36864
	ds_read_b128 v[230:233], v175 offset:37888
	ds_read_b128 v[234:237], v175 offset:38912
	ds_read_b128 v[238:241], v175 offset:39936
	global_load_lds_dwordx4 v[250:251], off
	v_lshl_add_u64 v[250:251], s[56:57], 0, v[150:151]
	s_mov_b32 m0, s65
	s_nop 0
	global_load_lds_dwordx4 v[250:251], off
	s_waitcnt vmcnt(8)
	s_waitcnt lgkmcnt(0)
	s_setprio 1
	s_barrier
	v_mfma_f32_16x16x32_bf16 v[126:129], v[176:179], v[210:213], v[126:129]
	v_mfma_f32_16x16x32_bf16 v[122:125], v[184:187], v[210:213], v[122:125]
	v_mfma_f32_16x16x32_bf16 v[110:113], v[176:179], v[218:221], v[110:113]
	v_mfma_f32_16x16x32_bf16 v[106:109], v[184:187], v[218:221], v[106:109]
	v_mfma_f32_16x16x32_bf16 v[94:97], v[176:179], v[226:229], v[94:97]
	v_mfma_f32_16x16x32_bf16 v[90:93], v[184:187], v[226:229], v[90:93]
	v_mfma_f32_16x16x32_bf16 v[78:81], v[176:179], v[234:237], v[78:81]
	v_mfma_f32_16x16x32_bf16 v[74:77], v[184:187], v[234:237], v[74:77]
	v_mfma_f32_16x16x32_bf16 v[126:129], v[180:183], v[214:217], v[126:129]
	v_mfma_f32_16x16x32_bf16 v[122:125], v[188:191], v[214:217], v[122:125]
	v_mfma_f32_16x16x32_bf16 v[110:113], v[180:183], v[222:225], v[110:113]
	v_mfma_f32_16x16x32_bf16 v[106:109], v[188:191], v[222:225], v[106:109]
	v_mfma_f32_16x16x32_bf16 v[94:97], v[180:183], v[230:233], v[94:97]
	v_mfma_f32_16x16x32_bf16 v[90:93], v[188:191], v[230:233], v[90:93]
	v_mfma_f32_16x16x32_bf16 v[78:81], v[180:183], v[238:241], v[78:81]
	v_mfma_f32_16x16x32_bf16 v[74:77], v[188:191], v[238:241], v[74:77]
	s_setprio 0
	s_setprio 1
	v_mfma_f32_16x16x32_bf16 v[118:121], v[192:195], v[210:213], v[118:121]
	v_mfma_f32_16x16x32_bf16 v[114:117], v[200:203], v[210:213], v[114:117]
	v_mfma_f32_16x16x32_bf16 v[102:105], v[192:195], v[218:221], v[102:105]
	v_mfma_f32_16x16x32_bf16 v[98:101], v[200:203], v[218:221], v[98:101]
	v_mfma_f32_16x16x32_bf16 v[86:89], v[192:195], v[226:229], v[86:89]
	v_mfma_f32_16x16x32_bf16 v[82:85], v[200:203], v[226:229], v[82:85]
	v_mfma_f32_16x16x32_bf16 v[70:73], v[192:195], v[234:237], v[70:73]
	v_mfma_f32_16x16x32_bf16 v[66:69], v[200:203], v[234:237], v[66:69]
	v_mfma_f32_16x16x32_bf16 v[118:121], v[196:199], v[214:217], v[118:121]
	v_mfma_f32_16x16x32_bf16 v[114:117], v[204:207], v[214:217], v[114:117]
	v_mfma_f32_16x16x32_bf16 v[102:105], v[196:199], v[222:225], v[102:105]
	v_mfma_f32_16x16x32_bf16 v[98:101], v[204:207], v[222:225], v[98:101]
	v_mfma_f32_16x16x32_bf16 v[86:89], v[196:199], v[230:233], v[86:89]
	v_mfma_f32_16x16x32_bf16 v[82:85], v[204:207], v[230:233], v[82:85]
	v_mfma_f32_16x16x32_bf16 v[70:73], v[196:199], v[238:241], v[70:73]
	v_mfma_f32_16x16x32_bf16 v[66:69], v[204:207], v[238:241], v[66:69]
	s_barrier
; #define PG8_STAGE(bufoff, gbase, voff) do { _Pragma("unroll") for (int _i = 0; _i < 2; ++_i) \
;         __builtin_amdgcn_global_load_lds((const unsigned*)((const char*)(gbase) + (voff)[_i]), (PG8_LAS unsigned*)(lds + (bufoff) + ldsw + _i * 8192), 16, 0, 0); } while (0)
; #define PG8_LDA(dst, b, h) do { _Pragma("unroll") for (int m = 0; m < 4; ++m) _Pragma("unroll") for (int k = 0; k < 2; ++k) dst[m][k] = *(const PG8_LAS bf16x8*)(lds + PG8_SA(b, h) + aoff + m * 2048 + k * 1024); } while (0)
; #define PG8_MMA(ai, bj, At, Bt) do { __builtin_amdgcn_s_setprio(1); _Pragma("unroll") for (int m = 0; m < 4; ++m) _Pragma("unroll") for (int n = 0; n < 2; ++n) _Pragma("unroll") for (int k = 0; k < 2; ++k) \
;         acc[ai][bj][m][n] = __builtin_amdgcn_mfma_f32_16x16x32_bf16(Bt[n][k], At[m][k], acc[ai][bj][m][n], 0, 0, 0); __builtin_amdgcn_s_setprio(0); } while (0)
; #define PG8_WAIT_V(n) asm volatile("s_waitcnt vmcnt(" #n ")" ::: "memory")
; #define PG8_WAIT_L(n) asm volatile("s_waitcnt lgkmcnt(" #n ")" ::: "memory")
; #define PG8_BAR __builtin_amdgcn_s_barrier()
; #define PG8_SCHED __builtin_amdgcn_sched_barrier(0)
;     ...
;             PG8_LDA(At, 1, 1); PG8_STAGE(PG8_SB(1, 0), b3, voffB); PG8_STAGE(PG8_SB(1, 1), b3 + hstep, voffB); PG8_STAGE(PG8_SA(1, 0), a3, voffA);
;             PG8_WAIT_V(8); PG8_WAIT_L(0); PG8_BAR; PG8_MMA(1, 0, At, B0); PG8_MMA(1, 1, At, B1); PG8_BAR; PG8_SCHED;
;         }
;         if constexpr (ALIGN_EPI) { if (wr == 0) PG8_BAR; }
	s_setprio 0
	s_add_i32 s56, s81, s0
	v_lshl_add_u64 v[242:243], v[242:243], 0, s[26:27]
	s_mov_b32 m0, s56
	ds_read_b128 v[210:213], v175 offset:49152
	ds_read_b128 v[214:217], v175 offset:50176
	ds_read_b128 v[218:221], v175 offset:51200
	ds_read_b128 v[222:225], v175 offset:52224
	ds_read_b128 v[226:229], v175 offset:53248
	ds_read_b128 v[230:233], v175 offset:54272
	ds_read_b128 v[234:237], v175 offset:55296
	ds_read_b128 v[238:241], v175 offset:56320
	global_load_lds_dwordx4 v[242:243], off
	v_lshl_add_u64 v[242:243], v[244:245], 0, s[26:27]
	s_add_i32 m0, s56, 0x2000
	v_lshl_add_u64 v[208:209], v[208:209], 0, s[36:37]
	s_add_i32 s56, s82, s0
	global_load_lds_dwordx4 v[242:243], off
	v_lshl_add_u64 v[242:243], v[208:209], 0, v[148:149]
	s_mov_b32 m0, s56
	v_lshl_add_u64 v[208:209], v[208:209], 0, v[152:153]
	global_load_lds_dwordx4 v[242:243], off
	s_add_i32 m0, s56, 0x2000
	s_nop 0
	global_load_lds_dwordx4 v[208:209], off
	v_lshl_add_u64 v[208:209], v[246:247], 0, s[26:27]
	s_mov_b32 m0, s78
	s_nop 0
	global_load_lds_dwordx4 v[208:209], off
	v_lshl_add_u64 v[208:209], v[248:249], 0, s[26:27]
	s_mov_b32 m0, s79
	s_nop 0
	global_load_lds_dwordx4 v[208:209], off
	s_waitcnt vmcnt(8)
	s_waitcnt lgkmcnt(0)
	s_setprio 1
	s_barrier
	v_mfma_f32_16x16x32_bf16 v[62:65], v[176:179], v[210:213], v[62:65]
	v_mfma_f32_16x16x32_bf16 v[58:61], v[184:187], v[210:213], v[58:61]
	v_mfma_f32_16x16x32_bf16 v[46:49], v[176:179], v[218:221], v[46:49]
	v_mfma_f32_16x16x32_bf16 v[42:45], v[184:187], v[218:221], v[42:45]
	v_mfma_f32_16x16x32_bf16 v[30:33], v[176:179], v[226:229], v[30:33]
	v_mfma_f32_16x16x32_bf16 v[26:29], v[184:187], v[226:229], v[26:29]
	v_mfma_f32_16x16x32_bf16 v[14:17], v[176:179], v[234:237], v[14:17]
	v_mfma_f32_16x16x32_bf16 v[10:13], v[184:187], v[234:237], v[10:13]
	v_mfma_f32_16x16x32_bf16 v[62:65], v[180:183], v[214:217], v[62:65]
	v_mfma_f32_16x16x32_bf16 v[58:61], v[188:191], v[214:217], v[58:61]
	v_mfma_f32_16x16x32_bf16 v[46:49], v[180:183], v[222:225], v[46:49]
	v_mfma_f32_16x16x32_bf16 v[42:45], v[188:191], v[222:225], v[42:45]
	v_mfma_f32_16x16x32_bf16 v[30:33], v[180:183], v[230:233], v[30:33]
	v_mfma_f32_16x16x32_bf16 v[26:29], v[188:191], v[230:233], v[26:29]
	v_mfma_f32_16x16x32_bf16 v[14:17], v[180:183], v[238:241], v[14:17]
	v_mfma_f32_16x16x32_bf16 v[10:13], v[188:191], v[238:241], v[10:13]
	s_setprio 0
	s_setprio 1
	v_mfma_f32_16x16x32_bf16 v[54:57], v[192:195], v[210:213], v[54:57]
	v_mfma_f32_16x16x32_bf16 v[50:53], v[200:203], v[210:213], v[50:53]
	v_mfma_f32_16x16x32_bf16 v[38:41], v[192:195], v[218:221], v[38:41]
	v_mfma_f32_16x16x32_bf16 v[34:37], v[200:203], v[218:221], v[34:37]
	v_mfma_f32_16x16x32_bf16 v[22:25], v[192:195], v[226:229], v[22:25]
	v_mfma_f32_16x16x32_bf16 v[18:21], v[200:203], v[226:229], v[18:21]
	v_mfma_f32_16x16x32_bf16 v[6:9], v[192:195], v[234:237], v[6:9]
	v_mfma_f32_16x16x32_bf16 v[2:5], v[200:203], v[234:237], v[2:5]
	v_mfma_f32_16x16x32_bf16 v[54:57], v[196:199], v[214:217], v[54:57]
	v_mfma_f32_16x16x32_bf16 v[50:53], v[204:207], v[214:217], v[50:53]
	v_mfma_f32_16x16x32_bf16 v[38:41], v[196:199], v[222:225], v[38:41]
	v_mfma_f32_16x16x32_bf16 v[34:37], v[204:207], v[222:225], v[34:37]
	v_mfma_f32_16x16x32_bf16 v[22:25], v[196:199], v[230:233], v[22:25]
	v_mfma_f32_16x16x32_bf16 v[18:21], v[204:207], v[230:233], v[18:21]
	v_mfma_f32_16x16x32_bf16 v[6:9], v[196:199], v[238:241], v[6:9]
	v_mfma_f32_16x16x32_bf16 v[2:5], v[204:207], v[238:241], v[2:5]
	s_barrier
	s_setprio 0
	s_add_i32 s80, s80, 2
	s_add_u32 s54, s54, 0x100
	s_addc_u32 s55, s55, 0
	s_cmp_gt_u32 s80, 13
	v_lshl_add_u64 v[164:165], v[164:165], 0, s[30:31]
	s_cbranch_scc0 .LBB0_4534
	s_and_b64 vcc, exec, s[44:45]
	s_cbranch_vccz .LBB0_4537
	s_barrier
